# v36 + static s_setprio 1 for waves 4..7 (second wave of each SIMD) inside the six bf16-weight GEMM K-loops (in-proj, S, Y, GLU, out-proj x2), reset after each loop
# speedup vs baseline: 1.0066x; 1.0066x over previous
.LBB0_429:
	s_ashr_i32 s1, s0, 5
	s_lshr_b32 s2, s1, 30
	s_add_i32 s4, s1, s2
	s_and_b32 s2, s4, 0x3ffffc
	s_sub_i32 s1, s1, s2
	s_lshl_b32 s47, s1, 10
	s_lshl_b32 s1, s0, 5
	s_and_b32 s1, s1, 0x300
	s_or_b32 s28, s47, s1
	s_ashr_i32 s29, s28, 31
	s_lshl_b64 s[2:3], s[28:29], 1
	s_add_u32 s6, s36, s2
	s_addc_u32 s7, s37, s3
	s_lshl_b32 s1, s4, 9
	s_lshl_b32 s0, s0, 8
	s_and_b32 s8, s1, 0xfffff800
	s_and_b32 s9, s0, 0x700
	s_or_b32 s50, s8, s9
	v_readfirstlane_b32 s0, v0
	s_lshr_b32 s29, s0, 6
	v_or_b32_e32 v2, s50, v149
	v_lshlrev_b32_e32 v2, 12, v2
	s_lshl_b32 s14, s29, 1
	v_or_b32_e32 v18, v2, v154
	v_add_u32_e32 v19, v2, v163
	v_add_u32_e32 v20, v2, v164
	v_or_b32_e32 v2, s14, v156
	s_and_b32 s1, s29, 4
	s_bfe_u32 s51, s0, 0x20006
	v_and_or_b32 v4, v2, 3, s1
	s_lshr_b32 s1, s0, 1
	s_and_b32 s52, s1, 0x7fffff80
	s_lshl_b32 s1, s51, 7
	s_or_b32 s2, s1, 32
	v_bitop3_b32 v152, s2, v165, v161 bitop3:0xde
	s_or_b32 s2, s1, 64
	v_bitop3_b32 v153, s1, v165, v161 bitop3:0xde
	v_bitop3_b32 v151, s2, v165, v161 bitop3:0xde
	s_or_b32 s1, s1, 0x60
	s_lshl_b32 s2, s29, 10
	v_bitop3_b32 v146, s1, v165, v161 bitop3:0xde
	s_add_i32 s2, s2, 0
	s_mov_b32 s1, m0
	s_mov_b32 m0, s2
	s_nop 0
	global_load_lds_dwordx4 v18, s[16:17]
	s_mov_b32 m0, s1
	s_add_i32 s1, s2, 0x2000
	s_mov_b32 s3, m0
	s_mov_b32 m0, s1
	s_nop 0
	global_load_lds_dwordx4 v19, s[16:17]
	s_mov_b32 m0, s3
	s_add_i32 s1, s2, 0x4000
	v_or_b32_e32 v3, 0x80000, v18
	s_mov_b32 s3, m0
	s_mov_b32 m0, s1
	s_nop 0
	global_load_lds_dwordx4 v3, s[16:17]
	s_mov_b32 m0, s3
	s_add_i32 s1, s2, 0x6000
	s_lshl_b64 s[4:5], s[14:15], 13
	s_add_u32 s4, s6, s4
	v_lshlrev_b32_e32 v4, 5, v4
	v_or_b32_e32 v5, s52, v1
	v_lshlrev_b32_e32 v2, 9, v2
	s_addc_u32 s5, s7, s5
	v_lshlrev_b32_e32 v34, 7, v5
	v_bitop3_b32 v168, v4, v2, v157 bitop3:0xde
	s_mov_b32 s3, m0
	s_mov_b32 m0, s1
	s_nop 0
	global_load_lds_dwordx4 v20, s[16:17]
	s_mov_b32 m0, s3
	global_load_dwordx4 v[2:5], v162, s[4:5]
	s_add_i32 s4, s14, 16
	s_mov_b32 s5, s15
	s_lshl_b64 s[4:5], s[4:5], 13
	s_add_u32 s4, s6, s4
	s_addc_u32 s5, s7, s5
	global_load_dwordx4 v[6:9], v162, s[4:5]
	s_add_i32 s4, s14, 32
	s_mov_b32 s5, s15
	s_lshl_b64 s[4:5], s[4:5], 13
	s_add_u32 s4, s6, s4
	s_addc_u32 s5, s7, s5
	global_load_dwordx4 v[10:13], v162, s[4:5]
	s_add_i32 s4, s14, 48
	s_mov_b32 s5, s15
	s_lshl_b64 s[4:5], s[4:5], 13
	s_add_u32 s4, s6, s4
	s_addc_u32 s5, s7, s5
	s_add_i32 s1, s2, 0x8000
	global_load_dwordx4 v[14:17], v162, s[4:5]
	v_or_b32_e32 v21, 0x80, v18
	s_mov_b32 s3, m0
	s_mov_b32 m0, s1
	s_nop 0
	global_load_lds_dwordx4 v21, s[16:17]
	s_mov_b32 m0, s3
	s_add_i32 s1, s2, 0xa000
	v_or_b32_e32 v18, 0x80080, v18
	v_or_b32_e32 v19, 0x80, v19
	s_mov_b32 s3, m0
	s_mov_b32 m0, s1
	s_nop 0
	global_load_lds_dwordx4 v19, s[16:17]
	s_mov_b32 m0, s3
	s_add_i32 s1, s2, 0xc000
	s_mov_b32 s3, m0
	s_mov_b32 m0, s1
	s_nop 0
	global_load_lds_dwordx4 v18, s[16:17]
	s_mov_b32 m0, s3
	v_or_b32_e32 v18, 0x80, v20
	s_add_i32 s4, s14, 64
	s_mov_b32 s5, s15
	s_add_i32 s1, s2, 0xe000
	s_mov_b32 s3, m0
	s_mov_b32 m0, s1
	s_nop 0
	global_load_lds_dwordx4 v18, s[16:17]
	s_mov_b32 m0, s3
	s_waitcnt vmcnt(4)
	s_lshl_b64 s[4:5], s[4:5], 13
	v_add_u32_e32 v18, 0, v168
	s_add_u32 s4, s6, s4
	v_add_u32_e32 v172, 0x18000, v18
	s_addc_u32 s5, s7, s5
	ds_write_b128 v172, v[2:5]
	ds_write_b128 v172, v[6:9] offset:8192
	ds_write_b128 v172, v[10:13] offset:16384
	ds_write_b128 v172, v[14:17] offset:24576
	global_load_dwordx4 v[14:17], v162, s[4:5]
	s_add_i32 s4, s14, 0x50
	s_mov_b32 s5, s15
	s_lshl_b64 s[4:5], s[4:5], 13
	s_add_u32 s4, s6, s4
	s_addc_u32 s5, s7, s5
	global_load_dwordx4 v[10:13], v162, s[4:5]
	s_add_i32 s4, s14, 0x60
	s_mov_b32 s5, s15
	s_lshl_b64 s[4:5], s[4:5], 13
	s_add_u32 s4, s6, s4
	s_addc_u32 s5, s7, s5
	s_addk_i32 s14, 0x70
	global_load_dwordx4 v[6:9], v162, s[4:5]
	s_lshl_b64 s[4:5], s[14:15], 13
	s_add_u32 s4, s6, s4
	s_addc_u32 s5, s7, s5
	s_lshl_b64 s[0:1], s[0:1], 8
	global_load_dwordx4 v[2:5], v162, s[4:5]
	s_waitcnt lgkmcnt(0)
	s_barrier
	s_and_b32 s1, s1, 0xff
	s_and_b32 s0, s0, 0xffffc000
	v_or_b32_e32 v18, s8, v149
	s_add_u32 s3, s6, s0
	v_or_b32_e32 v18, s9, v18
	v_or_b32_e32 v169, v34, v159
	v_or_b32_e32 v171, v34, v160
	s_addc_u32 s4, s7, s1
	v_lshl_add_u32 v173, v18, 12, v166
	s_mov_b32 s5, 0
	s_mov_b64 s[0:1], 0
	s_mov_b32 s6, 0x8000
	s_mov_b32 s7, 0x10000
	v_mov_b32_e32 v18, 0
	v_mov_b32_e32 v19, v147
	v_mov_b32_e32 v20, v147
	v_mov_b32_e32 v21, v147
	v_mov_b32_e32 v22, 0
	v_mov_b32_e32 v23, v147
	v_mov_b32_e32 v24, v147
	v_mov_b32_e32 v25, v147
	v_mov_b32_e32 v26, 0
	v_mov_b32_e32 v27, v147
	v_mov_b32_e32 v28, v147
	v_mov_b32_e32 v29, v147
	v_mov_b32_e32 v30, 0
	v_mov_b32_e32 v31, v147
	v_mov_b32_e32 v32, v147
	v_mov_b32_e32 v33, v147
	v_mov_b32_e32 v34, 0
	v_mov_b32_e32 v35, v147
	v_mov_b32_e32 v36, v147
	v_mov_b32_e32 v37, v147
	v_mov_b32_e32 v38, 0
	v_mov_b32_e32 v39, v147
	v_mov_b32_e32 v40, v147
	v_mov_b32_e32 v41, v147
	v_mov_b32_e32 v46, 0
	v_mov_b32_e32 v47, v147
	v_mov_b32_e32 v48, v147
	v_mov_b32_e32 v49, v147
	v_mov_b32_e32 v62, 0
	v_mov_b32_e32 v63, v147
	v_mov_b32_e32 v64, v147
	v_mov_b32_e32 v65, v147
	v_mov_b32_e32 v66, 0
	v_mov_b32_e32 v67, v147
	v_mov_b32_e32 v68, v147
	v_mov_b32_e32 v69, v147
	v_mov_b32_e32 v78, 0
	v_mov_b32_e32 v79, v147
	v_mov_b32_e32 v80, v147
	v_mov_b32_e32 v81, v147
	v_mov_b32_e32 v90, 0
	v_mov_b32_e32 v91, v147
	v_mov_b32_e32 v92, v147
	v_mov_b32_e32 v93, v147
	v_mov_b32_e32 v94, 0
	v_mov_b32_e32 v95, v147
	v_mov_b32_e32 v96, v147
	v_mov_b32_e32 v97, v147
	v_mov_b32_e32 v114, 0
	v_mov_b32_e32 v115, v147
	v_mov_b32_e32 v116, v147
	v_mov_b32_e32 v117, v147
	v_mov_b32_e32 v122, 0
	v_mov_b32_e32 v123, v147
	v_mov_b32_e32 v124, v147
	v_mov_b32_e32 v125, v147
	v_mov_b32_e32 v138, 0
	v_mov_b32_e32 v139, v147
	v_mov_b32_e32 v140, v147
	v_mov_b32_e32 v141, v147
	v_mov_b32_e32 v142, 0
	v_mov_b32_e32 v143, v147
	v_mov_b32_e32 v144, v147
	v_mov_b32_e32 v145, v147
	v_mov_b32_e32 v118, 0
	v_mov_b32_e32 v119, v147
	v_mov_b32_e32 v120, v147
	v_mov_b32_e32 v121, v147
	v_mov_b32_e32 v126, 0
	v_mov_b32_e32 v127, v147
	v_mov_b32_e32 v128, v147
	v_mov_b32_e32 v129, v147
	v_mov_b32_e32 v134, 0
	v_mov_b32_e32 v135, v147
	v_mov_b32_e32 v136, v147
	v_mov_b32_e32 v137, v147
	v_mov_b32_e32 v130, 0
	v_mov_b32_e32 v131, v147
	v_mov_b32_e32 v132, v147
	v_mov_b32_e32 v133, v147
	v_mov_b32_e32 v98, 0
	v_mov_b32_e32 v99, v147
	v_mov_b32_e32 v100, v147
	v_mov_b32_e32 v101, v147
	v_mov_b32_e32 v102, 0
	v_mov_b32_e32 v103, v147
	v_mov_b32_e32 v104, v147
	v_mov_b32_e32 v105, v147
	v_mov_b32_e32 v110, 0
	v_mov_b32_e32 v111, v147
	v_mov_b32_e32 v112, v147
	v_mov_b32_e32 v113, v147
	v_mov_b32_e32 v106, 0
	v_mov_b32_e32 v107, v147
	v_mov_b32_e32 v108, v147
	v_mov_b32_e32 v109, v147
	v_mov_b32_e32 v70, 0
	v_mov_b32_e32 v71, v147
	v_mov_b32_e32 v72, v147
	v_mov_b32_e32 v73, v147
	v_mov_b32_e32 v82, 0
	v_mov_b32_e32 v83, v147
	v_mov_b32_e32 v84, v147
	v_mov_b32_e32 v85, v147
	v_mov_b32_e32 v86, 0
	v_mov_b32_e32 v87, v147
	v_mov_b32_e32 v88, v147
	v_mov_b32_e32 v89, v147
	v_mov_b32_e32 v74, 0
	v_mov_b32_e32 v75, v147
	v_mov_b32_e32 v76, v147
	v_mov_b32_e32 v77, v147
	v_mov_b32_e32 v42, 0
	v_mov_b32_e32 v43, v147
	v_mov_b32_e32 v44, v147
	v_mov_b32_e32 v45, v147
	v_mov_b32_e32 v54, 0
	v_mov_b32_e32 v55, v147
	v_mov_b32_e32 v56, v147
	v_mov_b32_e32 v57, v147
	v_mov_b32_e32 v58, 0
	v_mov_b32_e32 v59, v147
	v_mov_b32_e32 v60, v147
	v_mov_b32_e32 v61, v147
	v_mov_b32_e32 v50, 0
	v_mov_b32_e32 v51, v147
	v_mov_b32_e32 v52, v147
	v_mov_b32_e32 v53, v147
	s_cmp_lt_u32 s80, 4
	s_cbranch_scc1 .Lprio_ip
	s_setprio 1
.Lprio_ip:
.LBB0_430:
	s_add_i32 s9, s6, 0xffff8000
	s_and_b32 s9, s9, 0x8000
	s_add_i32 s9, s9, 0
	s_add_i32 s8, s5, 0
	s_add_i32 s9, s9, 0x18000
	v_add_u32_e32 v204, s9, v153
	v_add_u32_e32 v206, s8, v169
	v_add_u32_e32 v212, s9, v151
	v_add_u32_e32 v208, s9, v152
.Lrot_ip:
	ds_read_b64_tr_b16 v[174:175], v204
	ds_read_b64_tr_b16 v[176:177], v204 offset:2048
	ds_read_b64_tr_b16 v[178:179], v208
	ds_read_b64_tr_b16 v[180:181], v208 offset:2048
	ds_read_b128 v[182:185], v206
	ds_read_b128 v[186:189], v206 offset:2048
	ds_read_b64_tr_b16 v[190:191], v212
	ds_read_b64_tr_b16 v[192:193], v212 offset:2048
	v_add_u32_e32 v214, s9, v146
	ds_read_b64_tr_b16 v[194:195], v214
	ds_read_b64_tr_b16 v[196:197], v214 offset:2048
	ds_read_b128 v[198:201], v206 offset:4096
	s_waitcnt lgkmcnt(6)
	v_mfma_f32_16x16x32_bf16 v[62:65], v[174:177], v[182:185], v[62:65]
	v_add_u32_e32 v202, 0xfff40000, v173
	s_add_i32 s9, s2, s7
	s_mov_b32 s14, m0
	s_mov_b32 m0, s9
	s_nop 0
	global_load_lds_dwordx4 v202, s[16:17]
	s_mov_b32 m0, s14
	v_mfma_f32_16x16x32_bf16 v[46:49], v[178:181], v[182:185], v[46:49]
	s_waitcnt lgkmcnt(3)
	v_mfma_f32_16x16x32_bf16 v[38:41], v[190:193], v[182:185], v[38:41]
	s_waitcnt lgkmcnt(1)
	v_mfma_f32_16x16x32_bf16 v[34:37], v[194:197], v[182:185], v[34:37]
	v_mfma_f32_16x16x32_bf16 v[30:33], v[174:177], v[186:189], v[30:33]
	ds_read_b128 v[182:185], v206 offset:6144
	v_add_u32_e32 v202, 0xfff80000, v173
	s_add_i32 s14, s9, 0x2000
	v_mfma_f32_16x16x32_bf16 v[26:29], v[178:181], v[186:189], v[26:29]
	s_mov_b32 s30, m0
	s_mov_b32 m0, s14
	s_nop 0
	global_load_lds_dwordx4 v202, s[16:17]
	s_mov_b32 m0, s30
	v_mfma_f32_16x16x32_bf16 v[22:25], v[190:193], v[186:189], v[22:25]
	v_mfma_f32_16x16x32_bf16 v[18:21], v[194:197], v[186:189], v[18:21]
	s_waitcnt lgkmcnt(1)
	v_mfma_f32_16x16x32_bf16 v[66:69], v[174:177], v[198:201], v[66:69]
	ds_read_b128 v[186:189], v206 offset:8192
	v_add_u32_e32 v202, 0xfffc0000, v173
	s_add_i32 s14, s9, 0x4000
	v_mfma_f32_16x16x32_bf16 v[78:81], v[178:181], v[198:201], v[78:81]
	s_mov_b32 s30, m0
	s_mov_b32 m0, s14
	s_nop 0
	global_load_lds_dwordx4 v202, s[16:17]
	s_mov_b32 m0, s30
	v_mfma_f32_16x16x32_bf16 v[90:93], v[190:193], v[198:201], v[90:93]
	v_mfma_f32_16x16x32_bf16 v[94:97], v[194:197], v[198:201], v[94:97]
	s_waitcnt lgkmcnt(1)
	v_mfma_f32_16x16x32_bf16 v[114:117], v[174:177], v[182:185], v[114:117]
	ds_read_b128 v[198:201], v206 offset:10240
	s_addk_i32 s9, 0x6000
	s_mov_b32 s14, m0
	s_mov_b32 m0, s9
	s_nop 0
	global_load_lds_dwordx4 v173, s[16:17]
	s_mov_b32 m0, s14
	v_mfma_f32_16x16x32_bf16 v[122:125], v[178:181], v[182:185], v[122:125]
	v_mfma_f32_16x16x32_bf16 v[138:141], v[190:193], v[182:185], v[138:141]
	v_mfma_f32_16x16x32_bf16 v[142:145], v[194:197], v[182:185], v[142:145]
	ds_read_b128 v[182:185], v206 offset:12288
	ds_read_b64_tr_b16 v[202:203], v204 offset:16384
	ds_read_b64_tr_b16 v[204:205], v204 offset:18432
	s_waitcnt lgkmcnt(4)
	v_mfma_f32_16x16x32_bf16 v[118:121], v[174:177], v[186:189], v[118:121]
	v_mfma_f32_16x16x32_bf16 v[126:129], v[178:181], v[186:189], v[126:129]
	v_mfma_f32_16x16x32_bf16 v[134:137], v[190:193], v[186:189], v[134:137]
	v_mfma_f32_16x16x32_bf16 v[130:133], v[194:197], v[186:189], v[130:133]
	ds_read_b128 v[186:189], v206 offset:14336
	ds_read_b64_tr_b16 v[206:207], v208 offset:16384
	ds_read_b64_tr_b16 v[208:209], v208 offset:18432
	s_waitcnt lgkmcnt(6)
	v_mfma_f32_16x16x32_bf16 v[98:101], v[174:177], v[198:201], v[98:101]
	v_mfma_f32_16x16x32_bf16 v[102:105], v[178:181], v[198:201], v[102:105]
	v_mfma_f32_16x16x32_bf16 v[110:113], v[190:193], v[198:201], v[110:113]
	v_mfma_f32_16x16x32_bf16 v[106:109], v[194:197], v[198:201], v[106:109]
	v_add_u32_e32 v215, s8, v171
	ds_read_b128 v[198:201], v215
	ds_read_b64_tr_b16 v[210:211], v212 offset:16384
	ds_read_b64_tr_b16 v[212:213], v212 offset:18432
	s_waitcnt lgkmcnt(8)
	v_mfma_f32_16x16x32_bf16 v[70:73], v[174:177], v[182:185], v[70:73]
	v_mfma_f32_16x16x32_bf16 v[82:85], v[178:181], v[182:185], v[82:85]
	v_mfma_f32_16x16x32_bf16 v[86:89], v[190:193], v[182:185], v[86:89]
	v_mfma_f32_16x16x32_bf16 v[74:77], v[194:197], v[182:185], v[74:77]
	s_waitcnt lgkmcnt(5)
	v_mfma_f32_16x16x32_bf16 v[42:45], v[174:177], v[186:189], v[42:45]
	ds_read_b128 v[174:177], v215 offset:2048
	s_and_b32 s8, s6, 0x8000
	v_mfma_f32_16x16x32_bf16 v[54:57], v[178:181], v[186:189], v[54:57]
	ds_read_b64_tr_b16 v[178:179], v214 offset:16384
	ds_read_b64_tr_b16 v[180:181], v214 offset:18432
	v_mfma_f32_16x16x32_bf16 v[58:61], v[190:193], v[186:189], v[58:61]
	v_mfma_f32_16x16x32_bf16 v[50:53], v[194:197], v[186:189], v[50:53]
	s_waitcnt lgkmcnt(5)
	v_mfma_f32_16x16x32_bf16 v[62:65], v[202:205], v[198:201], v[62:65]
	ds_read_b128 v[182:185], v215 offset:4096
	s_add_u32 s14, s3, s0
	s_addc_u32 s30, s4, s1
	v_mfma_f32_16x16x32_bf16 v[46:49], v[206:209], v[198:201], v[46:49]
	s_waitcnt vmcnt(7)
	v_add_u32_e32 v190, s8, v172
	s_add_u32 s8, s14, 0x100000
	s_waitcnt lgkmcnt(4)
	v_mfma_f32_16x16x32_bf16 v[38:41], v[210:213], v[198:201], v[38:41]
	ds_write_b128 v190, v[14:17]
	s_addc_u32 s9, s30, 0
	global_load_dwordx4 v[14:17], v162, s[8:9]
	s_waitcnt lgkmcnt(2)
	v_mfma_f32_16x16x32_bf16 v[34:37], v[178:181], v[198:201], v[34:37]
	v_mfma_f32_16x16x32_bf16 v[30:33], v[202:205], v[174:177], v[30:33]
	ds_read_b128 v[186:189], v215 offset:6144
	s_waitcnt vmcnt(7)
	s_add_u32 s8, s14, 0x120000
	v_mfma_f32_16x16x32_bf16 v[26:29], v[206:209], v[174:177], v[26:29]
	ds_write_b128 v190, v[10:13] offset:8192
	s_addc_u32 s9, s30, 0
	global_load_dwordx4 v[10:13], v162, s[8:9]
	v_mfma_f32_16x16x32_bf16 v[22:25], v[210:213], v[174:177], v[22:25]
	v_mfma_f32_16x16x32_bf16 v[18:21], v[178:181], v[174:177], v[18:21]
	s_waitcnt lgkmcnt(3)
	v_mfma_f32_16x16x32_bf16 v[66:69], v[202:205], v[182:185], v[66:69]
	ds_read_b128 v[174:177], v215 offset:8192
	s_waitcnt vmcnt(7)
	s_add_u32 s8, s14, 0x140000
	v_mfma_f32_16x16x32_bf16 v[78:81], v[206:209], v[182:185], v[78:81]
	ds_write_b128 v190, v[6:9] offset:16384
	s_addc_u32 s9, s30, 0
	global_load_dwordx4 v[6:9], v162, s[8:9]
	v_mfma_f32_16x16x32_bf16 v[90:93], v[210:213], v[182:185], v[90:93]
	v_mfma_f32_16x16x32_bf16 v[94:97], v[178:181], v[182:185], v[94:97]
	s_waitcnt lgkmcnt(3)
	v_mfma_f32_16x16x32_bf16 v[114:117], v[202:205], v[186:189], v[114:117]
	ds_read_b128 v[182:185], v215 offset:10240
	s_waitcnt vmcnt(7)
	s_add_u32 s8, s14, 0x160000
	v_mfma_f32_16x16x32_bf16 v[122:125], v[206:209], v[186:189], v[122:125]
	ds_write_b128 v190, v[2:5] offset:24576
	s_addc_u32 s9, s30, 0
	global_load_dwordx4 v[2:5], v162, s[8:9]
	v_mfma_f32_16x16x32_bf16 v[138:141], v[210:213], v[186:189], v[138:141]
	v_mfma_f32_16x16x32_bf16 v[142:145], v[178:181], v[186:189], v[142:145]
	s_waitcnt lgkmcnt(3)
	v_mfma_f32_16x16x32_bf16 v[118:121], v[202:205], v[174:177], v[118:121]
	ds_read_b128 v[186:189], v215 offset:12288
	v_mfma_f32_16x16x32_bf16 v[126:129], v[206:209], v[174:177], v[126:129]
	v_mfma_f32_16x16x32_bf16 v[134:137], v[210:213], v[174:177], v[134:137]
	v_mfma_f32_16x16x32_bf16 v[130:133], v[178:181], v[174:177], v[130:133]
	s_waitcnt lgkmcnt(2)
	v_mfma_f32_16x16x32_bf16 v[98:101], v[202:205], v[182:185], v[98:101]
	ds_read_b128 v[174:177], v215 offset:14336
	v_mfma_f32_16x16x32_bf16 v[102:105], v[206:209], v[182:185], v[102:105]
	v_mfma_f32_16x16x32_bf16 v[110:113], v[210:213], v[182:185], v[110:113]
	v_mfma_f32_16x16x32_bf16 v[106:109], v[178:181], v[182:185], v[106:109]
	s_waitcnt lgkmcnt(1)
	v_mfma_f32_16x16x32_bf16 v[70:73], v[202:205], v[186:189], v[70:73]
	v_mfma_f32_16x16x32_bf16 v[82:85], v[206:209], v[186:189], v[82:85]
	v_mfma_f32_16x16x32_bf16 v[86:89], v[210:213], v[186:189], v[86:89]
	v_mfma_f32_16x16x32_bf16 v[74:77], v[178:181], v[186:189], v[74:77]
	s_waitcnt lgkmcnt(0)
	v_mfma_f32_16x16x32_bf16 v[42:45], v[202:205], v[174:177], v[42:45]
	v_mfma_f32_16x16x32_bf16 v[54:57], v[206:209], v[174:177], v[54:57]
	v_mfma_f32_16x16x32_bf16 v[58:61], v[210:213], v[174:177], v[58:61]
	v_mfma_f32_16x16x32_bf16 v[50:53], v[178:181], v[174:177], v[50:53]
	s_add_i32 s8, s5, 0x8000
	s_cmp_lg_u32 s5, 0x10000
	s_cselect_b32 s5, s8, 0
	s_add_i32 s8, s7, 0x8000
	s_cmp_lg_u32 s7, 0x10000
	s_cselect_b32 s7, s8, 0
	s_add_u32 s0, s0, 0x80000
	s_addc_u32 s1, s1, 0
	s_add_i32 s6, s6, 0x8000
	v_add_u32_e32 v173, 0x80, v173
	s_add_i32 s9, s6, 0xffff8000
	s_and_b32 s9, s9, 0x8000
	s_add_i32 s9, s9, 0
	s_add_i32 s8, s5, 0
	s_add_i32 s9, s9, 0x18000
	v_add_u32_e32 v204, s9, v153
	v_add_u32_e32 v206, s8, v169
	v_add_u32_e32 v212, s9, v151
	v_add_u32_e32 v208, s9, v152
	s_waitcnt lgkmcnt(0)
	s_barrier
	s_cmp_lg_u32 s0, 0xf00000
	s_cbranch_scc1 .Lrot_ip
	s_setprio 0
	s_add_i32 s0, 0, 0x18000
	v_add_u32_e32 v202, s0, v153
	v_add_u32_e32 v169, 0, v169
	v_add_u32_e32 v210, s0, v151
	v_add_u32_e32 v212, s0, v146
	ds_read_b64_tr_b16 v[172:173], v202
	ds_read_b64_tr_b16 v[174:175], v202 offset:2048
	v_add_u32_e32 v206, s0, v152
	ds_read_b128 v[176:179], v169
	ds_read_b64_tr_b16 v[180:181], v206
	ds_read_b64_tr_b16 v[182:183], v206 offset:2048
	ds_read_b128 v[184:187], v169 offset:2048
	ds_read_b64_tr_b16 v[188:189], v210
	ds_read_b64_tr_b16 v[190:191], v210 offset:2048
	ds_read_b64_tr_b16 v[192:193], v212
	ds_read_b64_tr_b16 v[194:195], v212 offset:2048
	s_waitcnt lgkmcnt(7)
	v_mfma_f32_16x16x32_bf16 v[62:65], v[172:175], v[176:179], v[62:65]
	ds_read_b128 v[196:199], v169 offset:4096
	s_waitcnt lgkmcnt(6)
	v_mfma_f32_16x16x32_bf16 v[46:49], v[180:183], v[176:179], v[46:49]
	s_waitcnt lgkmcnt(3)
	v_mfma_f32_16x16x32_bf16 v[38:41], v[188:191], v[176:179], v[38:41]
	s_waitcnt lgkmcnt(1)
	v_mfma_f32_16x16x32_bf16 v[34:37], v[192:195], v[176:179], v[34:37]
	v_mfma_f32_16x16x32_bf16 v[30:33], v[172:175], v[184:187], v[30:33]
	ds_read_b128 v[176:179], v169 offset:6144
	v_mfma_f32_16x16x32_bf16 v[26:29], v[180:183], v[184:187], v[26:29]
	v_mfma_f32_16x16x32_bf16 v[22:25], v[188:191], v[184:187], v[22:25]
	v_mfma_f32_16x16x32_bf16 v[18:21], v[192:195], v[184:187], v[18:21]
	s_waitcnt lgkmcnt(1)
	v_mfma_f32_16x16x32_bf16 v[66:69], v[172:175], v[196:199], v[66:69]
	ds_read_b128 v[184:187], v169 offset:8192
	v_mfma_f32_16x16x32_bf16 v[78:81], v[180:183], v[196:199], v[78:81]
	v_mfma_f32_16x16x32_bf16 v[90:93], v[188:191], v[196:199], v[90:93]
	v_mfma_f32_16x16x32_bf16 v[94:97], v[192:195], v[196:199], v[94:97]
	s_waitcnt lgkmcnt(1)
	v_mfma_f32_16x16x32_bf16 v[114:117], v[172:175], v[176:179], v[114:117]
	ds_read_b128 v[196:199], v169 offset:10240
	v_mfma_f32_16x16x32_bf16 v[122:125], v[180:183], v[176:179], v[122:125]
	v_mfma_f32_16x16x32_bf16 v[138:141], v[188:191], v[176:179], v[138:141]
	v_mfma_f32_16x16x32_bf16 v[142:145], v[192:195], v[176:179], v[142:145]
	ds_read_b128 v[176:179], v169 offset:12288
	ds_read_b64_tr_b16 v[200:201], v202 offset:16384
	ds_read_b64_tr_b16 v[202:203], v202 offset:18432
	s_waitcnt lgkmcnt(4)
	v_mfma_f32_16x16x32_bf16 v[118:121], v[172:175], v[184:187], v[118:121]
	v_mfma_f32_16x16x32_bf16 v[126:129], v[180:183], v[184:187], v[126:129]
	v_mfma_f32_16x16x32_bf16 v[134:137], v[188:191], v[184:187], v[134:137]
	v_mfma_f32_16x16x32_bf16 v[130:133], v[192:195], v[184:187], v[130:133]
	ds_read_b128 v[184:187], v169 offset:14336
	ds_read_b64_tr_b16 v[204:205], v206 offset:16384
	ds_read_b64_tr_b16 v[206:207], v206 offset:18432
	s_waitcnt lgkmcnt(6)
	v_mfma_f32_16x16x32_bf16 v[98:101], v[172:175], v[196:199], v[98:101]
	v_mfma_f32_16x16x32_bf16 v[102:105], v[180:183], v[196:199], v[102:105]
	v_mfma_f32_16x16x32_bf16 v[110:113], v[188:191], v[196:199], v[110:113]
	v_mfma_f32_16x16x32_bf16 v[106:109], v[192:195], v[196:199], v[106:109]
	v_add_u32_e32 v171, 0, v171
	ds_read_b128 v[196:199], v171
	ds_read_b64_tr_b16 v[208:209], v210 offset:16384
	ds_read_b64_tr_b16 v[210:211], v210 offset:18432
	s_waitcnt lgkmcnt(8)
	v_mfma_f32_16x16x32_bf16 v[70:73], v[172:175], v[176:179], v[70:73]
	v_mfma_f32_16x16x32_bf16 v[82:85], v[180:183], v[176:179], v[82:85]
	v_mfma_f32_16x16x32_bf16 v[86:89], v[188:191], v[176:179], v[86:89]
	v_mfma_f32_16x16x32_bf16 v[74:77], v[192:195], v[176:179], v[74:77]
	s_waitcnt lgkmcnt(5)
	v_mfma_f32_16x16x32_bf16 v[42:45], v[172:175], v[184:187], v[42:45]
	ds_read_b128 v[172:175], v171 offset:2048
	ds_read_b64_tr_b16 v[176:177], v212 offset:16384
	ds_read_b64_tr_b16 v[178:179], v212 offset:18432
	v_mfma_f32_16x16x32_bf16 v[54:57], v[180:183], v[184:187], v[54:57]
	v_mfma_f32_16x16x32_bf16 v[58:61], v[188:191], v[184:187], v[58:61]
	v_mfma_f32_16x16x32_bf16 v[50:53], v[192:195], v[184:187], v[50:53]
	ds_read_b128 v[180:183], v171 offset:4096
	s_waitcnt vmcnt(3)
	v_add_u32_e32 v168, s38, v168
	s_waitcnt lgkmcnt(6)
	v_mfma_f32_16x16x32_bf16 v[62:65], v[200:203], v[196:199], v[62:65]
	ds_write_b128 v168, v[14:17]
	v_mfma_f32_16x16x32_bf16 v[46:49], v[204:207], v[196:199], v[46:49]
	s_waitcnt lgkmcnt(5)
	v_mfma_f32_16x16x32_bf16 v[38:41], v[208:211], v[196:199], v[38:41]
	s_waitcnt lgkmcnt(2)
	v_mfma_f32_16x16x32_bf16 v[14:17], v[176:179], v[196:199], v[34:37]
	s_nop 2
	ds_read_b128 v[34:37], v171 offset:6144
	s_waitcnt vmcnt(2)
	v_mfma_f32_16x16x32_bf16 v[30:33], v[200:203], v[172:175], v[30:33]
	ds_write_b128 v168, v[10:13] offset:8192
	v_mfma_f32_16x16x32_bf16 v[26:29], v[204:207], v[172:175], v[26:29]
	v_mfma_f32_16x16x32_bf16 v[22:25], v[208:211], v[172:175], v[22:25]
	v_mfma_f32_16x16x32_bf16 v[10:13], v[176:179], v[172:175], v[18:21]
	s_waitcnt lgkmcnt(3)
	v_mfma_f32_16x16x32_bf16 v[18:21], v[200:203], v[180:183], v[66:69]
	v_mfma_f32_16x16x32_bf16 v[66:69], v[204:207], v[180:183], v[78:81]
	v_mfma_f32_16x16x32_bf16 v[78:81], v[208:211], v[180:183], v[90:93]
	s_nop 2
	ds_read_b128 v[90:93], v171 offset:8192
	s_waitcnt vmcnt(1)
	ds_write_b128 v168, v[6:9] offset:16384
	v_mfma_f32_16x16x32_bf16 v[6:9], v[176:179], v[180:183], v[94:97]
	s_waitcnt lgkmcnt(3)
	v_mfma_f32_16x16x32_bf16 v[94:97], v[200:203], v[34:37], v[114:117]
	v_mfma_f32_16x16x32_bf16 v[114:117], v[204:207], v[34:37], v[122:125]
	v_mfma_f32_16x16x32_bf16 v[122:125], v[208:211], v[34:37], v[138:141]
	s_nop 2
	ds_read_b128 v[138:141], v171 offset:10240
	s_waitcnt vmcnt(0)
	ds_write_b128 v168, v[2:5] offset:24576
	v_mfma_f32_16x16x32_bf16 v[2:5], v[176:179], v[34:37], v[142:145]
	s_waitcnt lgkmcnt(3)
	v_mfma_f32_16x16x32_bf16 v[34:37], v[200:203], v[90:93], v[118:121]
	v_mfma_f32_16x16x32_bf16 v[118:121], v[204:207], v[90:93], v[126:129]
	v_mfma_f32_16x16x32_bf16 v[126:129], v[208:211], v[90:93], v[134:137]
	s_nop 2
	ds_read_b128 v[134:137], v171 offset:12288
	v_mfma_f32_16x16x32_bf16 v[90:93], v[176:179], v[90:93], v[130:133]
	s_waitcnt lgkmcnt(2)
	v_mfma_f32_16x16x32_bf16 v[98:101], v[200:203], v[138:141], v[98:101]
	s_nop 0
	ds_read_b128 v[130:133], v171 offset:14336
	v_mfma_f32_16x16x32_bf16 v[102:105], v[204:207], v[138:141], v[102:105]
	v_mfma_f32_16x16x32_bf16 v[110:113], v[208:211], v[138:141], v[110:113]
	v_mfma_f32_16x16x32_bf16 v[106:109], v[176:179], v[138:141], v[106:109]
	s_waitcnt lgkmcnt(1)
	v_mfma_f32_16x16x32_bf16 v[70:73], v[200:203], v[134:137], v[70:73]
	v_mfma_f32_16x16x32_bf16 v[82:85], v[204:207], v[134:137], v[82:85]
	v_mfma_f32_16x16x32_bf16 v[86:89], v[208:211], v[134:137], v[86:89]
	v_mfma_f32_16x16x32_bf16 v[74:77], v[176:179], v[134:137], v[74:77]
	s_waitcnt lgkmcnt(0)
	v_mfma_f32_16x16x32_bf16 v[42:45], v[200:203], v[130:133], v[42:45]
	v_mfma_f32_16x16x32_bf16 v[54:57], v[204:207], v[130:133], v[54:57]
	v_mfma_f32_16x16x32_bf16 v[58:61], v[208:211], v[130:133], v[58:61]
	v_mfma_f32_16x16x32_bf16 v[50:53], v[176:179], v[130:133], v[50:53]
	s_waitcnt lgkmcnt(0)
	s_barrier
	v_add_u32_e32 v153, s38, v153
	v_add_u32_e32 v152, s38, v152
	v_add_u32_e32 v151, s38, v151
	ds_read_b64_tr_b16 v[130:131], v153
	ds_read_b64_tr_b16 v[132:133], v153 offset:2048
	ds_read_b64_tr_b16 v[134:135], v152
	ds_read_b64_tr_b16 v[136:137], v152 offset:2048
	ds_read_b128 v[138:141], v169 offset:32768
	ds_read_b64_tr_b16 v[142:143], v151
	ds_read_b128 v[172:175], v169 offset:34816
	ds_read_b128 v[176:179], v169 offset:36864
	ds_read_b64_tr_b16 v[144:145], v151 offset:2048
	v_add_u32_e32 v146, s38, v146
	ds_read_b64_tr_b16 v[180:181], v146
	ds_read_b64_tr_b16 v[182:183], v146 offset:2048
	s_waitcnt lgkmcnt(6)
	v_mfma_f32_16x16x32_bf16 v[62:65], v[130:133], v[138:141], v[62:65]
	v_mfma_f32_16x16x32_bf16 v[46:49], v[134:137], v[138:141], v[46:49]
	s_waitcnt lgkmcnt(2)
	v_mfma_f32_16x16x32_bf16 v[38:41], v[142:145], v[138:141], v[38:41]
	s_waitcnt lgkmcnt(0)
	v_mfma_f32_16x16x32_bf16 v[14:17], v[180:183], v[138:141], v[14:17]
	v_mfma_f32_16x16x32_bf16 v[30:33], v[130:133], v[172:175], v[30:33]
	ds_read_b128 v[138:141], v169 offset:38912
	v_mfma_f32_16x16x32_bf16 v[26:29], v[134:137], v[172:175], v[26:29]
	v_mfma_f32_16x16x32_bf16 v[22:25], v[142:145], v[172:175], v[22:25]
	v_mfma_f32_16x16x32_bf16 v[10:13], v[180:183], v[172:175], v[10:13]
	v_mfma_f32_16x16x32_bf16 v[18:21], v[130:133], v[176:179], v[18:21]
	ds_read_b128 v[172:175], v169 offset:40960
	v_mfma_f32_16x16x32_bf16 v[66:69], v[134:137], v[176:179], v[66:69]
	v_mfma_f32_16x16x32_bf16 v[78:81], v[142:145], v[176:179], v[78:81]
	v_mfma_f32_16x16x32_bf16 v[6:9], v[180:183], v[176:179], v[6:9]
	s_waitcnt lgkmcnt(1)
	v_mfma_f32_16x16x32_bf16 v[176:179], v[130:133], v[138:141], v[94:97]
	s_nop 2
	ds_read_b128 v[94:97], v169 offset:43008
	v_mfma_f32_16x16x32_bf16 v[2:5], v[180:183], v[138:141], v[2:5]
	v_mfma_f32_16x16x32_bf16 v[184:187], v[134:137], v[138:141], v[114:117]
	v_mfma_f32_16x16x32_bf16 v[188:191], v[142:145], v[138:141], v[122:125]
	s_nop 1
	ds_read_b128 v[114:117], v169 offset:45056
	ds_read_b64_tr_b16 v[196:197], v153 offset:16384
	ds_read_b64_tr_b16 v[198:199], v153 offset:18432
	s_waitcnt lgkmcnt(4)
	v_mfma_f32_16x16x32_bf16 v[34:37], v[130:133], v[172:175], v[34:37]
	v_mfma_f32_16x16x32_bf16 v[138:141], v[134:137], v[172:175], v[118:121]
	v_mfma_f32_16x16x32_bf16 v[192:195], v[142:145], v[172:175], v[126:129]
	v_mfma_f32_16x16x32_bf16 v[172:175], v[180:183], v[172:175], v[90:93]
	s_nop 2
	ds_read_b128 v[90:93], v169 offset:47104
	ds_read_b64_tr_b16 v[212:213], v152 offset:16384
	ds_read_b64_tr_b16 v[214:215], v152 offset:18432
	s_waitcnt lgkmcnt(6)
	v_mfma_f32_16x16x32_bf16 v[200:203], v[130:133], v[94:97], v[98:101]
	v_mfma_f32_16x16x32_bf16 v[204:207], v[134:137], v[94:97], v[102:105]
	v_mfma_f32_16x16x32_bf16 v[208:211], v[142:145], v[94:97], v[110:113]
	v_mfma_f32_16x16x32_bf16 v[216:219], v[180:183], v[94:97], v[106:109]
	s_waitcnt lgkmcnt(5)
	v_mfma_f32_16x16x32_bf16 v[220:223], v[130:133], v[114:117], v[70:73]
	s_nop 2
	ds_read_b128 v[70:73], v171 offset:32768
	ds_read_b64_tr_b16 v[232:233], v151 offset:16384
	ds_read_b64_tr_b16 v[234:235], v151 offset:18432
	v_mfma_f32_16x16x32_bf16 v[224:227], v[134:137], v[114:117], v[82:85]
	v_mfma_f32_16x16x32_bf16 v[228:231], v[142:145], v[114:117], v[86:89]
	v_mfma_f32_16x16x32_bf16 v[236:239], v[180:183], v[114:117], v[74:77]
	s_waitcnt lgkmcnt(5)
	v_mfma_f32_16x16x32_bf16 v[130:133], v[130:133], v[90:93], v[42:45]
	s_nop 2
	ds_read_b128 v[42:45], v171 offset:34816
	ds_read_b64_tr_b16 v[240:241], v146 offset:16384
	ds_read_b64_tr_b16 v[242:243], v146 offset:18432
	v_mfma_f32_16x16x32_bf16 v[134:137], v[134:137], v[90:93], v[54:57]
	v_mfma_f32_16x16x32_bf16 v[142:145], v[142:145], v[90:93], v[58:61]
	v_mfma_f32_16x16x32_bf16 v[180:183], v[180:183], v[90:93], v[50:53]
	s_waitcnt lgkmcnt(3)
	v_mfma_f32_16x16x32_bf16 v[118:121], v[232:235], v[70:73], v[38:41]
	s_nop 2
	ds_read_b128 v[38:41], v171 offset:36864
	v_mfma_f32_16x16x32_bf16 v[126:129], v[196:199], v[70:73], v[62:65]
	v_mfma_f32_16x16x32_bf16 v[122:125], v[212:215], v[70:73], v[46:49]
	s_waitcnt lgkmcnt(1)
	v_mfma_f32_16x16x32_bf16 v[114:117], v[240:243], v[70:73], v[14:17]
	s_nop 2
	ds_read_b128 v[14:17], v171 offset:38912
	v_mfma_f32_16x16x32_bf16 v[110:113], v[196:199], v[42:45], v[30:33]
	v_mfma_f32_16x16x32_bf16 v[106:109], v[212:215], v[42:45], v[26:29]
	v_mfma_f32_16x16x32_bf16 v[102:105], v[232:235], v[42:45], v[22:25]
	v_mfma_f32_16x16x32_bf16 v[98:101], v[240:243], v[42:45], v[10:13]
	s_nop 2
	ds_read_b128 v[10:13], v171 offset:40960
	s_waitcnt lgkmcnt(2)
	v_mfma_f32_16x16x32_bf16 v[94:97], v[196:199], v[38:41], v[18:21]
	v_mfma_f32_16x16x32_bf16 v[90:93], v[212:215], v[38:41], v[66:69]
	v_mfma_f32_16x16x32_bf16 v[86:89], v[232:235], v[38:41], v[78:81]
	v_mfma_f32_16x16x32_bf16 v[82:85], v[240:243], v[38:41], v[6:9]
	s_nop 2
	ds_read_b128 v[6:9], v171 offset:43008
	s_waitcnt lgkmcnt(2)
	v_mfma_f32_16x16x32_bf16 v[78:81], v[196:199], v[14:17], v[176:179]
	v_mfma_f32_16x16x32_bf16 v[74:77], v[212:215], v[14:17], v[184:187]
	v_mfma_f32_16x16x32_bf16 v[70:73], v[232:235], v[14:17], v[188:191]
	v_mfma_f32_16x16x32_bf16 v[66:69], v[240:243], v[14:17], v[2:5]
	s_nop 2
	ds_read_b128 v[2:5], v171 offset:45056
	s_waitcnt lgkmcnt(2)
	v_mfma_f32_16x16x32_bf16 v[62:65], v[196:199], v[10:13], v[34:37]
	v_mfma_f32_16x16x32_bf16 v[58:61], v[212:215], v[10:13], v[138:141]
	v_mfma_f32_16x16x32_bf16 v[54:57], v[232:235], v[10:13], v[192:195]
	v_mfma_f32_16x16x32_bf16 v[50:53], v[240:243], v[10:13], v[172:175]
	s_waitcnt lgkmcnt(1)
	v_mfma_f32_16x16x32_bf16 v[46:49], v[196:199], v[6:9], v[200:203]
	ds_read_b128 v[138:141], v171 offset:47104
	v_mfma_f32_16x16x32_bf16 v[42:45], v[212:215], v[6:9], v[204:207]
	v_mfma_f32_16x16x32_bf16 v[38:41], v[232:235], v[6:9], v[208:211]
	v_mfma_f32_16x16x32_bf16 v[34:37], v[240:243], v[6:9], v[216:219]
	s_waitcnt lgkmcnt(1)
	v_mfma_f32_16x16x32_bf16 v[30:33], v[196:199], v[2:5], v[220:223]
	v_mfma_f32_16x16x32_bf16 v[26:29], v[212:215], v[2:5], v[224:227]
	v_mfma_f32_16x16x32_bf16 v[22:25], v[232:235], v[2:5], v[228:231]
	v_mfma_f32_16x16x32_bf16 v[18:21], v[240:243], v[2:5], v[236:239]
	s_waitcnt lgkmcnt(0)
	v_mfma_f32_16x16x32_bf16 v[14:17], v[196:199], v[138:141], v[130:133]
	v_mfma_f32_16x16x32_bf16 v[10:13], v[212:215], v[138:141], v[134:137]
	v_mfma_f32_16x16x32_bf16 v[6:9], v[232:235], v[138:141], v[142:145]
	v_mfma_f32_16x16x32_bf16 v[2:5], v[240:243], v[138:141], v[180:183]
	s_waitcnt lgkmcnt(0)
	s_barrier
	v_mov_b32_e32 v151, v155
	v_mov_b32_e32 v168, v1
	s_cmpk_gt_i32 s28, 0x3ff
	s_mov_b64 s[0:1], -1
	s_cbranch_scc1 .LBB0_607
	s_add_i32 s0, s52, s50
	v_add_u32_e32 v140, s0, v168
	s_lshl_b32 s0, s51, 6
	s_or_b32 s0, s0, s28
	v_lshlrev_b32_e32 v132, 2, v151
	v_add_u32_e32 v146, s0, v132
	v_ashrrev_i32_e32 v141, 31, v140
	v_lshlrev_b64 v[142:143], 11, v[140:141]
	v_cmp_lt_i32_e64 s[4:5], s39, v146
	s_and_saveexec_b64 s[0:1], s[4:5]
	s_xor_b64 s[0:1], exec, s[0:1]
	s_cbranch_execz .LBB0_442
	v_cmp_lt_u32_e32 vcc, s41, v146
	s_and_saveexec_b64 s[2:3], vcc
	s_xor_b64 s[2:3], exec, s[2:3]
	s_cbranch_execz .LBB0_439
	v_cmp_lt_u32_e32 vcc, s42, v146
	v_cvt_pk_bf16_f32 v130, v126, v127
	v_cvt_pk_bf16_f32 v131, v128, v129
	s_and_saveexec_b64 s[6:7], vcc
	s_xor_b64 s[6:7], exec, s[6:7]
	s_cbranch_execz .LBB0_436
	v_lshl_add_u64 v[134:135], s[24:25], 0, v[142:143]
	v_lshl_add_u64 v[134:135], v[146:147], 1, v[134:135]
	v_add_co_u32_e32 v134, vcc, 0xfffff000, v134
	s_nop 1
	v_addc_co_u32_e32 v135, vcc, -1, v135, vcc
	global_store_dwordx2 v[134:135], v[130:131], off offset:-2048

.LBB0_877:
	s_lshl_b32 s6, s38, 10
	s_and_b32 s6, s6, 0x40000
	s_lshl_b64 s[24:25], s[2:3], 18
	s_add_u32 s52, s36, s24
	v_readfirstlane_b32 s24, v0
	s_addc_u32 s53, s37, s25
	s_lshr_b32 s25, s24, 6
	v_or_b32_e32 v176, s6, v168
	s_lshl_b32 s6, s25, 1
	v_or_b32_e32 v2, s6, v1
	s_and_b32 s26, s25, 4
	s_bfe_u32 s3, s24, 0x20006
	v_and_or_b32 v3, v2, 3, s26
	s_lshr_b32 s26, s24, 1
	s_and_b32 s50, s26, 0x7fffff80
	s_lshl_b32 s26, s3, 7
	s_lshl_b32 s51, s25, 10
	s_waitcnt vmcnt(0)
	s_barrier
	s_or_b32 s27, s26, 32
	s_add_i32 s51, s51, 0
	s_mov_b32 s25, m0
	s_mov_b32 m0, s51
	s_nop 0
	global_load_lds_dwordx4 v21, s[22:23]
	s_mov_b32 m0, s25
	v_bitop3_b32 v173, s26, v167, v161 bitop3:0xde
	v_bitop3_b32 v172, s27, v167, v161 bitop3:0xde
	s_or_b32 s27, s26, 64
	s_or_b32 s26, s26, 0x60
	s_add_i32 s25, s51, 0x2000
	v_bitop3_b32 v169, s26, v167, v161 bitop3:0xde
	s_mov_b32 s26, m0
	s_mov_b32 m0, s25
	s_nop 0
	global_load_lds_dwordx4 v20, s[22:23]
	s_mov_b32 m0, s26
	s_add_i32 s25, s51, 0x4000
	s_mov_b32 s26, m0
	s_mov_b32 m0, s25
	s_nop 0
	global_load_lds_dwordx4 v19, s[22:23]
	s_mov_b32 m0, s26
	s_add_i32 s25, s51, 0x6000
	s_mov_b32 s26, m0
	s_mov_b32 m0, s25
	s_nop 0
	global_load_lds_dwordx4 v18, s[22:23]
	s_mov_b32 m0, s26
	v_bitop3_b32 v171, s27, v167, v161 bitop3:0xde
	s_lshl_b64 s[26:27], s[6:7], 9
	s_add_u32 s26, s52, s26
	v_lshlrev_b32_e32 v3, 5, v3
	v_or_b32_e32 v4, s50, v154
	v_lshlrev_b32_e32 v2, 9, v2
	s_addc_u32 s27, s53, s27
	v_lshlrev_b32_e32 v34, 7, v4
	v_bitop3_b32 v174, v3, v2, v157 bitop3:0xde
	global_load_dwordx4 v[2:5], v151, s[26:27]
	s_add_i32 s26, s6, 16
	s_mov_b32 s27, s7
	s_lshl_b64 s[26:27], s[26:27], 9
	s_add_u32 s26, s52, s26
	s_addc_u32 s27, s53, s27
	global_load_dwordx4 v[6:9], v151, s[26:27]
	s_add_i32 s26, s6, 32
	s_mov_b32 s27, s7
	s_lshl_b64 s[26:27], s[26:27], 9
	s_add_u32 s26, s52, s26
	s_addc_u32 s27, s53, s27
	global_load_dwordx4 v[10:13], v151, s[26:27]
	s_add_i32 s26, s6, 48
	s_mov_b32 s27, s7
	s_lshl_b64 s[26:27], s[26:27], 9
	s_add_u32 s26, s52, s26
	s_addc_u32 s27, s53, s27
	s_add_i32 s25, s51, 0x8000
	global_load_dwordx4 v[14:17], v151, s[26:27]
	s_mov_b32 s26, m0
	s_mov_b32 m0, s25
	s_nop 0
	global_load_lds_dwordx4 v25, s[22:23]
	s_mov_b32 m0, s26
	s_add_i32 s25, s51, 0xa000
	s_mov_b32 s26, m0
	s_mov_b32 m0, s25
	s_nop 0
	global_load_lds_dwordx4 v22, s[22:23]
	s_mov_b32 m0, s26
	s_add_i32 s25, s51, 0xc000
	s_mov_b32 s26, m0
	s_mov_b32 m0, s25
	s_nop 0
	global_load_lds_dwordx4 v23, s[22:23]
	s_mov_b32 m0, s26
	s_add_i32 s25, s51, 0xe000
	s_mov_b32 s26, m0
	s_mov_b32 m0, s25
	s_nop 0
	global_load_lds_dwordx4 v24, s[22:23]
	s_mov_b32 m0, s26
	s_add_i32 s26, s6, 64
	s_mov_b32 s27, s7
	s_waitcnt vmcnt(4)
	s_lshl_b64 s[26:27], s[26:27], 9
	v_add_u32_e32 v18, 0, v174
	s_add_u32 s26, s52, s26
	v_add_u32_e32 v178, 0x18000, v18
	s_addc_u32 s27, s53, s27
	ds_write_b128 v178, v[2:5]
	ds_write_b128 v178, v[6:9] offset:8192
	ds_write_b128 v178, v[10:13] offset:16384
	ds_write_b128 v178, v[14:17] offset:24576
	global_load_dwordx4 v[14:17], v151, s[26:27]
	s_add_i32 s26, s6, 0x50
	s_mov_b32 s27, s7
	s_lshl_b64 s[26:27], s[26:27], 9
	s_add_u32 s26, s52, s26
	s_addc_u32 s27, s53, s27
	global_load_dwordx4 v[10:13], v151, s[26:27]
	s_add_i32 s26, s6, 0x60
	s_mov_b32 s27, s7
	s_lshl_b64 s[26:27], s[26:27], 9
	s_add_u32 s26, s52, s26
	s_addc_u32 s27, s53, s27
	s_addk_i32 s6, 0x70
	global_load_dwordx4 v[6:9], v151, s[26:27]
	s_lshl_b64 s[26:27], s[6:7], 9
	s_add_u32 s26, s52, s26
	s_addc_u32 s27, s53, s27
	s_lshl_b64 s[24:25], s[24:25], 4
	global_load_dwordx4 v[2:5], v151, s[26:27]
	s_waitcnt lgkmcnt(0)
	s_barrier
	s_and_b32 s25, s25, 15
	s_and_b32 s6, s24, 0xfffffc00
	s_add_u32 s6, s52, s6
	v_mov_b32_e32 v18, 0
	v_or_b32_e32 v175, v34, v159
	v_or_b32_e32 v177, v34, v156
	s_addc_u32 s52, s53, s25
	s_mov_b32 s53, 0x10000
	s_mov_b32 s73, 0
	s_mov_b64 s[24:25], 0
	v_mov_b32_e32 v19, v18
	v_mov_b32_e32 v20, v18
	v_mov_b32_e32 v21, v18
	v_mov_b32_e32 v22, v18
	v_mov_b32_e32 v23, v18
	v_mov_b32_e32 v24, v18
	v_mov_b32_e32 v25, v18
	v_mov_b32_e32 v26, v18
	v_mov_b32_e32 v27, v18
	v_mov_b32_e32 v28, v18
	v_mov_b32_e32 v29, v18
	v_mov_b32_e32 v30, v18
	v_mov_b32_e32 v31, v18
	v_mov_b32_e32 v32, v18
	v_mov_b32_e32 v33, v18
	v_mov_b32_e32 v34, v18
	v_mov_b32_e32 v35, v18
	v_mov_b32_e32 v36, v18
	v_mov_b32_e32 v37, v18
	v_mov_b32_e32 v38, v18
	v_mov_b32_e32 v39, v18
	v_mov_b32_e32 v40, v18
	v_mov_b32_e32 v41, v18
	v_mov_b32_e32 v46, v18
	v_mov_b32_e32 v47, v18
	v_mov_b32_e32 v48, v18
	v_mov_b32_e32 v49, v18
	v_mov_b32_e32 v62, v18
	v_mov_b32_e32 v63, v18
	v_mov_b32_e32 v64, v18
	v_mov_b32_e32 v65, v18
	v_mov_b32_e32 v66, v18
	v_mov_b32_e32 v67, v18
	v_mov_b32_e32 v68, v18
	v_mov_b32_e32 v69, v18
	v_mov_b32_e32 v78, v18
	v_mov_b32_e32 v79, v18
	v_mov_b32_e32 v80, v18
	v_mov_b32_e32 v81, v18
	v_mov_b32_e32 v90, v18
	v_mov_b32_e32 v91, v18
	v_mov_b32_e32 v92, v18
	v_mov_b32_e32 v93, v18
	v_mov_b32_e32 v94, v18
	v_mov_b32_e32 v95, v18
	v_mov_b32_e32 v96, v18
	v_mov_b32_e32 v97, v18
	v_mov_b32_e32 v114, v18
	v_mov_b32_e32 v115, v18
	v_mov_b32_e32 v116, v18
	v_mov_b32_e32 v117, v18
	v_mov_b32_e32 v122, v18
	v_mov_b32_e32 v123, v18
	v_mov_b32_e32 v124, v18
	v_mov_b32_e32 v125, v18
	v_mov_b32_e32 v138, v18
	v_mov_b32_e32 v139, v18
	v_mov_b32_e32 v140, v18
	v_mov_b32_e32 v141, v18
	v_mov_b32_e32 v142, v18
	v_mov_b32_e32 v143, v18
	v_mov_b32_e32 v144, v18
	v_mov_b32_e32 v145, v18
	v_mov_b32_e32 v118, v18
	v_mov_b32_e32 v119, v18
	v_mov_b32_e32 v120, v18
	v_mov_b32_e32 v121, v18
	v_mov_b32_e32 v126, v18
	v_mov_b32_e32 v127, v18
	v_mov_b32_e32 v128, v18
	v_mov_b32_e32 v129, v18
	v_mov_b32_e32 v134, v18
	v_mov_b32_e32 v135, v18
	v_mov_b32_e32 v136, v18
	v_mov_b32_e32 v137, v18
	v_mov_b32_e32 v130, v18
	v_mov_b32_e32 v131, v18
	v_mov_b32_e32 v132, v18
	v_mov_b32_e32 v133, v18
	v_mov_b32_e32 v98, v18
	v_mov_b32_e32 v99, v18
	v_mov_b32_e32 v100, v18
	v_mov_b32_e32 v101, v18
	v_mov_b32_e32 v102, v18
	v_mov_b32_e32 v103, v18
	v_mov_b32_e32 v104, v18
	v_mov_b32_e32 v105, v18
	v_mov_b32_e32 v110, v18
	v_mov_b32_e32 v111, v18
	v_mov_b32_e32 v112, v18
	v_mov_b32_e32 v113, v18
	v_mov_b32_e32 v106, v18
	v_mov_b32_e32 v107, v18
	v_mov_b32_e32 v108, v18
	v_mov_b32_e32 v109, v18
	v_mov_b32_e32 v70, v18
	v_mov_b32_e32 v71, v18
	v_mov_b32_e32 v72, v18
	v_mov_b32_e32 v73, v18
	v_mov_b32_e32 v82, v18
	v_mov_b32_e32 v83, v18
	v_mov_b32_e32 v84, v18
	v_mov_b32_e32 v85, v18
	v_mov_b32_e32 v86, v18
	v_mov_b32_e32 v87, v18
	v_mov_b32_e32 v88, v18
	v_mov_b32_e32 v89, v18
	v_mov_b32_e32 v74, v18
	v_mov_b32_e32 v75, v18
	v_mov_b32_e32 v76, v18
	v_mov_b32_e32 v77, v18
	v_mov_b32_e32 v42, v18
	v_mov_b32_e32 v43, v18
	v_mov_b32_e32 v44, v18
	v_mov_b32_e32 v45, v18
	v_mov_b32_e32 v54, v18
	v_mov_b32_e32 v55, v18
	v_mov_b32_e32 v56, v18
	v_mov_b32_e32 v57, v18
	v_mov_b32_e32 v58, v18
	v_mov_b32_e32 v59, v18
	v_mov_b32_e32 v60, v18
	v_mov_b32_e32 v61, v18
	v_mov_b32_e32 v50, v18
	v_mov_b32_e32 v51, v18
	v_mov_b32_e32 v52, v18
	v_mov_b32_e32 v53, v18
	s_cmp_lt_u32 s80, 4
	s_cbranch_scc1 .Lprio_sg
	s_setprio 1
.Lprio_sg:
.LBB0_878:
	s_and_b32 s26, s24, 0x8000
	s_add_i32 s26, s26, 0
	s_add_i32 s74, s73, 0
	s_add_i32 s26, s26, 0x18000
	v_add_u32_e32 v179, s26, v173
	v_add_u32_e32 v212, s74, v175
	v_add_u32_e32 v218, s26, v171
	v_add_u32_e32 v220, s26, v169
	v_add_u32_e32 v214, s26, v172
	ds_read_b64_tr_b16 v[180:181], v179
	ds_read_b64_tr_b16 v[182:183], v179 offset:2048
	ds_read_b64_tr_b16 v[184:185], v214
	ds_read_b64_tr_b16 v[186:187], v214 offset:2048
	ds_read_b128 v[188:191], v212
	ds_read_b64_tr_b16 v[192:193], v218
	ds_read_b64_tr_b16 v[194:195], v218 offset:2048
	ds_read_b128 v[196:199], v212 offset:2048
	ds_read_b64_tr_b16 v[200:201], v220
	ds_read_b64_tr_b16 v[202:203], v220 offset:2048
	s_waitcnt lgkmcnt(5)
	v_mfma_f32_16x16x32_bf16 v[62:65], v[180:183], v[188:191], v[62:65]
	ds_read_b128 v[204:207], v212 offset:4096
	s_add_u32 s26, s24, 0x8000
	s_addc_u32 s27, s25, 0
	v_mfma_f32_16x16x32_bf16 v[46:49], v[184:187], v[188:191], v[46:49]
	v_add_u32_e32 v208, 0xfffd0000, v176
	s_add_i32 s75, s51, s53
	s_mov_b32 s76, m0
	s_mov_b32 m0, s75
	s_nop 0
	global_load_lds_dwordx4 v208, s[22:23]
	s_mov_b32 m0, s76
	s_waitcnt lgkmcnt(4)
	v_mfma_f32_16x16x32_bf16 v[38:41], v[192:195], v[188:191], v[38:41]
	s_waitcnt lgkmcnt(1)
	v_mfma_f32_16x16x32_bf16 v[34:37], v[200:203], v[188:191], v[34:37]
	v_mfma_f32_16x16x32_bf16 v[30:33], v[180:183], v[196:199], v[30:33]
	ds_read_b128 v[188:191], v212 offset:6144
	v_add_u32_e32 v208, 0xfffe0000, v176
	s_add_i32 s76, s75, 0x2000
	v_mfma_f32_16x16x32_bf16 v[26:29], v[184:187], v[196:199], v[26:29]
	s_mov_b32 s77, m0
	s_mov_b32 m0, s76
	s_nop 0
	global_load_lds_dwordx4 v208, s[22:23]
	s_mov_b32 m0, s77
	v_mfma_f32_16x16x32_bf16 v[22:25], v[192:195], v[196:199], v[22:25]
	v_mfma_f32_16x16x32_bf16 v[18:21], v[200:203], v[196:199], v[18:21]
	s_waitcnt lgkmcnt(1)
	v_mfma_f32_16x16x32_bf16 v[66:69], v[180:183], v[204:207], v[66:69]
	ds_read_b128 v[196:199], v212 offset:8192
	v_add_u32_e32 v208, 0xffff0000, v176
	s_add_i32 s76, s75, 0x4000
	v_mfma_f32_16x16x32_bf16 v[78:81], v[184:187], v[204:207], v[78:81]
	s_mov_b32 s77, m0
	s_mov_b32 m0, s76
	s_nop 0
	global_load_lds_dwordx4 v208, s[22:23]
	s_mov_b32 m0, s77
	v_mfma_f32_16x16x32_bf16 v[90:93], v[192:195], v[204:207], v[90:93]
	v_mfma_f32_16x16x32_bf16 v[94:97], v[200:203], v[204:207], v[94:97]
	s_waitcnt lgkmcnt(1)
	v_mfma_f32_16x16x32_bf16 v[114:117], v[180:183], v[188:191], v[114:117]
	ds_read_b128 v[204:207], v212 offset:10240
	s_addk_i32 s75, 0x6000
	s_mov_b32 s76, m0
	s_mov_b32 m0, s75
	s_nop 0
	global_load_lds_dwordx4 v176, s[22:23]
	s_mov_b32 m0, s76
	v_mfma_f32_16x16x32_bf16 v[122:125], v[184:187], v[188:191], v[122:125]
	v_mfma_f32_16x16x32_bf16 v[138:141], v[192:195], v[188:191], v[138:141]
	v_mfma_f32_16x16x32_bf16 v[142:145], v[200:203], v[188:191], v[142:145]
	ds_read_b128 v[188:191], v212 offset:12288
	ds_read_b64_tr_b16 v[208:209], v179 offset:16384
	ds_read_b64_tr_b16 v[210:211], v179 offset:18432
	s_waitcnt lgkmcnt(4)
	v_mfma_f32_16x16x32_bf16 v[118:121], v[180:183], v[196:199], v[118:121]
	v_mfma_f32_16x16x32_bf16 v[126:129], v[184:187], v[196:199], v[126:129]
	v_mfma_f32_16x16x32_bf16 v[134:137], v[192:195], v[196:199], v[134:137]
	v_mfma_f32_16x16x32_bf16 v[130:133], v[200:203], v[196:199], v[130:133]
	ds_read_b128 v[196:199], v212 offset:14336
	ds_read_b64_tr_b16 v[212:213], v214 offset:16384
	ds_read_b64_tr_b16 v[214:215], v214 offset:18432
	s_waitcnt lgkmcnt(6)
	v_mfma_f32_16x16x32_bf16 v[98:101], v[180:183], v[204:207], v[98:101]
	v_mfma_f32_16x16x32_bf16 v[102:105], v[184:187], v[204:207], v[102:105]
	v_mfma_f32_16x16x32_bf16 v[110:113], v[192:195], v[204:207], v[110:113]
	v_mfma_f32_16x16x32_bf16 v[106:109], v[200:203], v[204:207], v[106:109]
	v_add_u32_e32 v179, s74, v177
	ds_read_b128 v[204:207], v179
	ds_read_b64_tr_b16 v[216:217], v218 offset:16384
	ds_read_b64_tr_b16 v[218:219], v218 offset:18432
	s_waitcnt lgkmcnt(8)
	v_mfma_f32_16x16x32_bf16 v[70:73], v[180:183], v[188:191], v[70:73]
	v_mfma_f32_16x16x32_bf16 v[82:85], v[184:187], v[188:191], v[82:85]
	v_mfma_f32_16x16x32_bf16 v[86:89], v[192:195], v[188:191], v[86:89]
	v_mfma_f32_16x16x32_bf16 v[74:77], v[200:203], v[188:191], v[74:77]
	s_waitcnt lgkmcnt(5)
	v_mfma_f32_16x16x32_bf16 v[42:45], v[180:183], v[196:199], v[42:45]
	ds_read_b128 v[180:183], v179 offset:2048
	s_and_b32 s74, s26, 0x8000
	v_mfma_f32_16x16x32_bf16 v[54:57], v[184:187], v[196:199], v[54:57]
	ds_read_b64_tr_b16 v[184:185], v220 offset:16384
	ds_read_b64_tr_b16 v[186:187], v220 offset:18432
	v_mfma_f32_16x16x32_bf16 v[58:61], v[192:195], v[196:199], v[58:61]
	v_mfma_f32_16x16x32_bf16 v[50:53], v[200:203], v[196:199], v[50:53]
	s_waitcnt lgkmcnt(5)
	v_mfma_f32_16x16x32_bf16 v[62:65], v[208:211], v[204:207], v[62:65]
	ds_read_b128 v[188:191], v179 offset:4096
	v_add_u32_e32 v196, s74, v178
	s_add_u32 s74, s6, s24
	v_mfma_f32_16x16x32_bf16 v[46:49], v[212:215], v[204:207], v[46:49]
	s_addc_u32 s75, s52, s25
	s_add_u32 s24, s74, 0x10000
	s_waitcnt vmcnt(7)
	s_waitcnt lgkmcnt(4)
	v_mfma_f32_16x16x32_bf16 v[38:41], v[216:219], v[204:207], v[38:41]
	s_addc_u32 s25, s75, 0
	ds_write_b128 v196, v[14:17]
	global_load_dwordx4 v[14:17], v151, s[24:25]
	s_waitcnt lgkmcnt(2)
	v_mfma_f32_16x16x32_bf16 v[34:37], v[184:187], v[204:207], v[34:37]
	v_mfma_f32_16x16x32_bf16 v[30:33], v[208:211], v[180:183], v[30:33]
	ds_read_b128 v[192:195], v179 offset:6144
	s_add_u32 s24, s74, 0x12000
	s_waitcnt vmcnt(7)
	v_mfma_f32_16x16x32_bf16 v[26:29], v[212:215], v[180:183], v[26:29]
	s_addc_u32 s25, s75, 0
	ds_write_b128 v196, v[10:13] offset:8192
	global_load_dwordx4 v[10:13], v151, s[24:25]
	v_mfma_f32_16x16x32_bf16 v[22:25], v[216:219], v[180:183], v[22:25]
	v_mfma_f32_16x16x32_bf16 v[18:21], v[184:187], v[180:183], v[18:21]
	s_waitcnt lgkmcnt(3)
	v_mfma_f32_16x16x32_bf16 v[66:69], v[208:211], v[188:191], v[66:69]
	ds_read_b128 v[180:183], v179 offset:8192
	s_add_u32 s24, s74, 0x14000
	s_waitcnt vmcnt(7)
	v_mfma_f32_16x16x32_bf16 v[78:81], v[212:215], v[188:191], v[78:81]
	s_addc_u32 s25, s75, 0
	ds_write_b128 v196, v[6:9] offset:16384
	global_load_dwordx4 v[6:9], v151, s[24:25]
	v_mfma_f32_16x16x32_bf16 v[90:93], v[216:219], v[188:191], v[90:93]
	v_mfma_f32_16x16x32_bf16 v[94:97], v[184:187], v[188:191], v[94:97]
	s_waitcnt lgkmcnt(3)
	v_mfma_f32_16x16x32_bf16 v[114:117], v[208:211], v[192:195], v[114:117]
	ds_read_b128 v[188:191], v179 offset:10240
	s_add_u32 s24, s74, 0x16000
	s_waitcnt vmcnt(7)
	v_mfma_f32_16x16x32_bf16 v[122:125], v[212:215], v[192:195], v[122:125]
	s_addc_u32 s25, s75, 0
	ds_write_b128 v196, v[2:5] offset:24576
	global_load_dwordx4 v[2:5], v151, s[24:25]
	v_mfma_f32_16x16x32_bf16 v[138:141], v[216:219], v[192:195], v[138:141]
	v_mfma_f32_16x16x32_bf16 v[142:145], v[184:187], v[192:195], v[142:145]
	s_waitcnt lgkmcnt(3)
	v_mfma_f32_16x16x32_bf16 v[118:121], v[208:211], v[180:183], v[118:121]
	ds_read_b128 v[192:195], v179 offset:12288
	v_mfma_f32_16x16x32_bf16 v[126:129], v[212:215], v[180:183], v[126:129]
	v_mfma_f32_16x16x32_bf16 v[134:137], v[216:219], v[180:183], v[134:137]
	v_mfma_f32_16x16x32_bf16 v[130:133], v[184:187], v[180:183], v[130:133]
	s_waitcnt lgkmcnt(2)
	v_mfma_f32_16x16x32_bf16 v[98:101], v[208:211], v[188:191], v[98:101]
	ds_read_b128 v[180:183], v179 offset:14336
	v_mfma_f32_16x16x32_bf16 v[102:105], v[212:215], v[188:191], v[102:105]
	v_mfma_f32_16x16x32_bf16 v[110:113], v[216:219], v[188:191], v[110:113]
	v_mfma_f32_16x16x32_bf16 v[106:109], v[184:187], v[188:191], v[106:109]
	s_waitcnt lgkmcnt(1)
	v_mfma_f32_16x16x32_bf16 v[70:73], v[208:211], v[192:195], v[70:73]
	v_mfma_f32_16x16x32_bf16 v[82:85], v[212:215], v[192:195], v[82:85]
	v_mfma_f32_16x16x32_bf16 v[86:89], v[216:219], v[192:195], v[86:89]
	v_mfma_f32_16x16x32_bf16 v[74:77], v[184:187], v[192:195], v[74:77]
	s_waitcnt lgkmcnt(0)
	v_mfma_f32_16x16x32_bf16 v[42:45], v[208:211], v[180:183], v[42:45]
	v_mfma_f32_16x16x32_bf16 v[54:57], v[212:215], v[180:183], v[54:57]
	v_mfma_f32_16x16x32_bf16 v[58:61], v[216:219], v[180:183], v[58:61]
	v_mfma_f32_16x16x32_bf16 v[50:53], v[184:187], v[180:183], v[50:53]
	s_add_i32 s24, s73, 0x8000
	s_cmp_lg_u32 s73, 0x10000
	s_waitcnt lgkmcnt(0)
	s_barrier
	s_cselect_b32 s73, s24, 0
	s_add_i32 s24, s53, 0x8000
	s_cmp_lg_u32 s53, 0x10000
	v_add_u32_e32 v176, 0x80, v176
	s_cselect_b32 s53, s24, 0
	s_cmp_lg_u32 s26, 0x30000
	s_mov_b64 s[24:25], s[26:27]
	s_cbranch_scc1 .LBB0_878
	s_setprio 0
	v_add_u32_e32 v176, s40, v173
	v_add_u32_e32 v218, 0, v175
	v_add_u32_e32 v175, s40, v171
	v_add_u32_e32 v219, s40, v169
	v_add_u32_e32 v212, s40, v172
	ds_read_b64_tr_b16 v[178:179], v176
	ds_read_b64_tr_b16 v[180:181], v176 offset:2048
	ds_read_b64_tr_b16 v[182:183], v212
	ds_read_b64_tr_b16 v[184:185], v212 offset:2048
	ds_read_b128 v[186:189], v218
	ds_read_b128 v[190:193], v218 offset:2048
	ds_read_b64_tr_b16 v[194:195], v175
	ds_read_b64_tr_b16 v[196:197], v175 offset:2048
	ds_read_b64_tr_b16 v[198:199], v219
	ds_read_b64_tr_b16 v[200:201], v219 offset:2048
	ds_read_b128 v[202:205], v218 offset:4096
	s_waitcnt lgkmcnt(6)
	v_mfma_f32_16x16x32_bf16 v[62:65], v[178:181], v[186:189], v[62:65]
	v_mfma_f32_16x16x32_bf16 v[46:49], v[182:185], v[186:189], v[46:49]
	s_waitcnt lgkmcnt(3)
	v_mfma_f32_16x16x32_bf16 v[38:41], v[194:197], v[186:189], v[38:41]
	s_waitcnt lgkmcnt(1)
	v_mfma_f32_16x16x32_bf16 v[34:37], v[198:201], v[186:189], v[34:37]
	ds_read_b128 v[186:189], v218 offset:6144
	v_mfma_f32_16x16x32_bf16 v[30:33], v[178:181], v[190:193], v[30:33]
	v_mfma_f32_16x16x32_bf16 v[26:29], v[182:185], v[190:193], v[26:29]
	v_mfma_f32_16x16x32_bf16 v[22:25], v[194:197], v[190:193], v[22:25]
	v_mfma_f32_16x16x32_bf16 v[18:21], v[198:201], v[190:193], v[18:21]
	ds_read_b128 v[190:193], v218 offset:8192
	s_waitcnt lgkmcnt(2)
	v_mfma_f32_16x16x32_bf16 v[66:69], v[178:181], v[202:205], v[66:69]
	v_mfma_f32_16x16x32_bf16 v[78:81], v[182:185], v[202:205], v[78:81]
	v_mfma_f32_16x16x32_bf16 v[90:93], v[194:197], v[202:205], v[90:93]
	v_mfma_f32_16x16x32_bf16 v[94:97], v[198:201], v[202:205], v[94:97]
	ds_read_b128 v[202:205], v218 offset:10240
	s_waitcnt lgkmcnt(2)
	v_mfma_f32_16x16x32_bf16 v[114:117], v[178:181], v[186:189], v[114:117]
	v_mfma_f32_16x16x32_bf16 v[122:125], v[182:185], v[186:189], v[122:125]
	v_mfma_f32_16x16x32_bf16 v[138:141], v[194:197], v[186:189], v[138:141]
	v_mfma_f32_16x16x32_bf16 v[142:145], v[198:201], v[186:189], v[142:145]
	ds_read_b128 v[186:189], v218 offset:12288
	ds_read_b64_tr_b16 v[206:207], v176 offset:16384
	ds_read_b64_tr_b16 v[208:209], v176 offset:18432
	s_waitcnt lgkmcnt(4)
	v_mfma_f32_16x16x32_bf16 v[118:121], v[178:181], v[190:193], v[118:121]
	v_mfma_f32_16x16x32_bf16 v[126:129], v[182:185], v[190:193], v[126:129]
	v_mfma_f32_16x16x32_bf16 v[134:137], v[194:197], v[190:193], v[134:137]
	v_mfma_f32_16x16x32_bf16 v[130:133], v[198:201], v[190:193], v[130:133]
	ds_read_b128 v[190:193], v218 offset:14336
	ds_read_b64_tr_b16 v[210:211], v212 offset:16384
	ds_read_b64_tr_b16 v[212:213], v212 offset:18432
	s_waitcnt lgkmcnt(6)
	v_mfma_f32_16x16x32_bf16 v[98:101], v[178:181], v[202:205], v[98:101]
	v_mfma_f32_16x16x32_bf16 v[102:105], v[182:185], v[202:205], v[102:105]
	v_mfma_f32_16x16x32_bf16 v[110:113], v[194:197], v[202:205], v[110:113]
	v_mfma_f32_16x16x32_bf16 v[106:109], v[198:201], v[202:205], v[106:109]
	v_add_u32_e32 v244, 0, v177
	ds_read_b128 v[202:205], v244
	ds_read_b64_tr_b16 v[214:215], v175 offset:16384
	ds_read_b64_tr_b16 v[216:217], v175 offset:18432
	s_waitcnt lgkmcnt(8)
	v_mfma_f32_16x16x32_bf16 v[70:73], v[178:181], v[186:189], v[70:73]
	v_mfma_f32_16x16x32_bf16 v[82:85], v[182:185], v[186:189], v[82:85]
	v_mfma_f32_16x16x32_bf16 v[86:89], v[194:197], v[186:189], v[86:89]
	v_mfma_f32_16x16x32_bf16 v[74:77], v[198:201], v[186:189], v[74:77]
	s_waitcnt lgkmcnt(5)
	v_mfma_f32_16x16x32_bf16 v[42:45], v[178:181], v[190:193], v[42:45]
	v_mfma_f32_16x16x32_bf16 v[54:57], v[182:185], v[190:193], v[54:57]
	ds_read_b128 v[176:179], v244 offset:2048
	ds_read_b64_tr_b16 v[180:181], v219 offset:16384
	ds_read_b64_tr_b16 v[182:183], v219 offset:18432
	v_mfma_f32_16x16x32_bf16 v[58:61], v[194:197], v[190:193], v[58:61]
	v_mfma_f32_16x16x32_bf16 v[50:53], v[198:201], v[190:193], v[50:53]
	ds_read_b128 v[184:187], v244 offset:4096
	s_waitcnt vmcnt(3)
	v_add_u32_e32 v174, s46, v174
	s_waitcnt lgkmcnt(6)
	v_mfma_f32_16x16x32_bf16 v[62:65], v[206:209], v[202:205], v[62:65]
	ds_write_b128 v174, v[14:17]
	v_mfma_f32_16x16x32_bf16 v[46:49], v[210:213], v[202:205], v[46:49]
	s_waitcnt lgkmcnt(5)
	v_mfma_f32_16x16x32_bf16 v[38:41], v[214:217], v[202:205], v[38:41]
	s_waitcnt lgkmcnt(2)
	v_mfma_f32_16x16x32_bf16 v[14:17], v[180:183], v[202:205], v[34:37]
	s_nop 2
	ds_read_b128 v[34:37], v244 offset:6144
	s_waitcnt vmcnt(2)
	v_mfma_f32_16x16x32_bf16 v[30:33], v[206:209], v[176:179], v[30:33]
	ds_write_b128 v174, v[10:13] offset:8192
	v_mfma_f32_16x16x32_bf16 v[26:29], v[210:213], v[176:179], v[26:29]
	v_mfma_f32_16x16x32_bf16 v[22:25], v[214:217], v[176:179], v[22:25]
	v_mfma_f32_16x16x32_bf16 v[10:13], v[180:183], v[176:179], v[18:21]
	s_waitcnt lgkmcnt(3)
	v_mfma_f32_16x16x32_bf16 v[18:21], v[206:209], v[184:187], v[66:69]
	v_mfma_f32_16x16x32_bf16 v[66:69], v[210:213], v[184:187], v[78:81]
	v_mfma_f32_16x16x32_bf16 v[78:81], v[214:217], v[184:187], v[90:93]
	s_nop 2
	ds_read_b128 v[90:93], v244 offset:8192
	s_waitcnt vmcnt(1)
	ds_write_b128 v174, v[6:9] offset:16384
	v_mfma_f32_16x16x32_bf16 v[6:9], v[180:183], v[184:187], v[94:97]
	s_waitcnt lgkmcnt(3)
	v_mfma_f32_16x16x32_bf16 v[94:97], v[206:209], v[34:37], v[114:117]
	v_mfma_f32_16x16x32_bf16 v[114:117], v[210:213], v[34:37], v[122:125]
	v_mfma_f32_16x16x32_bf16 v[122:125], v[214:217], v[34:37], v[138:141]
	s_nop 2
	ds_read_b128 v[138:141], v244 offset:10240
	s_waitcnt vmcnt(0)
	ds_write_b128 v174, v[2:5] offset:24576
	v_mfma_f32_16x16x32_bf16 v[2:5], v[180:183], v[34:37], v[142:145]
	s_waitcnt lgkmcnt(3)
	v_mfma_f32_16x16x32_bf16 v[34:37], v[206:209], v[90:93], v[118:121]
	v_mfma_f32_16x16x32_bf16 v[118:121], v[210:213], v[90:93], v[126:129]
	v_mfma_f32_16x16x32_bf16 v[126:129], v[214:217], v[90:93], v[134:137]
	s_nop 2
	ds_read_b128 v[134:137], v244 offset:12288
	v_mfma_f32_16x16x32_bf16 v[90:93], v[180:183], v[90:93], v[130:133]
	s_nop 2
	ds_read_b128 v[130:133], v244 offset:14336
	s_waitcnt lgkmcnt(3)
	v_mfma_f32_16x16x32_bf16 v[98:101], v[206:209], v[138:141], v[98:101]
	v_mfma_f32_16x16x32_bf16 v[102:105], v[210:213], v[138:141], v[102:105]
	v_mfma_f32_16x16x32_bf16 v[110:113], v[214:217], v[138:141], v[110:113]
	v_mfma_f32_16x16x32_bf16 v[106:109], v[180:183], v[138:141], v[106:109]
	s_waitcnt lgkmcnt(1)
	v_mfma_f32_16x16x32_bf16 v[70:73], v[206:209], v[134:137], v[70:73]
	v_mfma_f32_16x16x32_bf16 v[82:85], v[210:213], v[134:137], v[82:85]
	v_mfma_f32_16x16x32_bf16 v[86:89], v[214:217], v[134:137], v[86:89]
	v_mfma_f32_16x16x32_bf16 v[74:77], v[180:183], v[134:137], v[74:77]
	s_waitcnt lgkmcnt(0)
	v_mfma_f32_16x16x32_bf16 v[42:45], v[206:209], v[130:133], v[42:45]
	v_mfma_f32_16x16x32_bf16 v[54:57], v[210:213], v[130:133], v[54:57]
	v_mfma_f32_16x16x32_bf16 v[58:61], v[214:217], v[130:133], v[58:61]
	v_mfma_f32_16x16x32_bf16 v[50:53], v[180:183], v[130:133], v[50:53]
	s_waitcnt lgkmcnt(0)
	s_barrier
	v_add_u32_e32 v188, s46, v173
	v_add_u32_e32 v202, s46, v172
	v_add_u32_e32 v171, s46, v171
	ds_read_b64_tr_b16 v[130:131], v188
	ds_read_b64_tr_b16 v[132:133], v188 offset:2048
	ds_read_b64_tr_b16 v[134:135], v202
	ds_read_b64_tr_b16 v[136:137], v202 offset:2048
	ds_read_b128 v[138:141], v218 offset:32768
	ds_read_b64_tr_b16 v[142:143], v171
	ds_read_b128 v[172:175], v218 offset:34816
	ds_read_b128 v[176:179], v218 offset:36864
	ds_read_b64_tr_b16 v[144:145], v171 offset:2048
	v_add_u32_e32 v169, s46, v169
	ds_read_b64_tr_b16 v[180:181], v169
	ds_read_b64_tr_b16 v[182:183], v169 offset:2048
	s_waitcnt lgkmcnt(6)
	v_mfma_f32_16x16x32_bf16 v[62:65], v[130:133], v[138:141], v[62:65]
	v_mfma_f32_16x16x32_bf16 v[46:49], v[134:137], v[138:141], v[46:49]
	s_waitcnt lgkmcnt(2)
	v_mfma_f32_16x16x32_bf16 v[38:41], v[142:145], v[138:141], v[38:41]
	s_waitcnt lgkmcnt(0)
	v_mfma_f32_16x16x32_bf16 v[14:17], v[180:183], v[138:141], v[14:17]
	ds_read_b128 v[138:141], v218 offset:38912
	v_mfma_f32_16x16x32_bf16 v[30:33], v[130:133], v[172:175], v[30:33]
	v_mfma_f32_16x16x32_bf16 v[26:29], v[134:137], v[172:175], v[26:29]
	v_mfma_f32_16x16x32_bf16 v[22:25], v[142:145], v[172:175], v[22:25]
	v_mfma_f32_16x16x32_bf16 v[10:13], v[180:183], v[172:175], v[10:13]
	ds_read_b128 v[172:175], v218 offset:40960
	v_mfma_f32_16x16x32_bf16 v[18:21], v[130:133], v[176:179], v[18:21]
	v_mfma_f32_16x16x32_bf16 v[66:69], v[134:137], v[176:179], v[66:69]
	v_mfma_f32_16x16x32_bf16 v[78:81], v[142:145], v[176:179], v[78:81]
	v_mfma_f32_16x16x32_bf16 v[6:9], v[180:183], v[176:179], v[6:9]
	s_waitcnt lgkmcnt(1)
	v_mfma_f32_16x16x32_bf16 v[176:179], v[130:133], v[138:141], v[94:97]
	s_nop 2
	ds_read_b128 v[94:97], v218 offset:43008
	v_mfma_f32_16x16x32_bf16 v[184:187], v[134:137], v[138:141], v[114:117]
	v_mfma_f32_16x16x32_bf16 v[122:125], v[142:145], v[138:141], v[122:125]
	v_mfma_f32_16x16x32_bf16 v[2:5], v[180:183], v[138:141], v[2:5]
	s_nop 0
	ds_read_b128 v[114:117], v218 offset:45056
	ds_read_b64_tr_b16 v[138:139], v188 offset:16384
	ds_read_b64_tr_b16 v[140:141], v188 offset:18432
	s_waitcnt lgkmcnt(4)
	v_mfma_f32_16x16x32_bf16 v[34:37], v[130:133], v[172:175], v[34:37]
	v_mfma_f32_16x16x32_bf16 v[118:121], v[134:137], v[172:175], v[118:121]
	v_mfma_f32_16x16x32_bf16 v[126:129], v[142:145], v[172:175], v[126:129]
	v_mfma_f32_16x16x32_bf16 v[172:175], v[180:183], v[172:175], v[90:93]
	s_nop 2
	ds_read_b128 v[90:93], v218 offset:47104
	ds_read_b64_tr_b16 v[200:201], v202 offset:16384
	ds_read_b64_tr_b16 v[202:203], v202 offset:18432
	s_waitcnt lgkmcnt(6)
	v_mfma_f32_16x16x32_bf16 v[188:191], v[130:133], v[94:97], v[98:101]
	v_mfma_f32_16x16x32_bf16 v[192:195], v[134:137], v[94:97], v[102:105]
	v_mfma_f32_16x16x32_bf16 v[196:199], v[142:145], v[94:97], v[110:113]
	v_mfma_f32_16x16x32_bf16 v[204:207], v[180:183], v[94:97], v[106:109]
	s_waitcnt lgkmcnt(5)
	v_mfma_f32_16x16x32_bf16 v[208:211], v[130:133], v[114:117], v[70:73]
	s_nop 2
	ds_read_b128 v[70:73], v244 offset:32768
	ds_read_b64_tr_b16 v[220:221], v171 offset:16384
	ds_read_b64_tr_b16 v[222:223], v171 offset:18432
	v_mfma_f32_16x16x32_bf16 v[212:215], v[134:137], v[114:117], v[82:85]
	v_mfma_f32_16x16x32_bf16 v[216:219], v[142:145], v[114:117], v[86:89]
	v_mfma_f32_16x16x32_bf16 v[224:227], v[180:183], v[114:117], v[74:77]
	s_waitcnt lgkmcnt(5)
	v_mfma_f32_16x16x32_bf16 v[130:133], v[130:133], v[90:93], v[42:45]
	s_nop 2
	ds_read_b128 v[42:45], v244 offset:34816
	ds_read_b64_tr_b16 v[228:229], v169 offset:16384
	ds_read_b64_tr_b16 v[230:231], v169 offset:18432
	v_mfma_f32_16x16x32_bf16 v[134:137], v[134:137], v[90:93], v[54:57]
	v_mfma_f32_16x16x32_bf16 v[142:145], v[142:145], v[90:93], v[58:61]
	v_mfma_f32_16x16x32_bf16 v[180:183], v[180:183], v[90:93], v[50:53]
	s_waitcnt lgkmcnt(3)
	v_mfma_f32_16x16x32_bf16 v[240:243], v[220:223], v[70:73], v[38:41]
	s_nop 2
	ds_read_b128 v[38:41], v244 offset:36864
	v_mfma_f32_16x16x32_bf16 v[232:235], v[138:141], v[70:73], v[62:65]
	v_mfma_f32_16x16x32_bf16 v[236:239], v[200:203], v[70:73], v[46:49]
	s_waitcnt lgkmcnt(1)
	v_mfma_f32_16x16x32_bf16 v[114:117], v[228:231], v[70:73], v[14:17]
	s_nop 2
	ds_read_b128 v[14:17], v244 offset:38912
	v_mfma_f32_16x16x32_bf16 v[110:113], v[138:141], v[42:45], v[30:33]
	v_mfma_f32_16x16x32_bf16 v[106:109], v[200:203], v[42:45], v[26:29]
	v_mfma_f32_16x16x32_bf16 v[102:105], v[220:223], v[42:45], v[22:25]
	v_mfma_f32_16x16x32_bf16 v[98:101], v[228:231], v[42:45], v[10:13]
	s_nop 2
	ds_read_b128 v[10:13], v244 offset:40960
	s_waitcnt lgkmcnt(2)
	v_mfma_f32_16x16x32_bf16 v[94:97], v[138:141], v[38:41], v[18:21]
	v_mfma_f32_16x16x32_bf16 v[90:93], v[200:203], v[38:41], v[66:69]
	v_mfma_f32_16x16x32_bf16 v[86:89], v[220:223], v[38:41], v[78:81]
	v_mfma_f32_16x16x32_bf16 v[82:85], v[228:231], v[38:41], v[6:9]
	s_nop 2
	ds_read_b128 v[6:9], v244 offset:43008
	s_waitcnt lgkmcnt(2)
	v_mfma_f32_16x16x32_bf16 v[78:81], v[138:141], v[14:17], v[176:179]
	v_mfma_f32_16x16x32_bf16 v[74:77], v[200:203], v[14:17], v[184:187]
	v_mfma_f32_16x16x32_bf16 v[70:73], v[220:223], v[14:17], v[122:125]
	v_mfma_f32_16x16x32_bf16 v[66:69], v[228:231], v[14:17], v[2:5]
	s_nop 2
	ds_read_b128 v[2:5], v244 offset:45056
	s_waitcnt lgkmcnt(2)
	v_mfma_f32_16x16x32_bf16 v[62:65], v[138:141], v[10:13], v[34:37]
	v_mfma_f32_16x16x32_bf16 v[58:61], v[200:203], v[10:13], v[118:121]
	v_mfma_f32_16x16x32_bf16 v[54:57], v[220:223], v[10:13], v[126:129]
	v_mfma_f32_16x16x32_bf16 v[50:53], v[228:231], v[10:13], v[172:175]
	s_nop 0
	ds_read_b128 v[118:121], v244 offset:47104
	s_waitcnt lgkmcnt(2)
	v_mfma_f32_16x16x32_bf16 v[46:49], v[138:141], v[6:9], v[188:191]
	v_mfma_f32_16x16x32_bf16 v[42:45], v[200:203], v[6:9], v[192:195]
	v_mfma_f32_16x16x32_bf16 v[38:41], v[220:223], v[6:9], v[196:199]
	v_mfma_f32_16x16x32_bf16 v[34:37], v[228:231], v[6:9], v[204:207]
	s_waitcnt lgkmcnt(1)
	v_mfma_f32_16x16x32_bf16 v[30:33], v[138:141], v[2:5], v[208:211]
	v_mfma_f32_16x16x32_bf16 v[26:29], v[200:203], v[2:5], v[212:215]
	v_mfma_f32_16x16x32_bf16 v[22:25], v[220:223], v[2:5], v[216:219]
	v_mfma_f32_16x16x32_bf16 v[18:21], v[228:231], v[2:5], v[224:227]
	s_waitcnt lgkmcnt(0)
	v_mfma_f32_16x16x32_bf16 v[14:17], v[138:141], v[118:121], v[130:133]
	v_mfma_f32_16x16x32_bf16 v[10:13], v[200:203], v[118:121], v[134:137]
	v_mfma_f32_16x16x32_bf16 v[6:9], v[220:223], v[118:121], v[142:145]
	v_mfma_f32_16x16x32_bf16 v[2:5], v[228:231], v[118:121], v[180:183]
	v_mov_b32_e32 v118, v155
	v_mov_b32_e32 v122, v154
	s_add_i32 s50, s50, s33
	s_waitcnt lgkmcnt(0)
	s_barrier
	v_pk_mul_f32 v[124:125], v[234:235], s[18:19] op_sel_hi:[1,0]
	v_add_u32_e32 v128, s50, v122
	v_ashrrev_i32_e32 v120, 7, v128
	v_ashrrev_i32_e32 v121, 31, v120
	v_lshlrev_b64 v[130:131], 11, v[120:121]
	v_lshlrev_b32_e32 v120, 4, v122
	v_pk_mul_f32 v[122:123], v[232:233], s[18:19] op_sel_hi:[1,0]
	v_pk_mul_f32 v[124:125], v[234:235], v[124:125]
	v_pk_mul_f32 v[122:123], v[232:233], v[122:123]
	v_pk_fma_f32 v[124:125], v[234:235], v[124:125], v[234:235]
	v_pk_fma_f32 v[122:123], v[232:233], v[122:123], v[232:233]
	v_pk_mul_f32 v[124:125], v[124:125], s[20:21] op_sel_hi:[1,0]
	v_pk_mul_f32 v[122:123], v[122:123], s[20:21] op_sel_hi:[1,0]
	v_exp_f32_e32 v124, v124
	v_exp_f32_e32 v122, v122
	v_exp_f32_e32 v123, v123
	v_exp_f32_e32 v125, v125
	s_lshl_b32 s3, s3, 6
	s_lshl_b32 s2, s2, 4
	v_pk_add_f32 v[122:123], v[122:123], 1.0 op_sel_hi:[1,0]
	v_pk_add_f32 v[124:125], v[124:125], 1.0 op_sel_hi:[1,0]
	v_rcp_f32_e32 v122, v122
	v_rcp_f32_e32 v123, v123
	v_rcp_f32_e32 v124, v124
	v_rcp_f32_e32 v125, v125
	v_lshl_add_u32 v129, v118, 2, s3
	s_ashr_i32 s3, s2, 31
	s_lshl_b64 s[2:3], s[2:3], 1
	v_and_or_b32 v130, v120, s44, v130
	v_ashrrev_i32_e32 v120, 4, v129
	s_add_u32 s2, s19, s2
	v_lshlrev_b32_e32 v118, 3, v118
	v_ashrrev_i32_e32 v121, 31, v120
	s_addc_u32 s3, s21, s3
	v_and_b32_e32 v118, 24, v118
	v_mov_b32_e32 v119, v149
	v_lshl_add_u64 v[126:127], v[130:131], 0, v[120:121]
	v_pk_mul_f32 v[122:123], v[232:233], v[122:123]
	v_pk_mul_f32 v[124:125], v[234:235], v[124:125]
	v_lshl_add_u64 v[118:119], s[2:3], 0, v[118:119]
	v_cvt_pk_bf16_f32 v122, v122, v123
	v_cvt_pk_bf16_f32 v123, v124, v125
	v_lshlrev_b64 v[124:125], 11, v[126:127]
	v_lshl_add_u64 v[124:125], v[118:119], 0, v[124:125]
	global_store_dwordx2 v[124:125], v[122:123], off sc1
	s_nop 1
	v_pk_mul_f32 v[124:125], v[236:237], s[18:19] op_sel_hi:[1,0]
	v_pk_mul_f32 v[126:127], v[238:239], s[18:19] op_sel_hi:[1,0]
	v_pk_mul_f32 v[124:125], v[236:237], v[124:125]
	v_pk_mul_f32 v[126:127], v[238:239], v[126:127]
	v_pk_fma_f32 v[124:125], v[236:237], v[124:125], v[236:237]
	v_pk_fma_f32 v[126:127], v[238:239], v[126:127], v[238:239]
	v_pk_mul_f32 v[124:125], v[124:125], s[20:21] op_sel_hi:[1,0]
	v_pk_mul_f32 v[126:127], v[126:127], s[20:21] op_sel_hi:[1,0]
	v_exp_f32_e32 v124, v124
	v_exp_f32_e32 v125, v125
	v_exp_f32_e32 v126, v126
	v_exp_f32_e32 v127, v127
	v_add_u32_e32 v122, 16, v129
	v_pk_add_f32 v[124:125], v[124:125], 1.0 op_sel_hi:[1,0]
	v_ashrrev_i32_e32 v122, 4, v122
	v_pk_add_f32 v[126:127], v[126:127], 1.0 op_sel_hi:[1,0]
	v_rcp_f32_e32 v124, v124
	v_rcp_f32_e32 v125, v125
	v_rcp_f32_e32 v126, v126
	v_rcp_f32_e32 v127, v127
	v_ashrrev_i32_e32 v123, 31, v122
	v_lshl_add_u64 v[132:133], v[130:131], 0, v[122:123]
	v_pk_mul_f32 v[124:125], v[236:237], v[124:125]
	v_pk_mul_f32 v[126:127], v[238:239], v[126:127]
	v_cvt_pk_bf16_f32 v124, v124, v125
	v_cvt_pk_bf16_f32 v125, v126, v127
	v_lshlrev_b64 v[126:127], 11, v[132:133]
	v_lshl_add_u64 v[126:127], v[118:119], 0, v[126:127]
	global_store_dwordx2 v[126:127], v[124:125], off sc1
	s_nop 1
	v_pk_mul_f32 v[126:127], v[240:241], s[18:19] op_sel_hi:[1,0]
	v_pk_mul_f32 v[132:133], v[242:243], s[18:19] op_sel_hi:[1,0]
	v_pk_mul_f32 v[126:127], v[240:241], v[126:127]
	v_pk_mul_f32 v[132:133], v[242:243], v[132:133]
	v_pk_fma_f32 v[126:127], v[240:241], v[126:127], v[240:241]
	v_pk_fma_f32 v[132:133], v[242:243], v[132:133], v[242:243]
	v_pk_mul_f32 v[126:127], v[126:127], s[20:21] op_sel_hi:[1,0]
	v_pk_mul_f32 v[132:133], v[132:133], s[20:21] op_sel_hi:[1,0]
	v_exp_f32_e32 v126, v126
	v_exp_f32_e32 v127, v127
	v_exp_f32_e32 v132, v132
	v_exp_f32_e32 v133, v133
	v_add_u32_e32 v124, 32, v129
	v_pk_add_f32 v[126:127], v[126:127], 1.0 op_sel_hi:[1,0]
	v_ashrrev_i32_e32 v124, 4, v124
	v_pk_add_f32 v[132:133], v[132:133], 1.0 op_sel_hi:[1,0]
	v_rcp_f32_e32 v126, v126
	v_rcp_f32_e32 v127, v127
	v_rcp_f32_e32 v132, v132
	v_rcp_f32_e32 v133, v133
	v_ashrrev_i32_e32 v125, 31, v124
	v_lshl_add_u64 v[134:135], v[130:131], 0, v[124:125]
	v_pk_mul_f32 v[126:127], v[240:241], v[126:127]
	v_pk_mul_f32 v[132:133], v[242:243], v[132:133]
	v_cvt_pk_bf16_f32 v126, v126, v127
	v_cvt_pk_bf16_f32 v127, v132, v133
	v_lshlrev_b64 v[132:133], 11, v[134:135]
	v_lshl_add_u64 v[132:133], v[118:119], 0, v[132:133]
	global_store_dwordx2 v[132:133], v[126:127], off sc1
	s_nop 1
	v_pk_mul_f32 v[132:133], v[114:115], s[18:19] op_sel_hi:[1,0]
	v_pk_mul_f32 v[134:135], v[116:117], s[18:19] op_sel_hi:[1,0]
	v_pk_mul_f32 v[132:133], v[114:115], v[132:133]
	v_pk_mul_f32 v[134:135], v[116:117], v[134:135]
	v_pk_fma_f32 v[132:133], v[114:115], v[132:133], v[114:115]
	v_pk_fma_f32 v[134:135], v[116:117], v[134:135], v[116:117]
	v_pk_mul_f32 v[132:133], v[132:133], s[20:21] op_sel_hi:[1,0]
	v_pk_mul_f32 v[134:135], v[134:135], s[20:21] op_sel_hi:[1,0]
	v_exp_f32_e32 v132, v132
	v_exp_f32_e32 v133, v133
	v_exp_f32_e32 v134, v134
	v_exp_f32_e32 v135, v135
	v_add_u32_e32 v126, 48, v129
	v_pk_add_f32 v[132:133], v[132:133], 1.0 op_sel_hi:[1,0]
	v_ashrrev_i32_e32 v126, 4, v126
	v_pk_add_f32 v[134:135], v[134:135], 1.0 op_sel_hi:[1,0]
	v_rcp_f32_e32 v132, v132
	v_rcp_f32_e32 v133, v133
	v_rcp_f32_e32 v134, v134
	v_rcp_f32_e32 v135, v135
	v_ashrrev_i32_e32 v127, 31, v126
	v_lshl_add_u64 v[130:131], v[130:131], 0, v[126:127]
	v_pk_mul_f32 v[114:115], v[114:115], v[132:133]
	v_pk_mul_f32 v[116:117], v[116:117], v[134:135]
	v_cvt_pk_bf16_f32 v114, v114, v115
	v_cvt_pk_bf16_f32 v115, v116, v117
	v_lshlrev_b64 v[116:117], 11, v[130:131]
	v_lshl_add_u64 v[116:117], v[118:119], 0, v[116:117]
	global_store_dwordx2 v[116:117], v[114:115], off sc1
	s_nop 1
	v_add_u32_e32 v116, 16, v128
	v_ashrrev_i32_e32 v114, 7, v116
	v_lshlrev_b32_e32 v129, 4, v116
	v_pk_mul_f32 v[116:117], v[110:111], s[18:19] op_sel_hi:[1,0]
	v_pk_mul_f32 v[130:131], v[112:113], s[18:19] op_sel_hi:[1,0]
	v_pk_mul_f32 v[116:117], v[110:111], v[116:117]
	v_pk_mul_f32 v[130:131], v[112:113], v[130:131]
	v_pk_fma_f32 v[116:117], v[110:111], v[116:117], v[110:111]
	v_pk_fma_f32 v[130:131], v[112:113], v[130:131], v[112:113]
	v_pk_mul_f32 v[116:117], v[116:117], s[20:21] op_sel_hi:[1,0]
	v_pk_mul_f32 v[130:131], v[130:131], s[20:21] op_sel_hi:[1,0]
	v_exp_f32_e32 v116, v116
	v_exp_f32_e32 v117, v117
	v_exp_f32_e32 v130, v130
	v_exp_f32_e32 v131, v131
	v_ashrrev_i32_e32 v115, 31, v114
	v_pk_add_f32 v[116:117], v[116:117], 1.0 op_sel_hi:[1,0]
	v_lshlrev_b64 v[114:115], 11, v[114:115]
	v_pk_add_f32 v[130:131], v[130:131], 1.0 op_sel_hi:[1,0]
	v_rcp_f32_e32 v116, v116
	v_rcp_f32_e32 v117, v117
	v_rcp_f32_e32 v130, v130
	v_rcp_f32_e32 v131, v131
	v_and_or_b32 v114, v129, s44, v114
	v_pk_mul_f32 v[110:111], v[110:111], v[116:117]
	v_pk_mul_f32 v[116:117], v[106:107], s[18:19] op_sel_hi:[1,0]
	v_pk_mul_f32 v[112:113], v[112:113], v[130:131]
	v_pk_mul_f32 v[130:131], v[108:109], s[18:19] op_sel_hi:[1,0]
	v_pk_mul_f32 v[116:117], v[106:107], v[116:117]
	v_pk_mul_f32 v[130:131], v[108:109], v[130:131]
	v_pk_fma_f32 v[116:117], v[106:107], v[116:117], v[106:107]
	v_pk_fma_f32 v[130:131], v[108:109], v[130:131], v[108:109]
	v_pk_mul_f32 v[116:117], v[116:117], s[20:21] op_sel_hi:[1,0]
	v_pk_mul_f32 v[130:131], v[130:131], s[20:21] op_sel_hi:[1,0]
	v_exp_f32_e32 v116, v116
	v_exp_f32_e32 v117, v117
	v_exp_f32_e32 v130, v130
	v_exp_f32_e32 v131, v131
	v_lshl_add_u64 v[132:133], v[114:115], 0, v[120:121]
	v_pk_add_f32 v[116:117], v[116:117], 1.0 op_sel_hi:[1,0]
	v_cvt_pk_bf16_f32 v110, v110, v111
	v_pk_add_f32 v[130:131], v[130:131], 1.0 op_sel_hi:[1,0]
	v_rcp_f32_e32 v116, v116
	v_rcp_f32_e32 v117, v117
	v_rcp_f32_e32 v130, v130
	v_rcp_f32_e32 v131, v131
	v_cvt_pk_bf16_f32 v111, v112, v113
	v_lshlrev_b64 v[112:113], 11, v[132:133]
	v_lshl_add_u64 v[112:113], v[118:119], 0, v[112:113]
	global_store_dwordx2 v[112:113], v[110:111], off sc1
	s_nop 1
	v_lshl_add_u64 v[110:111], v[114:115], 0, v[122:123]
	v_pk_mul_f32 v[106:107], v[106:107], v[116:117]
	v_pk_mul_f32 v[108:109], v[108:109], v[130:131]
	v_cvt_pk_bf16_f32 v106, v106, v107
	v_cvt_pk_bf16_f32 v107, v108, v109
	v_lshlrev_b64 v[108:109], 11, v[110:111]
	v_pk_mul_f32 v[110:111], v[102:103], s[18:19] op_sel_hi:[1,0]
	v_pk_mul_f32 v[112:113], v[104:105], s[18:19] op_sel_hi:[1,0]
	v_pk_mul_f32 v[110:111], v[102:103], v[110:111]
	v_pk_mul_f32 v[112:113], v[104:105], v[112:113]
	v_pk_fma_f32 v[110:111], v[102:103], v[110:111], v[102:103]
	v_pk_fma_f32 v[112:113], v[104:105], v[112:113], v[104:105]
	v_pk_mul_f32 v[110:111], v[110:111], s[20:21] op_sel_hi:[1,0]
	v_pk_mul_f32 v[112:113], v[112:113], s[20:21] op_sel_hi:[1,0]
	v_exp_f32_e32 v110, v110
	v_exp_f32_e32 v111, v111
	v_exp_f32_e32 v112, v112
	v_exp_f32_e32 v113, v113
	v_lshl_add_u64 v[108:109], v[118:119], 0, v[108:109]
	v_pk_add_f32 v[110:111], v[110:111], 1.0 op_sel_hi:[1,0]
	global_store_dwordx2 v[108:109], v[106:107], off sc1
	s_nop 1
	v_pk_add_f32 v[112:113], v[112:113], 1.0 op_sel_hi:[1,0]
	v_rcp_f32_e32 v110, v110
	v_rcp_f32_e32 v111, v111
	v_rcp_f32_e32 v112, v112
	v_rcp_f32_e32 v113, v113
	v_lshl_add_u64 v[106:107], v[114:115], 0, v[124:125]
	v_pk_mul_f32 v[102:103], v[102:103], v[110:111]
	v_pk_mul_f32 v[108:109], v[100:101], s[18:19] op_sel_hi:[1,0]
	v_pk_mul_f32 v[104:105], v[104:105], v[112:113]
	v_cvt_pk_bf16_f32 v102, v102, v103
	v_cvt_pk_bf16_f32 v103, v104, v105
	v_lshlrev_b64 v[104:105], 11, v[106:107]
	v_pk_mul_f32 v[106:107], v[98:99], s[18:19] op_sel_hi:[1,0]
	v_pk_mul_f32 v[108:109], v[100:101], v[108:109]
	v_pk_mul_f32 v[106:107], v[98:99], v[106:107]
	v_pk_fma_f32 v[108:109], v[100:101], v[108:109], v[100:101]
	v_pk_fma_f32 v[106:107], v[98:99], v[106:107], v[98:99]
	v_pk_mul_f32 v[108:109], v[108:109], s[20:21] op_sel_hi:[1,0]
	v_pk_mul_f32 v[106:107], v[106:107], s[20:21] op_sel_hi:[1,0]
	v_exp_f32_e32 v108, v108
	v_exp_f32_e32 v106, v106
	v_exp_f32_e32 v107, v107
	v_exp_f32_e32 v109, v109
	v_lshl_add_u64 v[104:105], v[118:119], 0, v[104:105]
	global_store_dwordx2 v[104:105], v[102:103], off sc1
	s_nop 1
	v_pk_add_f32 v[106:107], v[106:107], 1.0 op_sel_hi:[1,0]
	v_pk_add_f32 v[108:109], v[108:109], 1.0 op_sel_hi:[1,0]
	v_rcp_f32_e32 v106, v106
	v_rcp_f32_e32 v107, v107
	v_rcp_f32_e32 v108, v108
	v_rcp_f32_e32 v109, v109
	v_lshl_add_u64 v[102:103], v[114:115], 0, v[126:127]
	v_pk_mul_f32 v[98:99], v[98:99], v[106:107]
	s_add_i32 s47, s72, s47
	v_pk_mul_f32 v[100:101], v[100:101], v[108:109]
	v_cvt_pk_bf16_f32 v98, v98, v99
	v_cvt_pk_bf16_f32 v99, v100, v101
	v_lshlrev_b64 v[100:101], 11, v[102:103]
	v_lshl_add_u64 v[100:101], v[118:119], 0, v[100:101]
	global_store_dwordx2 v[100:101], v[98:99], off sc1
	s_nop 1
	v_add_u32_e32 v100, 32, v128
	v_ashrrev_i32_e32 v98, 7, v100
	v_lshlrev_b32_e32 v104, 4, v100
	v_pk_mul_f32 v[100:101], v[94:95], s[18:19] op_sel_hi:[1,0]
	v_pk_mul_f32 v[102:103], v[96:97], s[18:19] op_sel_hi:[1,0]
	v_pk_mul_f32 v[100:101], v[94:95], v[100:101]
	v_pk_mul_f32 v[102:103], v[96:97], v[102:103]
	v_pk_fma_f32 v[100:101], v[94:95], v[100:101], v[94:95]
	v_pk_fma_f32 v[102:103], v[96:97], v[102:103], v[96:97]
	v_pk_mul_f32 v[100:101], v[100:101], s[20:21] op_sel_hi:[1,0]
	v_pk_mul_f32 v[102:103], v[102:103], s[20:21] op_sel_hi:[1,0]
	v_exp_f32_e32 v100, v100
	v_exp_f32_e32 v101, v101
	v_exp_f32_e32 v102, v102
	v_exp_f32_e32 v103, v103
	v_ashrrev_i32_e32 v99, 31, v98
	v_pk_add_f32 v[100:101], v[100:101], 1.0 op_sel_hi:[1,0]
	v_lshlrev_b64 v[98:99], 11, v[98:99]
	v_pk_add_f32 v[102:103], v[102:103], 1.0 op_sel_hi:[1,0]
	v_rcp_f32_e32 v100, v100
	v_rcp_f32_e32 v101, v101
	v_rcp_f32_e32 v102, v102
	v_rcp_f32_e32 v103, v103
	v_and_or_b32 v98, v104, s44, v98
	v_pk_mul_f32 v[94:95], v[94:95], v[100:101]
	v_pk_mul_f32 v[100:101], v[90:91], s[18:19] op_sel_hi:[1,0]
	v_pk_mul_f32 v[96:97], v[96:97], v[102:103]
	v_pk_mul_f32 v[102:103], v[92:93], s[18:19] op_sel_hi:[1,0]
	v_pk_mul_f32 v[100:101], v[90:91], v[100:101]
	v_pk_mul_f32 v[102:103], v[92:93], v[102:103]
	v_pk_fma_f32 v[100:101], v[90:91], v[100:101], v[90:91]
	v_pk_fma_f32 v[102:103], v[92:93], v[102:103], v[92:93]
	v_pk_mul_f32 v[100:101], v[100:101], s[20:21] op_sel_hi:[1,0]
	v_pk_mul_f32 v[102:103], v[102:103], s[20:21] op_sel_hi:[1,0]
	v_exp_f32_e32 v100, v100
	v_exp_f32_e32 v101, v101
	v_exp_f32_e32 v102, v102
	v_exp_f32_e32 v103, v103
	v_lshl_add_u64 v[104:105], v[98:99], 0, v[120:121]
	v_pk_add_f32 v[100:101], v[100:101], 1.0 op_sel_hi:[1,0]
	v_cvt_pk_bf16_f32 v94, v94, v95
	v_pk_add_f32 v[102:103], v[102:103], 1.0 op_sel_hi:[1,0]
	v_rcp_f32_e32 v100, v100
	v_rcp_f32_e32 v101, v101
	v_rcp_f32_e32 v102, v102
	v_rcp_f32_e32 v103, v103
	v_cvt_pk_bf16_f32 v95, v96, v97
	v_lshlrev_b64 v[96:97], 11, v[104:105]
	v_lshl_add_u64 v[96:97], v[118:119], 0, v[96:97]
	global_store_dwordx2 v[96:97], v[94:95], off sc1
	s_nop 1
	v_lshl_add_u64 v[94:95], v[98:99], 0, v[122:123]
	v_pk_mul_f32 v[90:91], v[90:91], v[100:101]
	v_pk_mul_f32 v[92:93], v[92:93], v[102:103]
	v_cvt_pk_bf16_f32 v90, v90, v91
	v_cvt_pk_bf16_f32 v91, v92, v93
	v_lshlrev_b64 v[92:93], 11, v[94:95]
	v_pk_mul_f32 v[94:95], v[86:87], s[18:19] op_sel_hi:[1,0]
	v_pk_mul_f32 v[96:97], v[88:89], s[18:19] op_sel_hi:[1,0]
	v_pk_mul_f32 v[94:95], v[86:87], v[94:95]
	v_pk_mul_f32 v[96:97], v[88:89], v[96:97]
	v_pk_fma_f32 v[94:95], v[86:87], v[94:95], v[86:87]
	v_pk_fma_f32 v[96:97], v[88:89], v[96:97], v[88:89]
	v_pk_mul_f32 v[94:95], v[94:95], s[20:21] op_sel_hi:[1,0]
	v_pk_mul_f32 v[96:97], v[96:97], s[20:21] op_sel_hi:[1,0]
	v_exp_f32_e32 v94, v94
	v_exp_f32_e32 v95, v95
	v_exp_f32_e32 v96, v96
	v_exp_f32_e32 v97, v97
	v_lshl_add_u64 v[92:93], v[118:119], 0, v[92:93]
	v_pk_add_f32 v[94:95], v[94:95], 1.0 op_sel_hi:[1,0]
	global_store_dwordx2 v[92:93], v[90:91], off sc1
	s_nop 1
	v_pk_add_f32 v[96:97], v[96:97], 1.0 op_sel_hi:[1,0]
	v_rcp_f32_e32 v94, v94
	v_rcp_f32_e32 v95, v95
	v_rcp_f32_e32 v96, v96
	v_rcp_f32_e32 v97, v97
	v_lshl_add_u64 v[90:91], v[98:99], 0, v[124:125]
	v_pk_mul_f32 v[86:87], v[86:87], v[94:95]
	v_pk_mul_f32 v[92:93], v[84:85], s[18:19] op_sel_hi:[1,0]
	v_pk_mul_f32 v[88:89], v[88:89], v[96:97]
	v_cvt_pk_bf16_f32 v86, v86, v87
	v_cvt_pk_bf16_f32 v87, v88, v89
	v_lshlrev_b64 v[88:89], 11, v[90:91]
	v_pk_mul_f32 v[90:91], v[82:83], s[18:19] op_sel_hi:[1,0]
	v_pk_mul_f32 v[92:93], v[84:85], v[92:93]
	v_pk_mul_f32 v[90:91], v[82:83], v[90:91]
	v_pk_fma_f32 v[92:93], v[84:85], v[92:93], v[84:85]
	v_pk_fma_f32 v[90:91], v[82:83], v[90:91], v[82:83]
	v_pk_mul_f32 v[92:93], v[92:93], s[20:21] op_sel_hi:[1,0]
	v_pk_mul_f32 v[90:91], v[90:91], s[20:21] op_sel_hi:[1,0]
	v_exp_f32_e32 v92, v92
	v_exp_f32_e32 v90, v90
	v_exp_f32_e32 v91, v91
	v_exp_f32_e32 v93, v93
	v_lshl_add_u64 v[88:89], v[118:119], 0, v[88:89]
	global_store_dwordx2 v[88:89], v[86:87], off sc1
	s_nop 1
	v_pk_add_f32 v[90:91], v[90:91], 1.0 op_sel_hi:[1,0]
	v_pk_add_f32 v[92:93], v[92:93], 1.0 op_sel_hi:[1,0]
	v_rcp_f32_e32 v90, v90
	v_rcp_f32_e32 v91, v91
	v_rcp_f32_e32 v92, v92
	v_rcp_f32_e32 v93, v93
	v_lshl_add_u64 v[86:87], v[98:99], 0, v[126:127]
	v_pk_mul_f32 v[82:83], v[82:83], v[90:91]
	s_add_i32 s38, s38, s39
	v_pk_mul_f32 v[84:85], v[84:85], v[92:93]
	v_cvt_pk_bf16_f32 v82, v82, v83
	v_cvt_pk_bf16_f32 v83, v84, v85
	v_lshlrev_b64 v[84:85], 11, v[86:87]
	v_lshl_add_u64 v[84:85], v[118:119], 0, v[84:85]
	global_store_dwordx2 v[84:85], v[82:83], off sc1
	s_nop 1
	v_add_u32_e32 v84, 48, v128
	v_ashrrev_i32_e32 v82, 7, v84
	v_lshlrev_b32_e32 v88, 4, v84
	v_pk_mul_f32 v[84:85], v[78:79], s[18:19] op_sel_hi:[1,0]
	v_pk_mul_f32 v[86:87], v[80:81], s[18:19] op_sel_hi:[1,0]
	v_pk_mul_f32 v[84:85], v[78:79], v[84:85]
	v_pk_mul_f32 v[86:87], v[80:81], v[86:87]
	v_pk_fma_f32 v[84:85], v[78:79], v[84:85], v[78:79]
	v_pk_fma_f32 v[86:87], v[80:81], v[86:87], v[80:81]
	v_pk_mul_f32 v[84:85], v[84:85], s[20:21] op_sel_hi:[1,0]
	v_pk_mul_f32 v[86:87], v[86:87], s[20:21] op_sel_hi:[1,0]
	v_exp_f32_e32 v84, v84
	v_exp_f32_e32 v85, v85
	v_exp_f32_e32 v86, v86
	v_exp_f32_e32 v87, v87
	v_ashrrev_i32_e32 v83, 31, v82
	v_pk_add_f32 v[84:85], v[84:85], 1.0 op_sel_hi:[1,0]
	v_lshlrev_b64 v[82:83], 11, v[82:83]
	v_pk_add_f32 v[86:87], v[86:87], 1.0 op_sel_hi:[1,0]
	v_rcp_f32_e32 v84, v84
	v_rcp_f32_e32 v85, v85
	v_rcp_f32_e32 v86, v86
	v_rcp_f32_e32 v87, v87
	v_and_or_b32 v82, v88, s44, v82
	v_pk_mul_f32 v[78:79], v[78:79], v[84:85]
	v_pk_mul_f32 v[84:85], v[74:75], s[18:19] op_sel_hi:[1,0]
	v_pk_mul_f32 v[80:81], v[80:81], v[86:87]
	v_pk_mul_f32 v[86:87], v[76:77], s[18:19] op_sel_hi:[1,0]
	v_pk_mul_f32 v[84:85], v[74:75], v[84:85]
	v_pk_mul_f32 v[86:87], v[76:77], v[86:87]
	v_pk_fma_f32 v[84:85], v[74:75], v[84:85], v[74:75]
	v_pk_fma_f32 v[86:87], v[76:77], v[86:87], v[76:77]
	v_pk_mul_f32 v[84:85], v[84:85], s[20:21] op_sel_hi:[1,0]
	v_pk_mul_f32 v[86:87], v[86:87], s[20:21] op_sel_hi:[1,0]
	v_exp_f32_e32 v84, v84
	v_exp_f32_e32 v85, v85
	v_exp_f32_e32 v86, v86
	v_exp_f32_e32 v87, v87
	v_lshl_add_u64 v[88:89], v[82:83], 0, v[120:121]
	v_pk_add_f32 v[84:85], v[84:85], 1.0 op_sel_hi:[1,0]
	v_cvt_pk_bf16_f32 v78, v78, v79
	v_pk_add_f32 v[86:87], v[86:87], 1.0 op_sel_hi:[1,0]
	v_rcp_f32_e32 v84, v84
	v_rcp_f32_e32 v85, v85
	v_rcp_f32_e32 v86, v86
	v_rcp_f32_e32 v87, v87
	v_cvt_pk_bf16_f32 v79, v80, v81
	v_lshlrev_b64 v[80:81], 11, v[88:89]
	v_lshl_add_u64 v[80:81], v[118:119], 0, v[80:81]
	global_store_dwordx2 v[80:81], v[78:79], off sc1
	s_nop 1
	v_lshl_add_u64 v[78:79], v[82:83], 0, v[122:123]
	v_pk_mul_f32 v[74:75], v[74:75], v[84:85]
	v_pk_mul_f32 v[76:77], v[76:77], v[86:87]
	v_cvt_pk_bf16_f32 v74, v74, v75
	v_cvt_pk_bf16_f32 v75, v76, v77
	v_lshlrev_b64 v[76:77], 11, v[78:79]
	v_pk_mul_f32 v[78:79], v[70:71], s[18:19] op_sel_hi:[1,0]
	v_pk_mul_f32 v[80:81], v[72:73], s[18:19] op_sel_hi:[1,0]
	v_pk_mul_f32 v[78:79], v[70:71], v[78:79]
	v_pk_mul_f32 v[80:81], v[72:73], v[80:81]
	v_pk_fma_f32 v[78:79], v[70:71], v[78:79], v[70:71]
	v_pk_fma_f32 v[80:81], v[72:73], v[80:81], v[72:73]
	v_pk_mul_f32 v[78:79], v[78:79], s[20:21] op_sel_hi:[1,0]
	v_pk_mul_f32 v[80:81], v[80:81], s[20:21] op_sel_hi:[1,0]
	v_exp_f32_e32 v78, v78
	v_exp_f32_e32 v79, v79
	v_exp_f32_e32 v80, v80
	v_exp_f32_e32 v81, v81
	v_lshl_add_u64 v[76:77], v[118:119], 0, v[76:77]
	v_pk_add_f32 v[78:79], v[78:79], 1.0 op_sel_hi:[1,0]
	global_store_dwordx2 v[76:77], v[74:75], off sc1
	s_nop 1
	v_pk_add_f32 v[80:81], v[80:81], 1.0 op_sel_hi:[1,0]
	v_rcp_f32_e32 v78, v78
	v_rcp_f32_e32 v79, v79
	v_rcp_f32_e32 v80, v80
	v_rcp_f32_e32 v81, v81
	v_lshl_add_u64 v[74:75], v[82:83], 0, v[124:125]
	v_pk_mul_f32 v[70:71], v[70:71], v[78:79]
	v_pk_mul_f32 v[76:77], v[68:69], s[18:19] op_sel_hi:[1,0]
	v_pk_mul_f32 v[72:73], v[72:73], v[80:81]
	v_cvt_pk_bf16_f32 v70, v70, v71
	v_cvt_pk_bf16_f32 v71, v72, v73
	v_lshlrev_b64 v[72:73], 11, v[74:75]
	v_pk_mul_f32 v[74:75], v[66:67], s[18:19] op_sel_hi:[1,0]
	v_pk_mul_f32 v[76:77], v[68:69], v[76:77]
	v_pk_mul_f32 v[74:75], v[66:67], v[74:75]
	v_pk_fma_f32 v[76:77], v[68:69], v[76:77], v[68:69]
	v_pk_fma_f32 v[74:75], v[66:67], v[74:75], v[66:67]
	v_pk_mul_f32 v[76:77], v[76:77], s[20:21] op_sel_hi:[1,0]
	v_pk_mul_f32 v[74:75], v[74:75], s[20:21] op_sel_hi:[1,0]
	v_exp_f32_e32 v76, v76
	v_exp_f32_e32 v74, v74
	v_exp_f32_e32 v75, v75
	v_exp_f32_e32 v77, v77
	v_lshl_add_u64 v[72:73], v[118:119], 0, v[72:73]
	global_store_dwordx2 v[72:73], v[70:71], off sc1
	s_nop 1
	v_pk_add_f32 v[74:75], v[74:75], 1.0 op_sel_hi:[1,0]
	v_pk_add_f32 v[76:77], v[76:77], 1.0 op_sel_hi:[1,0]
	v_rcp_f32_e32 v74, v74
	v_rcp_f32_e32 v75, v75
	v_rcp_f32_e32 v76, v76
	v_rcp_f32_e32 v77, v77
	v_lshl_add_u64 v[70:71], v[82:83], 0, v[126:127]
	v_pk_mul_f32 v[66:67], v[66:67], v[74:75]
	s_cmpk_gt_i32 s47, 0x7f
	v_pk_mul_f32 v[68:69], v[68:69], v[76:77]
	v_cvt_pk_bf16_f32 v66, v66, v67
	v_cvt_pk_bf16_f32 v67, v68, v69
	v_lshlrev_b64 v[68:69], 11, v[70:71]
	v_lshl_add_u64 v[68:69], v[118:119], 0, v[68:69]
	global_store_dwordx2 v[68:69], v[66:67], off sc1
	s_nop 1
	v_add_u32_e32 v68, 64, v128
	v_ashrrev_i32_e32 v66, 7, v68
	v_lshlrev_b32_e32 v72, 4, v68
	v_pk_mul_f32 v[68:69], v[62:63], s[18:19] op_sel_hi:[1,0]
	v_pk_mul_f32 v[70:71], v[64:65], s[18:19] op_sel_hi:[1,0]
	v_pk_mul_f32 v[68:69], v[62:63], v[68:69]
	v_pk_mul_f32 v[70:71], v[64:65], v[70:71]
	v_pk_fma_f32 v[68:69], v[62:63], v[68:69], v[62:63]
	v_pk_fma_f32 v[70:71], v[64:65], v[70:71], v[64:65]
	v_pk_mul_f32 v[68:69], v[68:69], s[20:21] op_sel_hi:[1,0]
	v_pk_mul_f32 v[70:71], v[70:71], s[20:21] op_sel_hi:[1,0]
	v_exp_f32_e32 v68, v68
	v_exp_f32_e32 v69, v69
	v_exp_f32_e32 v70, v70
	v_exp_f32_e32 v71, v71
	v_ashrrev_i32_e32 v67, 31, v66
	v_pk_add_f32 v[68:69], v[68:69], 1.0 op_sel_hi:[1,0]
	v_lshlrev_b64 v[66:67], 11, v[66:67]
	v_pk_add_f32 v[70:71], v[70:71], 1.0 op_sel_hi:[1,0]
	v_rcp_f32_e32 v68, v68
	v_rcp_f32_e32 v69, v69
	v_rcp_f32_e32 v70, v70
	v_rcp_f32_e32 v71, v71
	v_and_or_b32 v66, v72, s44, v66
	v_pk_mul_f32 v[62:63], v[62:63], v[68:69]
	v_pk_mul_f32 v[68:69], v[58:59], s[18:19] op_sel_hi:[1,0]
	v_pk_mul_f32 v[64:65], v[64:65], v[70:71]
	v_pk_mul_f32 v[70:71], v[60:61], s[18:19] op_sel_hi:[1,0]
	v_pk_mul_f32 v[68:69], v[58:59], v[68:69]
	v_pk_mul_f32 v[70:71], v[60:61], v[70:71]
	v_pk_fma_f32 v[68:69], v[58:59], v[68:69], v[58:59]
	v_pk_fma_f32 v[70:71], v[60:61], v[70:71], v[60:61]
	v_pk_mul_f32 v[68:69], v[68:69], s[20:21] op_sel_hi:[1,0]
	v_pk_mul_f32 v[70:71], v[70:71], s[20:21] op_sel_hi:[1,0]
	v_exp_f32_e32 v68, v68
	v_exp_f32_e32 v69, v69
	v_exp_f32_e32 v70, v70
	v_exp_f32_e32 v71, v71
	v_lshl_add_u64 v[72:73], v[66:67], 0, v[120:121]
	v_pk_add_f32 v[68:69], v[68:69], 1.0 op_sel_hi:[1,0]
	v_cvt_pk_bf16_f32 v62, v62, v63
	v_pk_add_f32 v[70:71], v[70:71], 1.0 op_sel_hi:[1,0]
	v_rcp_f32_e32 v68, v68
	v_rcp_f32_e32 v69, v69
	v_rcp_f32_e32 v70, v70
	v_rcp_f32_e32 v71, v71
	v_cvt_pk_bf16_f32 v63, v64, v65
	v_lshlrev_b64 v[64:65], 11, v[72:73]
	v_lshl_add_u64 v[64:65], v[118:119], 0, v[64:65]
	global_store_dwordx2 v[64:65], v[62:63], off sc1
	s_nop 1
	v_lshl_add_u64 v[62:63], v[66:67], 0, v[122:123]
	v_pk_mul_f32 v[58:59], v[58:59], v[68:69]
	v_pk_mul_f32 v[60:61], v[60:61], v[70:71]
	v_cvt_pk_bf16_f32 v58, v58, v59
	v_cvt_pk_bf16_f32 v59, v60, v61
	v_lshlrev_b64 v[60:61], 11, v[62:63]
	v_pk_mul_f32 v[62:63], v[54:55], s[18:19] op_sel_hi:[1,0]
	v_pk_mul_f32 v[64:65], v[56:57], s[18:19] op_sel_hi:[1,0]
	v_pk_mul_f32 v[62:63], v[54:55], v[62:63]
	v_pk_mul_f32 v[64:65], v[56:57], v[64:65]
	v_pk_fma_f32 v[62:63], v[54:55], v[62:63], v[54:55]
	v_pk_fma_f32 v[64:65], v[56:57], v[64:65], v[56:57]
	v_pk_mul_f32 v[62:63], v[62:63], s[20:21] op_sel_hi:[1,0]
	v_pk_mul_f32 v[64:65], v[64:65], s[20:21] op_sel_hi:[1,0]
	v_exp_f32_e32 v62, v62
	v_exp_f32_e32 v63, v63
	v_exp_f32_e32 v64, v64
	v_exp_f32_e32 v65, v65
	v_lshl_add_u64 v[60:61], v[118:119], 0, v[60:61]
	v_pk_add_f32 v[62:63], v[62:63], 1.0 op_sel_hi:[1,0]
	global_store_dwordx2 v[60:61], v[58:59], off sc1
	s_nop 1
	v_pk_add_f32 v[64:65], v[64:65], 1.0 op_sel_hi:[1,0]
	v_rcp_f32_e32 v62, v62
	v_rcp_f32_e32 v63, v63
	v_rcp_f32_e32 v64, v64
	v_rcp_f32_e32 v65, v65
	v_lshl_add_u64 v[58:59], v[66:67], 0, v[124:125]
	v_pk_mul_f32 v[54:55], v[54:55], v[62:63]
	v_pk_mul_f32 v[60:61], v[52:53], s[18:19] op_sel_hi:[1,0]
	v_pk_mul_f32 v[56:57], v[56:57], v[64:65]
	v_cvt_pk_bf16_f32 v54, v54, v55
	v_cvt_pk_bf16_f32 v55, v56, v57
	v_lshlrev_b64 v[56:57], 11, v[58:59]
	v_pk_mul_f32 v[58:59], v[50:51], s[18:19] op_sel_hi:[1,0]
	v_pk_mul_f32 v[60:61], v[52:53], v[60:61]
	v_pk_mul_f32 v[58:59], v[50:51], v[58:59]
	v_pk_fma_f32 v[60:61], v[52:53], v[60:61], v[52:53]
	v_pk_fma_f32 v[58:59], v[50:51], v[58:59], v[50:51]
	v_pk_mul_f32 v[60:61], v[60:61], s[20:21] op_sel_hi:[1,0]
	v_pk_mul_f32 v[58:59], v[58:59], s[20:21] op_sel_hi:[1,0]
	v_exp_f32_e32 v60, v60
	v_exp_f32_e32 v58, v58
	v_exp_f32_e32 v59, v59
	v_exp_f32_e32 v61, v61
	v_lshl_add_u64 v[56:57], v[118:119], 0, v[56:57]
	global_store_dwordx2 v[56:57], v[54:55], off sc1
	s_nop 1
	v_pk_add_f32 v[58:59], v[58:59], 1.0 op_sel_hi:[1,0]
	v_pk_add_f32 v[60:61], v[60:61], 1.0 op_sel_hi:[1,0]
	v_rcp_f32_e32 v58, v58
	v_rcp_f32_e32 v59, v59
	v_rcp_f32_e32 v60, v60
	v_rcp_f32_e32 v61, v61
	v_lshl_add_u64 v[54:55], v[66:67], 0, v[126:127]
	v_pk_mul_f32 v[50:51], v[50:51], v[58:59]
	v_pk_mul_f32 v[52:53], v[52:53], v[60:61]
	v_cvt_pk_bf16_f32 v50, v50, v51
	v_cvt_pk_bf16_f32 v51, v52, v53
	v_lshlrev_b64 v[52:53], 11, v[54:55]
	v_lshl_add_u64 v[52:53], v[118:119], 0, v[52:53]
	global_store_dwordx2 v[52:53], v[50:51], off sc1
	s_nop 1
	v_add_u32_e32 v52, 0x50, v128
	v_ashrrev_i32_e32 v50, 7, v52
	v_lshlrev_b32_e32 v56, 4, v52
	v_pk_mul_f32 v[52:53], v[46:47], s[18:19] op_sel_hi:[1,0]
	v_pk_mul_f32 v[54:55], v[48:49], s[18:19] op_sel_hi:[1,0]
	v_pk_mul_f32 v[52:53], v[46:47], v[52:53]
	v_pk_mul_f32 v[54:55], v[48:49], v[54:55]
	v_pk_fma_f32 v[52:53], v[46:47], v[52:53], v[46:47]
	v_pk_fma_f32 v[54:55], v[48:49], v[54:55], v[48:49]
	v_pk_mul_f32 v[52:53], v[52:53], s[20:21] op_sel_hi:[1,0]
	v_pk_mul_f32 v[54:55], v[54:55], s[20:21] op_sel_hi:[1,0]
	v_exp_f32_e32 v52, v52
	v_exp_f32_e32 v53, v53
	v_exp_f32_e32 v54, v54
	v_exp_f32_e32 v55, v55
	v_ashrrev_i32_e32 v51, 31, v50
	v_pk_add_f32 v[52:53], v[52:53], 1.0 op_sel_hi:[1,0]
	v_lshlrev_b64 v[50:51], 11, v[50:51]
	v_pk_add_f32 v[54:55], v[54:55], 1.0 op_sel_hi:[1,0]
	v_rcp_f32_e32 v52, v52
	v_rcp_f32_e32 v53, v53
	v_rcp_f32_e32 v54, v54
	v_rcp_f32_e32 v55, v55
	v_and_or_b32 v50, v56, s44, v50
	v_pk_mul_f32 v[46:47], v[46:47], v[52:53]
	v_pk_mul_f32 v[52:53], v[42:43], s[18:19] op_sel_hi:[1,0]
	v_pk_mul_f32 v[48:49], v[48:49], v[54:55]
	v_pk_mul_f32 v[54:55], v[44:45], s[18:19] op_sel_hi:[1,0]
	v_pk_mul_f32 v[52:53], v[42:43], v[52:53]
	v_pk_mul_f32 v[54:55], v[44:45], v[54:55]
	v_pk_fma_f32 v[52:53], v[42:43], v[52:53], v[42:43]
	v_pk_fma_f32 v[54:55], v[44:45], v[54:55], v[44:45]
	v_pk_mul_f32 v[52:53], v[52:53], s[20:21] op_sel_hi:[1,0]
	v_pk_mul_f32 v[54:55], v[54:55], s[20:21] op_sel_hi:[1,0]
	v_exp_f32_e32 v52, v52
	v_exp_f32_e32 v53, v53
	v_exp_f32_e32 v54, v54
	v_exp_f32_e32 v55, v55
	v_lshl_add_u64 v[56:57], v[50:51], 0, v[120:121]
	v_pk_add_f32 v[52:53], v[52:53], 1.0 op_sel_hi:[1,0]
	v_cvt_pk_bf16_f32 v46, v46, v47
	v_pk_add_f32 v[54:55], v[54:55], 1.0 op_sel_hi:[1,0]
	v_rcp_f32_e32 v52, v52
	v_rcp_f32_e32 v53, v53
	v_rcp_f32_e32 v54, v54
	v_rcp_f32_e32 v55, v55
	v_cvt_pk_bf16_f32 v47, v48, v49
	v_lshlrev_b64 v[48:49], 11, v[56:57]
	v_lshl_add_u64 v[48:49], v[118:119], 0, v[48:49]
	global_store_dwordx2 v[48:49], v[46:47], off sc1
	s_nop 1
	v_lshl_add_u64 v[46:47], v[50:51], 0, v[122:123]
	v_pk_mul_f32 v[42:43], v[42:43], v[52:53]
	v_pk_mul_f32 v[44:45], v[44:45], v[54:55]
	v_cvt_pk_bf16_f32 v42, v42, v43
	v_cvt_pk_bf16_f32 v43, v44, v45
	v_lshlrev_b64 v[44:45], 11, v[46:47]
	v_pk_mul_f32 v[46:47], v[38:39], s[18:19] op_sel_hi:[1,0]
	v_pk_mul_f32 v[48:49], v[40:41], s[18:19] op_sel_hi:[1,0]
	v_pk_mul_f32 v[46:47], v[38:39], v[46:47]
	v_pk_mul_f32 v[48:49], v[40:41], v[48:49]
	v_pk_fma_f32 v[46:47], v[38:39], v[46:47], v[38:39]
	v_pk_fma_f32 v[48:49], v[40:41], v[48:49], v[40:41]
	v_pk_mul_f32 v[46:47], v[46:47], s[20:21] op_sel_hi:[1,0]
	v_pk_mul_f32 v[48:49], v[48:49], s[20:21] op_sel_hi:[1,0]
	v_exp_f32_e32 v46, v46
	v_exp_f32_e32 v47, v47
	v_exp_f32_e32 v48, v48
	v_exp_f32_e32 v49, v49
	v_lshl_add_u64 v[44:45], v[118:119], 0, v[44:45]
	v_pk_add_f32 v[46:47], v[46:47], 1.0 op_sel_hi:[1,0]
	global_store_dwordx2 v[44:45], v[42:43], off sc1
	s_nop 1
	v_pk_add_f32 v[48:49], v[48:49], 1.0 op_sel_hi:[1,0]
	v_rcp_f32_e32 v46, v46
	v_rcp_f32_e32 v47, v47
	v_rcp_f32_e32 v48, v48
	v_rcp_f32_e32 v49, v49
	v_lshl_add_u64 v[42:43], v[50:51], 0, v[124:125]
	v_pk_mul_f32 v[38:39], v[38:39], v[46:47]
	v_pk_mul_f32 v[44:45], v[36:37], s[18:19] op_sel_hi:[1,0]
	v_pk_mul_f32 v[40:41], v[40:41], v[48:49]
	v_cvt_pk_bf16_f32 v38, v38, v39
	v_cvt_pk_bf16_f32 v39, v40, v41
	v_lshlrev_b64 v[40:41], 11, v[42:43]
	v_pk_mul_f32 v[42:43], v[34:35], s[18:19] op_sel_hi:[1,0]
	v_pk_mul_f32 v[44:45], v[36:37], v[44:45]
	v_pk_mul_f32 v[42:43], v[34:35], v[42:43]
	v_pk_fma_f32 v[44:45], v[36:37], v[44:45], v[36:37]
	v_pk_fma_f32 v[42:43], v[34:35], v[42:43], v[34:35]
	v_pk_mul_f32 v[44:45], v[44:45], s[20:21] op_sel_hi:[1,0]
	v_pk_mul_f32 v[42:43], v[42:43], s[20:21] op_sel_hi:[1,0]
	v_exp_f32_e32 v44, v44
	v_exp_f32_e32 v42, v42
	v_exp_f32_e32 v43, v43
	v_exp_f32_e32 v45, v45
	v_lshl_add_u64 v[40:41], v[118:119], 0, v[40:41]
	global_store_dwordx2 v[40:41], v[38:39], off sc1
	s_nop 1
	v_pk_add_f32 v[42:43], v[42:43], 1.0 op_sel_hi:[1,0]
	v_pk_add_f32 v[44:45], v[44:45], 1.0 op_sel_hi:[1,0]
	v_rcp_f32_e32 v42, v42
	v_rcp_f32_e32 v43, v43
	v_rcp_f32_e32 v44, v44
	v_rcp_f32_e32 v45, v45
	v_lshl_add_u64 v[38:39], v[50:51], 0, v[126:127]
	v_pk_mul_f32 v[34:35], v[34:35], v[42:43]
	v_pk_mul_f32 v[36:37], v[36:37], v[44:45]
	v_cvt_pk_bf16_f32 v34, v34, v35
	v_cvt_pk_bf16_f32 v35, v36, v37
	v_lshlrev_b64 v[36:37], 11, v[38:39]
	v_lshl_add_u64 v[36:37], v[118:119], 0, v[36:37]
	global_store_dwordx2 v[36:37], v[34:35], off sc1
	s_nop 1
	v_add_u32_e32 v36, 0x60, v128
	v_ashrrev_i32_e32 v34, 7, v36
	v_lshlrev_b32_e32 v40, 4, v36
	v_pk_mul_f32 v[36:37], v[30:31], s[18:19] op_sel_hi:[1,0]
	v_pk_mul_f32 v[38:39], v[32:33], s[18:19] op_sel_hi:[1,0]
	v_pk_mul_f32 v[36:37], v[30:31], v[36:37]
	v_pk_mul_f32 v[38:39], v[32:33], v[38:39]
	v_pk_fma_f32 v[36:37], v[30:31], v[36:37], v[30:31]
	v_pk_fma_f32 v[38:39], v[32:33], v[38:39], v[32:33]
	v_pk_mul_f32 v[36:37], v[36:37], s[20:21] op_sel_hi:[1,0]
	v_pk_mul_f32 v[38:39], v[38:39], s[20:21] op_sel_hi:[1,0]
	v_exp_f32_e32 v36, v36
	v_exp_f32_e32 v37, v37
	v_exp_f32_e32 v38, v38
	v_exp_f32_e32 v39, v39
	v_ashrrev_i32_e32 v35, 31, v34
	v_pk_add_f32 v[36:37], v[36:37], 1.0 op_sel_hi:[1,0]
	v_lshlrev_b64 v[34:35], 11, v[34:35]
	v_pk_add_f32 v[38:39], v[38:39], 1.0 op_sel_hi:[1,0]
	v_rcp_f32_e32 v36, v36
	v_rcp_f32_e32 v37, v37
	v_rcp_f32_e32 v38, v38
	v_rcp_f32_e32 v39, v39
	v_and_or_b32 v34, v40, s44, v34
	v_pk_mul_f32 v[30:31], v[30:31], v[36:37]
	v_pk_mul_f32 v[36:37], v[26:27], s[18:19] op_sel_hi:[1,0]
	v_pk_mul_f32 v[32:33], v[32:33], v[38:39]
	v_pk_mul_f32 v[38:39], v[28:29], s[18:19] op_sel_hi:[1,0]
	v_pk_mul_f32 v[36:37], v[26:27], v[36:37]
	v_pk_mul_f32 v[38:39], v[28:29], v[38:39]
	v_pk_fma_f32 v[36:37], v[26:27], v[36:37], v[26:27]
	v_pk_fma_f32 v[38:39], v[28:29], v[38:39], v[28:29]
	v_pk_mul_f32 v[36:37], v[36:37], s[20:21] op_sel_hi:[1,0]
	v_pk_mul_f32 v[38:39], v[38:39], s[20:21] op_sel_hi:[1,0]
	v_exp_f32_e32 v36, v36
	v_exp_f32_e32 v37, v37
	v_exp_f32_e32 v38, v38
	v_exp_f32_e32 v39, v39
	v_lshl_add_u64 v[40:41], v[34:35], 0, v[120:121]
	v_pk_add_f32 v[36:37], v[36:37], 1.0 op_sel_hi:[1,0]
	v_cvt_pk_bf16_f32 v30, v30, v31
	v_pk_add_f32 v[38:39], v[38:39], 1.0 op_sel_hi:[1,0]
	v_rcp_f32_e32 v36, v36
	v_rcp_f32_e32 v37, v37
	v_rcp_f32_e32 v38, v38
	v_rcp_f32_e32 v39, v39
	v_cvt_pk_bf16_f32 v31, v32, v33
	v_lshlrev_b64 v[32:33], 11, v[40:41]
	v_lshl_add_u64 v[32:33], v[118:119], 0, v[32:33]
	global_store_dwordx2 v[32:33], v[30:31], off sc1
	s_nop 1
	v_lshl_add_u64 v[30:31], v[34:35], 0, v[122:123]
	v_pk_mul_f32 v[26:27], v[26:27], v[36:37]
	v_pk_mul_f32 v[28:29], v[28:29], v[38:39]
	v_cvt_pk_bf16_f32 v26, v26, v27
	v_cvt_pk_bf16_f32 v27, v28, v29
	v_lshlrev_b64 v[28:29], 11, v[30:31]
	v_pk_mul_f32 v[30:31], v[22:23], s[18:19] op_sel_hi:[1,0]
	v_pk_mul_f32 v[32:33], v[24:25], s[18:19] op_sel_hi:[1,0]
	v_pk_mul_f32 v[30:31], v[22:23], v[30:31]
	v_pk_mul_f32 v[32:33], v[24:25], v[32:33]
	v_pk_fma_f32 v[30:31], v[22:23], v[30:31], v[22:23]
	v_pk_fma_f32 v[32:33], v[24:25], v[32:33], v[24:25]
	v_pk_mul_f32 v[30:31], v[30:31], s[20:21] op_sel_hi:[1,0]
	v_pk_mul_f32 v[32:33], v[32:33], s[20:21] op_sel_hi:[1,0]
	v_exp_f32_e32 v30, v30
	v_exp_f32_e32 v31, v31
	v_exp_f32_e32 v32, v32
	v_exp_f32_e32 v33, v33
	v_lshl_add_u64 v[28:29], v[118:119], 0, v[28:29]
	v_pk_add_f32 v[30:31], v[30:31], 1.0 op_sel_hi:[1,0]
	global_store_dwordx2 v[28:29], v[26:27], off sc1
	s_nop 1
	v_pk_add_f32 v[32:33], v[32:33], 1.0 op_sel_hi:[1,0]
	v_rcp_f32_e32 v30, v30
	v_rcp_f32_e32 v31, v31
	v_rcp_f32_e32 v32, v32
	v_rcp_f32_e32 v33, v33
	v_lshl_add_u64 v[26:27], v[34:35], 0, v[124:125]
	v_pk_mul_f32 v[22:23], v[22:23], v[30:31]
	v_pk_mul_f32 v[28:29], v[20:21], s[18:19] op_sel_hi:[1,0]
	v_pk_mul_f32 v[24:25], v[24:25], v[32:33]
	v_cvt_pk_bf16_f32 v22, v22, v23
	v_cvt_pk_bf16_f32 v23, v24, v25
	v_lshlrev_b64 v[24:25], 11, v[26:27]
	v_pk_mul_f32 v[26:27], v[18:19], s[18:19] op_sel_hi:[1,0]
	v_pk_mul_f32 v[28:29], v[20:21], v[28:29]
	v_pk_mul_f32 v[26:27], v[18:19], v[26:27]
	v_pk_fma_f32 v[28:29], v[20:21], v[28:29], v[20:21]
	v_pk_fma_f32 v[26:27], v[18:19], v[26:27], v[18:19]
	v_pk_mul_f32 v[28:29], v[28:29], s[20:21] op_sel_hi:[1,0]
	v_pk_mul_f32 v[26:27], v[26:27], s[20:21] op_sel_hi:[1,0]
	v_exp_f32_e32 v28, v28
	v_exp_f32_e32 v26, v26
	v_exp_f32_e32 v27, v27
	v_exp_f32_e32 v29, v29
	v_lshl_add_u64 v[24:25], v[118:119], 0, v[24:25]
	global_store_dwordx2 v[24:25], v[22:23], off sc1
	s_nop 1
	v_pk_add_f32 v[26:27], v[26:27], 1.0 op_sel_hi:[1,0]
	v_pk_add_f32 v[28:29], v[28:29], 1.0 op_sel_hi:[1,0]
	v_rcp_f32_e32 v26, v26
	v_rcp_f32_e32 v27, v27
	v_rcp_f32_e32 v28, v28
	v_rcp_f32_e32 v29, v29
	v_lshl_add_u64 v[22:23], v[34:35], 0, v[126:127]
	v_pk_mul_f32 v[18:19], v[18:19], v[26:27]
	v_pk_mul_f32 v[20:21], v[20:21], v[28:29]
	v_cvt_pk_bf16_f32 v18, v18, v19
	v_cvt_pk_bf16_f32 v19, v20, v21
	v_lshlrev_b64 v[20:21], 11, v[22:23]
	v_lshl_add_u64 v[20:21], v[118:119], 0, v[20:21]
	global_store_dwordx2 v[20:21], v[18:19], off sc1
	s_nop 1
	v_add_u32_e32 v20, 0x70, v128
	v_ashrrev_i32_e32 v18, 7, v20
	v_lshlrev_b32_e32 v24, 4, v20
	v_pk_mul_f32 v[20:21], v[14:15], s[18:19] op_sel_hi:[1,0]
	v_pk_mul_f32 v[22:23], v[16:17], s[18:19] op_sel_hi:[1,0]
	v_pk_mul_f32 v[20:21], v[14:15], v[20:21]
	v_pk_mul_f32 v[22:23], v[16:17], v[22:23]
	v_pk_fma_f32 v[20:21], v[14:15], v[20:21], v[14:15]
	v_pk_fma_f32 v[22:23], v[16:17], v[22:23], v[16:17]
	v_pk_mul_f32 v[20:21], v[20:21], s[20:21] op_sel_hi:[1,0]
	v_pk_mul_f32 v[22:23], v[22:23], s[20:21] op_sel_hi:[1,0]
	v_exp_f32_e32 v20, v20
	v_exp_f32_e32 v21, v21
	v_exp_f32_e32 v22, v22
	v_exp_f32_e32 v23, v23
	v_ashrrev_i32_e32 v19, 31, v18
	v_pk_add_f32 v[20:21], v[20:21], 1.0 op_sel_hi:[1,0]
	v_lshlrev_b64 v[18:19], 11, v[18:19]
	v_pk_add_f32 v[22:23], v[22:23], 1.0 op_sel_hi:[1,0]
	v_rcp_f32_e32 v20, v20
	v_rcp_f32_e32 v21, v21
	v_rcp_f32_e32 v22, v22
	v_rcp_f32_e32 v23, v23
	v_and_or_b32 v18, v24, s44, v18
	v_pk_mul_f32 v[14:15], v[14:15], v[20:21]
	v_pk_mul_f32 v[20:21], v[10:11], s[18:19] op_sel_hi:[1,0]
	v_pk_mul_f32 v[16:17], v[16:17], v[22:23]
	v_pk_mul_f32 v[22:23], v[12:13], s[18:19] op_sel_hi:[1,0]
	v_pk_mul_f32 v[20:21], v[10:11], v[20:21]
	v_pk_mul_f32 v[22:23], v[12:13], v[22:23]
	v_pk_fma_f32 v[20:21], v[10:11], v[20:21], v[10:11]
	v_pk_fma_f32 v[22:23], v[12:13], v[22:23], v[12:13]
	v_pk_mul_f32 v[20:21], v[20:21], s[20:21] op_sel_hi:[1,0]
	v_pk_mul_f32 v[22:23], v[22:23], s[20:21] op_sel_hi:[1,0]
	v_exp_f32_e32 v20, v20
	v_exp_f32_e32 v21, v21
	v_exp_f32_e32 v22, v22
	v_exp_f32_e32 v23, v23
	v_lshl_add_u64 v[24:25], v[18:19], 0, v[120:121]
	v_pk_add_f32 v[20:21], v[20:21], 1.0 op_sel_hi:[1,0]
	v_cvt_pk_bf16_f32 v14, v14, v15
	v_pk_add_f32 v[22:23], v[22:23], 1.0 op_sel_hi:[1,0]
	v_rcp_f32_e32 v20, v20
	v_rcp_f32_e32 v21, v21
	v_rcp_f32_e32 v22, v22
	v_rcp_f32_e32 v23, v23
	v_cvt_pk_bf16_f32 v15, v16, v17
	v_lshlrev_b64 v[16:17], 11, v[24:25]
	v_lshl_add_u64 v[16:17], v[118:119], 0, v[16:17]
	global_store_dwordx2 v[16:17], v[14:15], off sc1
	s_nop 1
	v_lshl_add_u64 v[14:15], v[18:19], 0, v[122:123]
	v_pk_mul_f32 v[10:11], v[10:11], v[20:21]
	v_pk_mul_f32 v[12:13], v[12:13], v[22:23]
	v_cvt_pk_bf16_f32 v10, v10, v11
	v_cvt_pk_bf16_f32 v11, v12, v13
	v_lshlrev_b64 v[12:13], 11, v[14:15]
	v_pk_mul_f32 v[14:15], v[6:7], s[18:19] op_sel_hi:[1,0]
	v_pk_mul_f32 v[16:17], v[8:9], s[18:19] op_sel_hi:[1,0]
	v_pk_mul_f32 v[14:15], v[6:7], v[14:15]
	v_pk_mul_f32 v[16:17], v[8:9], v[16:17]
	v_pk_fma_f32 v[14:15], v[6:7], v[14:15], v[6:7]
	v_pk_fma_f32 v[16:17], v[8:9], v[16:17], v[8:9]
	v_pk_mul_f32 v[14:15], v[14:15], s[20:21] op_sel_hi:[1,0]
	v_pk_mul_f32 v[16:17], v[16:17], s[20:21] op_sel_hi:[1,0]
	v_exp_f32_e32 v14, v14
	v_exp_f32_e32 v15, v15
	v_exp_f32_e32 v16, v16
	v_exp_f32_e32 v17, v17
	v_lshl_add_u64 v[12:13], v[118:119], 0, v[12:13]
	v_pk_add_f32 v[14:15], v[14:15], 1.0 op_sel_hi:[1,0]
	global_store_dwordx2 v[12:13], v[10:11], off sc1
	s_nop 1
	v_pk_add_f32 v[16:17], v[16:17], 1.0 op_sel_hi:[1,0]
	v_rcp_f32_e32 v14, v14
	v_rcp_f32_e32 v15, v15
	v_rcp_f32_e32 v16, v16
	v_rcp_f32_e32 v17, v17
	v_lshl_add_u64 v[10:11], v[18:19], 0, v[124:125]
	v_pk_mul_f32 v[6:7], v[6:7], v[14:15]
	v_pk_mul_f32 v[12:13], v[4:5], s[18:19] op_sel_hi:[1,0]
	v_pk_mul_f32 v[8:9], v[8:9], v[16:17]
	v_cvt_pk_bf16_f32 v6, v6, v7
	v_cvt_pk_bf16_f32 v7, v8, v9
	v_lshlrev_b64 v[8:9], 11, v[10:11]
	v_pk_mul_f32 v[10:11], v[2:3], s[18:19] op_sel_hi:[1,0]
	v_pk_mul_f32 v[12:13], v[4:5], v[12:13]
	v_pk_mul_f32 v[10:11], v[2:3], v[10:11]
	v_pk_fma_f32 v[12:13], v[4:5], v[12:13], v[4:5]
	v_pk_fma_f32 v[10:11], v[2:3], v[10:11], v[2:3]
	v_pk_mul_f32 v[12:13], v[12:13], s[20:21] op_sel_hi:[1,0]
	v_pk_mul_f32 v[10:11], v[10:11], s[20:21] op_sel_hi:[1,0]
	v_exp_f32_e32 v12, v12
	v_exp_f32_e32 v10, v10
	v_exp_f32_e32 v11, v11
	v_exp_f32_e32 v13, v13
	v_lshl_add_u64 v[8:9], v[118:119], 0, v[8:9]
	global_store_dwordx2 v[8:9], v[6:7], off sc1
	s_nop 1
	v_pk_add_f32 v[10:11], v[10:11], 1.0 op_sel_hi:[1,0]
	v_pk_add_f32 v[12:13], v[12:13], 1.0 op_sel_hi:[1,0]
	v_rcp_f32_e32 v10, v10
	v_rcp_f32_e32 v11, v11
	v_rcp_f32_e32 v12, v12
	v_rcp_f32_e32 v13, v13
	v_lshl_add_u64 v[6:7], v[18:19], 0, v[126:127]
	v_pk_mul_f32 v[2:3], v[2:3], v[10:11]
	v_pk_mul_f32 v[4:5], v[4:5], v[12:13]
	v_cvt_pk_bf16_f32 v2, v2, v3
	v_cvt_pk_bf16_f32 v3, v4, v5
	v_lshlrev_b64 v[4:5], 11, v[6:7]
	v_lshl_add_u64 v[4:5], v[118:119], 0, v[4:5]
	global_store_dwordx2 v[4:5], v[2:3], off sc1
	s_nop 1
	s_barrier
	s_cbranch_scc0 .LBB0_874

.LBB0_947:
	s_or_b64 exec, exec, s[0:1]
	s_add_u32 s0, s70, 0x9038000
	s_addc_u32 s1, s71, 0
	s_ashr_i32 s22, s96, 2
	s_and_b32 s2, s22, 0xfffff8
	s_and_b32 s23, s96, 7
	s_bfe_u32 s8, s96, 0x20003
	s_or_b32 s2, s2, s23
	s_lshl_b32 s6, s8, 8
	s_lshl_b32 s4, s8, 9
	s_add_u32 s4, s70, s4
	s_addc_u32 s5, s71, 0
	s_add_u32 s24, s4, 0x20168000
	v_readfirstlane_b32 s4, v0
	s_addc_u32 s25, s5, 0
	s_lshr_b32 s10, s4, 6
	s_lshl_b32 s9, s2, 8
	s_lshl_b32 s2, s10, 1
	s_waitcnt vmcnt(23)
	v_lshlrev_b32_e32 v2, 4, v164
	v_or_b32_e32 v5, s2, v1
	s_and_b32 s5, s10, 4
	v_and_b32_e32 v146, 0x70, v2
	v_or_b32_e32 v2, s9, v147
	s_waitcnt vmcnt(7)
	v_and_or_b32 v6, v5, 3, s5
	s_lshr_b32 s5, s4, 1
	s_lshl_b32 s7, s10, 10
	s_barrier
	s_waitcnt vmcnt(4)
	v_lshl_or_b32 v18, v2, 11, v146
	s_and_b32 s16, s5, 0x7fffff80
	s_add_i32 s7, s7, 0
	s_mov_b32 s5, m0
	s_mov_b32 m0, s7
	s_nop 0
	global_load_lds_dwordx4 v18, s[0:1]
	s_mov_b32 m0, s5
	s_add_i32 s5, s7, 0x2000
	v_or_b32_e32 v2, 0x20000, v18
	s_mov_b32 s18, m0
	s_mov_b32 m0, s5
	s_nop 0
	global_load_lds_dwordx4 v2, s[0:1]
	s_mov_b32 m0, s18
	s_add_i32 s5, s7, 0x4000
	s_mov_b32 s3, 0
	v_or_b32_e32 v3, 0x40000, v18
	v_or_b32_e32 v4, 0x60000, v18
	s_bfe_u32 s17, s4, 0x20006
	s_mov_b32 s18, m0
	s_mov_b32 m0, s5
	s_nop 0
	global_load_lds_dwordx4 v3, s[0:1]
	s_mov_b32 m0, s18
	s_add_i32 s5, s7, 0x6000
	s_mov_b32 s18, m0
	s_mov_b32 m0, s5
	s_nop 0
	global_load_lds_dwordx4 v4, s[0:1]
	s_mov_b32 m0, s18
	s_lshl_b32 s11, s17, 7
	s_lshl_b64 s[18:19], s[2:3], 11
	s_add_u32 s18, s24, s18
	v_lshlrev_b32_e32 v6, 5, v6
	v_xor_b32_e32 v8, s11, v161
	v_lshlrev_b32_e32 v5, 9, v5
	s_addc_u32 s19, s25, s19
	v_lshl_or_b32 v163, v1, 11, v157
	v_or3_b32 v152, v162, v8, v160
	v_bitop3_b32 v8, s11, v161, 32 bitop3:0x36
	v_bitop3_b32 v157, v6, v5, v157 bitop3:0xde
	global_load_dwordx4 v[2:5], v163, s[18:19]
	s_add_i32 s18, s2, 16
	s_mov_b32 s19, s3
	v_or3_b32 v151, v162, v8, v160
	v_bitop3_b32 v8, s11, v161, 64 bitop3:0x36
	s_lshl_b64 s[18:19], s[18:19], 11
	v_or3_b32 v149, v162, v8, v160
	v_mov_b32_e32 v8, 0x60
	s_add_u32 s18, s24, s18
	v_or_b32_e32 v7, s16, v154
	v_bitop3_b32 v8, s11, v161, v8 bitop3:0x36
	s_addc_u32 s19, s25, s19
	v_or3_b32 v148, v162, v8, v160
	v_lshlrev_b32_e32 v34, 7, v7
	global_load_dwordx4 v[6:9], v163, s[18:19]
	s_add_i32 s18, s2, 32
	s_mov_b32 s19, s3
	s_lshl_b64 s[18:19], s[18:19], 11
	s_add_u32 s18, s24, s18
	s_addc_u32 s19, s25, s19
	global_load_dwordx4 v[10:13], v163, s[18:19]
	s_add_i32 s18, s2, 48
	s_mov_b32 s19, s3
	s_lshl_b64 s[18:19], s[18:19], 11
	s_add_u32 s18, s24, s18
	s_addc_u32 s19, s25, s19
	s_add_i32 s5, s7, 0x8000
	v_or_b32_e32 v19, 0x80, v18
	global_load_dwordx4 v[14:17], v163, s[18:19]
	s_mov_b32 s19, m0
	s_mov_b32 m0, s5
	s_nop 0
	global_load_lds_dwordx4 v19, s[0:1]
	s_mov_b32 m0, s19
	v_or_b32_e32 v19, 0x20080, v18
	s_add_i32 s5, s7, 0xa000
	s_mov_b32 s19, m0
	s_mov_b32 m0, s5
	s_nop 0
	global_load_lds_dwordx4 v19, s[0:1]
	s_mov_b32 m0, s19
	v_or_b32_e32 v19, 0x40080, v18
	s_add_i32 s5, s7, 0xc000
	v_or_b32_e32 v18, 0x60080, v18
	s_add_i32 s20, s2, 64
	s_mov_b32 s21, s3
	s_mov_b32 s19, m0
	s_mov_b32 m0, s5
	s_nop 0
	global_load_lds_dwordx4 v19, s[0:1]
	s_mov_b32 m0, s19
	s_add_i32 s5, s7, 0xe000
	s_mov_b32 s19, m0
	s_mov_b32 m0, s5
	s_nop 0
	global_load_lds_dwordx4 v18, s[0:1]
	s_mov_b32 m0, s19
	s_waitcnt vmcnt(2)
	s_waitcnt vmcnt(4)
	s_lshl_b64 s[20:21], s[20:21], 11
	v_add_u32_e32 v18, 0, v157
	s_add_u32 s20, s24, s20
	v_or_b32_e32 v150, v34, v159
	v_add_u32_e32 v159, 0x18000, v18
	s_addc_u32 s21, s25, s21
	ds_write_b128 v159, v[2:5]
	ds_write_b128 v159, v[6:9] offset:8192
	ds_write_b128 v159, v[10:13] offset:16384
	ds_write_b128 v159, v[14:17] offset:24576
	global_load_dwordx4 v[14:17], v163, s[20:21]
	s_add_i32 s20, s2, 0x50
	s_mov_b32 s21, s3
	s_lshl_b64 s[20:21], s[20:21], 11
	s_add_u32 s20, s24, s20
	s_addc_u32 s21, s25, s21
	global_load_dwordx4 v[10:13], v163, s[20:21]
	s_add_i32 s20, s2, 0x60
	s_mov_b32 s21, s3
	s_lshl_b64 s[20:21], s[20:21], 11
	s_add_u32 s20, s24, s20
	s_addc_u32 s21, s25, s21
	s_addk_i32 s2, 0x70
	global_load_dwordx4 v[6:9], v163, s[20:21]
	s_lshl_b64 s[20:21], s[2:3], 11
	s_add_u32 s20, s24, s20
	s_addc_u32 s21, s25, s21
	s_lshl_b64 s[4:5], s[4:5], 6
	s_and_b32 s5, s5, 63
	s_and_b32 s2, s4, 0xfffff000
	s_add_u32 s2, s24, s2
	s_addc_u32 s19, s25, s5
	s_lshl_b32 s4, s22, 19
	s_and_b32 s4, s4, 0xffc00000
	s_lshl_b32 s5, s23, 19
	global_load_dwordx4 v[2:5], v163, s[20:21]
	s_or_b32 s20, s4, s5
	v_lshlrev_b32_e32 v18, 11, v147
	s_waitcnt lgkmcnt(0)
	s_barrier
	v_or_b32_e32 v147, s20, v18
	v_or_b32_e32 v18, s4, v18
	v_or_b32_e32 v153, v34, v156
	v_or_b32_e32 v156, s5, v18
	v_mov_b32_e32 v18, 0
	s_mov_b32 s18, 0x8000
	s_mov_b32 s20, 0x10000
	s_mov_b64 s[4:5], 0
	v_mov_b32_e32 v19, v18
	v_mov_b32_e32 v20, v18
	v_mov_b32_e32 v21, v18
	v_mov_b32_e32 v30, v18
	v_mov_b32_e32 v31, v18
	v_mov_b32_e32 v32, v18
	v_mov_b32_e32 v33, v18
	v_mov_b32_e32 v22, v18
	v_mov_b32_e32 v23, v18
	v_mov_b32_e32 v24, v18
	v_mov_b32_e32 v25, v18
	v_mov_b32_e32 v26, v18
	v_mov_b32_e32 v27, v18
	v_mov_b32_e32 v28, v18
	v_mov_b32_e32 v29, v18
	v_mov_b32_e32 v34, v18
	v_mov_b32_e32 v35, v18
	v_mov_b32_e32 v36, v18
	v_mov_b32_e32 v37, v18
	s_waitcnt vmcnt(1)
	v_mov_b32_e32 v38, v18
	v_mov_b32_e32 v39, v18
	v_mov_b32_e32 v40, v18
	v_mov_b32_e32 v41, v18
	s_waitcnt vmcnt(0)
	v_mov_b32_e32 v42, v18
	v_mov_b32_e32 v43, v18
	v_mov_b32_e32 v44, v18
	v_mov_b32_e32 v45, v18
	v_mov_b32_e32 v50, v18
	v_mov_b32_e32 v51, v18
	v_mov_b32_e32 v52, v18
	v_mov_b32_e32 v53, v18
	v_mov_b32_e32 v66, v18
	v_mov_b32_e32 v67, v18
	v_mov_b32_e32 v68, v18
	v_mov_b32_e32 v69, v18
	v_mov_b32_e32 v78, v18
	v_mov_b32_e32 v79, v18
	v_mov_b32_e32 v80, v18
	v_mov_b32_e32 v81, v18
	v_mov_b32_e32 v90, v18
	v_mov_b32_e32 v91, v18
	v_mov_b32_e32 v92, v18
	v_mov_b32_e32 v93, v18
	v_mov_b32_e32 v94, v18
	v_mov_b32_e32 v95, v18
	v_mov_b32_e32 v96, v18
	v_mov_b32_e32 v97, v18
	v_mov_b32_e32 v118, v18
	v_mov_b32_e32 v119, v18
	v_mov_b32_e32 v120, v18
	v_mov_b32_e32 v121, v18
	v_mov_b32_e32 v126, v18
	v_mov_b32_e32 v127, v18
	v_mov_b32_e32 v128, v18
	v_mov_b32_e32 v129, v18
	v_mov_b32_e32 v138, v18
	v_mov_b32_e32 v139, v18
	v_mov_b32_e32 v140, v18
	v_mov_b32_e32 v141, v18
	v_mov_b32_e32 v142, v18
	v_mov_b32_e32 v143, v18
	v_mov_b32_e32 v144, v18
	v_mov_b32_e32 v145, v18
	v_mov_b32_e32 v114, v18
	v_mov_b32_e32 v115, v18
	v_mov_b32_e32 v116, v18
	v_mov_b32_e32 v117, v18
	v_mov_b32_e32 v122, v18
	v_mov_b32_e32 v123, v18
	v_mov_b32_e32 v124, v18
	v_mov_b32_e32 v125, v18
	v_mov_b32_e32 v134, v18
	v_mov_b32_e32 v135, v18
	v_mov_b32_e32 v136, v18
	v_mov_b32_e32 v137, v18
	v_mov_b32_e32 v130, v18
	v_mov_b32_e32 v131, v18
	v_mov_b32_e32 v132, v18
	v_mov_b32_e32 v133, v18
	v_mov_b32_e32 v98, v18
	v_mov_b32_e32 v99, v18
	v_mov_b32_e32 v100, v18
	v_mov_b32_e32 v101, v18
	v_mov_b32_e32 v102, v18
	v_mov_b32_e32 v103, v18
	v_mov_b32_e32 v104, v18
	v_mov_b32_e32 v105, v18
	v_mov_b32_e32 v110, v18
	v_mov_b32_e32 v111, v18
	v_mov_b32_e32 v112, v18
	v_mov_b32_e32 v113, v18
	v_mov_b32_e32 v106, v18
	v_mov_b32_e32 v107, v18
	v_mov_b32_e32 v108, v18
	v_mov_b32_e32 v109, v18
	v_mov_b32_e32 v70, v18
	v_mov_b32_e32 v71, v18
	v_mov_b32_e32 v72, v18
	v_mov_b32_e32 v73, v18
	v_mov_b32_e32 v82, v18
	v_mov_b32_e32 v83, v18
	v_mov_b32_e32 v84, v18
	v_mov_b32_e32 v85, v18
	v_mov_b32_e32 v86, v18
	v_mov_b32_e32 v87, v18
	v_mov_b32_e32 v88, v18
	v_mov_b32_e32 v89, v18
	v_mov_b32_e32 v74, v18
	v_mov_b32_e32 v75, v18
	v_mov_b32_e32 v76, v18
	v_mov_b32_e32 v77, v18
	v_mov_b32_e32 v46, v18
	v_mov_b32_e32 v47, v18
	v_mov_b32_e32 v48, v18
	v_mov_b32_e32 v49, v18
	v_mov_b32_e32 v58, v18
	v_mov_b32_e32 v59, v18
	v_mov_b32_e32 v60, v18
	v_mov_b32_e32 v61, v18
	v_mov_b32_e32 v62, v18
	v_mov_b32_e32 v63, v18
	v_mov_b32_e32 v64, v18
	v_mov_b32_e32 v65, v18
	v_mov_b32_e32 v54, v18
	v_mov_b32_e32 v55, v18
	v_mov_b32_e32 v56, v18
	v_mov_b32_e32 v57, v18
	s_cmp_lt_u32 s80, 4
	s_cbranch_scc1 .Lprio_yg
	s_setprio 1
.Lprio_yg:
.LBB0_948:
	s_add_i32 s22, s18, 0xffff8000
	s_and_b32 s22, s22, 0x8000
	s_add_i32 s22, s22, 0
	s_add_i32 s21, s3, 0
	s_add_i32 s22, s22, 0x18000
	v_add_u32_e32 v160, s22, v152
	v_add_u32_e32 v162, s21, v150
	v_add_u32_e32 v168, s22, v149
	v_add_u32_e32 v161, s22, v151
	ds_read_b64_tr_b16 v[164:165], v160
	ds_read_b64_tr_b16 v[166:167], v160 offset:2048
	ds_read_b64_tr_b16 v[172:173], v161
	ds_read_b64_tr_b16 v[174:175], v161 offset:2048
	ds_read_b128 v[176:179], v162
	ds_read_b128 v[180:183], v162 offset:2048
	ds_read_b64_tr_b16 v[184:185], v168
	ds_read_b64_tr_b16 v[186:187], v168 offset:2048
	v_add_u32_e32 v169, s22, v148
	ds_read_b64_tr_b16 v[188:189], v169
	ds_read_b64_tr_b16 v[190:191], v169 offset:2048
	ds_read_b128 v[192:195], v162 offset:4096
	s_waitcnt lgkmcnt(6)
	v_mfma_f32_16x16x32_bf16 v[18:21], v[164:167], v[176:179], v[18:21]
	v_add_u32_e32 v171, v146, v156
	v_add_u32_e32 v196, 0x100, v171
	s_add_i32 s22, s7, s20
	v_mfma_f32_16x16x32_bf16 v[30:33], v[172:175], v[176:179], v[30:33]
	s_mov_b32 s23, m0
	s_mov_b32 m0, s22
	s_nop 0
	global_load_lds_dwordx4 v196, s[0:1]
	s_mov_b32 m0, s23
	s_waitcnt lgkmcnt(3)
	v_mfma_f32_16x16x32_bf16 v[22:25], v[184:187], v[176:179], v[22:25]
	s_waitcnt lgkmcnt(1)
	v_mfma_f32_16x16x32_bf16 v[26:29], v[188:191], v[176:179], v[26:29]
	v_mfma_f32_16x16x32_bf16 v[34:37], v[164:167], v[180:183], v[34:37]
	ds_read_b128 v[176:179], v162 offset:6144
	v_add_u32_e32 v196, v146, v147
	v_add_u32_e32 v197, 0x20100, v196
	v_mfma_f32_16x16x32_bf16 v[38:41], v[172:175], v[180:183], v[38:41]
	s_add_i32 s23, s22, 0x2000
	s_mov_b32 s24, m0
	s_mov_b32 m0, s23
	s_nop 0
	global_load_lds_dwordx4 v197, s[0:1]
	s_mov_b32 m0, s24
	v_mfma_f32_16x16x32_bf16 v[42:45], v[184:187], v[180:183], v[42:45]
	v_mfma_f32_16x16x32_bf16 v[50:53], v[188:191], v[180:183], v[50:53]
	s_waitcnt lgkmcnt(1)
	v_mfma_f32_16x16x32_bf16 v[66:69], v[164:167], v[192:195], v[66:69]
	ds_read_b128 v[180:183], v162 offset:8192
	v_add_u32_e32 v171, 0x40100, v171
	s_add_i32 s23, s22, 0x4000
	v_mfma_f32_16x16x32_bf16 v[78:81], v[172:175], v[192:195], v[78:81]
	s_mov_b32 s24, m0
	s_mov_b32 m0, s23
	s_nop 0
	global_load_lds_dwordx4 v171, s[0:1]
	s_mov_b32 m0, s24
	v_mfma_f32_16x16x32_bf16 v[90:93], v[184:187], v[192:195], v[90:93]
	v_mfma_f32_16x16x32_bf16 v[94:97], v[188:191], v[192:195], v[94:97]
	s_waitcnt lgkmcnt(1)
	v_mfma_f32_16x16x32_bf16 v[118:121], v[164:167], v[176:179], v[118:121]
	ds_read_b128 v[192:195], v162 offset:10240
	v_add_u32_e32 v171, 0x60100, v196
	s_addk_i32 s22, 0x6000
	v_mfma_f32_16x16x32_bf16 v[126:129], v[172:175], v[176:179], v[126:129]
	s_mov_b32 s23, m0
	s_mov_b32 m0, s22
	s_nop 0
	global_load_lds_dwordx4 v171, s[0:1]
	s_mov_b32 m0, s23
	v_mfma_f32_16x16x32_bf16 v[138:141], v[184:187], v[176:179], v[138:141]
	v_mfma_f32_16x16x32_bf16 v[142:145], v[188:191], v[176:179], v[142:145]
	ds_read_b128 v[176:179], v162 offset:12288
	ds_read_b64_tr_b16 v[196:197], v160 offset:16384
	ds_read_b64_tr_b16 v[198:199], v160 offset:18432
	s_waitcnt lgkmcnt(4)
	v_mfma_f32_16x16x32_bf16 v[114:117], v[164:167], v[180:183], v[114:117]
	v_mfma_f32_16x16x32_bf16 v[122:125], v[172:175], v[180:183], v[122:125]
	v_mfma_f32_16x16x32_bf16 v[134:137], v[184:187], v[180:183], v[134:137]
	v_mfma_f32_16x16x32_bf16 v[130:133], v[188:191], v[180:183], v[130:133]
	ds_read_b128 v[180:183], v162 offset:14336
	ds_read_b64_tr_b16 v[200:201], v161 offset:16384
	ds_read_b64_tr_b16 v[202:203], v161 offset:18432
	s_waitcnt lgkmcnt(6)
	v_mfma_f32_16x16x32_bf16 v[98:101], v[164:167], v[192:195], v[98:101]
	v_mfma_f32_16x16x32_bf16 v[102:105], v[172:175], v[192:195], v[102:105]
	v_mfma_f32_16x16x32_bf16 v[110:113], v[184:187], v[192:195], v[110:113]
	v_mfma_f32_16x16x32_bf16 v[106:109], v[188:191], v[192:195], v[106:109]
	v_add_u32_e32 v160, s21, v153
	ds_read_b128 v[192:195], v160
	ds_read_b64_tr_b16 v[204:205], v168 offset:16384
	ds_read_b64_tr_b16 v[206:207], v168 offset:18432
	s_waitcnt lgkmcnt(8)
	v_mfma_f32_16x16x32_bf16 v[70:73], v[164:167], v[176:179], v[70:73]
	v_mfma_f32_16x16x32_bf16 v[82:85], v[172:175], v[176:179], v[82:85]
	v_mfma_f32_16x16x32_bf16 v[86:89], v[184:187], v[176:179], v[86:89]
	v_mfma_f32_16x16x32_bf16 v[74:77], v[188:191], v[176:179], v[74:77]
	s_waitcnt lgkmcnt(5)
	v_mfma_f32_16x16x32_bf16 v[46:49], v[164:167], v[180:183], v[46:49]
	ds_read_b128 v[164:167], v160 offset:2048
	s_and_b32 s21, s18, 0x8000
	v_mfma_f32_16x16x32_bf16 v[58:61], v[172:175], v[180:183], v[58:61]
	ds_read_b64_tr_b16 v[172:173], v169 offset:16384
	ds_read_b64_tr_b16 v[174:175], v169 offset:18432
	v_mfma_f32_16x16x32_bf16 v[62:65], v[184:187], v[180:183], v[62:65]
	v_mfma_f32_16x16x32_bf16 v[54:57], v[188:191], v[180:183], v[54:57]
	s_waitcnt lgkmcnt(5)
	v_mfma_f32_16x16x32_bf16 v[18:21], v[196:199], v[192:195], v[18:21]
	ds_read_b128 v[176:179], v160 offset:4096
	v_add_u32_e32 v161, s21, v159
	s_add_u32 s21, s2, s4
	v_mfma_f32_16x16x32_bf16 v[30:33], v[200:203], v[192:195], v[30:33]
	s_addc_u32 s24, s19, s5
	s_waitcnt vmcnt(7)
	s_add_u32 s22, s21, 0x40000
	s_waitcnt lgkmcnt(4)
	v_mfma_f32_16x16x32_bf16 v[22:25], v[204:207], v[192:195], v[22:25]
	ds_write_b128 v161, v[14:17]
	s_addc_u32 s23, s24, 0
	global_load_dwordx4 v[14:17], v163, s[22:23]
	s_waitcnt lgkmcnt(2)
	v_mfma_f32_16x16x32_bf16 v[26:29], v[172:175], v[192:195], v[26:29]
	v_mfma_f32_16x16x32_bf16 v[34:37], v[196:199], v[164:167], v[34:37]
	ds_read_b128 v[180:183], v160 offset:6144
	s_waitcnt vmcnt(7)
	s_add_u32 s22, s21, 0x48000
	v_mfma_f32_16x16x32_bf16 v[38:41], v[200:203], v[164:167], v[38:41]
	ds_write_b128 v161, v[10:13] offset:8192
	s_addc_u32 s23, s24, 0
	global_load_dwordx4 v[10:13], v163, s[22:23]
	v_mfma_f32_16x16x32_bf16 v[42:45], v[204:207], v[164:167], v[42:45]
	v_mfma_f32_16x16x32_bf16 v[50:53], v[172:175], v[164:167], v[50:53]
	s_waitcnt lgkmcnt(3)
	v_mfma_f32_16x16x32_bf16 v[66:69], v[196:199], v[176:179], v[66:69]
	ds_read_b128 v[164:167], v160 offset:8192
	s_waitcnt vmcnt(7)
	s_add_u32 s22, s21, 0x50000
	v_mfma_f32_16x16x32_bf16 v[78:81], v[200:203], v[176:179], v[78:81]
	ds_write_b128 v161, v[6:9] offset:16384
	s_addc_u32 s23, s24, 0
	global_load_dwordx4 v[6:9], v163, s[22:23]
	v_mfma_f32_16x16x32_bf16 v[90:93], v[204:207], v[176:179], v[90:93]
	v_mfma_f32_16x16x32_bf16 v[94:97], v[172:175], v[176:179], v[94:97]
	s_waitcnt lgkmcnt(3)
	v_mfma_f32_16x16x32_bf16 v[118:121], v[196:199], v[180:183], v[118:121]
	ds_read_b128 v[176:179], v160 offset:10240
	s_waitcnt vmcnt(7)
	s_add_u32 s22, s21, 0x58000
	v_mfma_f32_16x16x32_bf16 v[126:129], v[200:203], v[180:183], v[126:129]
	ds_write_b128 v161, v[2:5] offset:24576
	s_addc_u32 s23, s24, 0
	global_load_dwordx4 v[2:5], v163, s[22:23]
	v_mfma_f32_16x16x32_bf16 v[138:141], v[204:207], v[180:183], v[138:141]
	v_mfma_f32_16x16x32_bf16 v[142:145], v[172:175], v[180:183], v[142:145]
	s_waitcnt lgkmcnt(3)
	v_mfma_f32_16x16x32_bf16 v[114:117], v[196:199], v[164:167], v[114:117]
	ds_read_b128 v[180:183], v160 offset:12288
	v_mfma_f32_16x16x32_bf16 v[122:125], v[200:203], v[164:167], v[122:125]
	v_mfma_f32_16x16x32_bf16 v[134:137], v[204:207], v[164:167], v[134:137]
	v_mfma_f32_16x16x32_bf16 v[130:133], v[172:175], v[164:167], v[130:133]
	s_waitcnt lgkmcnt(2)
	v_mfma_f32_16x16x32_bf16 v[98:101], v[196:199], v[176:179], v[98:101]
	ds_read_b128 v[164:167], v160 offset:14336
	v_mfma_f32_16x16x32_bf16 v[102:105], v[200:203], v[176:179], v[102:105]
	v_mfma_f32_16x16x32_bf16 v[110:113], v[204:207], v[176:179], v[110:113]
	v_mfma_f32_16x16x32_bf16 v[106:109], v[172:175], v[176:179], v[106:109]
	s_waitcnt lgkmcnt(1)
	v_mfma_f32_16x16x32_bf16 v[70:73], v[196:199], v[180:183], v[70:73]
	v_mfma_f32_16x16x32_bf16 v[82:85], v[200:203], v[180:183], v[82:85]
	v_mfma_f32_16x16x32_bf16 v[86:89], v[204:207], v[180:183], v[86:89]
	v_mfma_f32_16x16x32_bf16 v[74:77], v[172:175], v[180:183], v[74:77]
	s_waitcnt lgkmcnt(0)
	v_mfma_f32_16x16x32_bf16 v[46:49], v[196:199], v[164:167], v[46:49]
	v_mfma_f32_16x16x32_bf16 v[58:61], v[200:203], v[164:167], v[58:61]
	v_mfma_f32_16x16x32_bf16 v[62:65], v[204:207], v[164:167], v[62:65]
	v_mfma_f32_16x16x32_bf16 v[54:57], v[172:175], v[164:167], v[54:57]
	s_add_i32 s21, s3, 0x8000
	s_cmp_lg_u32 s3, 0x10000
	s_cselect_b32 s3, s21, 0
	s_add_i32 s21, s20, 0x8000
	s_cmp_lg_u32 s20, 0x10000
	s_waitcnt lgkmcnt(0)
	s_barrier
	s_cselect_b32 s20, s21, 0
	s_add_u32 s4, s4, 0x20000
	s_addc_u32 s5, s5, 0
	s_add_i32 s18, s18, 0x8000
	v_add_u32_e32 v147, 0x80, v147
	s_cmp_lg_u32 s4, 0x1c0000
	v_add_u32_e32 v156, 0x80, v156
	s_cbranch_scc1 .LBB0_948
	s_setprio 0
	s_add_u32 s4, s70, 0xc038000
	s_addc_u32 s5, s71, 0
	s_add_u32 s2, s70, 0xa038000
	s_addc_u32 s3, s71, 0
	s_add_i32 s7, 0, 0x18000
	s_add_i32 s18, 0, 0x10000
	v_add_u32_e32 v168, s7, v152
	v_add_u32_e32 v171, s18, v150
	v_add_u32_e32 v202, s7, v149
	v_add_u32_e32 v204, s7, v148
	v_add_u32_e32 v169, s7, v151
	ds_read_b64_tr_b16 v[160:161], v168
	ds_read_b64_tr_b16 v[162:163], v168 offset:2048
	ds_read_b64_tr_b16 v[164:165], v169
	ds_read_b64_tr_b16 v[166:167], v169 offset:2048
	ds_read_b128 v[172:175], v171
	ds_read_b64_tr_b16 v[176:177], v202
	ds_read_b64_tr_b16 v[178:179], v202 offset:2048
	ds_read_b128 v[180:183], v171 offset:2048
	ds_read_b64_tr_b16 v[184:185], v204
	ds_read_b64_tr_b16 v[186:187], v204 offset:2048
	ds_read_b128 v[188:191], v171 offset:4096
	v_and_b32_e32 v156, 31, v0
	v_lshlrev_b32_e32 v159, 3, v156
	s_mov_b32 s7, 0
	v_mov_b32_e32 v147, 0
	v_cmp_eq_u32_e32 vcc, 0, v156
	s_waitcnt lgkmcnt(6)
	v_mfma_f32_16x16x32_bf16 v[18:21], v[160:163], v[172:175], v[18:21]
	v_lshlrev_b32_e32 v146, 4, v156
	v_mfma_f32_16x16x32_bf16 v[30:33], v[164:167], v[172:175], v[30:33]
	s_waitcnt lgkmcnt(4)
	v_mfma_f32_16x16x32_bf16 v[22:25], v[176:179], v[172:175], v[22:25]
	s_waitcnt lgkmcnt(1)
	v_mfma_f32_16x16x32_bf16 v[26:29], v[184:187], v[172:175], v[26:29]
	ds_read_b128 v[172:175], v171 offset:6144
	v_mfma_f32_16x16x32_bf16 v[34:37], v[160:163], v[180:183], v[34:37]
	v_mfma_f32_16x16x32_bf16 v[38:41], v[164:167], v[180:183], v[38:41]
	v_mfma_f32_16x16x32_bf16 v[42:45], v[176:179], v[180:183], v[42:45]
	v_mfma_f32_16x16x32_bf16 v[50:53], v[184:187], v[180:183], v[50:53]
	ds_read_b128 v[180:183], v171 offset:8192
	s_waitcnt lgkmcnt(2)
	v_mfma_f32_16x16x32_bf16 v[66:69], v[160:163], v[188:191], v[66:69]
	v_mfma_f32_16x16x32_bf16 v[78:81], v[164:167], v[188:191], v[78:81]
	v_mfma_f32_16x16x32_bf16 v[90:93], v[176:179], v[188:191], v[90:93]
	v_mfma_f32_16x16x32_bf16 v[94:97], v[184:187], v[188:191], v[94:97]
	ds_read_b128 v[188:191], v171 offset:10240
	s_waitcnt lgkmcnt(2)
	v_mfma_f32_16x16x32_bf16 v[118:121], v[160:163], v[172:175], v[118:121]
	v_mfma_f32_16x16x32_bf16 v[126:129], v[164:167], v[172:175], v[126:129]
	v_mfma_f32_16x16x32_bf16 v[138:141], v[176:179], v[172:175], v[138:141]
	v_mfma_f32_16x16x32_bf16 v[142:145], v[184:187], v[172:175], v[142:145]
	ds_read_b128 v[172:175], v171 offset:12288
	ds_read_b64_tr_b16 v[192:193], v168 offset:16384
	ds_read_b64_tr_b16 v[194:195], v168 offset:18432
	s_waitcnt lgkmcnt(4)
	v_mfma_f32_16x16x32_bf16 v[114:117], v[160:163], v[180:183], v[114:117]
	v_mfma_f32_16x16x32_bf16 v[122:125], v[164:167], v[180:183], v[122:125]
	v_mfma_f32_16x16x32_bf16 v[134:137], v[176:179], v[180:183], v[134:137]
	v_mfma_f32_16x16x32_bf16 v[130:133], v[184:187], v[180:183], v[130:133]
	ds_read_b128 v[180:183], v171 offset:14336
	ds_read_b64_tr_b16 v[196:197], v169 offset:16384
	ds_read_b64_tr_b16 v[198:199], v169 offset:18432
	s_waitcnt lgkmcnt(6)
	v_mfma_f32_16x16x32_bf16 v[98:101], v[160:163], v[188:191], v[98:101]
	v_mfma_f32_16x16x32_bf16 v[102:105], v[164:167], v[188:191], v[102:105]
	v_mfma_f32_16x16x32_bf16 v[110:113], v[176:179], v[188:191], v[110:113]
	v_mfma_f32_16x16x32_bf16 v[106:109], v[184:187], v[188:191], v[106:109]
	v_add_u32_e32 v156, s18, v153
	ds_read_b128 v[188:191], v156
	ds_read_b64_tr_b16 v[200:201], v202 offset:16384
	ds_read_b64_tr_b16 v[202:203], v202 offset:18432
	s_waitcnt lgkmcnt(8)
	v_mfma_f32_16x16x32_bf16 v[70:73], v[160:163], v[172:175], v[70:73]
	v_mfma_f32_16x16x32_bf16 v[82:85], v[164:167], v[172:175], v[82:85]
	v_mfma_f32_16x16x32_bf16 v[86:89], v[176:179], v[172:175], v[86:89]
	v_mfma_f32_16x16x32_bf16 v[74:77], v[184:187], v[172:175], v[74:77]
	s_waitcnt lgkmcnt(5)
	v_mfma_f32_16x16x32_bf16 v[46:49], v[160:163], v[180:183], v[46:49]
	v_mfma_f32_16x16x32_bf16 v[58:61], v[164:167], v[180:183], v[58:61]
	ds_read_b128 v[160:163], v156 offset:2048
	ds_read_b64_tr_b16 v[164:165], v204 offset:16384
	ds_read_b64_tr_b16 v[166:167], v204 offset:18432
	v_mfma_f32_16x16x32_bf16 v[62:65], v[176:179], v[180:183], v[62:65]
	v_mfma_f32_16x16x32_bf16 v[54:57], v[184:187], v[180:183], v[54:57]
	ds_read_b128 v[172:175], v156 offset:4096
	s_add_i32 s18, 0, 0x20000
	s_waitcnt vmcnt(3)
	v_add_u32_e32 v157, s18, v157
	s_waitcnt lgkmcnt(6)
	v_mfma_f32_16x16x32_bf16 v[18:21], v[192:195], v[188:191], v[18:21]
	ds_write_b128 v157, v[14:17]
	v_mfma_f32_16x16x32_bf16 v[30:33], v[196:199], v[188:191], v[30:33]
	s_waitcnt lgkmcnt(5)
	v_mfma_f32_16x16x32_bf16 v[22:25], v[200:203], v[188:191], v[22:25]
	s_waitcnt lgkmcnt(2)
	v_mfma_f32_16x16x32_bf16 v[14:17], v[164:167], v[188:191], v[26:29]
	v_mfma_f32_16x16x32_bf16 v[26:29], v[192:195], v[160:163], v[34:37]
	v_mfma_f32_16x16x32_bf16 v[34:37], v[196:199], v[160:163], v[38:41]
	v_mfma_f32_16x16x32_bf16 v[38:41], v[200:203], v[160:163], v[42:45]
	s_nop 2
	ds_read_b128 v[42:45], v156 offset:6144
	s_waitcnt vmcnt(2)
	ds_write_b128 v157, v[10:13] offset:8192
	v_mfma_f32_16x16x32_bf16 v[10:13], v[164:167], v[160:163], v[50:53]
	s_waitcnt lgkmcnt(3)
	v_mfma_f32_16x16x32_bf16 v[50:53], v[192:195], v[172:175], v[66:69]
	v_mfma_f32_16x16x32_bf16 v[66:69], v[196:199], v[172:175], v[78:81]
	v_mfma_f32_16x16x32_bf16 v[78:81], v[200:203], v[172:175], v[90:93]
	s_nop 2
	ds_read_b128 v[90:93], v156 offset:8192
	s_waitcnt vmcnt(1)
	ds_write_b128 v157, v[6:9] offset:16384
	v_mfma_f32_16x16x32_bf16 v[6:9], v[164:167], v[172:175], v[94:97]
	s_waitcnt lgkmcnt(3)
	v_mfma_f32_16x16x32_bf16 v[94:97], v[192:195], v[42:45], v[118:121]
	v_mfma_f32_16x16x32_bf16 v[118:121], v[196:199], v[42:45], v[126:129]
	v_mfma_f32_16x16x32_bf16 v[126:129], v[200:203], v[42:45], v[138:141]
	s_nop 2
	ds_read_b128 v[138:141], v156 offset:10240
	s_waitcnt vmcnt(0)
	ds_write_b128 v157, v[2:5] offset:24576
	v_mfma_f32_16x16x32_bf16 v[2:5], v[164:167], v[42:45], v[142:145]
	s_waitcnt lgkmcnt(3)
	v_mfma_f32_16x16x32_bf16 v[42:45], v[192:195], v[90:93], v[114:117]
	v_mfma_f32_16x16x32_bf16 v[114:117], v[196:199], v[90:93], v[122:125]
	v_mfma_f32_16x16x32_bf16 v[122:125], v[200:203], v[90:93], v[134:137]
	s_nop 2
	ds_read_b128 v[134:137], v156 offset:12288
	v_mfma_f32_16x16x32_bf16 v[90:93], v[164:167], v[90:93], v[130:133]
	s_nop 2
	ds_read_b128 v[130:133], v156 offset:14336
	s_waitcnt lgkmcnt(3)
	v_mfma_f32_16x16x32_bf16 v[98:101], v[192:195], v[138:141], v[98:101]
	v_mfma_f32_16x16x32_bf16 v[102:105], v[196:199], v[138:141], v[102:105]
	v_mfma_f32_16x16x32_bf16 v[110:113], v[200:203], v[138:141], v[110:113]
	v_mfma_f32_16x16x32_bf16 v[106:109], v[164:167], v[138:141], v[106:109]
	s_waitcnt lgkmcnt(1)
	v_mfma_f32_16x16x32_bf16 v[70:73], v[192:195], v[134:137], v[70:73]
	v_mfma_f32_16x16x32_bf16 v[82:85], v[196:199], v[134:137], v[82:85]
	v_mfma_f32_16x16x32_bf16 v[86:89], v[200:203], v[134:137], v[86:89]
	v_mfma_f32_16x16x32_bf16 v[74:77], v[164:167], v[134:137], v[74:77]
	s_waitcnt lgkmcnt(0)
	v_mfma_f32_16x16x32_bf16 v[46:49], v[192:195], v[130:133], v[46:49]
	v_mfma_f32_16x16x32_bf16 v[58:61], v[196:199], v[130:133], v[58:61]
	v_mfma_f32_16x16x32_bf16 v[62:65], v[200:203], v[130:133], v[62:65]
	v_mfma_f32_16x16x32_bf16 v[54:57], v[164:167], v[130:133], v[54:57]
	s_waitcnt lgkmcnt(0)
	s_barrier
	v_add_u32_e32 v152, s18, v152
	v_add_u32_e32 v157, 0, v150
	v_add_u32_e32 v168, s18, v149
	v_add_u32_e32 v169, s18, v148
	v_add_u32_e32 v156, s18, v151
	ds_read_b64_tr_b16 v[130:131], v152
	ds_read_b64_tr_b16 v[132:133], v152 offset:2048
	ds_read_b64_tr_b16 v[134:135], v156
	ds_read_b64_tr_b16 v[136:137], v156 offset:2048
	ds_read_b128 v[138:141], v157
	ds_read_b128 v[142:145], v157 offset:2048
	ds_read_b64_tr_b16 v[160:161], v168
	ds_read_b64_tr_b16 v[162:163], v168 offset:2048
	ds_read_b64_tr_b16 v[148:149], v169
	ds_read_b64_tr_b16 v[150:151], v169 offset:2048
	ds_read_b128 v[164:167], v157 offset:4096
	s_waitcnt lgkmcnt(6)
	v_mfma_f32_16x16x32_bf16 v[18:21], v[130:133], v[138:141], v[18:21]
	v_mfma_f32_16x16x32_bf16 v[30:33], v[134:137], v[138:141], v[30:33]
	s_waitcnt lgkmcnt(3)
	v_mfma_f32_16x16x32_bf16 v[22:25], v[160:163], v[138:141], v[22:25]
	s_waitcnt lgkmcnt(1)
	v_mfma_f32_16x16x32_bf16 v[14:17], v[148:151], v[138:141], v[14:17]
	ds_read_b128 v[138:141], v157 offset:6144
	v_mfma_f32_16x16x32_bf16 v[10:13], v[148:151], v[142:145], v[10:13]
	v_mfma_f32_16x16x32_bf16 v[26:29], v[130:133], v[142:145], v[26:29]
	v_mfma_f32_16x16x32_bf16 v[34:37], v[134:137], v[142:145], v[34:37]
	v_mfma_f32_16x16x32_bf16 v[38:41], v[160:163], v[142:145], v[38:41]
	ds_read_b128 v[142:145], v157 offset:8192
	s_waitcnt lgkmcnt(2)
	v_mfma_f32_16x16x32_bf16 v[6:9], v[148:151], v[164:167], v[6:9]
	v_mfma_f32_16x16x32_bf16 v[50:53], v[130:133], v[164:167], v[50:53]
	v_mfma_f32_16x16x32_bf16 v[66:69], v[134:137], v[164:167], v[66:69]
	v_mfma_f32_16x16x32_bf16 v[78:81], v[160:163], v[164:167], v[78:81]
	s_waitcnt lgkmcnt(1)
	v_mfma_f32_16x16x32_bf16 v[164:167], v[134:137], v[138:141], v[118:121]
	s_nop 2
	ds_read_b128 v[118:121], v157 offset:10240
	v_mfma_f32_16x16x32_bf16 v[2:5], v[148:151], v[138:141], v[2:5]
	v_mfma_f32_16x16x32_bf16 v[94:97], v[130:133], v[138:141], v[94:97]
	v_mfma_f32_16x16x32_bf16 v[172:175], v[160:163], v[138:141], v[126:129]
	s_waitcnt lgkmcnt(1)
	v_mfma_f32_16x16x32_bf16 v[138:141], v[134:137], v[142:145], v[114:117]
	s_nop 2
	ds_read_b128 v[114:117], v157 offset:12288
	ds_read_b64_tr_b16 v[180:181], v152 offset:16384
	ds_read_b64_tr_b16 v[182:183], v152 offset:18432
	v_mfma_f32_16x16x32_bf16 v[42:45], v[130:133], v[142:145], v[42:45]
	v_mfma_f32_16x16x32_bf16 v[176:179], v[160:163], v[142:145], v[122:125]
	v_mfma_f32_16x16x32_bf16 v[142:145], v[148:151], v[142:145], v[90:93]
	s_nop 2
	ds_read_b128 v[90:93], v157 offset:14336
	ds_read_b64_tr_b16 v[196:197], v156 offset:16384
	ds_read_b64_tr_b16 v[198:199], v156 offset:18432
	s_waitcnt lgkmcnt(6)
	v_mfma_f32_16x16x32_bf16 v[184:187], v[130:133], v[118:121], v[98:101]
	v_mfma_f32_16x16x32_bf16 v[188:191], v[134:137], v[118:121], v[102:105]
	v_mfma_f32_16x16x32_bf16 v[192:195], v[160:163], v[118:121], v[110:113]
	v_mfma_f32_16x16x32_bf16 v[200:203], v[148:151], v[118:121], v[106:109]
	v_add_u32_e32 v152, 0, v153
	s_waitcnt lgkmcnt(5)
	v_mfma_f32_16x16x32_bf16 v[204:207], v[130:133], v[114:117], v[70:73]
	s_nop 2
	ds_read_b128 v[70:73], v152
	ds_read_b64_tr_b16 v[216:217], v168 offset:16384
	ds_read_b64_tr_b16 v[218:219], v168 offset:18432
	v_mfma_f32_16x16x32_bf16 v[208:211], v[134:137], v[114:117], v[82:85]
	v_mfma_f32_16x16x32_bf16 v[212:215], v[160:163], v[114:117], v[86:89]
	v_mfma_f32_16x16x32_bf16 v[220:223], v[148:151], v[114:117], v[74:77]
	s_waitcnt lgkmcnt(5)
	v_mfma_f32_16x16x32_bf16 v[224:227], v[130:133], v[90:93], v[46:49]
	s_nop 2
	ds_read_b128 v[46:49], v152 offset:2048
	ds_read_b64_tr_b16 v[232:233], v169 offset:16384
	ds_read_b64_tr_b16 v[234:235], v169 offset:18432
	v_mfma_f32_16x16x32_bf16 v[228:231], v[134:137], v[90:93], v[58:61]
	v_mfma_f32_16x16x32_bf16 v[160:163], v[160:163], v[90:93], v[62:65]
	v_mfma_f32_16x16x32_bf16 v[148:151], v[148:151], v[90:93], v[54:57]
	s_waitcnt lgkmcnt(5)
	v_mfma_f32_16x16x32_bf16 v[236:239], v[180:183], v[70:73], v[18:21]
	s_nop 2
	ds_read_b128 v[18:21], v152 offset:4096
	v_mfma_f32_16x16x32_bf16 v[240:243], v[196:199], v[70:73], v[30:33]
	s_waitcnt lgkmcnt(4)
	v_mfma_f32_16x16x32_bf16 v[134:137], v[216:219], v[70:73], v[22:25]
	s_waitcnt lgkmcnt(1)
	v_mfma_f32_16x16x32_bf16 v[130:133], v[232:235], v[70:73], v[14:17]
	s_nop 2
	ds_read_b128 v[14:17], v152 offset:6144
	v_mfma_f32_16x16x32_bf16 v[126:129], v[180:183], v[46:49], v[26:29]
	v_mfma_f32_16x16x32_bf16 v[122:125], v[196:199], v[46:49], v[34:37]
	v_mfma_f32_16x16x32_bf16 v[118:121], v[216:219], v[46:49], v[38:41]
	v_mfma_f32_16x16x32_bf16 v[114:117], v[232:235], v[46:49], v[10:13]
	s_nop 2
	ds_read_b128 v[10:13], v152 offset:8192
	s_waitcnt lgkmcnt(2)
	v_mfma_f32_16x16x32_bf16 v[110:113], v[180:183], v[18:21], v[50:53]
	v_mfma_f32_16x16x32_bf16 v[106:109], v[196:199], v[18:21], v[66:69]
	v_mfma_f32_16x16x32_bf16 v[102:105], v[216:219], v[18:21], v[78:81]
	v_mfma_f32_16x16x32_bf16 v[98:101], v[232:235], v[18:21], v[6:9]
	s_nop 2
	ds_read_b128 v[6:9], v152 offset:10240
	s_waitcnt lgkmcnt(2)
	v_mfma_f32_16x16x32_bf16 v[94:97], v[180:183], v[14:17], v[94:97]
	v_mfma_f32_16x16x32_bf16 v[90:93], v[196:199], v[14:17], v[164:167]
	v_mfma_f32_16x16x32_bf16 v[86:89], v[216:219], v[14:17], v[172:175]
	v_mfma_f32_16x16x32_bf16 v[82:85], v[232:235], v[14:17], v[2:5]
	s_nop 2
	ds_read_b128 v[2:5], v152 offset:12288
	s_waitcnt lgkmcnt(2)
	v_mfma_f32_16x16x32_bf16 v[78:81], v[180:183], v[10:13], v[42:45]
	v_mfma_f32_16x16x32_bf16 v[74:77], v[196:199], v[10:13], v[138:141]
	v_mfma_f32_16x16x32_bf16 v[70:73], v[216:219], v[10:13], v[176:179]
	v_mfma_f32_16x16x32_bf16 v[66:69], v[232:235], v[10:13], v[142:145]
	ds_read_b128 v[14:17], v152 offset:14336
	s_waitcnt lgkmcnt(2)
	v_mfma_f32_16x16x32_bf16 v[62:65], v[180:183], v[6:9], v[184:187]
	v_mfma_f32_16x16x32_bf16 v[58:61], v[196:199], v[6:9], v[188:191]
	v_mfma_f32_16x16x32_bf16 v[54:57], v[216:219], v[6:9], v[192:195]
	v_mfma_f32_16x16x32_bf16 v[50:53], v[232:235], v[6:9], v[200:203]
	s_waitcnt lgkmcnt(1)
	v_mfma_f32_16x16x32_bf16 v[46:49], v[180:183], v[2:5], v[204:207]
	v_mfma_f32_16x16x32_bf16 v[42:45], v[196:199], v[2:5], v[208:211]
	v_mfma_f32_16x16x32_bf16 v[38:41], v[216:219], v[2:5], v[212:215]
	v_mfma_f32_16x16x32_bf16 v[34:37], v[232:235], v[2:5], v[220:223]
	s_waitcnt lgkmcnt(0)
	v_mfma_f32_16x16x32_bf16 v[10:13], v[216:219], v[14:17], v[160:163]
	v_mfma_f32_16x16x32_bf16 v[2:5], v[232:235], v[14:17], v[148:151]
	v_mfma_f32_16x16x32_bf16 v[26:29], v[180:183], v[14:17], v[224:227]
	v_mfma_f32_16x16x32_bf16 v[18:21], v[196:199], v[14:17], v[228:231]
	s_lshl_b32 s17, s17, 6
	s_or_b32 s17, s17, s6
	s_waitcnt lgkmcnt(0)
	s_barrier
	s_add_i32 s11, s11, 0
	v_lshl_add_u32 v6, v155, 2, s17
	s_add_i32 s17, s16, s9
	v_add_u32_e32 v138, s17, v154
	v_ashrrev_i32_e32 v139, 31, v138
	v_ashrrev_i32_e32 v7, 31, v6
	v_lshlrev_b64 v[8:9], 11, v[138:139]
	v_lshl_add_u64 v[8:9], s[0:1], 0, v[8:9]
	v_lshlrev_b64 v[140:141], 1, v[6:7]
	v_lshl_add_u64 v[142:143], v[8:9], 0, v[140:141]
	v_lshl_add_u64 v[6:7], v[6:7], 2, s[94:95]
	global_load_dwordx2 v[202:203], v[142:143], off
	global_load_dwordx4 v[30:33], v[6:7], off
	global_load_dwordx4 v[22:25], v[6:7], off offset:64
	global_load_dwordx4 v[14:17], v[6:7], off offset:128
	s_nop 0
	global_load_dwordx4 v[6:9], v[6:7], off offset:192
	s_nop 0
	global_load_dwordx2 v[204:205], v[142:143], off offset:32
	global_load_dwordx2 v[206:207], v[142:143], off offset:64
	global_load_dwordx2 v[200:201], v[142:143], off offset:96
	v_add_u32_e32 v142, 16, v138
	v_ashrrev_i32_e32 v143, 31, v142
	v_lshlrev_b64 v[142:143], 11, v[142:143]
	v_lshl_add_u64 v[142:143], s[0:1], 0, v[142:143]
	v_lshl_add_u64 v[142:143], v[142:143], 0, v[140:141]
	global_load_dwordx2 v[198:199], v[142:143], off
	global_load_dwordx2 v[196:197], v[142:143], off offset:32
	global_load_dwordx2 v[194:195], v[142:143], off offset:64
	global_load_dwordx2 v[192:193], v[142:143], off offset:96
	v_add_u32_e32 v142, 32, v138
	v_ashrrev_i32_e32 v143, 31, v142
	v_lshlrev_b64 v[142:143], 11, v[142:143]
	v_lshl_add_u64 v[142:143], s[0:1], 0, v[142:143]
	v_lshl_add_u64 v[142:143], v[142:143], 0, v[140:141]
	global_load_dwordx2 v[190:191], v[142:143], off
	global_load_dwordx2 v[188:189], v[142:143], off offset:32
	global_load_dwordx2 v[186:187], v[142:143], off offset:64
	global_load_dwordx2 v[184:185], v[142:143], off offset:96
	v_add_u32_e32 v142, 48, v138
	v_ashrrev_i32_e32 v143, 31, v142
	v_lshlrev_b64 v[142:143], 11, v[142:143]
	v_lshl_add_u64 v[142:143], s[0:1], 0, v[142:143]
	v_lshl_add_u64 v[142:143], v[142:143], 0, v[140:141]
	global_load_dwordx2 v[182:183], v[142:143], off
	global_load_dwordx2 v[180:181], v[142:143], off offset:32
	global_load_dwordx2 v[178:179], v[142:143], off offset:64
	global_load_dwordx2 v[176:177], v[142:143], off offset:96
	v_add_u32_e32 v142, 64, v138
	v_ashrrev_i32_e32 v143, 31, v142
	v_lshlrev_b64 v[142:143], 11, v[142:143]
	v_lshl_add_u64 v[142:143], s[0:1], 0, v[142:143]
	v_lshl_add_u64 v[142:143], v[142:143], 0, v[140:141]
	global_load_dwordx2 v[174:175], v[142:143], off
	global_load_dwordx2 v[172:173], v[142:143], off offset:32
	global_load_dwordx2 v[168:169], v[142:143], off offset:64
	global_load_dwordx2 v[166:167], v[142:143], off offset:96
	v_add_u32_e32 v142, 0x50, v138
	v_ashrrev_i32_e32 v143, 31, v142
	v_lshlrev_b64 v[142:143], 11, v[142:143]
	v_lshl_add_u64 v[142:143], s[0:1], 0, v[142:143]
	v_lshl_add_u64 v[142:143], v[142:143], 0, v[140:141]
	global_load_dwordx2 v[164:165], v[142:143], off
	global_load_dwordx2 v[162:163], v[142:143], off offset:32
	global_load_dwordx2 v[160:161], v[142:143], off offset:64
	global_load_dwordx2 v[156:157], v[142:143], off offset:96
	v_add_u32_e32 v142, 0x60, v138
	v_add_u32_e32 v138, 0x70, v138
	v_ashrrev_i32_e32 v143, 31, v142
	v_ashrrev_i32_e32 v139, 31, v138
	v_lshlrev_b64 v[142:143], 11, v[142:143]
	v_lshlrev_b64 v[138:139], 11, v[138:139]
	v_lshl_add_u64 v[142:143], s[0:1], 0, v[142:143]
	v_lshl_add_u64 v[138:139], s[0:1], 0, v[138:139]
	s_movk_i32 s1, 0x210
	s_mov_b32 s0, 0xbfb8aa3b
	v_add_u32_e32 v171, s16, v154
	v_lshlrev_b32_e32 v208, 3, v155
	v_mul_lo_u32 v171, v171, s1
	v_add3_u32 v171, s11, v208, v171
	v_lshl_add_u64 v[142:143], v[142:143], 0, v[140:141]
	v_lshl_add_u64 v[138:139], v[138:139], 0, v[140:141]
	global_load_dwordx2 v[154:155], v[142:143], off
	global_load_dwordx2 v[152:153], v[142:143], off offset:32
	global_load_dwordx2 v[150:151], v[142:143], off offset:64
	global_load_dwordx2 v[148:149], v[142:143], off offset:96
	global_load_dwordx2 v[144:145], v[138:139], off
	s_nop 0
	global_load_dwordx2 v[142:143], v[138:139], off offset:32
	global_load_dwordx2 v[140:141], v[138:139], off offset:64
	s_nop 0
	global_load_dwordx2 v[138:139], v[138:139], off offset:96
	v_lshl_or_b32 v1, s10, 5, v1
	s_lshl_b32 s6, s6, 1
	s_waitcnt vmcnt(34)
	v_pk_add_f32 v[210:211], v[238:239], v[32:33]
	v_pk_add_f32 v[212:213], v[236:237], v[30:31]
	v_pk_mul_f32 v[210:211], v[210:211], s[0:1] op_sel_hi:[1,0]
	v_pk_mul_f32 v[212:213], v[212:213], s[0:1] op_sel_hi:[1,0]
	v_exp_f32_e32 v210, v210
	v_exp_f32_e32 v212, v212
	v_exp_f32_e32 v213, v213
	v_exp_f32_e32 v211, v211
	v_lshlrev_b32_e32 v208, 16, v202
	v_and_b32_e32 v209, 0xffff0000, v202
	v_pk_add_f32 v[212:213], v[212:213], 1.0 op_sel_hi:[1,0]
	v_pk_add_f32 v[210:211], v[210:211], 1.0 op_sel_hi:[1,0]
	v_rcp_f32_e32 v212, v212
	v_rcp_f32_e32 v213, v213
	v_rcp_f32_e32 v210, v210
	v_rcp_f32_e32 v211, v211
	v_lshlrev_b32_e32 v202, 16, v203
	v_and_b32_e32 v203, 0xffff0000, v203
	v_pk_mul_f32 v[208:209], v[212:213], v[208:209]
	v_pk_mul_f32 v[202:203], v[210:211], v[202:203]
	s_waitcnt vmcnt(33)
	v_pk_add_f32 v[210:211], v[242:243], v[24:25]
	v_pk_add_f32 v[212:213], v[240:241], v[22:23]
	v_pk_mul_f32 v[210:211], v[210:211], s[0:1] op_sel_hi:[1,0]
	v_pk_mul_f32 v[212:213], v[212:213], s[0:1] op_sel_hi:[1,0]
	v_exp_f32_e32 v210, v210
	v_exp_f32_e32 v212, v212
	v_exp_f32_e32 v213, v213
	v_exp_f32_e32 v211, v211
	s_waitcnt vmcnt(32)
	v_pk_add_f32 v[134:135], v[134:135], v[14:15]
	v_pk_add_f32 v[136:137], v[136:137], v[16:17]
	v_pk_mul_f32 v[134:135], v[134:135], s[0:1] op_sel_hi:[1,0]
	v_pk_mul_f32 v[136:137], v[136:137], s[0:1] op_sel_hi:[1,0]
	v_exp_f32_e32 v134, v134
	v_exp_f32_e32 v135, v135
	v_pk_add_f32 v[212:213], v[212:213], 1.0 op_sel_hi:[1,0]
	v_pk_add_f32 v[210:211], v[210:211], 1.0 op_sel_hi:[1,0]
	v_exp_f32_e32 v136, v136
	v_exp_f32_e32 v137, v137
	s_waitcnt vmcnt(31)
	v_pk_add_f32 v[130:131], v[130:131], v[6:7]
	v_rcp_f32_e32 v212, v212
	v_rcp_f32_e32 v213, v213
	v_rcp_f32_e32 v210, v210
	v_rcp_f32_e32 v211, v211
	v_pk_add_f32 v[132:133], v[132:133], v[8:9]
	v_pk_mul_f32 v[130:131], v[130:131], s[0:1] op_sel_hi:[1,0]
	v_pk_mul_f32 v[132:133], v[132:133], s[0:1] op_sel_hi:[1,0]
	v_exp_f32_e32 v130, v130
	v_exp_f32_e32 v131, v131
	v_pk_add_f32 v[134:135], v[134:135], 1.0 op_sel_hi:[1,0]
	v_exp_f32_e32 v132, v132
	v_exp_f32_e32 v133, v133
	v_cvt_pk_bf16_f32 v208, v208, v209
	v_cvt_pk_bf16_f32 v209, v202, v203
	s_waitcnt vmcnt(30)
	v_lshlrev_b32_e32 v202, 16, v204
	v_and_b32_e32 v203, 0xffff0000, v204
	v_lshlrev_b32_e32 v204, 16, v205
	v_and_b32_e32 v205, 0xffff0000, v205
	v_rcp_f32_e32 v134, v134
	v_rcp_f32_e32 v135, v135
	v_pk_add_f32 v[136:137], v[136:137], 1.0 op_sel_hi:[1,0]
	v_pk_add_f32 v[126:127], v[126:127], v[30:31]
	v_pk_mul_f32 v[202:203], v[212:213], v[202:203]
	v_pk_mul_f32 v[204:205], v[210:211], v[204:205]
	v_rcp_f32_e32 v136, v136
	v_rcp_f32_e32 v137, v137
	v_pk_add_f32 v[128:129], v[128:129], v[32:33]
	v_pk_mul_f32 v[126:127], v[126:127], s[0:1] op_sel_hi:[1,0]
	v_cvt_pk_bf16_f32 v202, v202, v203
	v_cvt_pk_bf16_f32 v203, v204, v205
	v_pk_add_f32 v[130:131], v[130:131], 1.0 op_sel_hi:[1,0]
	v_exp_f32_e32 v126, v126
	v_exp_f32_e32 v127, v127
	v_pk_mul_f32 v[128:129], v[128:129], s[0:1] op_sel_hi:[1,0]
	ds_write2_b64 v171, v[208:209], v[202:203] offset1:4
	s_waitcnt vmcnt(29)
	v_lshlrev_b32_e32 v202, 16, v206
	v_and_b32_e32 v203, 0xffff0000, v206
	v_rcp_f32_e32 v130, v130
	v_rcp_f32_e32 v131, v131
	v_pk_add_f32 v[132:133], v[132:133], 1.0 op_sel_hi:[1,0]
	v_exp_f32_e32 v128, v128
	v_exp_f32_e32 v129, v129
	v_pk_add_f32 v[122:123], v[122:123], v[22:23]
	v_pk_mul_f32 v[134:135], v[134:135], v[202:203]
	v_lshlrev_b32_e32 v202, 16, v207
	v_and_b32_e32 v203, 0xffff0000, v207
	v_rcp_f32_e32 v132, v132
	v_rcp_f32_e32 v133, v133
	v_pk_add_f32 v[124:125], v[124:125], v[24:25]
	v_pk_mul_f32 v[122:123], v[122:123], s[0:1] op_sel_hi:[1,0]
	v_pk_mul_f32 v[136:137], v[136:137], v[202:203]
	v_exp_f32_e32 v122, v122
	v_exp_f32_e32 v123, v123
	v_pk_mul_f32 v[124:125], v[124:125], s[0:1] op_sel_hi:[1,0]
	v_cvt_pk_bf16_f32 v134, v134, v135
	v_cvt_pk_bf16_f32 v135, v136, v137
	s_waitcnt vmcnt(28)
	v_lshlrev_b32_e32 v136, 16, v200
	v_and_b32_e32 v137, 0xffff0000, v200
	v_pk_add_f32 v[126:127], v[126:127], 1.0 op_sel_hi:[1,0]
	v_exp_f32_e32 v124, v124
	v_exp_f32_e32 v125, v125
	v_pk_mul_f32 v[130:131], v[130:131], v[136:137]
	v_lshlrev_b32_e32 v136, 16, v201
	v_and_b32_e32 v137, 0xffff0000, v201
	v_rcp_f32_e32 v126, v126
	v_rcp_f32_e32 v127, v127
	v_pk_add_f32 v[128:129], v[128:129], 1.0 op_sel_hi:[1,0]
	v_pk_add_f32 v[118:119], v[118:119], v[14:15]
	v_pk_mul_f32 v[132:133], v[132:133], v[136:137]
	v_rcp_f32_e32 v128, v128
	v_rcp_f32_e32 v129, v129
	v_pk_add_f32 v[120:121], v[120:121], v[16:17]
	v_pk_mul_f32 v[118:119], v[118:119], s[0:1] op_sel_hi:[1,0]
	v_cvt_pk_bf16_f32 v130, v130, v131
	v_cvt_pk_bf16_f32 v131, v132, v133
	v_pk_add_f32 v[122:123], v[122:123], 1.0 op_sel_hi:[1,0]
	v_exp_f32_e32 v118, v118
	v_exp_f32_e32 v119, v119
	v_pk_mul_f32 v[120:121], v[120:121], s[0:1] op_sel_hi:[1,0]
	ds_write2_b64 v171, v[134:135], v[130:131] offset0:8 offset1:12
	s_waitcnt vmcnt(27)
	v_lshlrev_b32_e32 v130, 16, v198
	v_and_b32_e32 v131, 0xffff0000, v198
	v_rcp_f32_e32 v122, v122
	v_rcp_f32_e32 v123, v123
	v_pk_add_f32 v[124:125], v[124:125], 1.0 op_sel_hi:[1,0]
	v_exp_f32_e32 v120, v120
	v_exp_f32_e32 v121, v121
	v_pk_add_f32 v[114:115], v[114:115], v[6:7]
	v_pk_mul_f32 v[126:127], v[126:127], v[130:131]
	v_lshlrev_b32_e32 v130, 16, v199
	v_and_b32_e32 v131, 0xffff0000, v199
	v_rcp_f32_e32 v124, v124
	v_rcp_f32_e32 v125, v125
	v_pk_add_f32 v[116:117], v[116:117], v[8:9]
	v_pk_mul_f32 v[114:115], v[114:115], s[0:1] op_sel_hi:[1,0]
	v_pk_mul_f32 v[128:129], v[128:129], v[130:131]
	v_exp_f32_e32 v114, v114
	v_exp_f32_e32 v115, v115
	v_pk_mul_f32 v[116:117], v[116:117], s[0:1] op_sel_hi:[1,0]
	v_cvt_pk_bf16_f32 v126, v126, v127
	v_cvt_pk_bf16_f32 v127, v128, v129
	s_waitcnt vmcnt(26)
	v_lshlrev_b32_e32 v128, 16, v196
	v_and_b32_e32 v129, 0xffff0000, v196
	v_pk_add_f32 v[118:119], v[118:119], 1.0 op_sel_hi:[1,0]
	v_exp_f32_e32 v116, v116
	v_exp_f32_e32 v117, v117
	v_pk_mul_f32 v[122:123], v[122:123], v[128:129]
	v_lshlrev_b32_e32 v128, 16, v197
	v_and_b32_e32 v129, 0xffff0000, v197
	v_rcp_f32_e32 v118, v118
	v_rcp_f32_e32 v119, v119
	v_pk_add_f32 v[120:121], v[120:121], 1.0 op_sel_hi:[1,0]
	v_pk_add_f32 v[110:111], v[110:111], v[30:31]
	v_pk_mul_f32 v[124:125], v[124:125], v[128:129]
	v_rcp_f32_e32 v120, v120
	v_rcp_f32_e32 v121, v121
	v_pk_add_f32 v[112:113], v[112:113], v[32:33]
	v_pk_mul_f32 v[110:111], v[110:111], s[0:1] op_sel_hi:[1,0]
	v_cvt_pk_bf16_f32 v122, v122, v123
	v_cvt_pk_bf16_f32 v123, v124, v125
	v_add_u32_e32 v124, 0x2000, v171
	v_pk_add_f32 v[114:115], v[114:115], 1.0 op_sel_hi:[1,0]
	v_exp_f32_e32 v110, v110
	v_exp_f32_e32 v111, v111
	v_pk_mul_f32 v[112:113], v[112:113], s[0:1] op_sel_hi:[1,0]
	ds_write2_b64 v124, v[126:127], v[122:123] offset0:32 offset1:36
	s_waitcnt vmcnt(25)
	v_lshlrev_b32_e32 v122, 16, v194
	v_and_b32_e32 v123, 0xffff0000, v194
	v_rcp_f32_e32 v114, v114
	v_rcp_f32_e32 v115, v115
	v_pk_add_f32 v[116:117], v[116:117], 1.0 op_sel_hi:[1,0]
	v_exp_f32_e32 v112, v112
	v_exp_f32_e32 v113, v113
	v_pk_add_f32 v[106:107], v[106:107], v[22:23]
	v_pk_mul_f32 v[118:119], v[118:119], v[122:123]
	v_lshlrev_b32_e32 v122, 16, v195
	v_and_b32_e32 v123, 0xffff0000, v195
	v_rcp_f32_e32 v116, v116
	v_rcp_f32_e32 v117, v117
	v_pk_add_f32 v[108:109], v[108:109], v[24:25]
	v_pk_mul_f32 v[106:107], v[106:107], s[0:1] op_sel_hi:[1,0]
	v_pk_mul_f32 v[120:121], v[120:121], v[122:123]
	v_exp_f32_e32 v106, v106
	v_exp_f32_e32 v107, v107
	v_pk_mul_f32 v[108:109], v[108:109], s[0:1] op_sel_hi:[1,0]
	v_cvt_pk_bf16_f32 v118, v118, v119
	v_cvt_pk_bf16_f32 v119, v120, v121
	s_waitcnt vmcnt(24)
	v_lshlrev_b32_e32 v120, 16, v192
	v_and_b32_e32 v121, 0xffff0000, v192
	v_pk_add_f32 v[110:111], v[110:111], 1.0 op_sel_hi:[1,0]
	v_exp_f32_e32 v108, v108
	v_exp_f32_e32 v109, v109
	v_pk_mul_f32 v[114:115], v[114:115], v[120:121]
	v_lshlrev_b32_e32 v120, 16, v193
	v_and_b32_e32 v121, 0xffff0000, v193
	v_rcp_f32_e32 v110, v110
	v_rcp_f32_e32 v111, v111
	v_pk_add_f32 v[112:113], v[112:113], 1.0 op_sel_hi:[1,0]
	v_pk_add_f32 v[102:103], v[102:103], v[14:15]
	v_pk_mul_f32 v[116:117], v[116:117], v[120:121]
	v_rcp_f32_e32 v112, v112
	v_rcp_f32_e32 v113, v113
	v_pk_add_f32 v[104:105], v[104:105], v[16:17]
	v_pk_mul_f32 v[102:103], v[102:103], s[0:1] op_sel_hi:[1,0]
	v_cvt_pk_bf16_f32 v114, v114, v115
	v_cvt_pk_bf16_f32 v115, v116, v117
	v_pk_add_f32 v[106:107], v[106:107], 1.0 op_sel_hi:[1,0]
	v_exp_f32_e32 v102, v102
	v_exp_f32_e32 v103, v103
	v_pk_mul_f32 v[104:105], v[104:105], s[0:1] op_sel_hi:[1,0]
	ds_write2_b64 v124, v[118:119], v[114:115] offset0:40 offset1:44
	s_waitcnt vmcnt(23)
	v_lshlrev_b32_e32 v114, 16, v190
	v_and_b32_e32 v115, 0xffff0000, v190
	v_rcp_f32_e32 v106, v106
	v_rcp_f32_e32 v107, v107
	v_pk_add_f32 v[108:109], v[108:109], 1.0 op_sel_hi:[1,0]
	v_exp_f32_e32 v104, v104
	v_exp_f32_e32 v105, v105
	v_pk_add_f32 v[98:99], v[98:99], v[6:7]
	v_pk_mul_f32 v[110:111], v[110:111], v[114:115]
	v_lshlrev_b32_e32 v114, 16, v191
	v_and_b32_e32 v115, 0xffff0000, v191
	v_rcp_f32_e32 v108, v108
	v_rcp_f32_e32 v109, v109
	v_pk_add_f32 v[100:101], v[100:101], v[8:9]
	v_pk_mul_f32 v[98:99], v[98:99], s[0:1] op_sel_hi:[1,0]
	v_pk_mul_f32 v[112:113], v[112:113], v[114:115]
	v_exp_f32_e32 v98, v98
	v_exp_f32_e32 v99, v99
	v_pk_mul_f32 v[100:101], v[100:101], s[0:1] op_sel_hi:[1,0]
	v_cvt_pk_bf16_f32 v110, v110, v111
	v_cvt_pk_bf16_f32 v111, v112, v113
	s_waitcnt vmcnt(22)
	v_lshlrev_b32_e32 v112, 16, v188
	v_and_b32_e32 v113, 0xffff0000, v188
	v_pk_add_f32 v[102:103], v[102:103], 1.0 op_sel_hi:[1,0]
	v_exp_f32_e32 v100, v100
	v_exp_f32_e32 v101, v101
	v_pk_mul_f32 v[106:107], v[106:107], v[112:113]
	v_lshlrev_b32_e32 v112, 16, v189
	v_and_b32_e32 v113, 0xffff0000, v189
	v_rcp_f32_e32 v102, v102
	v_rcp_f32_e32 v103, v103
	v_pk_add_f32 v[104:105], v[104:105], 1.0 op_sel_hi:[1,0]
	v_pk_add_f32 v[94:95], v[94:95], v[30:31]
	v_pk_mul_f32 v[108:109], v[108:109], v[112:113]
	v_rcp_f32_e32 v104, v104
	v_rcp_f32_e32 v105, v105
	v_pk_add_f32 v[96:97], v[96:97], v[32:33]
	v_pk_mul_f32 v[94:95], v[94:95], s[0:1] op_sel_hi:[1,0]
	v_cvt_pk_bf16_f32 v106, v106, v107
	v_cvt_pk_bf16_f32 v107, v108, v109
	v_add_u32_e32 v108, 0x4000, v171
	v_pk_add_f32 v[98:99], v[98:99], 1.0 op_sel_hi:[1,0]
	v_exp_f32_e32 v94, v94
	v_exp_f32_e32 v95, v95
	v_pk_mul_f32 v[96:97], v[96:97], s[0:1] op_sel_hi:[1,0]
	ds_write2_b64 v108, v[110:111], v[106:107] offset0:64 offset1:68
	s_waitcnt vmcnt(21)
	v_lshlrev_b32_e32 v106, 16, v186
	v_and_b32_e32 v107, 0xffff0000, v186
	v_rcp_f32_e32 v98, v98
	v_rcp_f32_e32 v99, v99
	v_pk_add_f32 v[100:101], v[100:101], 1.0 op_sel_hi:[1,0]
	v_exp_f32_e32 v96, v96
	v_exp_f32_e32 v97, v97
	v_pk_add_f32 v[90:91], v[90:91], v[22:23]
	v_pk_mul_f32 v[102:103], v[102:103], v[106:107]
	v_lshlrev_b32_e32 v106, 16, v187
	v_and_b32_e32 v107, 0xffff0000, v187
	v_rcp_f32_e32 v100, v100
	v_rcp_f32_e32 v101, v101
	v_pk_add_f32 v[92:93], v[92:93], v[24:25]
	v_pk_mul_f32 v[90:91], v[90:91], s[0:1] op_sel_hi:[1,0]
	v_pk_mul_f32 v[104:105], v[104:105], v[106:107]
	v_exp_f32_e32 v90, v90
	v_exp_f32_e32 v91, v91
	v_pk_mul_f32 v[92:93], v[92:93], s[0:1] op_sel_hi:[1,0]
	v_cvt_pk_bf16_f32 v102, v102, v103
	v_cvt_pk_bf16_f32 v103, v104, v105
	s_waitcnt vmcnt(20)
	v_lshlrev_b32_e32 v104, 16, v184
	v_and_b32_e32 v105, 0xffff0000, v184
	v_pk_add_f32 v[94:95], v[94:95], 1.0 op_sel_hi:[1,0]
	v_exp_f32_e32 v92, v92
	v_exp_f32_e32 v93, v93
	v_pk_mul_f32 v[98:99], v[98:99], v[104:105]
	v_lshlrev_b32_e32 v104, 16, v185
	v_and_b32_e32 v105, 0xffff0000, v185
	v_rcp_f32_e32 v94, v94
	v_rcp_f32_e32 v95, v95
	v_pk_add_f32 v[96:97], v[96:97], 1.0 op_sel_hi:[1,0]
	v_pk_add_f32 v[86:87], v[86:87], v[14:15]
	v_pk_mul_f32 v[100:101], v[100:101], v[104:105]
	v_rcp_f32_e32 v96, v96
	v_rcp_f32_e32 v97, v97
	v_pk_add_f32 v[88:89], v[88:89], v[16:17]
	v_pk_mul_f32 v[86:87], v[86:87], s[0:1] op_sel_hi:[1,0]
	v_cvt_pk_bf16_f32 v98, v98, v99
	v_cvt_pk_bf16_f32 v99, v100, v101
	v_pk_add_f32 v[90:91], v[90:91], 1.0 op_sel_hi:[1,0]
	v_exp_f32_e32 v86, v86
	v_exp_f32_e32 v87, v87
	v_pk_mul_f32 v[88:89], v[88:89], s[0:1] op_sel_hi:[1,0]
	ds_write2_b64 v108, v[102:103], v[98:99] offset0:72 offset1:76
	s_waitcnt vmcnt(19)
	v_lshlrev_b32_e32 v98, 16, v182
	v_and_b32_e32 v99, 0xffff0000, v182
	v_rcp_f32_e32 v90, v90
	v_rcp_f32_e32 v91, v91
	v_pk_add_f32 v[92:93], v[92:93], 1.0 op_sel_hi:[1,0]
	v_exp_f32_e32 v88, v88
	v_exp_f32_e32 v89, v89
	v_pk_add_f32 v[82:83], v[82:83], v[6:7]
	v_pk_mul_f32 v[94:95], v[94:95], v[98:99]
	v_lshlrev_b32_e32 v98, 16, v183
	v_and_b32_e32 v99, 0xffff0000, v183
	v_rcp_f32_e32 v92, v92
	v_rcp_f32_e32 v93, v93
	v_pk_add_f32 v[84:85], v[84:85], v[8:9]
	v_pk_mul_f32 v[82:83], v[82:83], s[0:1] op_sel_hi:[1,0]
	v_pk_mul_f32 v[96:97], v[96:97], v[98:99]
	v_exp_f32_e32 v82, v82
	v_exp_f32_e32 v83, v83
	v_pk_mul_f32 v[84:85], v[84:85], s[0:1] op_sel_hi:[1,0]
	v_cvt_pk_bf16_f32 v94, v94, v95
	v_cvt_pk_bf16_f32 v95, v96, v97
	s_waitcnt vmcnt(18)
	v_lshlrev_b32_e32 v96, 16, v180
	v_and_b32_e32 v97, 0xffff0000, v180
	v_pk_add_f32 v[86:87], v[86:87], 1.0 op_sel_hi:[1,0]
	v_exp_f32_e32 v84, v84
	v_exp_f32_e32 v85, v85
	v_pk_mul_f32 v[90:91], v[90:91], v[96:97]
	v_lshlrev_b32_e32 v96, 16, v181
	v_and_b32_e32 v97, 0xffff0000, v181
	v_rcp_f32_e32 v86, v86
	v_rcp_f32_e32 v87, v87
	v_pk_add_f32 v[88:89], v[88:89], 1.0 op_sel_hi:[1,0]
	v_pk_add_f32 v[78:79], v[78:79], v[30:31]
	v_pk_mul_f32 v[92:93], v[92:93], v[96:97]
	v_rcp_f32_e32 v88, v88
	v_rcp_f32_e32 v89, v89
	v_pk_add_f32 v[80:81], v[80:81], v[32:33]
	v_pk_mul_f32 v[78:79], v[78:79], s[0:1] op_sel_hi:[1,0]
	v_cvt_pk_bf16_f32 v90, v90, v91
	v_cvt_pk_bf16_f32 v91, v92, v93
	v_add_u32_e32 v92, 0x6000, v171
	v_pk_add_f32 v[82:83], v[82:83], 1.0 op_sel_hi:[1,0]
	v_exp_f32_e32 v78, v78
	v_exp_f32_e32 v79, v79
	v_pk_mul_f32 v[80:81], v[80:81], s[0:1] op_sel_hi:[1,0]
	ds_write2_b64 v92, v[94:95], v[90:91] offset0:96 offset1:100
	s_waitcnt vmcnt(17)
	v_lshlrev_b32_e32 v90, 16, v178
	v_and_b32_e32 v91, 0xffff0000, v178
	v_rcp_f32_e32 v82, v82
	v_rcp_f32_e32 v83, v83
	v_pk_add_f32 v[84:85], v[84:85], 1.0 op_sel_hi:[1,0]
	v_exp_f32_e32 v80, v80
	v_exp_f32_e32 v81, v81
	v_pk_add_f32 v[74:75], v[74:75], v[22:23]
	v_pk_mul_f32 v[86:87], v[86:87], v[90:91]
	v_lshlrev_b32_e32 v90, 16, v179
	v_and_b32_e32 v91, 0xffff0000, v179
	v_rcp_f32_e32 v84, v84
	v_rcp_f32_e32 v85, v85
	v_pk_add_f32 v[76:77], v[76:77], v[24:25]
	v_pk_mul_f32 v[74:75], v[74:75], s[0:1] op_sel_hi:[1,0]
	v_pk_mul_f32 v[88:89], v[88:89], v[90:91]
	v_exp_f32_e32 v74, v74
	v_exp_f32_e32 v75, v75
	v_pk_mul_f32 v[76:77], v[76:77], s[0:1] op_sel_hi:[1,0]
	v_cvt_pk_bf16_f32 v86, v86, v87
	v_cvt_pk_bf16_f32 v87, v88, v89
	s_waitcnt vmcnt(16)
	v_lshlrev_b32_e32 v88, 16, v176
	v_and_b32_e32 v89, 0xffff0000, v176
	v_pk_add_f32 v[78:79], v[78:79], 1.0 op_sel_hi:[1,0]
	v_exp_f32_e32 v76, v76
	v_exp_f32_e32 v77, v77
	v_pk_mul_f32 v[82:83], v[82:83], v[88:89]
	v_lshlrev_b32_e32 v88, 16, v177
	v_and_b32_e32 v89, 0xffff0000, v177
	v_rcp_f32_e32 v78, v78
	v_rcp_f32_e32 v79, v79
	v_pk_add_f32 v[80:81], v[80:81], 1.0 op_sel_hi:[1,0]
	v_pk_add_f32 v[70:71], v[70:71], v[14:15]
	v_pk_mul_f32 v[84:85], v[84:85], v[88:89]
	v_rcp_f32_e32 v80, v80
	v_rcp_f32_e32 v81, v81
	v_pk_add_f32 v[72:73], v[72:73], v[16:17]
	v_pk_mul_f32 v[70:71], v[70:71], s[0:1] op_sel_hi:[1,0]
	v_cvt_pk_bf16_f32 v82, v82, v83
	v_cvt_pk_bf16_f32 v83, v84, v85
	v_pk_add_f32 v[74:75], v[74:75], 1.0 op_sel_hi:[1,0]
	v_exp_f32_e32 v70, v70
	v_exp_f32_e32 v71, v71
	v_pk_mul_f32 v[72:73], v[72:73], s[0:1] op_sel_hi:[1,0]
	ds_write2_b64 v92, v[86:87], v[82:83] offset0:104 offset1:108
	s_waitcnt vmcnt(15)
	v_lshlrev_b32_e32 v82, 16, v174
	v_and_b32_e32 v83, 0xffff0000, v174
	v_rcp_f32_e32 v74, v74
	v_rcp_f32_e32 v75, v75
	v_pk_add_f32 v[76:77], v[76:77], 1.0 op_sel_hi:[1,0]
	v_exp_f32_e32 v72, v72
	v_exp_f32_e32 v73, v73
	v_pk_add_f32 v[66:67], v[66:67], v[6:7]
	v_pk_mul_f32 v[78:79], v[78:79], v[82:83]
	v_lshlrev_b32_e32 v82, 16, v175
	v_and_b32_e32 v83, 0xffff0000, v175
	v_rcp_f32_e32 v76, v76
	v_rcp_f32_e32 v77, v77
	v_pk_add_f32 v[68:69], v[68:69], v[8:9]
	v_pk_mul_f32 v[66:67], v[66:67], s[0:1] op_sel_hi:[1,0]
	v_pk_mul_f32 v[80:81], v[80:81], v[82:83]
	v_exp_f32_e32 v66, v66
	v_exp_f32_e32 v67, v67
	v_pk_mul_f32 v[68:69], v[68:69], s[0:1] op_sel_hi:[1,0]
	v_cvt_pk_bf16_f32 v78, v78, v79
	v_cvt_pk_bf16_f32 v79, v80, v81
	s_waitcnt vmcnt(14)
	v_lshlrev_b32_e32 v80, 16, v172
	v_and_b32_e32 v81, 0xffff0000, v172
	v_pk_add_f32 v[70:71], v[70:71], 1.0 op_sel_hi:[1,0]
	v_exp_f32_e32 v68, v68
	v_exp_f32_e32 v69, v69
	v_pk_mul_f32 v[74:75], v[74:75], v[80:81]
	v_lshlrev_b32_e32 v80, 16, v173
	v_and_b32_e32 v81, 0xffff0000, v173
	v_rcp_f32_e32 v70, v70
	v_rcp_f32_e32 v71, v71
	v_pk_add_f32 v[72:73], v[72:73], 1.0 op_sel_hi:[1,0]
	v_pk_add_f32 v[62:63], v[62:63], v[30:31]
	v_pk_mul_f32 v[76:77], v[76:77], v[80:81]
	v_rcp_f32_e32 v72, v72
	v_rcp_f32_e32 v73, v73
	v_pk_add_f32 v[64:65], v[64:65], v[32:33]
	v_pk_mul_f32 v[62:63], v[62:63], s[0:1] op_sel_hi:[1,0]
	v_cvt_pk_bf16_f32 v74, v74, v75
	v_cvt_pk_bf16_f32 v75, v76, v77
	v_add_u32_e32 v76, 0x8000, v171
	v_pk_add_f32 v[66:67], v[66:67], 1.0 op_sel_hi:[1,0]
	v_exp_f32_e32 v62, v62
	v_exp_f32_e32 v63, v63
	v_pk_mul_f32 v[64:65], v[64:65], s[0:1] op_sel_hi:[1,0]
	ds_write2_b64 v76, v[78:79], v[74:75] offset0:128 offset1:132
	s_waitcnt vmcnt(13)
	v_lshlrev_b32_e32 v74, 16, v168
	v_and_b32_e32 v75, 0xffff0000, v168
	v_rcp_f32_e32 v66, v66
	v_rcp_f32_e32 v67, v67
	v_pk_add_f32 v[68:69], v[68:69], 1.0 op_sel_hi:[1,0]
	v_exp_f32_e32 v64, v64
	v_exp_f32_e32 v65, v65
	v_pk_add_f32 v[58:59], v[58:59], v[22:23]
	v_pk_mul_f32 v[70:71], v[70:71], v[74:75]
	v_lshlrev_b32_e32 v74, 16, v169
	v_and_b32_e32 v75, 0xffff0000, v169
	v_rcp_f32_e32 v68, v68
	v_rcp_f32_e32 v69, v69
	v_pk_add_f32 v[60:61], v[60:61], v[24:25]
	v_pk_mul_f32 v[58:59], v[58:59], s[0:1] op_sel_hi:[1,0]
	v_pk_mul_f32 v[72:73], v[72:73], v[74:75]
	v_exp_f32_e32 v58, v58
	v_exp_f32_e32 v59, v59
	v_pk_mul_f32 v[60:61], v[60:61], s[0:1] op_sel_hi:[1,0]
	v_cvt_pk_bf16_f32 v70, v70, v71
	v_cvt_pk_bf16_f32 v71, v72, v73
	s_waitcnt vmcnt(12)
	v_lshlrev_b32_e32 v72, 16, v166
	v_and_b32_e32 v73, 0xffff0000, v166
	v_pk_add_f32 v[62:63], v[62:63], 1.0 op_sel_hi:[1,0]
	v_exp_f32_e32 v60, v60
	v_exp_f32_e32 v61, v61
	v_pk_mul_f32 v[66:67], v[66:67], v[72:73]
	v_lshlrev_b32_e32 v72, 16, v167
	v_and_b32_e32 v73, 0xffff0000, v167
	v_rcp_f32_e32 v62, v62
	v_rcp_f32_e32 v63, v63
	v_pk_add_f32 v[64:65], v[64:65], 1.0 op_sel_hi:[1,0]
	v_pk_add_f32 v[54:55], v[54:55], v[14:15]
	v_pk_mul_f32 v[68:69], v[68:69], v[72:73]
	v_rcp_f32_e32 v64, v64
	v_rcp_f32_e32 v65, v65
	v_pk_add_f32 v[56:57], v[56:57], v[16:17]
	v_pk_mul_f32 v[54:55], v[54:55], s[0:1] op_sel_hi:[1,0]
	v_cvt_pk_bf16_f32 v66, v66, v67
	v_cvt_pk_bf16_f32 v67, v68, v69
	v_pk_add_f32 v[58:59], v[58:59], 1.0 op_sel_hi:[1,0]
	v_exp_f32_e32 v54, v54
	v_exp_f32_e32 v55, v55
	v_pk_mul_f32 v[56:57], v[56:57], s[0:1] op_sel_hi:[1,0]
	ds_write2_b64 v76, v[70:71], v[66:67] offset0:136 offset1:140
	s_waitcnt vmcnt(11)
	v_lshlrev_b32_e32 v66, 16, v164
	v_and_b32_e32 v67, 0xffff0000, v164
	v_rcp_f32_e32 v58, v58
	v_rcp_f32_e32 v59, v59
	v_pk_add_f32 v[60:61], v[60:61], 1.0 op_sel_hi:[1,0]
	v_exp_f32_e32 v56, v56
	v_exp_f32_e32 v57, v57
	v_pk_add_f32 v[50:51], v[50:51], v[6:7]
	v_pk_mul_f32 v[62:63], v[62:63], v[66:67]
	v_lshlrev_b32_e32 v66, 16, v165
	v_and_b32_e32 v67, 0xffff0000, v165
	v_rcp_f32_e32 v60, v60
	v_rcp_f32_e32 v61, v61
	v_pk_add_f32 v[52:53], v[52:53], v[8:9]
	v_pk_mul_f32 v[50:51], v[50:51], s[0:1] op_sel_hi:[1,0]
	v_pk_mul_f32 v[64:65], v[64:65], v[66:67]
	v_exp_f32_e32 v50, v50
	v_exp_f32_e32 v51, v51
	v_pk_mul_f32 v[52:53], v[52:53], s[0:1] op_sel_hi:[1,0]
	v_cvt_pk_bf16_f32 v62, v62, v63
	v_cvt_pk_bf16_f32 v63, v64, v65
	s_waitcnt vmcnt(10)
	v_lshlrev_b32_e32 v64, 16, v162
	v_and_b32_e32 v65, 0xffff0000, v162
	v_pk_add_f32 v[54:55], v[54:55], 1.0 op_sel_hi:[1,0]
	v_exp_f32_e32 v52, v52
	v_exp_f32_e32 v53, v53
	v_pk_mul_f32 v[58:59], v[58:59], v[64:65]
	v_lshlrev_b32_e32 v64, 16, v163
	v_and_b32_e32 v65, 0xffff0000, v163
	v_rcp_f32_e32 v54, v54
	v_rcp_f32_e32 v55, v55
	v_pk_add_f32 v[56:57], v[56:57], 1.0 op_sel_hi:[1,0]
	v_pk_add_f32 v[46:47], v[46:47], v[30:31]
	v_pk_mul_f32 v[60:61], v[60:61], v[64:65]
	v_rcp_f32_e32 v56, v56
	v_rcp_f32_e32 v57, v57
	v_pk_add_f32 v[48:49], v[48:49], v[32:33]
	v_pk_mul_f32 v[46:47], v[46:47], s[0:1] op_sel_hi:[1,0]
	v_cvt_pk_bf16_f32 v58, v58, v59
	v_cvt_pk_bf16_f32 v59, v60, v61
	v_add_u32_e32 v60, 0xa000, v171
	v_pk_add_f32 v[50:51], v[50:51], 1.0 op_sel_hi:[1,0]
	v_exp_f32_e32 v46, v46
	v_exp_f32_e32 v47, v47
	v_pk_mul_f32 v[48:49], v[48:49], s[0:1] op_sel_hi:[1,0]
	ds_write2_b64 v60, v[62:63], v[58:59] offset0:160 offset1:164
	s_waitcnt vmcnt(9)
	v_lshlrev_b32_e32 v58, 16, v160
	v_and_b32_e32 v59, 0xffff0000, v160
	v_rcp_f32_e32 v50, v50
	v_rcp_f32_e32 v51, v51
	v_pk_add_f32 v[52:53], v[52:53], 1.0 op_sel_hi:[1,0]
	v_exp_f32_e32 v48, v48
	v_exp_f32_e32 v49, v49
	v_pk_add_f32 v[42:43], v[42:43], v[22:23]
	v_pk_mul_f32 v[54:55], v[54:55], v[58:59]
	v_lshlrev_b32_e32 v58, 16, v161
	v_and_b32_e32 v59, 0xffff0000, v161
	v_rcp_f32_e32 v52, v52
	v_rcp_f32_e32 v53, v53
	v_pk_add_f32 v[44:45], v[44:45], v[24:25]
	v_pk_mul_f32 v[42:43], v[42:43], s[0:1] op_sel_hi:[1,0]
	v_pk_mul_f32 v[56:57], v[56:57], v[58:59]
	v_exp_f32_e32 v42, v42
	v_exp_f32_e32 v43, v43
	v_pk_mul_f32 v[44:45], v[44:45], s[0:1] op_sel_hi:[1,0]
	v_cvt_pk_bf16_f32 v54, v54, v55
	v_cvt_pk_bf16_f32 v55, v56, v57
	s_waitcnt vmcnt(8)
	v_lshlrev_b32_e32 v56, 16, v156
	v_and_b32_e32 v57, 0xffff0000, v156
	v_pk_add_f32 v[46:47], v[46:47], 1.0 op_sel_hi:[1,0]
	v_exp_f32_e32 v44, v44
	v_exp_f32_e32 v45, v45
	v_pk_mul_f32 v[50:51], v[50:51], v[56:57]
	v_lshlrev_b32_e32 v56, 16, v157
	v_and_b32_e32 v57, 0xffff0000, v157
	v_rcp_f32_e32 v46, v46
	v_rcp_f32_e32 v47, v47
	v_pk_add_f32 v[48:49], v[48:49], 1.0 op_sel_hi:[1,0]
	v_pk_add_f32 v[38:39], v[38:39], v[14:15]
	v_pk_mul_f32 v[52:53], v[52:53], v[56:57]
	v_rcp_f32_e32 v48, v48
	v_rcp_f32_e32 v49, v49
	v_pk_add_f32 v[40:41], v[40:41], v[16:17]
	v_pk_mul_f32 v[38:39], v[38:39], s[0:1] op_sel_hi:[1,0]
	v_cvt_pk_bf16_f32 v50, v50, v51
	v_cvt_pk_bf16_f32 v51, v52, v53
	v_pk_add_f32 v[42:43], v[42:43], 1.0 op_sel_hi:[1,0]
	v_exp_f32_e32 v38, v38
	v_exp_f32_e32 v39, v39
	v_pk_mul_f32 v[40:41], v[40:41], s[0:1] op_sel_hi:[1,0]
	ds_write2_b64 v60, v[54:55], v[50:51] offset0:168 offset1:172
	s_waitcnt vmcnt(7)
	v_lshlrev_b32_e32 v50, 16, v154
	v_and_b32_e32 v51, 0xffff0000, v154
	v_rcp_f32_e32 v42, v42
	v_rcp_f32_e32 v43, v43
	v_pk_add_f32 v[44:45], v[44:45], 1.0 op_sel_hi:[1,0]
	v_exp_f32_e32 v40, v40
	v_exp_f32_e32 v41, v41
	v_pk_add_f32 v[34:35], v[34:35], v[6:7]
	v_pk_mul_f32 v[46:47], v[46:47], v[50:51]
	v_lshlrev_b32_e32 v50, 16, v155
	v_and_b32_e32 v51, 0xffff0000, v155
	v_rcp_f32_e32 v44, v44
	v_rcp_f32_e32 v45, v45
	v_pk_add_f32 v[36:37], v[36:37], v[8:9]
	v_pk_mul_f32 v[34:35], v[34:35], s[0:1] op_sel_hi:[1,0]
	v_pk_mul_f32 v[48:49], v[48:49], v[50:51]
	v_exp_f32_e32 v34, v34
	v_exp_f32_e32 v35, v35
	v_pk_mul_f32 v[36:37], v[36:37], s[0:1] op_sel_hi:[1,0]
	v_cvt_pk_bf16_f32 v46, v46, v47
	v_cvt_pk_bf16_f32 v47, v48, v49
	s_waitcnt vmcnt(6)
	v_lshlrev_b32_e32 v48, 16, v152
	v_and_b32_e32 v49, 0xffff0000, v152
	v_pk_add_f32 v[38:39], v[38:39], 1.0 op_sel_hi:[1,0]
	v_exp_f32_e32 v36, v36
	v_exp_f32_e32 v37, v37
	v_pk_mul_f32 v[42:43], v[42:43], v[48:49]
	v_lshlrev_b32_e32 v48, 16, v153
	v_and_b32_e32 v49, 0xffff0000, v153
	v_rcp_f32_e32 v38, v38
	v_rcp_f32_e32 v39, v39
	v_pk_add_f32 v[40:41], v[40:41], 1.0 op_sel_hi:[1,0]
	v_pk_add_f32 v[28:29], v[28:29], v[32:33]
	v_pk_add_f32 v[26:27], v[26:27], v[30:31]
	v_pk_mul_f32 v[44:45], v[44:45], v[48:49]
	v_rcp_f32_e32 v40, v40
	v_rcp_f32_e32 v41, v41
	v_pk_mul_f32 v[26:27], v[26:27], s[0:1] op_sel_hi:[1,0]
	v_pk_mul_f32 v[28:29], v[28:29], s[0:1] op_sel_hi:[1,0]
	v_cvt_pk_bf16_f32 v42, v42, v43
	v_cvt_pk_bf16_f32 v43, v44, v45
	v_add_u32_e32 v44, 0xc000, v171
	v_pk_add_f32 v[34:35], v[34:35], 1.0 op_sel_hi:[1,0]
	v_exp_f32_e32 v26, v26
	v_exp_f32_e32 v27, v27
	v_exp_f32_e32 v28, v28
	v_exp_f32_e32 v29, v29
	v_pk_add_f32 v[20:21], v[20:21], v[24:25]
	v_pk_add_f32 v[18:19], v[18:19], v[22:23]
	ds_write2_b64 v44, v[46:47], v[42:43] offset0:192 offset1:196
	s_waitcnt vmcnt(5)
	v_lshlrev_b32_e32 v42, 16, v150
	v_and_b32_e32 v43, 0xffff0000, v150
	v_rcp_f32_e32 v34, v34
	v_rcp_f32_e32 v35, v35
	v_pk_add_f32 v[36:37], v[36:37], 1.0 op_sel_hi:[1,0]
	v_pk_mul_f32 v[18:19], v[18:19], s[0:1] op_sel_hi:[1,0]
	v_pk_mul_f32 v[20:21], v[20:21], s[0:1] op_sel_hi:[1,0]
	v_pk_mul_f32 v[38:39], v[38:39], v[42:43]
	v_lshlrev_b32_e32 v42, 16, v151
	v_and_b32_e32 v43, 0xffff0000, v151
	v_rcp_f32_e32 v36, v36
	v_rcp_f32_e32 v37, v37
	v_exp_f32_e32 v18, v18
	v_exp_f32_e32 v19, v19
	v_exp_f32_e32 v20, v20
	v_exp_f32_e32 v21, v21
	v_pk_mul_f32 v[40:41], v[40:41], v[42:43]
	v_pk_add_f32 v[12:13], v[12:13], v[16:17]
	v_pk_add_f32 v[10:11], v[10:11], v[14:15]
	v_cvt_pk_bf16_f32 v38, v38, v39
	v_cvt_pk_bf16_f32 v39, v40, v41
	s_waitcnt vmcnt(4)
	v_lshlrev_b32_e32 v40, 16, v148
	v_and_b32_e32 v41, 0xffff0000, v148
	v_pk_add_f32 v[26:27], v[26:27], 1.0 op_sel_hi:[1,0]
	v_pk_add_f32 v[28:29], v[28:29], 1.0 op_sel_hi:[1,0]
	v_pk_mul_f32 v[10:11], v[10:11], s[0:1] op_sel_hi:[1,0]
	v_pk_mul_f32 v[12:13], v[12:13], s[0:1] op_sel_hi:[1,0]
	v_pk_mul_f32 v[34:35], v[34:35], v[40:41]
	v_lshlrev_b32_e32 v40, 16, v149
	v_and_b32_e32 v41, 0xffff0000, v149
	v_rcp_f32_e32 v26, v26
	v_rcp_f32_e32 v27, v27
	v_rcp_f32_e32 v28, v28
	v_rcp_f32_e32 v29, v29
	v_exp_f32_e32 v10, v10
	v_exp_f32_e32 v11, v11
	v_exp_f32_e32 v12, v12
	v_exp_f32_e32 v13, v13
	v_pk_add_f32 v[4:5], v[4:5], v[8:9]
	v_pk_add_f32 v[2:3], v[2:3], v[6:7]
	v_pk_mul_f32 v[36:37], v[36:37], v[40:41]
	v_pk_add_f32 v[18:19], v[18:19], 1.0 op_sel_hi:[1,0]
	v_pk_add_f32 v[20:21], v[20:21], 1.0 op_sel_hi:[1,0]
	v_pk_mul_f32 v[2:3], v[2:3], s[0:1] op_sel_hi:[1,0]
	v_pk_mul_f32 v[4:5], v[4:5], s[0:1] op_sel_hi:[1,0]
	v_cvt_pk_bf16_f32 v34, v34, v35
	v_cvt_pk_bf16_f32 v35, v36, v37
	v_rcp_f32_e32 v18, v18
	v_rcp_f32_e32 v19, v19
	v_rcp_f32_e32 v20, v20
	v_rcp_f32_e32 v21, v21
	v_exp_f32_e32 v2, v2
	v_exp_f32_e32 v3, v3
	v_exp_f32_e32 v4, v4
	v_exp_f32_e32 v5, v5
	ds_write2_b64 v44, v[38:39], v[34:35] offset0:200 offset1:204
	s_waitcnt vmcnt(3)
	v_lshlrev_b32_e32 v34, 16, v144
	v_and_b32_e32 v35, 0xffff0000, v144
	v_lshlrev_b32_e32 v30, 16, v145
	v_and_b32_e32 v31, 0xffff0000, v145
	v_pk_mul_f32 v[26:27], v[26:27], v[34:35]
	v_pk_mul_f32 v[28:29], v[28:29], v[30:31]
	v_pk_add_f32 v[10:11], v[10:11], 1.0 op_sel_hi:[1,0]
	v_pk_add_f32 v[12:13], v[12:13], 1.0 op_sel_hi:[1,0]
	v_cvt_pk_bf16_f32 v26, v26, v27
	v_cvt_pk_bf16_f32 v27, v28, v29
	s_waitcnt vmcnt(2)
	v_lshlrev_b32_e32 v28, 16, v142
	v_and_b32_e32 v29, 0xffff0000, v142
	v_lshlrev_b32_e32 v22, 16, v143
	v_and_b32_e32 v23, 0xffff0000, v143
	v_rcp_f32_e32 v10, v10
	v_rcp_f32_e32 v11, v11
	v_rcp_f32_e32 v12, v12
	v_rcp_f32_e32 v13, v13
	v_pk_mul_f32 v[18:19], v[18:19], v[28:29]
	v_pk_mul_f32 v[20:21], v[20:21], v[22:23]
	v_pk_add_f32 v[2:3], v[2:3], 1.0 op_sel_hi:[1,0]
	v_pk_add_f32 v[4:5], v[4:5], 1.0 op_sel_hi:[1,0]
	v_cvt_pk_bf16_f32 v18, v18, v19
	v_cvt_pk_bf16_f32 v19, v20, v21
	v_add_u32_e32 v20, 0xe000, v171
	v_rcp_f32_e32 v2, v2
	v_rcp_f32_e32 v3, v3
	v_rcp_f32_e32 v4, v4
	v_rcp_f32_e32 v5, v5
	ds_write2_b64 v20, v[26:27], v[18:19] offset0:224 offset1:228
	s_waitcnt vmcnt(1)
	v_lshlrev_b32_e32 v18, 16, v140
	v_and_b32_e32 v19, 0xffff0000, v140
	v_lshlrev_b32_e32 v14, 16, v141
	v_and_b32_e32 v15, 0xffff0000, v141
	v_pk_mul_f32 v[10:11], v[10:11], v[18:19]
	v_pk_mul_f32 v[12:13], v[12:13], v[14:15]
	v_cvt_pk_bf16_f32 v10, v10, v11
	v_cvt_pk_bf16_f32 v11, v12, v13
	s_waitcnt vmcnt(0)
	v_lshlrev_b32_e32 v12, 16, v138
	v_and_b32_e32 v13, 0xffff0000, v138
	v_lshlrev_b32_e32 v6, 16, v139
	v_and_b32_e32 v7, 0xffff0000, v139
	v_pk_mul_f32 v[2:3], v[2:3], v[12:13]
	v_pk_mul_f32 v[4:5], v[4:5], v[6:7]
	v_cvt_pk_bf16_f32 v2, v2, v3
	v_cvt_pk_bf16_f32 v3, v4, v5
	ds_write2_b64 v20, v[10:11], v[2:3] offset0:232 offset1:236
	v_add_u32_e32 v2, 0, v146
	v_mul_lo_u32 v3, v1, s1
	s_waitcnt lgkmcnt(0)
	s_barrier
	v_add_u32_e32 v4, v2, v3
	ds_read_b128 v[12:15], v4
	s_waitcnt lgkmcnt(0)
	v_and_b32_e32 v3, 0xffff0000, v12
	v_lshlrev_b32_e32 v2, 16, v12
	v_mul_f32_e32 v3, v3, v3
	v_fmac_f32_e32 v3, v2, v2
	v_lshlrev_b32_e32 v2, 16, v13
	v_fmac_f32_e32 v3, v2, v2
	v_and_b32_e32 v2, 0xffff0000, v13
	v_fmac_f32_e32 v3, v2, v2
	v_lshlrev_b32_e32 v2, 16, v14
	v_fmac_f32_e32 v3, v2, v2
	v_and_b32_e32 v2, 0xffff0000, v14
	v_fmac_f32_e32 v3, v2, v2
	v_lshlrev_b32_e32 v2, 16, v15
	v_fmac_f32_e32 v3, v2, v2
	v_and_b32_e32 v2, 0xffff0000, v15
	v_fmac_f32_e32 v3, v2, v2
	v_mbcnt_lo_u32_b32 v2, -1, 0
	v_mbcnt_hi_u32_b32 v9, -1, v2
	v_and_b32_e32 v2, 64, v9
	v_add_u32_e32 v18, 64, v2
	v_xor_b32_e32 v2, 1, v9
	v_cmp_lt_i32_e64 s[0:1], v2, v18
	s_nop 1
	v_cndmask_b32_e64 v2, v9, v2, s[0:1]
	v_lshlrev_b32_e32 v5, 2, v2
	ds_bpermute_b32 v2, v5, v3
	s_waitcnt lgkmcnt(0)
	v_add_f32_e32 v2, v3, v2
	v_xor_b32_e32 v3, 2, v9
	v_cmp_lt_i32_e64 s[0:1], v3, v18
	s_nop 1
	v_cndmask_b32_e64 v3, v9, v3, s[0:1]
	v_lshlrev_b32_e32 v6, 2, v3
	ds_bpermute_b32 v3, v6, v2
	s_waitcnt lgkmcnt(0)
	v_add_f32_e32 v8, v2, v3
	v_xor_b32_e32 v2, 4, v9
	v_cmp_lt_i32_e64 s[0:1], v2, v18
	s_nop 1
	v_cndmask_b32_e64 v2, v9, v2, s[0:1]
	v_lshlrev_b32_e32 v7, 2, v2
	ds_bpermute_b32 v16, v7, v8
	v_add_u32_e32 v2, s9, v1
	v_ashrrev_i32_e32 v3, 31, v2
	v_lshlrev_b64 v[10:11], 12, v[2:3]
	v_lshl_add_u64 v[10:11], s[4:5], 0, v[10:11]
	s_waitcnt lgkmcnt(0)
	v_add_f32_e32 v19, v8, v16
	v_xor_b32_e32 v8, 8, v9
	v_cmp_lt_i32_e64 s[0:1], v8, v18
	v_lshl_add_u64 v[10:11], v[10:11], 0, s[6:7]
	v_lshl_add_u64 v[16:17], v[10:11], 0, v[146:147]
	v_cndmask_b32_e64 v8, v9, v8, s[0:1]
	v_lshlrev_b32_e32 v8, 2, v8
	ds_bpermute_b32 v20, v8, v19
	v_xor_b32_e32 v11, 16, v9
	v_cmp_lt_i32_e64 s[0:1], v11, v18
	global_store_dwordx4 v[16:17], v[12:15], off sc1
	s_nop 1
	s_waitcnt lgkmcnt(0)
	v_add_f32_e32 v10, v19, v20
	v_cndmask_b32_e64 v9, v9, v11, s[0:1]
	v_lshlrev_b32_e32 v9, 2, v9
	ds_bpermute_b32 v11, v9, v10
	s_and_saveexec_b64 s[0:1], vcc
	s_cbranch_execz .LBB0_951
	v_lshl_add_u64 v[2:3], v[2:3], 4, s[2:3]
	s_lshl_b32 s10, s8, 2
	s_mov_b32 s11, s7
	s_waitcnt lgkmcnt(0)
	v_add_f32_e32 v10, v10, v11
	v_lshl_add_u64 v[2:3], v[2:3], 0, s[10:11]
	global_store_dword v[2:3], v10, off

.LBB0_1038:
	s_ashr_i32 s30, s0, 2
	s_and_b32 s1, s30, 0xfffff8
	s_and_b32 s31, s0, 7
	s_bfe_u32 s20, s0, 0x20003
	s_or_b32 s1, s1, s31
	s_lshl_b32 s22, s20, 8
	s_lshl_b32 s0, s20, 9
	s_add_u32 s33, s16, s0
	s_addc_u32 s34, s17, 0
	s_lshl_b32 s21, s1, 8
	v_readfirstlane_b32 s0, v0
	s_lshr_b32 s23, s0, 6
	v_or_b32_e32 v2, s21, v159
	v_lshlrev_b32_e32 v2, 11, v2
	v_or_b32_e32 v3, 0x20000, v171
	s_lshl_b32 s2, s23, 1
	s_waitcnt vmcnt(4)
	v_or_b32_e32 v18, v2, v171
	v_add_u32_e32 v19, v2, v3
	v_add_u32_e32 v20, v2, v210
	s_bfe_u32 s26, s0, 0x20006
	v_or_b32_e32 v2, s2, v253
	s_and_b32 s1, s23, 4
	v_and_or_b32 v4, v2, 3, s1
	s_lshr_b32 s1, s0, 1
	s_lshl_b32 s24, s26, 7
	s_and_b32 s25, s1, 0x7fffff80
	s_or_b32 s1, s24, 32
	v_bitop3_b32 v151, s1, v212, v207 bitop3:0xde
	s_or_b32 s1, s24, 64
	v_bitop3_b32 v149, s1, v212, v207 bitop3:0xde
	s_or_b32 s1, s24, 0x60
	s_lshl_b32 s27, s23, 10
	v_bitop3_b32 v148, s1, v212, v207 bitop3:0xde
	s_add_i32 s27, s27, 0
	s_mov_b32 s1, m0
	s_mov_b32 m0, s27
	s_nop 0
	global_load_lds_dwordx4 v18, s[6:7]
	s_mov_b32 m0, s1
	s_add_i32 s1, s27, 0x2000
	s_mov_b32 s28, m0
	s_mov_b32 m0, s1
	s_nop 0
	global_load_lds_dwordx4 v19, s[6:7]
	s_mov_b32 m0, s28
	s_add_i32 s1, s27, 0x4000
	v_or_b32_e32 v3, 0x40000, v18
	s_mov_b32 s28, m0
	s_mov_b32 m0, s1
	s_nop 0
	global_load_lds_dwordx4 v3, s[6:7]
	s_mov_b32 m0, s28
	s_add_i32 s1, s27, 0x6000
	s_mov_b32 s28, m0
	s_mov_b32 m0, s1
	s_nop 0
	global_load_lds_dwordx4 v20, s[6:7]
	s_mov_b32 m0, s28
	s_lshl_b64 s[28:29], s[2:3], 11
	s_add_u32 s28, s33, s28
	v_lshlrev_b32_e32 v4, 5, v4
	s_waitcnt lgkmcnt(0)
	v_or_b32_e32 v5, s25, v1
	v_lshlrev_b32_e32 v2, 9, v2
	s_addc_u32 s29, s34, s29
	v_lshlrev_b32_e32 v34, 7, v5
	v_bitop3_b32 v154, v4, v2, v254 bitop3:0xde
	global_load_dwordx4 v[2:5], v208, s[28:29]
	s_add_i32 s28, s2, 16
	s_mov_b32 s29, s3
	s_lshl_b64 s[28:29], s[28:29], 11
	s_add_u32 s28, s33, s28
	s_addc_u32 s29, s34, s29
	global_load_dwordx4 v[6:9], v208, s[28:29]
	s_add_i32 s28, s2, 32
	s_mov_b32 s29, s3
	s_lshl_b64 s[28:29], s[28:29], 11
	s_add_u32 s28, s33, s28
	s_addc_u32 s29, s34, s29
	global_load_dwordx4 v[10:13], v208, s[28:29]
	s_add_i32 s28, s2, 48
	s_mov_b32 s29, s3
	s_lshl_b64 s[28:29], s[28:29], 11
	s_add_u32 s28, s33, s28
	s_addc_u32 s29, s34, s29
	s_add_i32 s1, s27, 0x8000
	global_load_dwordx4 v[14:17], v208, s[28:29]
	v_or_b32_e32 v21, 0x80, v18
	s_mov_b32 s28, m0
	s_mov_b32 m0, s1
	s_nop 0
	global_load_lds_dwordx4 v21, s[6:7]
	s_mov_b32 m0, s28
	s_add_i32 s1, s27, 0xa000
	v_or_b32_e32 v19, 0x80, v19
	s_mov_b32 s28, m0
	s_mov_b32 m0, s1
	s_nop 0
	global_load_lds_dwordx4 v19, s[6:7]
	s_mov_b32 m0, s28
	v_or_b32_e32 v18, 0x40080, v18
	s_add_i32 s1, s27, 0xc000
	s_mov_b32 s28, m0
	s_mov_b32 m0, s1
	s_nop 0
	global_load_lds_dwordx4 v18, s[6:7]
	s_mov_b32 m0, s28
	v_or_b32_e32 v18, 0x80, v20
	s_add_i32 s1, s27, 0xe000
	s_mov_b32 s28, m0
	s_mov_b32 m0, s1
	s_nop 0
	global_load_lds_dwordx4 v18, s[6:7]
	s_mov_b32 m0, s28
	s_add_i32 s28, s2, 64
	s_mov_b32 s29, s3
	s_waitcnt vmcnt(2)
	s_waitcnt vmcnt(4)
	s_lshl_b64 s[28:29], s[28:29], 11
	v_add_u32_e32 v18, 0, v154
	s_add_u32 s28, s33, s28
	v_add_u32_e32 v155, 0x18000, v18
	s_addc_u32 s29, s34, s29
	ds_write_b128 v155, v[2:5]
	ds_write_b128 v155, v[6:9] offset:8192
	ds_write_b128 v155, v[10:13] offset:16384
	ds_write_b128 v155, v[14:17] offset:24576
	global_load_dwordx4 v[14:17], v208, s[28:29]
	s_add_i32 s28, s2, 0x50
	s_mov_b32 s29, s3
	s_lshl_b64 s[28:29], s[28:29], 11
	s_add_u32 s28, s33, s28
	s_addc_u32 s29, s34, s29
	global_load_dwordx4 v[10:13], v208, s[28:29]
	s_add_i32 s28, s2, 0x60
	s_mov_b32 s29, s3
	s_lshl_b64 s[28:29], s[28:29], 11
	s_add_u32 s28, s33, s28
	s_addc_u32 s29, s34, s29
	s_addk_i32 s2, 0x70
	global_load_dwordx4 v[6:9], v208, s[28:29]
	s_lshl_b64 s[28:29], s[2:3], 11
	s_add_u32 s28, s33, s28
	s_addc_u32 s29, s34, s29
	s_lshl_b64 s[0:1], s[0:1], 6
	s_and_b32 s1, s1, 63
	s_and_b32 s0, s0, 0xfffff000
	s_add_u32 s2, s33, s0
	global_load_dwordx4 v[2:5], v208, s[28:29]
	s_addc_u32 s28, s34, s1
	s_lshl_b32 s0, s30, 19
	s_and_b32 s0, s0, 0xffc00000
	s_waitcnt lgkmcnt(0)
	s_barrier
	v_lshl_or_b32 v18, v159, 11, s0
	v_lshl_or_b32 v18, s31, 19, v18
	v_bitop3_b32 v152, s24, v212, v207 bitop3:0xde
	v_or_b32_e32 v150, v34, v209
	v_or_b32_e32 v153, v34, v206
	v_add_u32_e32 v156, v213, v18
	s_mov_b64 s[0:1], 0
	s_mov_b32 s29, 0x8000
	s_mov_b32 s30, 0
	s_mov_b32 s31, 0x10000
	v_mov_b32_e32 v18, v147
	v_mov_b32_e32 v19, v147
	v_mov_b32_e32 v20, v147
	v_mov_b32_e32 v21, v147
	v_mov_b32_e32 v22, v147
	v_mov_b32_e32 v23, v147
	v_mov_b32_e32 v24, v147
	v_mov_b32_e32 v25, v147
	v_mov_b32_e32 v26, v147
	v_mov_b32_e32 v27, v147
	v_mov_b32_e32 v28, v147
	v_mov_b32_e32 v29, v147
	v_mov_b32_e32 v30, v147
	v_mov_b32_e32 v31, v147
	v_mov_b32_e32 v32, v147
	v_mov_b32_e32 v33, v147
	v_mov_b32_e32 v34, v147
	v_mov_b32_e32 v35, v147
	v_mov_b32_e32 v36, v147
	v_mov_b32_e32 v37, v147
	s_waitcnt vmcnt(1)
	v_mov_b32_e32 v38, v147
	v_mov_b32_e32 v39, v147
	v_mov_b32_e32 v40, v147
	v_mov_b32_e32 v41, v147
	s_waitcnt vmcnt(0)
	v_mov_b32_e32 v42, v147
	v_mov_b32_e32 v43, v147
	v_mov_b32_e32 v44, v147
	v_mov_b32_e32 v45, v147
	v_mov_b32_e32 v54, v147
	v_mov_b32_e32 v55, v147
	v_mov_b32_e32 v56, v147
	v_mov_b32_e32 v57, v147
	v_mov_b32_e32 v66, v147
	v_mov_b32_e32 v67, v147
	v_mov_b32_e32 v68, v147
	v_mov_b32_e32 v69, v147
	v_mov_b32_e32 v78, v147
	v_mov_b32_e32 v79, v147
	v_mov_b32_e32 v80, v147
	v_mov_b32_e32 v81, v147
	v_mov_b32_e32 v90, v147
	v_mov_b32_e32 v91, v147
	v_mov_b32_e32 v92, v147
	v_mov_b32_e32 v93, v147
	v_mov_b32_e32 v94, v147
	v_mov_b32_e32 v95, v147
	v_mov_b32_e32 v96, v147
	v_mov_b32_e32 v97, v147
	v_mov_b32_e32 v114, v147
	v_mov_b32_e32 v115, v147
	v_mov_b32_e32 v116, v147
	v_mov_b32_e32 v117, v147
	v_mov_b32_e32 v122, v147
	v_mov_b32_e32 v123, v147
	v_mov_b32_e32 v124, v147
	v_mov_b32_e32 v125, v147
	v_mov_b32_e32 v138, v147
	v_mov_b32_e32 v139, v147
	v_mov_b32_e32 v140, v147
	v_mov_b32_e32 v141, v147
	v_mov_b32_e32 v142, v147
	v_mov_b32_e32 v143, v147
	v_mov_b32_e32 v144, v147
	v_mov_b32_e32 v145, v147
	v_mov_b32_e32 v118, v147
	v_mov_b32_e32 v119, v147
	v_mov_b32_e32 v120, v147
	v_mov_b32_e32 v121, v147
	v_mov_b32_e32 v126, v147
	v_mov_b32_e32 v127, v147
	v_mov_b32_e32 v128, v147
	v_mov_b32_e32 v129, v147
	v_mov_b32_e32 v134, v147
	v_mov_b32_e32 v135, v147
	v_mov_b32_e32 v136, v147
	v_mov_b32_e32 v137, v147
	v_mov_b32_e32 v130, v147
	v_mov_b32_e32 v131, v147
	v_mov_b32_e32 v132, v147
	v_mov_b32_e32 v133, v147
	v_mov_b32_e32 v98, v147
	v_mov_b32_e32 v99, v147
	v_mov_b32_e32 v100, v147
	v_mov_b32_e32 v101, v147
	v_mov_b32_e32 v102, v147
	v_mov_b32_e32 v103, v147
	v_mov_b32_e32 v104, v147
	v_mov_b32_e32 v105, v147
	v_mov_b32_e32 v110, v147
	v_mov_b32_e32 v111, v147
	v_mov_b32_e32 v112, v147
	v_mov_b32_e32 v113, v147
	v_mov_b32_e32 v106, v147
	v_mov_b32_e32 v107, v147
	v_mov_b32_e32 v108, v147
	v_mov_b32_e32 v109, v147
	v_mov_b32_e32 v70, v147
	v_mov_b32_e32 v71, v147
	v_mov_b32_e32 v72, v147
	v_mov_b32_e32 v73, v147
	v_mov_b32_e32 v82, v147
	v_mov_b32_e32 v83, v147
	v_mov_b32_e32 v84, v147
	v_mov_b32_e32 v85, v147
	v_mov_b32_e32 v86, v147
	v_mov_b32_e32 v87, v147
	v_mov_b32_e32 v88, v147
	v_mov_b32_e32 v89, v147
	v_mov_b32_e32 v74, v147
	v_mov_b32_e32 v75, v147
	v_mov_b32_e32 v76, v147
	v_mov_b32_e32 v77, v147
	v_mov_b32_e32 v46, v147
	v_mov_b32_e32 v47, v147
	v_mov_b32_e32 v48, v147
	v_mov_b32_e32 v49, v147
	v_mov_b32_e32 v58, v147
	v_mov_b32_e32 v59, v147
	v_mov_b32_e32 v60, v147
	v_mov_b32_e32 v61, v147
	v_mov_b32_e32 v62, v147
	v_mov_b32_e32 v63, v147
	v_mov_b32_e32 v64, v147
	v_mov_b32_e32 v65, v147
	v_mov_b32_e32 v50, v147
	v_mov_b32_e32 v51, v147
	v_mov_b32_e32 v52, v147
	v_mov_b32_e32 v53, v147
	s_cmp_lt_u32 s80, 4
	s_cbranch_scc1 .Lprio_gl
	s_setprio 1
.Lprio_gl:
.LBB0_1039:
	s_add_i32 s34, s29, 0xffff8000
	s_and_b32 s34, s34, 0x8000
	s_add_i32 s34, s34, 0
	s_add_i32 s33, s30, 0
	s_add_i32 s34, s34, 0x18000
	v_add_u32_e32 v157, s34, v152
	v_add_u32_e32 v169, s33, v150
	v_add_u32_e32 v200, s34, v149
	v_add_u32_e32 v168, s34, v151
.Lrot_gl:
	ds_read_b64_tr_b16 v[160:161], v157
	ds_read_b64_tr_b16 v[162:163], v157 offset:2048
	ds_read_b64_tr_b16 v[164:165], v168
	ds_read_b64_tr_b16 v[166:167], v168 offset:2048
	ds_read_b128 v[172:175], v169
	ds_read_b128 v[176:179], v169 offset:2048
	ds_read_b64_tr_b16 v[180:181], v200
	ds_read_b64_tr_b16 v[182:183], v200 offset:2048
	v_add_u32_e32 v201, s34, v148
	ds_read_b64_tr_b16 v[184:185], v201
	ds_read_b64_tr_b16 v[186:187], v201 offset:2048
	ds_read_b128 v[188:191], v169 offset:4096
	s_waitcnt lgkmcnt(6)
	v_mfma_f32_16x16x32_bf16 v[18:21], v[160:163], v[172:175], v[18:21]
	v_add_u32_e32 v192, 0xfffa0000, v156
	s_add_i32 s34, s27, s31
	s_mov_b32 s35, m0
	s_mov_b32 m0, s34
	s_nop 0
	global_load_lds_dwordx4 v192, s[6:7]
	s_mov_b32 m0, s35
	v_mfma_f32_16x16x32_bf16 v[22:25], v[164:167], v[172:175], v[22:25]
	s_waitcnt lgkmcnt(3)
	v_mfma_f32_16x16x32_bf16 v[26:29], v[180:183], v[172:175], v[26:29]
	s_waitcnt lgkmcnt(1)
	v_mfma_f32_16x16x32_bf16 v[30:33], v[184:187], v[172:175], v[30:33]
	v_mfma_f32_16x16x32_bf16 v[34:37], v[160:163], v[176:179], v[34:37]
	ds_read_b128 v[172:175], v169 offset:6144
	v_add_u32_e32 v192, 0xfffc0000, v156
	s_add_i32 s35, s34, 0x2000
	v_mfma_f32_16x16x32_bf16 v[38:41], v[164:167], v[176:179], v[38:41]
	s_mov_b32 s36, m0
	s_mov_b32 m0, s35
	s_nop 0
	global_load_lds_dwordx4 v192, s[6:7]
	s_mov_b32 m0, s36
	v_mfma_f32_16x16x32_bf16 v[42:45], v[180:183], v[176:179], v[42:45]
	v_mfma_f32_16x16x32_bf16 v[54:57], v[184:187], v[176:179], v[54:57]
	s_waitcnt lgkmcnt(1)
	v_mfma_f32_16x16x32_bf16 v[66:69], v[160:163], v[188:191], v[66:69]
	ds_read_b128 v[176:179], v169 offset:8192
	v_add_u32_e32 v192, 0xfffe0000, v156
	s_add_i32 s35, s34, 0x4000
	v_mfma_f32_16x16x32_bf16 v[78:81], v[164:167], v[188:191], v[78:81]
	s_mov_b32 s36, m0
	s_mov_b32 m0, s35
	s_nop 0
	global_load_lds_dwordx4 v192, s[6:7]
	s_mov_b32 m0, s36
	v_mfma_f32_16x16x32_bf16 v[90:93], v[180:183], v[188:191], v[90:93]
	v_mfma_f32_16x16x32_bf16 v[94:97], v[184:187], v[188:191], v[94:97]
	s_waitcnt lgkmcnt(1)
	v_mfma_f32_16x16x32_bf16 v[114:117], v[160:163], v[172:175], v[114:117]
	ds_read_b128 v[188:191], v169 offset:10240
	s_addk_i32 s34, 0x6000
	s_mov_b32 s35, m0
	s_mov_b32 m0, s34
	s_nop 0
	global_load_lds_dwordx4 v156, s[6:7]
	s_mov_b32 m0, s35
	v_mfma_f32_16x16x32_bf16 v[122:125], v[164:167], v[172:175], v[122:125]
	v_mfma_f32_16x16x32_bf16 v[138:141], v[180:183], v[172:175], v[138:141]
	v_mfma_f32_16x16x32_bf16 v[142:145], v[184:187], v[172:175], v[142:145]
	ds_read_b128 v[172:175], v169 offset:12288
	ds_read_b64_tr_b16 v[192:193], v157 offset:16384
	ds_read_b64_tr_b16 v[194:195], v157 offset:18432
	s_waitcnt lgkmcnt(4)
	v_mfma_f32_16x16x32_bf16 v[118:121], v[160:163], v[176:179], v[118:121]
	v_mfma_f32_16x16x32_bf16 v[126:129], v[164:167], v[176:179], v[126:129]
	v_mfma_f32_16x16x32_bf16 v[134:137], v[180:183], v[176:179], v[134:137]
	v_mfma_f32_16x16x32_bf16 v[130:133], v[184:187], v[176:179], v[130:133]
	ds_read_b128 v[176:179], v169 offset:14336
	ds_read_b64_tr_b16 v[196:197], v168 offset:16384
	ds_read_b64_tr_b16 v[198:199], v168 offset:18432
	s_waitcnt lgkmcnt(6)
	v_mfma_f32_16x16x32_bf16 v[98:101], v[160:163], v[188:191], v[98:101]
	v_mfma_f32_16x16x32_bf16 v[102:105], v[164:167], v[188:191], v[102:105]
	v_mfma_f32_16x16x32_bf16 v[110:113], v[180:183], v[188:191], v[110:113]
	v_mfma_f32_16x16x32_bf16 v[106:109], v[184:187], v[188:191], v[106:109]
	v_add_u32_e32 v157, s33, v153
	ds_read_b128 v[188:191], v157
	ds_read_b64_tr_b16 v[216:217], v200 offset:16384
	ds_read_b64_tr_b16 v[218:219], v200 offset:18432
	s_waitcnt lgkmcnt(8)
	v_mfma_f32_16x16x32_bf16 v[70:73], v[160:163], v[172:175], v[70:73]
	v_mfma_f32_16x16x32_bf16 v[82:85], v[164:167], v[172:175], v[82:85]
	v_mfma_f32_16x16x32_bf16 v[86:89], v[180:183], v[172:175], v[86:89]
	v_mfma_f32_16x16x32_bf16 v[74:77], v[184:187], v[172:175], v[74:77]
	s_waitcnt lgkmcnt(5)
	v_mfma_f32_16x16x32_bf16 v[46:49], v[160:163], v[176:179], v[46:49]
	ds_read_b128 v[160:163], v157 offset:2048
	s_and_b32 s33, s29, 0x8000
	v_mfma_f32_16x16x32_bf16 v[58:61], v[164:167], v[176:179], v[58:61]
	ds_read_b64_tr_b16 v[164:165], v201 offset:16384
	ds_read_b64_tr_b16 v[166:167], v201 offset:18432
	v_mfma_f32_16x16x32_bf16 v[62:65], v[180:183], v[176:179], v[62:65]
	v_mfma_f32_16x16x32_bf16 v[50:53], v[184:187], v[176:179], v[50:53]
	s_waitcnt lgkmcnt(5)
	v_mfma_f32_16x16x32_bf16 v[18:21], v[192:195], v[188:191], v[18:21]
	ds_read_b128 v[172:175], v157 offset:4096
	v_add_u32_e32 v168, s33, v155
	s_add_u32 s33, s2, s0
	v_mfma_f32_16x16x32_bf16 v[22:25], v[196:199], v[188:191], v[22:25]
	s_addc_u32 s36, s28, s1
	s_waitcnt vmcnt(7)
	s_add_u32 s34, s33, 0x40000
	s_waitcnt lgkmcnt(4)
	v_mfma_f32_16x16x32_bf16 v[26:29], v[216:219], v[188:191], v[26:29]
	ds_write_b128 v168, v[14:17]
	s_addc_u32 s35, s36, 0
	global_load_dwordx4 v[14:17], v208, s[34:35]
	s_waitcnt lgkmcnt(2)
	v_mfma_f32_16x16x32_bf16 v[30:33], v[164:167], v[188:191], v[30:33]
	v_mfma_f32_16x16x32_bf16 v[34:37], v[192:195], v[160:163], v[34:37]
	ds_read_b128 v[176:179], v157 offset:6144
	s_waitcnt vmcnt(7)
	s_add_u32 s34, s33, 0x48000
	v_mfma_f32_16x16x32_bf16 v[38:41], v[196:199], v[160:163], v[38:41]
	ds_write_b128 v168, v[10:13] offset:8192
	s_addc_u32 s35, s36, 0
	global_load_dwordx4 v[10:13], v208, s[34:35]
	v_mfma_f32_16x16x32_bf16 v[42:45], v[216:219], v[160:163], v[42:45]
	v_mfma_f32_16x16x32_bf16 v[54:57], v[164:167], v[160:163], v[54:57]
	s_waitcnt lgkmcnt(3)
	v_mfma_f32_16x16x32_bf16 v[66:69], v[192:195], v[172:175], v[66:69]
	ds_read_b128 v[160:163], v157 offset:8192
	s_waitcnt vmcnt(7)
	s_add_u32 s34, s33, 0x50000
	v_mfma_f32_16x16x32_bf16 v[78:81], v[196:199], v[172:175], v[78:81]
	ds_write_b128 v168, v[6:9] offset:16384
	s_addc_u32 s35, s36, 0
	global_load_dwordx4 v[6:9], v208, s[34:35]
	v_mfma_f32_16x16x32_bf16 v[90:93], v[216:219], v[172:175], v[90:93]
	v_mfma_f32_16x16x32_bf16 v[94:97], v[164:167], v[172:175], v[94:97]
	s_waitcnt lgkmcnt(3)
	v_mfma_f32_16x16x32_bf16 v[114:117], v[192:195], v[176:179], v[114:117]
	ds_read_b128 v[172:175], v157 offset:10240
	s_waitcnt vmcnt(7)
	s_add_u32 s34, s33, 0x58000
	v_mfma_f32_16x16x32_bf16 v[122:125], v[196:199], v[176:179], v[122:125]
	ds_write_b128 v168, v[2:5] offset:24576
	s_addc_u32 s35, s36, 0
	global_load_dwordx4 v[2:5], v208, s[34:35]
	v_mfma_f32_16x16x32_bf16 v[138:141], v[216:219], v[176:179], v[138:141]
	v_mfma_f32_16x16x32_bf16 v[142:145], v[164:167], v[176:179], v[142:145]
	s_waitcnt lgkmcnt(3)
	v_mfma_f32_16x16x32_bf16 v[118:121], v[192:195], v[160:163], v[118:121]
	ds_read_b128 v[176:179], v157 offset:12288
	v_mfma_f32_16x16x32_bf16 v[126:129], v[196:199], v[160:163], v[126:129]
	v_mfma_f32_16x16x32_bf16 v[134:137], v[216:219], v[160:163], v[134:137]
	v_mfma_f32_16x16x32_bf16 v[130:133], v[164:167], v[160:163], v[130:133]
	s_waitcnt lgkmcnt(2)
	v_mfma_f32_16x16x32_bf16 v[98:101], v[192:195], v[172:175], v[98:101]
	ds_read_b128 v[160:163], v157 offset:14336
	v_mfma_f32_16x16x32_bf16 v[102:105], v[196:199], v[172:175], v[102:105]
	v_mfma_f32_16x16x32_bf16 v[110:113], v[216:219], v[172:175], v[110:113]
	v_mfma_f32_16x16x32_bf16 v[106:109], v[164:167], v[172:175], v[106:109]
	s_waitcnt lgkmcnt(1)
	v_mfma_f32_16x16x32_bf16 v[70:73], v[192:195], v[176:179], v[70:73]
	v_mfma_f32_16x16x32_bf16 v[82:85], v[196:199], v[176:179], v[82:85]
	v_mfma_f32_16x16x32_bf16 v[86:89], v[216:219], v[176:179], v[86:89]
	v_mfma_f32_16x16x32_bf16 v[74:77], v[164:167], v[176:179], v[74:77]
	s_waitcnt lgkmcnt(0)
	v_mfma_f32_16x16x32_bf16 v[46:49], v[192:195], v[160:163], v[46:49]
	v_mfma_f32_16x16x32_bf16 v[58:61], v[196:199], v[160:163], v[58:61]
	v_mfma_f32_16x16x32_bf16 v[62:65], v[216:219], v[160:163], v[62:65]
	v_mfma_f32_16x16x32_bf16 v[50:53], v[164:167], v[160:163], v[50:53]
	s_add_i32 s33, s30, 0x8000
	s_cmp_lg_u32 s30, 0x10000
	s_cselect_b32 s30, s33, 0
	s_add_i32 s33, s31, 0x8000
	s_cmp_lg_u32 s31, 0x10000
	s_cselect_b32 s31, s33, 0
	s_add_u32 s0, s0, 0x20000
	s_addc_u32 s1, s1, 0
	s_add_i32 s29, s29, 0x8000
	v_add_u32_e32 v156, 0x80, v156
	s_add_i32 s34, s29, 0xffff8000
	s_and_b32 s34, s34, 0x8000
	s_add_i32 s34, s34, 0
	s_add_i32 s33, s30, 0
	s_add_i32 s34, s34, 0x18000
	v_add_u32_e32 v157, s34, v152
	v_add_u32_e32 v169, s33, v150
	v_add_u32_e32 v200, s34, v149
	v_add_u32_e32 v168, s34, v151
	s_waitcnt lgkmcnt(0)
	s_barrier
	s_cmp_lg_u32 s0, 0x1c0000
	s_cbranch_scc1 .Lrot_gl
	s_setprio 0
	s_add_i32 s0, 0, 0x18000
	s_add_i32 s1, 0, 0x10000
	v_add_u32_e32 v155, s0, v152
	v_add_u32_e32 v157, s1, v150
	v_add_u32_e32 v168, s0, v149
	v_add_u32_e32 v169, s0, v148
	v_add_u32_e32 v156, s0, v151
	ds_read_b64_tr_b16 v[160:161], v155
	ds_read_b64_tr_b16 v[162:163], v155 offset:2048
	ds_read_b64_tr_b16 v[164:165], v156
	ds_read_b64_tr_b16 v[166:167], v156 offset:2048
	ds_read_b128 v[172:175], v157
	ds_read_b128 v[176:179], v157 offset:2048
	ds_read_b64_tr_b16 v[180:181], v168
	ds_read_b64_tr_b16 v[182:183], v168 offset:2048
	ds_read_b64_tr_b16 v[184:185], v169
	ds_read_b64_tr_b16 v[186:187], v169 offset:2048
	ds_read_b128 v[188:191], v157 offset:4096
	s_waitcnt lgkmcnt(6)
	v_mfma_f32_16x16x32_bf16 v[18:21], v[160:163], v[172:175], v[18:21]
	v_mfma_f32_16x16x32_bf16 v[22:25], v[164:167], v[172:175], v[22:25]
	s_waitcnt lgkmcnt(3)
	v_mfma_f32_16x16x32_bf16 v[26:29], v[180:183], v[172:175], v[26:29]
	s_waitcnt lgkmcnt(1)
	v_mfma_f32_16x16x32_bf16 v[30:33], v[184:187], v[172:175], v[30:33]
	ds_read_b128 v[172:175], v157 offset:6144
	v_mfma_f32_16x16x32_bf16 v[34:37], v[160:163], v[176:179], v[34:37]
	v_mfma_f32_16x16x32_bf16 v[38:41], v[164:167], v[176:179], v[38:41]
	v_mfma_f32_16x16x32_bf16 v[42:45], v[180:183], v[176:179], v[42:45]
	v_mfma_f32_16x16x32_bf16 v[54:57], v[184:187], v[176:179], v[54:57]
	ds_read_b128 v[176:179], v157 offset:8192
	s_waitcnt lgkmcnt(2)
	v_mfma_f32_16x16x32_bf16 v[66:69], v[160:163], v[188:191], v[66:69]
	v_mfma_f32_16x16x32_bf16 v[78:81], v[164:167], v[188:191], v[78:81]
	v_mfma_f32_16x16x32_bf16 v[90:93], v[180:183], v[188:191], v[90:93]
	v_mfma_f32_16x16x32_bf16 v[94:97], v[184:187], v[188:191], v[94:97]
	ds_read_b128 v[188:191], v157 offset:10240
	s_waitcnt lgkmcnt(2)
	v_mfma_f32_16x16x32_bf16 v[114:117], v[160:163], v[172:175], v[114:117]
	v_mfma_f32_16x16x32_bf16 v[122:125], v[164:167], v[172:175], v[122:125]
	v_mfma_f32_16x16x32_bf16 v[138:141], v[180:183], v[172:175], v[138:141]
	v_mfma_f32_16x16x32_bf16 v[142:145], v[184:187], v[172:175], v[142:145]
	ds_read_b128 v[172:175], v157 offset:12288
	ds_read_b64_tr_b16 v[192:193], v155 offset:16384
	ds_read_b64_tr_b16 v[194:195], v155 offset:18432
	s_waitcnt lgkmcnt(4)
	v_mfma_f32_16x16x32_bf16 v[118:121], v[160:163], v[176:179], v[118:121]
	v_mfma_f32_16x16x32_bf16 v[126:129], v[164:167], v[176:179], v[126:129]
	v_mfma_f32_16x16x32_bf16 v[134:137], v[180:183], v[176:179], v[134:137]
	v_mfma_f32_16x16x32_bf16 v[130:133], v[184:187], v[176:179], v[130:133]
	ds_read_b128 v[176:179], v157 offset:14336
	ds_read_b64_tr_b16 v[196:197], v156 offset:16384
	ds_read_b64_tr_b16 v[198:199], v156 offset:18432
	s_waitcnt lgkmcnt(6)
	v_mfma_f32_16x16x32_bf16 v[98:101], v[160:163], v[188:191], v[98:101]
	v_mfma_f32_16x16x32_bf16 v[102:105], v[164:167], v[188:191], v[102:105]
	v_mfma_f32_16x16x32_bf16 v[110:113], v[180:183], v[188:191], v[110:113]
	v_mfma_f32_16x16x32_bf16 v[106:109], v[184:187], v[188:191], v[106:109]
	v_add_u32_e32 v155, s1, v153
	ds_read_b128 v[188:191], v155
	ds_read_b64_tr_b16 v[216:217], v168 offset:16384
	ds_read_b64_tr_b16 v[218:219], v168 offset:18432
	s_waitcnt lgkmcnt(8)
	v_mfma_f32_16x16x32_bf16 v[70:73], v[160:163], v[172:175], v[70:73]
	v_mfma_f32_16x16x32_bf16 v[82:85], v[164:167], v[172:175], v[82:85]
	v_mfma_f32_16x16x32_bf16 v[86:89], v[180:183], v[172:175], v[86:89]
	v_mfma_f32_16x16x32_bf16 v[74:77], v[184:187], v[172:175], v[74:77]
	s_waitcnt lgkmcnt(5)
	v_mfma_f32_16x16x32_bf16 v[46:49], v[160:163], v[176:179], v[46:49]
	v_mfma_f32_16x16x32_bf16 v[58:61], v[164:167], v[176:179], v[58:61]
	ds_read_b128 v[160:163], v155 offset:2048
	ds_read_b64_tr_b16 v[164:165], v169 offset:16384
	ds_read_b64_tr_b16 v[166:167], v169 offset:18432
	v_mfma_f32_16x16x32_bf16 v[62:65], v[180:183], v[176:179], v[62:65]
	v_mfma_f32_16x16x32_bf16 v[50:53], v[184:187], v[176:179], v[50:53]
	ds_read_b128 v[172:175], v155 offset:4096
	s_add_i32 s0, 0, 0x20000
	s_waitcnt vmcnt(3)
	v_add_u32_e32 v154, s0, v154
	s_waitcnt lgkmcnt(6)
	v_mfma_f32_16x16x32_bf16 v[18:21], v[192:195], v[188:191], v[18:21]
	ds_write_b128 v154, v[14:17]
	v_mfma_f32_16x16x32_bf16 v[22:25], v[196:199], v[188:191], v[22:25]
	s_waitcnt lgkmcnt(5)
	v_mfma_f32_16x16x32_bf16 v[26:29], v[216:219], v[188:191], v[26:29]
	s_waitcnt lgkmcnt(2)
	v_mfma_f32_16x16x32_bf16 v[14:17], v[164:167], v[188:191], v[30:33]
	v_mfma_f32_16x16x32_bf16 v[30:33], v[192:195], v[160:163], v[34:37]
	v_mfma_f32_16x16x32_bf16 v[34:37], v[196:199], v[160:163], v[38:41]
	v_mfma_f32_16x16x32_bf16 v[38:41], v[216:219], v[160:163], v[42:45]
	s_nop 2
	ds_read_b128 v[42:45], v155 offset:6144
	s_waitcnt vmcnt(2)
	ds_write_b128 v154, v[10:13] offset:8192
	v_mfma_f32_16x16x32_bf16 v[10:13], v[164:167], v[160:163], v[54:57]
	s_waitcnt lgkmcnt(3)
	v_mfma_f32_16x16x32_bf16 v[54:57], v[192:195], v[172:175], v[66:69]
	v_mfma_f32_16x16x32_bf16 v[66:69], v[196:199], v[172:175], v[78:81]
	v_mfma_f32_16x16x32_bf16 v[78:81], v[216:219], v[172:175], v[90:93]
	s_nop 2
	ds_read_b128 v[90:93], v155 offset:8192
	s_waitcnt vmcnt(1)
	ds_write_b128 v154, v[6:9] offset:16384
	v_mfma_f32_16x16x32_bf16 v[6:9], v[164:167], v[172:175], v[94:97]
	s_waitcnt lgkmcnt(3)
	v_mfma_f32_16x16x32_bf16 v[94:97], v[192:195], v[42:45], v[114:117]
	v_mfma_f32_16x16x32_bf16 v[114:117], v[196:199], v[42:45], v[122:125]
	v_mfma_f32_16x16x32_bf16 v[122:125], v[216:219], v[42:45], v[138:141]
	s_nop 2
	ds_read_b128 v[138:141], v155 offset:10240
	s_waitcnt vmcnt(0)
	ds_write_b128 v154, v[2:5] offset:24576
	v_mfma_f32_16x16x32_bf16 v[2:5], v[164:167], v[42:45], v[142:145]
	s_waitcnt lgkmcnt(3)
	v_mfma_f32_16x16x32_bf16 v[42:45], v[192:195], v[90:93], v[118:121]
	v_mfma_f32_16x16x32_bf16 v[118:121], v[196:199], v[90:93], v[126:129]
	v_mfma_f32_16x16x32_bf16 v[126:129], v[216:219], v[90:93], v[134:137]
	s_nop 2
	ds_read_b128 v[134:137], v155 offset:12288
	v_mfma_f32_16x16x32_bf16 v[90:93], v[164:167], v[90:93], v[130:133]
	s_nop 2
	ds_read_b128 v[130:133], v155 offset:14336
	s_waitcnt lgkmcnt(3)
	v_mfma_f32_16x16x32_bf16 v[98:101], v[192:195], v[138:141], v[98:101]
	v_mfma_f32_16x16x32_bf16 v[102:105], v[196:199], v[138:141], v[102:105]
	v_mfma_f32_16x16x32_bf16 v[110:113], v[216:219], v[138:141], v[110:113]
	v_mfma_f32_16x16x32_bf16 v[106:109], v[164:167], v[138:141], v[106:109]
	s_waitcnt lgkmcnt(1)
	v_mfma_f32_16x16x32_bf16 v[70:73], v[192:195], v[134:137], v[70:73]
	v_mfma_f32_16x16x32_bf16 v[82:85], v[196:199], v[134:137], v[82:85]
	v_mfma_f32_16x16x32_bf16 v[86:89], v[216:219], v[134:137], v[86:89]
	v_mfma_f32_16x16x32_bf16 v[74:77], v[164:167], v[134:137], v[74:77]
	s_waitcnt lgkmcnt(0)
	v_mfma_f32_16x16x32_bf16 v[46:49], v[192:195], v[130:133], v[46:49]
	v_mfma_f32_16x16x32_bf16 v[58:61], v[196:199], v[130:133], v[58:61]
	v_mfma_f32_16x16x32_bf16 v[62:65], v[216:219], v[130:133], v[62:65]
	v_mfma_f32_16x16x32_bf16 v[50:53], v[164:167], v[130:133], v[50:53]
	s_waitcnt lgkmcnt(0)
	s_barrier
	v_add_u32_e32 v152, s0, v152
	v_add_u32_e32 v169, 0, v150
	v_add_u32_e32 v200, s0, v149
	v_add_u32_e32 v201, s0, v148
	v_add_u32_e32 v168, s0, v151
	ds_read_b64_tr_b16 v[130:131], v152
	ds_read_b64_tr_b16 v[132:133], v152 offset:2048
	ds_read_b64_tr_b16 v[134:135], v168
	ds_read_b64_tr_b16 v[136:137], v168 offset:2048
	ds_read_b128 v[138:141], v169
	ds_read_b128 v[142:145], v169 offset:2048
	ds_read_b64_tr_b16 v[154:155], v200
	ds_read_b64_tr_b16 v[156:157], v200 offset:2048
	ds_read_b64_tr_b16 v[148:149], v201
	ds_read_b64_tr_b16 v[150:151], v201 offset:2048
	ds_read_b128 v[160:163], v169 offset:4096
	s_waitcnt lgkmcnt(6)
	v_mfma_f32_16x16x32_bf16 v[18:21], v[130:133], v[138:141], v[18:21]
	v_mfma_f32_16x16x32_bf16 v[22:25], v[134:137], v[138:141], v[22:25]
	s_waitcnt lgkmcnt(3)
	v_mfma_f32_16x16x32_bf16 v[26:29], v[154:157], v[138:141], v[26:29]
	s_waitcnt lgkmcnt(1)
	v_mfma_f32_16x16x32_bf16 v[14:17], v[148:151], v[138:141], v[14:17]
	ds_read_b128 v[138:141], v169 offset:6144
	v_mfma_f32_16x16x32_bf16 v[10:13], v[148:151], v[142:145], v[10:13]
	v_mfma_f32_16x16x32_bf16 v[30:33], v[130:133], v[142:145], v[30:33]
	v_mfma_f32_16x16x32_bf16 v[34:37], v[134:137], v[142:145], v[34:37]
	v_mfma_f32_16x16x32_bf16 v[38:41], v[154:157], v[142:145], v[38:41]
	ds_read_b128 v[142:145], v169 offset:8192
	s_waitcnt lgkmcnt(2)
	v_mfma_f32_16x16x32_bf16 v[6:9], v[148:151], v[160:163], v[6:9]
	v_mfma_f32_16x16x32_bf16 v[54:57], v[130:133], v[160:163], v[54:57]
	v_mfma_f32_16x16x32_bf16 v[66:69], v[134:137], v[160:163], v[66:69]
	v_mfma_f32_16x16x32_bf16 v[78:81], v[154:157], v[160:163], v[78:81]
	s_waitcnt lgkmcnt(1)
	v_mfma_f32_16x16x32_bf16 v[160:163], v[134:137], v[138:141], v[114:117]
	s_nop 2
	ds_read_b128 v[114:117], v169 offset:10240
	v_mfma_f32_16x16x32_bf16 v[2:5], v[148:151], v[138:141], v[2:5]
	v_mfma_f32_16x16x32_bf16 v[94:97], v[130:133], v[138:141], v[94:97]
	v_mfma_f32_16x16x32_bf16 v[164:167], v[154:157], v[138:141], v[122:125]
	s_waitcnt lgkmcnt(1)
	v_mfma_f32_16x16x32_bf16 v[138:141], v[134:137], v[142:145], v[118:121]
	s_nop 2
	ds_read_b128 v[118:121], v169 offset:12288
	ds_read_b64_tr_b16 v[176:177], v152 offset:16384
	ds_read_b64_tr_b16 v[178:179], v152 offset:18432
	v_mfma_f32_16x16x32_bf16 v[42:45], v[130:133], v[142:145], v[42:45]
	v_mfma_f32_16x16x32_bf16 v[172:175], v[154:157], v[142:145], v[126:129]
	v_mfma_f32_16x16x32_bf16 v[142:145], v[148:151], v[142:145], v[90:93]
	s_nop 2
	ds_read_b128 v[90:93], v169 offset:14336
	ds_read_b64_tr_b16 v[192:193], v168 offset:16384
	ds_read_b64_tr_b16 v[194:195], v168 offset:18432
	s_waitcnt lgkmcnt(6)
	v_mfma_f32_16x16x32_bf16 v[180:183], v[130:133], v[114:117], v[98:101]
	v_mfma_f32_16x16x32_bf16 v[184:187], v[134:137], v[114:117], v[102:105]
	v_mfma_f32_16x16x32_bf16 v[188:191], v[154:157], v[114:117], v[110:113]
	v_mfma_f32_16x16x32_bf16 v[196:199], v[148:151], v[114:117], v[106:109]
	v_add_u32_e32 v168, 0, v153
	s_waitcnt lgkmcnt(5)
	v_mfma_f32_16x16x32_bf16 v[216:219], v[130:133], v[118:121], v[70:73]
	s_nop 2
	ds_read_b128 v[70:73], v168
	ds_read_b64_tr_b16 v[228:229], v200 offset:16384
	ds_read_b64_tr_b16 v[230:231], v200 offset:18432
	v_mfma_f32_16x16x32_bf16 v[220:223], v[134:137], v[118:121], v[82:85]
	v_mfma_f32_16x16x32_bf16 v[224:227], v[154:157], v[118:121], v[86:89]
	v_mfma_f32_16x16x32_bf16 v[232:235], v[148:151], v[118:121], v[74:77]
	s_waitcnt lgkmcnt(5)
	v_mfma_f32_16x16x32_bf16 v[236:239], v[130:133], v[90:93], v[46:49]
	s_nop 2
	ds_read_b128 v[46:49], v168 offset:2048
	ds_read_b64_tr_b16 v[244:245], v201 offset:16384
	ds_read_b64_tr_b16 v[246:247], v201 offset:18432
	v_mfma_f32_16x16x32_bf16 v[240:243], v[134:137], v[90:93], v[58:61]
	v_mfma_f32_16x16x32_bf16 v[152:155], v[154:157], v[90:93], v[62:65]
	v_mfma_f32_16x16x32_bf16 v[148:151], v[148:151], v[90:93], v[50:53]
	s_waitcnt lgkmcnt(5)
	v_mfma_f32_16x16x32_bf16 v[248:251], v[176:179], v[70:73], v[18:21]
	s_nop 2
	ds_read_b128 v[18:21], v168 offset:4096
	v_mfma_f32_16x16x32_bf16 v[202:205], v[192:195], v[70:73], v[22:25]
	s_waitcnt lgkmcnt(4)
	v_mfma_f32_16x16x32_bf16 v[134:137], v[228:231], v[70:73], v[26:29]
	s_waitcnt lgkmcnt(1)
	v_mfma_f32_16x16x32_bf16 v[130:133], v[244:247], v[70:73], v[14:17]
	s_nop 2
	ds_read_b128 v[14:17], v168 offset:6144
	v_mfma_f32_16x16x32_bf16 v[126:129], v[176:179], v[46:49], v[30:33]
	v_mfma_f32_16x16x32_bf16 v[122:125], v[192:195], v[46:49], v[34:37]
	v_mfma_f32_16x16x32_bf16 v[118:121], v[228:231], v[46:49], v[38:41]
	v_mfma_f32_16x16x32_bf16 v[114:117], v[244:247], v[46:49], v[10:13]
	s_nop 2
	ds_read_b128 v[10:13], v168 offset:8192
	s_waitcnt lgkmcnt(2)
	v_mfma_f32_16x16x32_bf16 v[110:113], v[176:179], v[18:21], v[54:57]
	v_mfma_f32_16x16x32_bf16 v[106:109], v[192:195], v[18:21], v[66:69]
	v_mfma_f32_16x16x32_bf16 v[102:105], v[228:231], v[18:21], v[78:81]
	v_mfma_f32_16x16x32_bf16 v[98:101], v[244:247], v[18:21], v[6:9]
	s_nop 2
	ds_read_b128 v[6:9], v168 offset:10240
	s_waitcnt lgkmcnt(2)
	v_mfma_f32_16x16x32_bf16 v[94:97], v[176:179], v[14:17], v[94:97]
	v_mfma_f32_16x16x32_bf16 v[90:93], v[192:195], v[14:17], v[160:163]
	v_mfma_f32_16x16x32_bf16 v[86:89], v[228:231], v[14:17], v[164:167]
	v_mfma_f32_16x16x32_bf16 v[82:85], v[244:247], v[14:17], v[2:5]
	s_nop 2
	ds_read_b128 v[2:5], v168 offset:12288
	s_waitcnt lgkmcnt(2)
	v_mfma_f32_16x16x32_bf16 v[78:81], v[176:179], v[10:13], v[42:45]
	v_mfma_f32_16x16x32_bf16 v[74:77], v[192:195], v[10:13], v[138:141]
	v_mfma_f32_16x16x32_bf16 v[70:73], v[228:231], v[10:13], v[172:175]
	v_mfma_f32_16x16x32_bf16 v[66:69], v[244:247], v[10:13], v[142:145]
	ds_read_b128 v[14:17], v168 offset:14336
	s_waitcnt lgkmcnt(2)
	v_mfma_f32_16x16x32_bf16 v[62:65], v[176:179], v[6:9], v[180:183]
	v_mfma_f32_16x16x32_bf16 v[58:61], v[192:195], v[6:9], v[184:187]
	v_mfma_f32_16x16x32_bf16 v[54:57], v[228:231], v[6:9], v[188:191]
	v_mfma_f32_16x16x32_bf16 v[50:53], v[244:247], v[6:9], v[196:199]
	s_waitcnt lgkmcnt(1)
	v_mfma_f32_16x16x32_bf16 v[46:49], v[176:179], v[2:5], v[216:219]
	v_mfma_f32_16x16x32_bf16 v[42:45], v[192:195], v[2:5], v[220:223]
	v_mfma_f32_16x16x32_bf16 v[38:41], v[228:231], v[2:5], v[224:227]
	v_mfma_f32_16x16x32_bf16 v[34:37], v[244:247], v[2:5], v[232:235]
	s_waitcnt lgkmcnt(0)
	v_mfma_f32_16x16x32_bf16 v[10:13], v[228:231], v[14:17], v[152:155]
	v_mfma_f32_16x16x32_bf16 v[2:5], v[244:247], v[14:17], v[148:151]
	v_mfma_f32_16x16x32_bf16 v[26:29], v[176:179], v[14:17], v[236:239]
	v_mfma_f32_16x16x32_bf16 v[18:21], v[192:195], v[14:17], v[240:243]
	s_lshl_b32 s0, s26, 6
	v_mov_b32_e32 v144, v1
	v_mov_b32_e32 v145, v252
	s_or_b32 s0, s0, s22
	s_waitcnt lgkmcnt(0)
	s_barrier
	s_add_i32 s24, s24, 0
	v_lshl_add_u32 v6, v145, 2, s0
	s_add_i32 s0, s25, s21
	v_add_u32_e32 v138, s0, v144
	v_ashrrev_i32_e32 v139, 31, v138
	v_ashrrev_i32_e32 v7, 31, v6
	v_lshlrev_b64 v[8:9], 11, v[138:139]
	v_lshl_add_u64 v[8:9], s[6:7], 0, v[8:9]
	v_lshlrev_b64 v[140:141], 1, v[6:7]
	v_lshl_add_u64 v[142:143], v[8:9], 0, v[140:141]
	v_lshl_add_u64 v[6:7], v[6:7], 2, s[94:95]
	global_load_dwordx2 v[216:217], v[142:143], off
	global_load_dwordx4 v[30:33], v[6:7], off
	global_load_dwordx4 v[22:25], v[6:7], off offset:64
	global_load_dwordx4 v[14:17], v[6:7], off offset:128
	s_nop 0
	global_load_dwordx4 v[6:9], v[6:7], off offset:192
	s_nop 0
	global_load_dwordx2 v[218:219], v[142:143], off offset:32
	global_load_dwordx2 v[220:221], v[142:143], off offset:64
	global_load_dwordx2 v[200:201], v[142:143], off offset:96
	v_add_u32_e32 v142, 16, v138
	v_ashrrev_i32_e32 v143, 31, v142
	v_lshlrev_b64 v[142:143], 11, v[142:143]
	v_lshl_add_u64 v[142:143], s[6:7], 0, v[142:143]
	v_lshl_add_u64 v[142:143], v[142:143], 0, v[140:141]
	global_load_dwordx2 v[198:199], v[142:143], off
	global_load_dwordx2 v[196:197], v[142:143], off offset:32
	global_load_dwordx2 v[194:195], v[142:143], off offset:64
	global_load_dwordx2 v[192:193], v[142:143], off offset:96
	v_add_u32_e32 v142, 32, v138
	v_ashrrev_i32_e32 v143, 31, v142
	v_lshlrev_b64 v[142:143], 11, v[142:143]
	v_lshl_add_u64 v[142:143], s[6:7], 0, v[142:143]
	v_lshl_add_u64 v[142:143], v[142:143], 0, v[140:141]
	global_load_dwordx2 v[190:191], v[142:143], off
	global_load_dwordx2 v[188:189], v[142:143], off offset:32
	global_load_dwordx2 v[186:187], v[142:143], off offset:64
	global_load_dwordx2 v[184:185], v[142:143], off offset:96
	v_add_u32_e32 v142, 48, v138
	v_ashrrev_i32_e32 v143, 31, v142
	v_lshlrev_b64 v[142:143], 11, v[142:143]
	v_lshl_add_u64 v[142:143], s[6:7], 0, v[142:143]
	v_lshl_add_u64 v[142:143], v[142:143], 0, v[140:141]
	global_load_dwordx2 v[182:183], v[142:143], off
	global_load_dwordx2 v[180:181], v[142:143], off offset:32
	global_load_dwordx2 v[178:179], v[142:143], off offset:64
	global_load_dwordx2 v[176:177], v[142:143], off offset:96
	v_add_u32_e32 v142, 64, v138
	v_ashrrev_i32_e32 v143, 31, v142
	v_lshlrev_b64 v[142:143], 11, v[142:143]
	v_lshl_add_u64 v[142:143], s[6:7], 0, v[142:143]
	v_lshl_add_u64 v[142:143], v[142:143], 0, v[140:141]
	global_load_dwordx2 v[174:175], v[142:143], off
	global_load_dwordx2 v[172:173], v[142:143], off offset:32
	global_load_dwordx2 v[168:169], v[142:143], off offset:64
	global_load_dwordx2 v[166:167], v[142:143], off offset:96
	v_add_u32_e32 v142, 0x50, v138
	v_ashrrev_i32_e32 v143, 31, v142
	v_lshlrev_b64 v[142:143], 11, v[142:143]
	v_lshl_add_u64 v[142:143], s[6:7], 0, v[142:143]
	v_lshl_add_u64 v[142:143], v[142:143], 0, v[140:141]
	global_load_dwordx2 v[164:165], v[142:143], off
	global_load_dwordx2 v[162:163], v[142:143], off offset:32
	global_load_dwordx2 v[160:161], v[142:143], off offset:64
	global_load_dwordx2 v[156:157], v[142:143], off offset:96
	v_add_u32_e32 v215, s25, v144
	v_lshlrev_b32_e32 v222, 3, v145
	v_mul_lo_u32 v215, v215, s18
	v_add3_u32 v215, s24, v222, v215
	v_add_u32_e32 v142, 0x60, v138
	v_add_u32_e32 v138, 0x70, v138
	v_ashrrev_i32_e32 v143, 31, v142
	v_ashrrev_i32_e32 v139, 31, v138
	v_lshlrev_b64 v[142:143], 11, v[142:143]
	v_lshlrev_b64 v[138:139], 11, v[138:139]
	v_lshl_add_u64 v[142:143], s[6:7], 0, v[142:143]
	v_lshl_add_u64 v[138:139], s[6:7], 0, v[138:139]
	v_lshl_add_u64 v[142:143], v[142:143], 0, v[140:141]
	v_lshl_add_u64 v[138:139], v[138:139], 0, v[140:141]
	global_load_dwordx2 v[154:155], v[142:143], off
	global_load_dwordx2 v[152:153], v[142:143], off offset:32
	global_load_dwordx2 v[150:151], v[142:143], off offset:64
	global_load_dwordx2 v[148:149], v[142:143], off offset:96
	global_load_dwordx2 v[144:145], v[138:139], off
	s_nop 0
	global_load_dwordx2 v[142:143], v[138:139], off offset:32
	global_load_dwordx2 v[140:141], v[138:139], off offset:64
	s_nop 0
	global_load_dwordx2 v[138:139], v[138:139], off offset:96
	s_lshl_b32 s2, s22, 1
	s_waitcnt vmcnt(34)
	v_pk_add_f32 v[224:225], v[250:251], v[32:33]
	v_pk_add_f32 v[226:227], v[248:249], v[30:31]
	v_pk_mul_f32 v[224:225], v[224:225], s[14:15] op_sel_hi:[1,0]
	v_pk_mul_f32 v[226:227], v[226:227], s[14:15] op_sel_hi:[1,0]
	v_exp_f32_e32 v224, v224
	v_exp_f32_e32 v226, v226
	v_exp_f32_e32 v227, v227
	v_exp_f32_e32 v225, v225
	s_waitcnt vmcnt(33)
	v_pk_add_f32 v[202:203], v[202:203], v[22:23]
	v_pk_add_f32 v[204:205], v[204:205], v[24:25]
	v_pk_mul_f32 v[202:203], v[202:203], s[14:15] op_sel_hi:[1,0]
	v_pk_mul_f32 v[204:205], v[204:205], s[14:15] op_sel_hi:[1,0]
	v_exp_f32_e32 v202, v202
	v_exp_f32_e32 v203, v203
	v_exp_f32_e32 v204, v204
	v_exp_f32_e32 v205, v205
	v_pk_add_f32 v[226:227], v[226:227], 1.0 op_sel_hi:[1,0]
	v_pk_add_f32 v[224:225], v[224:225], 1.0 op_sel_hi:[1,0]
	s_waitcnt vmcnt(32)
	v_pk_add_f32 v[134:135], v[134:135], v[14:15]
	v_rcp_f32_e32 v226, v226
	v_rcp_f32_e32 v227, v227
	v_rcp_f32_e32 v224, v224
	v_rcp_f32_e32 v225, v225
	v_pk_add_f32 v[136:137], v[136:137], v[16:17]
	v_pk_mul_f32 v[134:135], v[134:135], s[14:15] op_sel_hi:[1,0]
	v_pk_add_f32 v[202:203], v[202:203], 1.0 op_sel_hi:[1,0]
	v_exp_f32_e32 v134, v134
	v_exp_f32_e32 v135, v135
	v_pk_mul_f32 v[136:137], v[136:137], s[14:15] op_sel_hi:[1,0]
	v_rcp_f32_e32 v202, v202
	v_rcp_f32_e32 v203, v203
	v_pk_add_f32 v[204:205], v[204:205], 1.0 op_sel_hi:[1,0]
	v_exp_f32_e32 v136, v136
	v_exp_f32_e32 v137, v137
	s_waitcnt vmcnt(31)
	v_pk_add_f32 v[130:131], v[130:131], v[6:7]
	v_lshlrev_b32_e32 v222, 16, v216
	v_and_b32_e32 v223, 0xffff0000, v216
	v_lshlrev_b32_e32 v216, 16, v217
	v_and_b32_e32 v217, 0xffff0000, v217
	v_rcp_f32_e32 v204, v204
	v_rcp_f32_e32 v205, v205
	v_pk_add_f32 v[132:133], v[132:133], v[8:9]
	v_pk_mul_f32 v[130:131], v[130:131], s[14:15] op_sel_hi:[1,0]
	v_pk_mul_f32 v[222:223], v[226:227], v[222:223]
	v_pk_mul_f32 v[216:217], v[224:225], v[216:217]
	v_exp_f32_e32 v130, v130
	v_exp_f32_e32 v131, v131
	v_pk_mul_f32 v[132:133], v[132:133], s[14:15] op_sel_hi:[1,0]
	v_cvt_pk_bf16_f32 v222, v222, v223
	v_cvt_pk_bf16_f32 v223, v216, v217
	s_waitcnt vmcnt(30)
	v_lshlrev_b32_e32 v216, 16, v218
	v_and_b32_e32 v217, 0xffff0000, v218
	v_pk_add_f32 v[134:135], v[134:135], 1.0 op_sel_hi:[1,0]
	v_exp_f32_e32 v132, v132
	v_exp_f32_e32 v133, v133
	v_pk_mul_f32 v[202:203], v[202:203], v[216:217]
	v_lshlrev_b32_e32 v216, 16, v219
	v_and_b32_e32 v217, 0xffff0000, v219
	v_rcp_f32_e32 v134, v134
	v_rcp_f32_e32 v135, v135
	v_pk_add_f32 v[136:137], v[136:137], 1.0 op_sel_hi:[1,0]
	v_pk_add_f32 v[126:127], v[126:127], v[30:31]
	v_pk_mul_f32 v[204:205], v[204:205], v[216:217]
	v_rcp_f32_e32 v136, v136
	v_rcp_f32_e32 v137, v137
	v_pk_add_f32 v[128:129], v[128:129], v[32:33]
	v_pk_mul_f32 v[126:127], v[126:127], s[14:15] op_sel_hi:[1,0]
	v_cvt_pk_bf16_f32 v202, v202, v203
	v_cvt_pk_bf16_f32 v203, v204, v205
	v_pk_add_f32 v[130:131], v[130:131], 1.0 op_sel_hi:[1,0]
	v_exp_f32_e32 v126, v126
	v_exp_f32_e32 v127, v127
	v_pk_mul_f32 v[128:129], v[128:129], s[14:15] op_sel_hi:[1,0]
	ds_write2_b64 v215, v[222:223], v[202:203] offset1:4
	s_waitcnt vmcnt(29)
	v_lshlrev_b32_e32 v202, 16, v220
	v_and_b32_e32 v203, 0xffff0000, v220
	v_rcp_f32_e32 v130, v130
	v_rcp_f32_e32 v131, v131
	v_pk_add_f32 v[132:133], v[132:133], 1.0 op_sel_hi:[1,0]
	v_exp_f32_e32 v128, v128
	v_exp_f32_e32 v129, v129
	v_pk_add_f32 v[122:123], v[122:123], v[22:23]
	v_pk_mul_f32 v[134:135], v[134:135], v[202:203]
	v_lshlrev_b32_e32 v202, 16, v221
	v_and_b32_e32 v203, 0xffff0000, v221
	v_rcp_f32_e32 v132, v132
	v_rcp_f32_e32 v133, v133
	v_pk_add_f32 v[124:125], v[124:125], v[24:25]
	v_pk_mul_f32 v[122:123], v[122:123], s[14:15] op_sel_hi:[1,0]
	v_pk_mul_f32 v[136:137], v[136:137], v[202:203]
	v_exp_f32_e32 v122, v122
	v_exp_f32_e32 v123, v123
	v_pk_mul_f32 v[124:125], v[124:125], s[14:15] op_sel_hi:[1,0]
	v_cvt_pk_bf16_f32 v134, v134, v135
	v_cvt_pk_bf16_f32 v135, v136, v137
	s_waitcnt vmcnt(28)
	v_lshlrev_b32_e32 v136, 16, v200
	v_and_b32_e32 v137, 0xffff0000, v200
	v_pk_add_f32 v[126:127], v[126:127], 1.0 op_sel_hi:[1,0]
	v_exp_f32_e32 v124, v124
	v_exp_f32_e32 v125, v125
	v_pk_mul_f32 v[130:131], v[130:131], v[136:137]
	v_lshlrev_b32_e32 v136, 16, v201
	v_and_b32_e32 v137, 0xffff0000, v201
	v_rcp_f32_e32 v126, v126
	v_rcp_f32_e32 v127, v127
	v_pk_add_f32 v[128:129], v[128:129], 1.0 op_sel_hi:[1,0]
	v_pk_add_f32 v[118:119], v[118:119], v[14:15]
	v_pk_mul_f32 v[132:133], v[132:133], v[136:137]
	v_rcp_f32_e32 v128, v128
	v_rcp_f32_e32 v129, v129
	v_pk_add_f32 v[120:121], v[120:121], v[16:17]
	v_pk_mul_f32 v[118:119], v[118:119], s[14:15] op_sel_hi:[1,0]
	v_cvt_pk_bf16_f32 v130, v130, v131
	v_cvt_pk_bf16_f32 v131, v132, v133
	v_pk_add_f32 v[122:123], v[122:123], 1.0 op_sel_hi:[1,0]
	v_exp_f32_e32 v118, v118
	v_exp_f32_e32 v119, v119
	v_pk_mul_f32 v[120:121], v[120:121], s[14:15] op_sel_hi:[1,0]
	ds_write2_b64 v215, v[134:135], v[130:131] offset0:8 offset1:12
	s_waitcnt vmcnt(27)
	v_lshlrev_b32_e32 v130, 16, v198
	v_and_b32_e32 v131, 0xffff0000, v198
	v_rcp_f32_e32 v122, v122
	v_rcp_f32_e32 v123, v123
	v_pk_add_f32 v[124:125], v[124:125], 1.0 op_sel_hi:[1,0]
	v_exp_f32_e32 v120, v120
	v_exp_f32_e32 v121, v121
	v_pk_add_f32 v[114:115], v[114:115], v[6:7]
	v_pk_mul_f32 v[126:127], v[126:127], v[130:131]
	v_lshlrev_b32_e32 v130, 16, v199
	v_and_b32_e32 v131, 0xffff0000, v199
	v_rcp_f32_e32 v124, v124
	v_rcp_f32_e32 v125, v125
	v_pk_add_f32 v[116:117], v[116:117], v[8:9]
	v_pk_mul_f32 v[114:115], v[114:115], s[14:15] op_sel_hi:[1,0]
	v_pk_mul_f32 v[128:129], v[128:129], v[130:131]
	v_exp_f32_e32 v114, v114
	v_exp_f32_e32 v115, v115
	v_pk_mul_f32 v[116:117], v[116:117], s[14:15] op_sel_hi:[1,0]
	v_cvt_pk_bf16_f32 v126, v126, v127
	v_cvt_pk_bf16_f32 v127, v128, v129
	s_waitcnt vmcnt(26)
	v_lshlrev_b32_e32 v128, 16, v196
	v_and_b32_e32 v129, 0xffff0000, v196
	v_pk_add_f32 v[118:119], v[118:119], 1.0 op_sel_hi:[1,0]
	v_exp_f32_e32 v116, v116
	v_exp_f32_e32 v117, v117
	v_pk_mul_f32 v[122:123], v[122:123], v[128:129]
	v_lshlrev_b32_e32 v128, 16, v197
	v_and_b32_e32 v129, 0xffff0000, v197
	v_rcp_f32_e32 v118, v118
	v_rcp_f32_e32 v119, v119
	v_pk_add_f32 v[120:121], v[120:121], 1.0 op_sel_hi:[1,0]
	v_pk_add_f32 v[110:111], v[110:111], v[30:31]
	v_pk_mul_f32 v[124:125], v[124:125], v[128:129]
	v_rcp_f32_e32 v120, v120
	v_rcp_f32_e32 v121, v121
	v_pk_add_f32 v[112:113], v[112:113], v[32:33]
	v_pk_mul_f32 v[110:111], v[110:111], s[14:15] op_sel_hi:[1,0]
	v_cvt_pk_bf16_f32 v122, v122, v123
	v_cvt_pk_bf16_f32 v123, v124, v125
	v_add_u32_e32 v124, 0x2000, v215
	v_pk_add_f32 v[114:115], v[114:115], 1.0 op_sel_hi:[1,0]
	v_exp_f32_e32 v110, v110
	v_exp_f32_e32 v111, v111
	v_pk_mul_f32 v[112:113], v[112:113], s[14:15] op_sel_hi:[1,0]
	ds_write2_b64 v124, v[126:127], v[122:123] offset0:32 offset1:36
	s_waitcnt vmcnt(25)
	v_lshlrev_b32_e32 v122, 16, v194
	v_and_b32_e32 v123, 0xffff0000, v194
	v_rcp_f32_e32 v114, v114
	v_rcp_f32_e32 v115, v115
	v_pk_add_f32 v[116:117], v[116:117], 1.0 op_sel_hi:[1,0]
	v_exp_f32_e32 v112, v112
	v_exp_f32_e32 v113, v113
	v_pk_add_f32 v[106:107], v[106:107], v[22:23]
	v_pk_mul_f32 v[118:119], v[118:119], v[122:123]
	v_lshlrev_b32_e32 v122, 16, v195
	v_and_b32_e32 v123, 0xffff0000, v195
	v_rcp_f32_e32 v116, v116
	v_rcp_f32_e32 v117, v117
	v_pk_add_f32 v[108:109], v[108:109], v[24:25]
	v_pk_mul_f32 v[106:107], v[106:107], s[14:15] op_sel_hi:[1,0]
	v_pk_mul_f32 v[120:121], v[120:121], v[122:123]
	v_exp_f32_e32 v106, v106
	v_exp_f32_e32 v107, v107
	v_pk_mul_f32 v[108:109], v[108:109], s[14:15] op_sel_hi:[1,0]
	v_cvt_pk_bf16_f32 v118, v118, v119
	v_cvt_pk_bf16_f32 v119, v120, v121
	s_waitcnt vmcnt(24)
	v_lshlrev_b32_e32 v120, 16, v192
	v_and_b32_e32 v121, 0xffff0000, v192
	v_pk_add_f32 v[110:111], v[110:111], 1.0 op_sel_hi:[1,0]
	v_exp_f32_e32 v108, v108
	v_exp_f32_e32 v109, v109
	v_pk_mul_f32 v[114:115], v[114:115], v[120:121]
	v_lshlrev_b32_e32 v120, 16, v193
	v_and_b32_e32 v121, 0xffff0000, v193
	v_rcp_f32_e32 v110, v110
	v_rcp_f32_e32 v111, v111
	v_pk_add_f32 v[112:113], v[112:113], 1.0 op_sel_hi:[1,0]
	v_pk_add_f32 v[102:103], v[102:103], v[14:15]
	v_pk_mul_f32 v[116:117], v[116:117], v[120:121]
	v_rcp_f32_e32 v112, v112
	v_rcp_f32_e32 v113, v113
	v_pk_add_f32 v[104:105], v[104:105], v[16:17]
	v_pk_mul_f32 v[102:103], v[102:103], s[14:15] op_sel_hi:[1,0]
	v_cvt_pk_bf16_f32 v114, v114, v115
	v_cvt_pk_bf16_f32 v115, v116, v117
	v_pk_add_f32 v[106:107], v[106:107], 1.0 op_sel_hi:[1,0]
	v_exp_f32_e32 v102, v102
	v_exp_f32_e32 v103, v103
	v_pk_mul_f32 v[104:105], v[104:105], s[14:15] op_sel_hi:[1,0]
	ds_write2_b64 v124, v[118:119], v[114:115] offset0:40 offset1:44
	s_waitcnt vmcnt(23)
	v_lshlrev_b32_e32 v114, 16, v190
	v_and_b32_e32 v115, 0xffff0000, v190
	v_rcp_f32_e32 v106, v106
	v_rcp_f32_e32 v107, v107
	v_pk_add_f32 v[108:109], v[108:109], 1.0 op_sel_hi:[1,0]
	v_exp_f32_e32 v104, v104
	v_exp_f32_e32 v105, v105
	v_pk_add_f32 v[98:99], v[98:99], v[6:7]
	v_pk_mul_f32 v[110:111], v[110:111], v[114:115]
	v_lshlrev_b32_e32 v114, 16, v191
	v_and_b32_e32 v115, 0xffff0000, v191
	v_rcp_f32_e32 v108, v108
	v_rcp_f32_e32 v109, v109
	v_pk_add_f32 v[100:101], v[100:101], v[8:9]
	v_pk_mul_f32 v[98:99], v[98:99], s[14:15] op_sel_hi:[1,0]
	v_pk_mul_f32 v[112:113], v[112:113], v[114:115]
	v_exp_f32_e32 v98, v98
	v_exp_f32_e32 v99, v99
	v_pk_mul_f32 v[100:101], v[100:101], s[14:15] op_sel_hi:[1,0]
	v_cvt_pk_bf16_f32 v110, v110, v111
	v_cvt_pk_bf16_f32 v111, v112, v113
	s_waitcnt vmcnt(22)
	v_lshlrev_b32_e32 v112, 16, v188
	v_and_b32_e32 v113, 0xffff0000, v188
	v_pk_add_f32 v[102:103], v[102:103], 1.0 op_sel_hi:[1,0]
	v_exp_f32_e32 v100, v100
	v_exp_f32_e32 v101, v101
	v_pk_mul_f32 v[106:107], v[106:107], v[112:113]
	v_lshlrev_b32_e32 v112, 16, v189
	v_and_b32_e32 v113, 0xffff0000, v189
	v_rcp_f32_e32 v102, v102
	v_rcp_f32_e32 v103, v103
	v_pk_add_f32 v[104:105], v[104:105], 1.0 op_sel_hi:[1,0]
	v_pk_add_f32 v[94:95], v[94:95], v[30:31]
	v_pk_mul_f32 v[108:109], v[108:109], v[112:113]
	v_rcp_f32_e32 v104, v104
	v_rcp_f32_e32 v105, v105
	v_pk_add_f32 v[96:97], v[96:97], v[32:33]
	v_pk_mul_f32 v[94:95], v[94:95], s[14:15] op_sel_hi:[1,0]
	v_cvt_pk_bf16_f32 v106, v106, v107
	v_cvt_pk_bf16_f32 v107, v108, v109
	v_add_u32_e32 v108, 0x4000, v215
	v_pk_add_f32 v[98:99], v[98:99], 1.0 op_sel_hi:[1,0]
	v_exp_f32_e32 v94, v94
	v_exp_f32_e32 v95, v95
	v_pk_mul_f32 v[96:97], v[96:97], s[14:15] op_sel_hi:[1,0]
	ds_write2_b64 v108, v[110:111], v[106:107] offset0:64 offset1:68
	s_waitcnt vmcnt(21)
	v_lshlrev_b32_e32 v106, 16, v186
	v_and_b32_e32 v107, 0xffff0000, v186
	v_rcp_f32_e32 v98, v98
	v_rcp_f32_e32 v99, v99
	v_pk_add_f32 v[100:101], v[100:101], 1.0 op_sel_hi:[1,0]
	v_exp_f32_e32 v96, v96
	v_exp_f32_e32 v97, v97
	v_pk_add_f32 v[90:91], v[90:91], v[22:23]
	v_pk_mul_f32 v[102:103], v[102:103], v[106:107]
	v_lshlrev_b32_e32 v106, 16, v187
	v_and_b32_e32 v107, 0xffff0000, v187
	v_rcp_f32_e32 v100, v100
	v_rcp_f32_e32 v101, v101
	v_pk_add_f32 v[92:93], v[92:93], v[24:25]
	v_pk_mul_f32 v[90:91], v[90:91], s[14:15] op_sel_hi:[1,0]
	v_pk_mul_f32 v[104:105], v[104:105], v[106:107]
	v_exp_f32_e32 v90, v90
	v_exp_f32_e32 v91, v91
	v_pk_mul_f32 v[92:93], v[92:93], s[14:15] op_sel_hi:[1,0]
	v_cvt_pk_bf16_f32 v102, v102, v103
	v_cvt_pk_bf16_f32 v103, v104, v105
	s_waitcnt vmcnt(20)
	v_lshlrev_b32_e32 v104, 16, v184
	v_and_b32_e32 v105, 0xffff0000, v184
	v_pk_add_f32 v[94:95], v[94:95], 1.0 op_sel_hi:[1,0]
	v_exp_f32_e32 v92, v92
	v_exp_f32_e32 v93, v93
	v_pk_mul_f32 v[98:99], v[98:99], v[104:105]
	v_lshlrev_b32_e32 v104, 16, v185
	v_and_b32_e32 v105, 0xffff0000, v185
	v_rcp_f32_e32 v94, v94
	v_rcp_f32_e32 v95, v95
	v_pk_add_f32 v[96:97], v[96:97], 1.0 op_sel_hi:[1,0]
	v_pk_add_f32 v[86:87], v[86:87], v[14:15]
	v_pk_mul_f32 v[100:101], v[100:101], v[104:105]
	v_rcp_f32_e32 v96, v96
	v_rcp_f32_e32 v97, v97
	v_pk_add_f32 v[88:89], v[88:89], v[16:17]
	v_pk_mul_f32 v[86:87], v[86:87], s[14:15] op_sel_hi:[1,0]
	v_cvt_pk_bf16_f32 v98, v98, v99
	v_cvt_pk_bf16_f32 v99, v100, v101
	v_pk_add_f32 v[90:91], v[90:91], 1.0 op_sel_hi:[1,0]
	v_exp_f32_e32 v86, v86
	v_exp_f32_e32 v87, v87
	v_pk_mul_f32 v[88:89], v[88:89], s[14:15] op_sel_hi:[1,0]
	ds_write2_b64 v108, v[102:103], v[98:99] offset0:72 offset1:76
	s_waitcnt vmcnt(19)
	v_lshlrev_b32_e32 v98, 16, v182
	v_and_b32_e32 v99, 0xffff0000, v182
	v_rcp_f32_e32 v90, v90
	v_rcp_f32_e32 v91, v91
	v_pk_add_f32 v[92:93], v[92:93], 1.0 op_sel_hi:[1,0]
	v_exp_f32_e32 v88, v88
	v_exp_f32_e32 v89, v89
	v_pk_add_f32 v[82:83], v[82:83], v[6:7]
	v_pk_mul_f32 v[94:95], v[94:95], v[98:99]
	v_lshlrev_b32_e32 v98, 16, v183
	v_and_b32_e32 v99, 0xffff0000, v183
	v_rcp_f32_e32 v92, v92
	v_rcp_f32_e32 v93, v93
	v_pk_add_f32 v[84:85], v[84:85], v[8:9]
	v_pk_mul_f32 v[82:83], v[82:83], s[14:15] op_sel_hi:[1,0]
	v_pk_mul_f32 v[96:97], v[96:97], v[98:99]
	v_exp_f32_e32 v82, v82
	v_exp_f32_e32 v83, v83
	v_pk_mul_f32 v[84:85], v[84:85], s[14:15] op_sel_hi:[1,0]
	v_cvt_pk_bf16_f32 v94, v94, v95
	v_cvt_pk_bf16_f32 v95, v96, v97
	s_waitcnt vmcnt(18)
	v_lshlrev_b32_e32 v96, 16, v180
	v_and_b32_e32 v97, 0xffff0000, v180
	v_pk_add_f32 v[86:87], v[86:87], 1.0 op_sel_hi:[1,0]
	v_exp_f32_e32 v84, v84
	v_exp_f32_e32 v85, v85
	v_pk_mul_f32 v[90:91], v[90:91], v[96:97]
	v_lshlrev_b32_e32 v96, 16, v181
	v_and_b32_e32 v97, 0xffff0000, v181
	v_rcp_f32_e32 v86, v86
	v_rcp_f32_e32 v87, v87
	v_pk_add_f32 v[88:89], v[88:89], 1.0 op_sel_hi:[1,0]
	v_pk_add_f32 v[78:79], v[78:79], v[30:31]
	v_pk_mul_f32 v[92:93], v[92:93], v[96:97]
	v_rcp_f32_e32 v88, v88
	v_rcp_f32_e32 v89, v89
	v_pk_add_f32 v[80:81], v[80:81], v[32:33]
	v_pk_mul_f32 v[78:79], v[78:79], s[14:15] op_sel_hi:[1,0]
	v_cvt_pk_bf16_f32 v90, v90, v91
	v_cvt_pk_bf16_f32 v91, v92, v93
	v_add_u32_e32 v92, 0x6000, v215
	v_pk_add_f32 v[82:83], v[82:83], 1.0 op_sel_hi:[1,0]
	v_exp_f32_e32 v78, v78
	v_exp_f32_e32 v79, v79
	v_pk_mul_f32 v[80:81], v[80:81], s[14:15] op_sel_hi:[1,0]
	ds_write2_b64 v92, v[94:95], v[90:91] offset0:96 offset1:100
	s_waitcnt vmcnt(17)
	v_lshlrev_b32_e32 v90, 16, v178
	v_and_b32_e32 v91, 0xffff0000, v178
	v_rcp_f32_e32 v82, v82
	v_rcp_f32_e32 v83, v83
	v_pk_add_f32 v[84:85], v[84:85], 1.0 op_sel_hi:[1,0]
	v_exp_f32_e32 v80, v80
	v_exp_f32_e32 v81, v81
	v_pk_add_f32 v[74:75], v[74:75], v[22:23]
	v_pk_mul_f32 v[86:87], v[86:87], v[90:91]
	v_lshlrev_b32_e32 v90, 16, v179
	v_and_b32_e32 v91, 0xffff0000, v179
	v_rcp_f32_e32 v84, v84
	v_rcp_f32_e32 v85, v85
	v_pk_add_f32 v[76:77], v[76:77], v[24:25]
	v_pk_mul_f32 v[74:75], v[74:75], s[14:15] op_sel_hi:[1,0]
	v_pk_mul_f32 v[88:89], v[88:89], v[90:91]
	v_exp_f32_e32 v74, v74
	v_exp_f32_e32 v75, v75
	v_pk_mul_f32 v[76:77], v[76:77], s[14:15] op_sel_hi:[1,0]
	v_cvt_pk_bf16_f32 v86, v86, v87
	v_cvt_pk_bf16_f32 v87, v88, v89
	s_waitcnt vmcnt(16)
	v_lshlrev_b32_e32 v88, 16, v176
	v_and_b32_e32 v89, 0xffff0000, v176
	v_pk_add_f32 v[78:79], v[78:79], 1.0 op_sel_hi:[1,0]
	v_exp_f32_e32 v76, v76
	v_exp_f32_e32 v77, v77
	v_pk_mul_f32 v[82:83], v[82:83], v[88:89]
	v_lshlrev_b32_e32 v88, 16, v177
	v_and_b32_e32 v89, 0xffff0000, v177
	v_rcp_f32_e32 v78, v78
	v_rcp_f32_e32 v79, v79
	v_pk_add_f32 v[80:81], v[80:81], 1.0 op_sel_hi:[1,0]
	v_pk_add_f32 v[70:71], v[70:71], v[14:15]
	v_pk_mul_f32 v[84:85], v[84:85], v[88:89]
	v_rcp_f32_e32 v80, v80
	v_rcp_f32_e32 v81, v81
	v_pk_add_f32 v[72:73], v[72:73], v[16:17]
	v_pk_mul_f32 v[70:71], v[70:71], s[14:15] op_sel_hi:[1,0]
	v_cvt_pk_bf16_f32 v82, v82, v83
	v_cvt_pk_bf16_f32 v83, v84, v85
	v_pk_add_f32 v[74:75], v[74:75], 1.0 op_sel_hi:[1,0]
	v_exp_f32_e32 v70, v70
	v_exp_f32_e32 v71, v71
	v_pk_mul_f32 v[72:73], v[72:73], s[14:15] op_sel_hi:[1,0]
	ds_write2_b64 v92, v[86:87], v[82:83] offset0:104 offset1:108
	s_waitcnt vmcnt(15)
	v_lshlrev_b32_e32 v82, 16, v174
	v_and_b32_e32 v83, 0xffff0000, v174
	v_rcp_f32_e32 v74, v74
	v_rcp_f32_e32 v75, v75
	v_pk_add_f32 v[76:77], v[76:77], 1.0 op_sel_hi:[1,0]
	v_exp_f32_e32 v72, v72
	v_exp_f32_e32 v73, v73
	v_pk_add_f32 v[66:67], v[66:67], v[6:7]
	v_pk_mul_f32 v[78:79], v[78:79], v[82:83]
	v_lshlrev_b32_e32 v82, 16, v175
	v_and_b32_e32 v83, 0xffff0000, v175
	v_rcp_f32_e32 v76, v76
	v_rcp_f32_e32 v77, v77
	v_pk_add_f32 v[68:69], v[68:69], v[8:9]
	v_pk_mul_f32 v[66:67], v[66:67], s[14:15] op_sel_hi:[1,0]
	v_pk_mul_f32 v[80:81], v[80:81], v[82:83]
	v_exp_f32_e32 v66, v66
	v_exp_f32_e32 v67, v67
	v_pk_mul_f32 v[68:69], v[68:69], s[14:15] op_sel_hi:[1,0]
	v_cvt_pk_bf16_f32 v78, v78, v79
	v_cvt_pk_bf16_f32 v79, v80, v81
	s_waitcnt vmcnt(14)
	v_lshlrev_b32_e32 v80, 16, v172
	v_and_b32_e32 v81, 0xffff0000, v172
	v_pk_add_f32 v[70:71], v[70:71], 1.0 op_sel_hi:[1,0]
	v_exp_f32_e32 v68, v68
	v_exp_f32_e32 v69, v69
	v_pk_mul_f32 v[74:75], v[74:75], v[80:81]
	v_lshlrev_b32_e32 v80, 16, v173
	v_and_b32_e32 v81, 0xffff0000, v173
	v_rcp_f32_e32 v70, v70
	v_rcp_f32_e32 v71, v71
	v_pk_add_f32 v[72:73], v[72:73], 1.0 op_sel_hi:[1,0]
	v_pk_add_f32 v[62:63], v[62:63], v[30:31]
	v_pk_mul_f32 v[76:77], v[76:77], v[80:81]
	v_rcp_f32_e32 v72, v72
	v_rcp_f32_e32 v73, v73
	v_pk_add_f32 v[64:65], v[64:65], v[32:33]
	v_pk_mul_f32 v[62:63], v[62:63], s[14:15] op_sel_hi:[1,0]
	v_cvt_pk_bf16_f32 v74, v74, v75
	v_cvt_pk_bf16_f32 v75, v76, v77
	v_add_u32_e32 v76, 0x8000, v215
	v_pk_add_f32 v[66:67], v[66:67], 1.0 op_sel_hi:[1,0]
	v_exp_f32_e32 v62, v62
	v_exp_f32_e32 v63, v63
	v_pk_mul_f32 v[64:65], v[64:65], s[14:15] op_sel_hi:[1,0]
	ds_write2_b64 v76, v[78:79], v[74:75] offset0:128 offset1:132
	s_waitcnt vmcnt(13)
	v_lshlrev_b32_e32 v74, 16, v168
	v_and_b32_e32 v75, 0xffff0000, v168
	v_rcp_f32_e32 v66, v66
	v_rcp_f32_e32 v67, v67
	v_pk_add_f32 v[68:69], v[68:69], 1.0 op_sel_hi:[1,0]
	v_exp_f32_e32 v64, v64
	v_exp_f32_e32 v65, v65
	v_pk_add_f32 v[58:59], v[58:59], v[22:23]
	v_pk_mul_f32 v[70:71], v[70:71], v[74:75]
	v_lshlrev_b32_e32 v74, 16, v169
	v_and_b32_e32 v75, 0xffff0000, v169
	v_rcp_f32_e32 v68, v68
	v_rcp_f32_e32 v69, v69
	v_pk_add_f32 v[60:61], v[60:61], v[24:25]
	v_pk_mul_f32 v[58:59], v[58:59], s[14:15] op_sel_hi:[1,0]
	v_pk_mul_f32 v[72:73], v[72:73], v[74:75]
	v_exp_f32_e32 v58, v58
	v_exp_f32_e32 v59, v59
	v_pk_mul_f32 v[60:61], v[60:61], s[14:15] op_sel_hi:[1,0]
	v_cvt_pk_bf16_f32 v70, v70, v71
	v_cvt_pk_bf16_f32 v71, v72, v73
	s_waitcnt vmcnt(12)
	v_lshlrev_b32_e32 v72, 16, v166
	v_and_b32_e32 v73, 0xffff0000, v166
	v_pk_add_f32 v[62:63], v[62:63], 1.0 op_sel_hi:[1,0]
	v_exp_f32_e32 v60, v60
	v_exp_f32_e32 v61, v61
	v_pk_mul_f32 v[66:67], v[66:67], v[72:73]
	v_lshlrev_b32_e32 v72, 16, v167
	v_and_b32_e32 v73, 0xffff0000, v167
	v_rcp_f32_e32 v62, v62
	v_rcp_f32_e32 v63, v63
	v_pk_add_f32 v[64:65], v[64:65], 1.0 op_sel_hi:[1,0]
	v_pk_add_f32 v[54:55], v[54:55], v[14:15]
	v_pk_mul_f32 v[68:69], v[68:69], v[72:73]
	v_rcp_f32_e32 v64, v64
	v_rcp_f32_e32 v65, v65
	v_pk_add_f32 v[56:57], v[56:57], v[16:17]
	v_pk_mul_f32 v[54:55], v[54:55], s[14:15] op_sel_hi:[1,0]
	v_cvt_pk_bf16_f32 v66, v66, v67
	v_cvt_pk_bf16_f32 v67, v68, v69
	v_pk_add_f32 v[58:59], v[58:59], 1.0 op_sel_hi:[1,0]
	v_exp_f32_e32 v54, v54
	v_exp_f32_e32 v55, v55
	v_pk_mul_f32 v[56:57], v[56:57], s[14:15] op_sel_hi:[1,0]
	ds_write2_b64 v76, v[70:71], v[66:67] offset0:136 offset1:140
	s_waitcnt vmcnt(11)
	v_lshlrev_b32_e32 v66, 16, v164
	v_and_b32_e32 v67, 0xffff0000, v164
	v_rcp_f32_e32 v58, v58
	v_rcp_f32_e32 v59, v59
	v_pk_add_f32 v[60:61], v[60:61], 1.0 op_sel_hi:[1,0]
	v_exp_f32_e32 v56, v56
	v_exp_f32_e32 v57, v57
	v_pk_add_f32 v[50:51], v[50:51], v[6:7]
	v_pk_mul_f32 v[62:63], v[62:63], v[66:67]
	v_lshlrev_b32_e32 v66, 16, v165
	v_and_b32_e32 v67, 0xffff0000, v165
	v_rcp_f32_e32 v60, v60
	v_rcp_f32_e32 v61, v61
	v_pk_add_f32 v[52:53], v[52:53], v[8:9]
	v_pk_mul_f32 v[50:51], v[50:51], s[14:15] op_sel_hi:[1,0]
	v_pk_mul_f32 v[64:65], v[64:65], v[66:67]
	v_exp_f32_e32 v50, v50
	v_exp_f32_e32 v51, v51
	v_pk_mul_f32 v[52:53], v[52:53], s[14:15] op_sel_hi:[1,0]
	v_cvt_pk_bf16_f32 v62, v62, v63
	v_cvt_pk_bf16_f32 v63, v64, v65
	s_waitcnt vmcnt(10)
	v_lshlrev_b32_e32 v64, 16, v162
	v_and_b32_e32 v65, 0xffff0000, v162
	v_pk_add_f32 v[54:55], v[54:55], 1.0 op_sel_hi:[1,0]
	v_exp_f32_e32 v52, v52
	v_exp_f32_e32 v53, v53
	v_pk_mul_f32 v[58:59], v[58:59], v[64:65]
	v_lshlrev_b32_e32 v64, 16, v163
	v_and_b32_e32 v65, 0xffff0000, v163
	v_rcp_f32_e32 v54, v54
	v_rcp_f32_e32 v55, v55
	v_pk_add_f32 v[56:57], v[56:57], 1.0 op_sel_hi:[1,0]
	v_pk_add_f32 v[46:47], v[46:47], v[30:31]
	v_pk_mul_f32 v[60:61], v[60:61], v[64:65]
	v_rcp_f32_e32 v56, v56
	v_rcp_f32_e32 v57, v57
	v_pk_add_f32 v[48:49], v[48:49], v[32:33]
	v_pk_mul_f32 v[46:47], v[46:47], s[14:15] op_sel_hi:[1,0]
	v_cvt_pk_bf16_f32 v58, v58, v59
	v_cvt_pk_bf16_f32 v59, v60, v61
	v_add_u32_e32 v60, 0xa000, v215
	v_pk_add_f32 v[50:51], v[50:51], 1.0 op_sel_hi:[1,0]
	v_exp_f32_e32 v46, v46
	v_exp_f32_e32 v47, v47
	v_pk_mul_f32 v[48:49], v[48:49], s[14:15] op_sel_hi:[1,0]
	ds_write2_b64 v60, v[62:63], v[58:59] offset0:160 offset1:164
	s_waitcnt vmcnt(9)
	v_lshlrev_b32_e32 v58, 16, v160
	v_and_b32_e32 v59, 0xffff0000, v160
	v_rcp_f32_e32 v50, v50
	v_rcp_f32_e32 v51, v51
	v_pk_add_f32 v[52:53], v[52:53], 1.0 op_sel_hi:[1,0]
	v_exp_f32_e32 v48, v48
	v_exp_f32_e32 v49, v49
	v_pk_add_f32 v[42:43], v[42:43], v[22:23]
	v_pk_mul_f32 v[54:55], v[54:55], v[58:59]
	v_lshlrev_b32_e32 v58, 16, v161
	v_and_b32_e32 v59, 0xffff0000, v161
	v_rcp_f32_e32 v52, v52
	v_rcp_f32_e32 v53, v53
	v_pk_add_f32 v[44:45], v[44:45], v[24:25]
	v_pk_mul_f32 v[42:43], v[42:43], s[14:15] op_sel_hi:[1,0]
	v_pk_mul_f32 v[56:57], v[56:57], v[58:59]
	v_exp_f32_e32 v42, v42
	v_exp_f32_e32 v43, v43
	v_pk_mul_f32 v[44:45], v[44:45], s[14:15] op_sel_hi:[1,0]
	v_cvt_pk_bf16_f32 v54, v54, v55
	v_cvt_pk_bf16_f32 v55, v56, v57
	s_waitcnt vmcnt(8)
	v_lshlrev_b32_e32 v56, 16, v156
	v_and_b32_e32 v57, 0xffff0000, v156
	v_pk_add_f32 v[46:47], v[46:47], 1.0 op_sel_hi:[1,0]
	v_exp_f32_e32 v44, v44
	v_exp_f32_e32 v45, v45
	v_pk_mul_f32 v[50:51], v[50:51], v[56:57]
	v_lshlrev_b32_e32 v56, 16, v157
	v_and_b32_e32 v57, 0xffff0000, v157
	v_rcp_f32_e32 v46, v46
	v_rcp_f32_e32 v47, v47
	v_pk_add_f32 v[48:49], v[48:49], 1.0 op_sel_hi:[1,0]
	v_pk_add_f32 v[38:39], v[38:39], v[14:15]
	v_pk_mul_f32 v[52:53], v[52:53], v[56:57]
	v_rcp_f32_e32 v48, v48
	v_rcp_f32_e32 v49, v49
	v_pk_add_f32 v[40:41], v[40:41], v[16:17]
	v_pk_mul_f32 v[38:39], v[38:39], s[14:15] op_sel_hi:[1,0]
	v_cvt_pk_bf16_f32 v50, v50, v51
	v_cvt_pk_bf16_f32 v51, v52, v53
	v_pk_add_f32 v[42:43], v[42:43], 1.0 op_sel_hi:[1,0]
	v_exp_f32_e32 v38, v38
	v_exp_f32_e32 v39, v39
	v_pk_mul_f32 v[40:41], v[40:41], s[14:15] op_sel_hi:[1,0]
	ds_write2_b64 v60, v[54:55], v[50:51] offset0:168 offset1:172
	s_waitcnt vmcnt(7)
	v_lshlrev_b32_e32 v50, 16, v154
	v_and_b32_e32 v51, 0xffff0000, v154
	v_rcp_f32_e32 v42, v42
	v_rcp_f32_e32 v43, v43
	v_pk_add_f32 v[44:45], v[44:45], 1.0 op_sel_hi:[1,0]
	v_exp_f32_e32 v40, v40
	v_exp_f32_e32 v41, v41
	v_pk_add_f32 v[34:35], v[34:35], v[6:7]
	v_pk_mul_f32 v[46:47], v[46:47], v[50:51]
	v_lshlrev_b32_e32 v50, 16, v155
	v_and_b32_e32 v51, 0xffff0000, v155
	v_rcp_f32_e32 v44, v44
	v_rcp_f32_e32 v45, v45
	v_pk_add_f32 v[36:37], v[36:37], v[8:9]
	v_pk_mul_f32 v[34:35], v[34:35], s[14:15] op_sel_hi:[1,0]
	v_pk_mul_f32 v[48:49], v[48:49], v[50:51]
	v_exp_f32_e32 v34, v34
	v_exp_f32_e32 v35, v35
	v_pk_mul_f32 v[36:37], v[36:37], s[14:15] op_sel_hi:[1,0]
	v_cvt_pk_bf16_f32 v46, v46, v47
	v_cvt_pk_bf16_f32 v47, v48, v49
	s_waitcnt vmcnt(6)
	v_lshlrev_b32_e32 v48, 16, v152
	v_and_b32_e32 v49, 0xffff0000, v152
	v_pk_add_f32 v[38:39], v[38:39], 1.0 op_sel_hi:[1,0]
	v_exp_f32_e32 v36, v36
	v_exp_f32_e32 v37, v37
	v_pk_mul_f32 v[42:43], v[42:43], v[48:49]
	v_lshlrev_b32_e32 v48, 16, v153
	v_and_b32_e32 v49, 0xffff0000, v153
	v_rcp_f32_e32 v38, v38
	v_rcp_f32_e32 v39, v39
	v_pk_add_f32 v[40:41], v[40:41], 1.0 op_sel_hi:[1,0]
	v_pk_add_f32 v[28:29], v[28:29], v[32:33]
	v_pk_add_f32 v[26:27], v[26:27], v[30:31]
	v_pk_mul_f32 v[44:45], v[44:45], v[48:49]
	v_rcp_f32_e32 v40, v40
	v_rcp_f32_e32 v41, v41
	v_pk_mul_f32 v[26:27], v[26:27], s[14:15] op_sel_hi:[1,0]
	v_pk_mul_f32 v[28:29], v[28:29], s[14:15] op_sel_hi:[1,0]
	v_cvt_pk_bf16_f32 v42, v42, v43
	v_cvt_pk_bf16_f32 v43, v44, v45
	v_add_u32_e32 v44, 0xc000, v215
	v_pk_add_f32 v[34:35], v[34:35], 1.0 op_sel_hi:[1,0]
	v_exp_f32_e32 v26, v26
	v_exp_f32_e32 v27, v27
	v_exp_f32_e32 v28, v28
	v_exp_f32_e32 v29, v29
	v_pk_add_f32 v[20:21], v[20:21], v[24:25]
	v_pk_add_f32 v[18:19], v[18:19], v[22:23]
	ds_write2_b64 v44, v[46:47], v[42:43] offset0:192 offset1:196
	s_waitcnt vmcnt(5)
	v_lshlrev_b32_e32 v42, 16, v150
	v_and_b32_e32 v43, 0xffff0000, v150
	v_rcp_f32_e32 v34, v34
	v_rcp_f32_e32 v35, v35
	v_pk_add_f32 v[36:37], v[36:37], 1.0 op_sel_hi:[1,0]
	v_pk_mul_f32 v[18:19], v[18:19], s[14:15] op_sel_hi:[1,0]
	v_pk_mul_f32 v[20:21], v[20:21], s[14:15] op_sel_hi:[1,0]
	v_pk_mul_f32 v[38:39], v[38:39], v[42:43]
	v_lshlrev_b32_e32 v42, 16, v151
	v_and_b32_e32 v43, 0xffff0000, v151
	v_rcp_f32_e32 v36, v36
	v_rcp_f32_e32 v37, v37
	v_exp_f32_e32 v18, v18
	v_exp_f32_e32 v19, v19
	v_exp_f32_e32 v20, v20
	v_exp_f32_e32 v21, v21
	v_pk_mul_f32 v[40:41], v[40:41], v[42:43]
	v_pk_add_f32 v[12:13], v[12:13], v[16:17]
	v_pk_add_f32 v[10:11], v[10:11], v[14:15]
	v_cvt_pk_bf16_f32 v38, v38, v39
	v_cvt_pk_bf16_f32 v39, v40, v41
	s_waitcnt vmcnt(4)
	v_lshlrev_b32_e32 v40, 16, v148
	v_and_b32_e32 v41, 0xffff0000, v148
	v_pk_add_f32 v[26:27], v[26:27], 1.0 op_sel_hi:[1,0]
	v_pk_add_f32 v[28:29], v[28:29], 1.0 op_sel_hi:[1,0]
	v_pk_mul_f32 v[10:11], v[10:11], s[14:15] op_sel_hi:[1,0]
	v_pk_mul_f32 v[12:13], v[12:13], s[14:15] op_sel_hi:[1,0]
	v_pk_mul_f32 v[34:35], v[34:35], v[40:41]
	v_lshlrev_b32_e32 v40, 16, v149
	v_and_b32_e32 v41, 0xffff0000, v149
	v_rcp_f32_e32 v26, v26
	v_rcp_f32_e32 v27, v27
	v_rcp_f32_e32 v28, v28
	v_rcp_f32_e32 v29, v29
	v_exp_f32_e32 v10, v10
	v_exp_f32_e32 v11, v11
	v_exp_f32_e32 v12, v12
	v_exp_f32_e32 v13, v13
	v_pk_add_f32 v[4:5], v[4:5], v[8:9]
	v_pk_add_f32 v[2:3], v[2:3], v[6:7]
	v_pk_mul_f32 v[36:37], v[36:37], v[40:41]
	v_pk_add_f32 v[18:19], v[18:19], 1.0 op_sel_hi:[1,0]
	v_pk_add_f32 v[20:21], v[20:21], 1.0 op_sel_hi:[1,0]
	v_pk_mul_f32 v[2:3], v[2:3], s[14:15] op_sel_hi:[1,0]
	v_pk_mul_f32 v[4:5], v[4:5], s[14:15] op_sel_hi:[1,0]
	v_cvt_pk_bf16_f32 v34, v34, v35
	v_cvt_pk_bf16_f32 v35, v36, v37
	v_rcp_f32_e32 v18, v18
	v_rcp_f32_e32 v19, v19
	v_rcp_f32_e32 v20, v20
	v_rcp_f32_e32 v21, v21
	v_exp_f32_e32 v2, v2
	v_exp_f32_e32 v3, v3
	v_exp_f32_e32 v4, v4
	v_exp_f32_e32 v5, v5
	ds_write2_b64 v44, v[38:39], v[34:35] offset0:200 offset1:204
	s_waitcnt vmcnt(3)
	v_lshlrev_b32_e32 v34, 16, v144
	v_and_b32_e32 v35, 0xffff0000, v144
	v_lshlrev_b32_e32 v30, 16, v145
	v_and_b32_e32 v31, 0xffff0000, v145
	v_pk_mul_f32 v[26:27], v[26:27], v[34:35]
	v_pk_mul_f32 v[28:29], v[28:29], v[30:31]
	v_pk_add_f32 v[10:11], v[10:11], 1.0 op_sel_hi:[1,0]
	v_pk_add_f32 v[12:13], v[12:13], 1.0 op_sel_hi:[1,0]
	v_cvt_pk_bf16_f32 v26, v26, v27
	v_cvt_pk_bf16_f32 v27, v28, v29
	s_waitcnt vmcnt(2)
	v_lshlrev_b32_e32 v28, 16, v142
	v_and_b32_e32 v29, 0xffff0000, v142
	v_lshlrev_b32_e32 v22, 16, v143
	v_and_b32_e32 v23, 0xffff0000, v143
	v_rcp_f32_e32 v10, v10
	v_rcp_f32_e32 v11, v11
	v_rcp_f32_e32 v12, v12
	v_rcp_f32_e32 v13, v13
	v_pk_mul_f32 v[18:19], v[18:19], v[28:29]
	v_pk_mul_f32 v[20:21], v[20:21], v[22:23]
	v_pk_add_f32 v[2:3], v[2:3], 1.0 op_sel_hi:[1,0]
	v_pk_add_f32 v[4:5], v[4:5], 1.0 op_sel_hi:[1,0]
	v_cvt_pk_bf16_f32 v18, v18, v19
	v_cvt_pk_bf16_f32 v19, v20, v21
	v_add_u32_e32 v20, 0xe000, v215
	v_rcp_f32_e32 v2, v2
	v_rcp_f32_e32 v3, v3
	v_rcp_f32_e32 v4, v4
	v_rcp_f32_e32 v5, v5
	ds_write2_b64 v20, v[26:27], v[18:19] offset0:224 offset1:228
	s_waitcnt vmcnt(1)
	v_lshlrev_b32_e32 v18, 16, v140
	v_and_b32_e32 v19, 0xffff0000, v140
	v_lshlrev_b32_e32 v14, 16, v141
	v_and_b32_e32 v15, 0xffff0000, v141
	v_pk_mul_f32 v[10:11], v[10:11], v[18:19]
	v_pk_mul_f32 v[12:13], v[12:13], v[14:15]
	v_cvt_pk_bf16_f32 v10, v10, v11
	v_cvt_pk_bf16_f32 v11, v12, v13
	s_waitcnt vmcnt(0)
	v_lshlrev_b32_e32 v12, 16, v138
	v_and_b32_e32 v13, 0xffff0000, v138
	v_lshlrev_b32_e32 v6, 16, v139
	v_and_b32_e32 v7, 0xffff0000, v139
	v_pk_mul_f32 v[2:3], v[2:3], v[12:13]
	v_pk_mul_f32 v[4:5], v[4:5], v[6:7]
	v_cvt_pk_bf16_f32 v2, v2, v3
	v_cvt_pk_bf16_f32 v3, v4, v5
	v_lshl_or_b32 v4, s23, 5, v253
	ds_write2_b64 v20, v[10:11], v[2:3] offset0:232 offset1:236
	v_mul_lo_u32 v2, v4, s18
	s_waitcnt lgkmcnt(0)
	s_barrier
	v_add_u32_e32 v5, v211, v2
	ds_read_b128 v[14:17], v5
	s_waitcnt lgkmcnt(0)
	v_and_b32_e32 v3, 0xffff0000, v14
	v_lshlrev_b32_e32 v2, 16, v14
	v_mul_f32_e32 v3, v3, v3
	v_fmac_f32_e32 v3, v2, v2
	v_lshlrev_b32_e32 v2, 16, v15
	v_fmac_f32_e32 v3, v2, v2
	v_and_b32_e32 v2, 0xffff0000, v15
	v_fmac_f32_e32 v3, v2, v2
	v_lshlrev_b32_e32 v2, 16, v16
	v_fmac_f32_e32 v3, v2, v2
	v_and_b32_e32 v2, 0xffff0000, v16
	v_fmac_f32_e32 v3, v2, v2
	v_lshlrev_b32_e32 v2, 16, v17
	v_fmac_f32_e32 v3, v2, v2
	v_and_b32_e32 v2, 0xffff0000, v17
	v_fmac_f32_e32 v3, v2, v2
	v_and_b32_e32 v2, 64, v214
	v_add_u32_e32 v12, 64, v2
	v_xor_b32_e32 v2, 1, v214
	v_cmp_lt_i32_e64 s[0:1], v2, v12
	s_nop 1
	v_cndmask_b32_e64 v2, v214, v2, s[0:1]
	v_lshlrev_b32_e32 v6, 2, v2
	ds_bpermute_b32 v2, v6, v3
	s_waitcnt lgkmcnt(0)
	v_add_f32_e32 v2, v3, v2
	v_xor_b32_e32 v3, 2, v214
	v_cmp_lt_i32_e64 s[0:1], v3, v12
	s_nop 1
	v_cndmask_b32_e64 v3, v214, v3, s[0:1]
	v_lshlrev_b32_e32 v7, 2, v3
	ds_bpermute_b32 v3, v7, v2
	s_waitcnt lgkmcnt(0)
	v_add_f32_e32 v9, v2, v3
	v_xor_b32_e32 v2, 4, v214
	v_cmp_lt_i32_e64 s[0:1], v2, v12
	s_nop 1
	v_cndmask_b32_e64 v2, v214, v2, s[0:1]
	v_lshlrev_b32_e32 v8, 2, v2
	ds_bpermute_b32 v13, v8, v9
	v_add_u32_e32 v2, s21, v4
	v_ashrrev_i32_e32 v3, 31, v2
	v_lshlrev_b64 v[10:11], 12, v[2:3]
	v_lshl_add_u64 v[10:11], s[8:9], 0, v[10:11]
	s_waitcnt lgkmcnt(0)
	v_add_f32_e32 v13, v9, v13
	v_xor_b32_e32 v9, 8, v214
	v_cmp_lt_i32_e64 s[0:1], v9, v12
	v_lshl_add_u64 v[10:11], v[10:11], 0, s[2:3]
	v_lshl_add_u64 v[18:19], v[10:11], 0, v[146:147]
	v_cndmask_b32_e64 v9, v214, v9, s[0:1]
	v_lshlrev_b32_e32 v9, 2, v9
	ds_bpermute_b32 v20, v9, v13
	v_xor_b32_e32 v10, 16, v214
	v_cmp_lt_i32_e64 s[0:1], v10, v12
	global_store_dwordx4 v[18:19], v[14:17], off sc1
	s_nop 1
	s_waitcnt lgkmcnt(0)
	v_add_f32_e32 v11, v13, v20
	v_cndmask_b32_e64 v10, v214, v10, s[0:1]
	v_lshlrev_b32_e32 v10, 2, v10
	ds_bpermute_b32 v12, v10, v11
	s_and_saveexec_b64 s[0:1], vcc
	s_cbranch_execz .LBB0_1042
	v_lshl_add_u64 v[2:3], v[2:3], 4, s[10:11]
	s_lshl_b32 s22, s20, 2
	s_mov_b32 s23, s3
	s_waitcnt lgkmcnt(0)
	v_add_f32_e32 v11, v11, v12
	v_lshl_add_u64 v[2:3], v[2:3], 0, s[22:23]
	global_store_dword v[2:3], v11, off

.LBB0_1128:
	s_ashr_i32 s5, s4, 5
	s_lshr_b32 s6, s4, 31
	s_add_i32 s6, s5, s6
	s_ashr_i32 s41, s6, 1
	s_and_b32 s6, s6, 0x3ffffe
	s_and_b32 s48, s4, 7
	s_sub_i32 s5, s5, s6
	s_lshl_b32 s4, s4, 5
	s_lshl_b32 s5, s5, 10
	s_and_b32 s4, s4, 0x300
	s_or_b32 s24, s5, s4
	s_lshl_b32 s7, s41, 3
	s_ashr_i32 s25, s24, 31
	s_or_b32 s37, s7, s48
	s_lshl_b64 s[22:23], s[24:25], 1
	s_add_u32 s49, s27, s22
	s_addc_u32 s50, s28, s23
	s_lshl_b32 s25, s37, 8
	v_readfirstlane_b32 s26, v0
	s_lshr_b32 s38, s26, 6
	v_or_b32_e32 v2, s25, v149
	v_lshlrev_b32_e32 v2, 12, v2
	s_lshr_b32 s4, s26, 1
	s_lshl_b32 s44, s38, 10
	v_or_b32_e32 v18, v2, v159
	s_and_b32 s39, s4, 0x7fffff80
	s_add_i32 s43, s44, 0
	s_mov_b32 s4, m0
	s_mov_b32 m0, s43
	s_nop 0
	global_load_lds_dwordx4 v18, s[10:11]
	s_mov_b32 m0, s4
	s_add_i32 s45, s44, 0x2000
	s_add_i32 s4, s45, 0
	s_add_i32 s46, s44, 0x4000
	v_add_u32_e32 v19, v2, v174
	s_bfe_u32 s42, s26, 0x20006
	s_mov_b32 s5, m0
	s_mov_b32 m0, s4
	s_nop 0
	global_load_lds_dwordx4 v19, s[10:11]
	s_mov_b32 m0, s5
	s_add_i32 s4, s46, 0
	s_add_i32 s47, s44, 0x6000
	v_or_b32_e32 v3, 0x80000, v18
	v_add_u32_e32 v20, v2, v175
	s_lshl_b32 s8, s38, 1
	s_lshl_b32 s40, s42, 7
	s_mov_b32 s5, m0
	s_mov_b32 m0, s4
	s_nop 0
	global_load_lds_dwordx4 v3, s[10:11]
	s_mov_b32 m0, s5
	s_add_i32 s4, s47, 0
	s_mov_b32 s5, m0
	s_mov_b32 m0, s4
	s_nop 0
	global_load_lds_dwordx4 v20, s[10:11]
	s_mov_b32 m0, s5
	s_and_b32 s6, s38, 4
	s_or_b32 s7, s40, 32
	s_or_b32 s51, s40, 64
	s_or_b32 s52, s40, 0x60
	s_lshl_b64 s[4:5], s[8:9], 12
	s_add_u32 s4, s49, s4
	s_addc_u32 s5, s50, s5
	global_load_dwordx4 v[2:5], v173, s[4:5]
	s_add_i32 s4, s8, 16
	s_mov_b32 s5, s9
	s_lshl_b64 s[4:5], s[4:5], 12
	s_add_u32 s4, s49, s4
	s_addc_u32 s5, s50, s5
	global_load_dwordx4 v[6:9], v173, s[4:5]
	s_add_i32 s4, s8, 32
	s_mov_b32 s5, s9
	s_lshl_b64 s[4:5], s[4:5], 12
	s_add_u32 s4, s49, s4
	s_addc_u32 s5, s50, s5
	global_load_dwordx4 v[10:13], v173, s[4:5]
	s_add_i32 s4, s8, 48
	s_mov_b32 s5, s9
	s_lshl_b64 s[4:5], s[4:5], 12
	s_add_u32 s4, s49, s4
	s_addc_u32 s5, s50, s5
	global_load_dwordx4 v[14:17], v173, s[4:5]
	s_add_i32 s4, s43, 0x8000
	v_or_b32_e32 v21, 0x80, v18
	s_mov_b32 s5, m0
	s_mov_b32 m0, s4
	s_nop 0
	global_load_lds_dwordx4 v21, s[10:11]
	s_mov_b32 m0, s5
	s_add_i32 s4, s43, 0xa000
	v_or_b32_e32 v19, 0x80, v19
	s_mov_b32 s5, m0
	s_mov_b32 m0, s4
	s_nop 0
	global_load_lds_dwordx4 v19, s[10:11]
	s_mov_b32 m0, s5
	v_or_b32_e32 v18, 0x80080, v18
	s_add_i32 s4, s43, 0xc000
	s_add_i32 s43, s43, 0xe000
	s_mov_b32 s5, m0
	s_mov_b32 m0, s4
	s_nop 0
	global_load_lds_dwordx4 v18, s[10:11]
	s_mov_b32 m0, s5
	v_or_b32_e32 v18, 0x80, v20
	s_mov_b32 s4, m0
	s_mov_b32 m0, s43
	s_nop 0
	global_load_lds_dwordx4 v18, s[10:11]
	s_mov_b32 m0, s4
	s_add_i32 s43, s39, s25
	s_waitcnt vmcnt(1)
	v_or_b32_e32 v38, s43, v170
	v_ashrrev_i32_e32 v39, 31, v38
	v_lshlrev_b64 v[18:19], 6, v[38:39]
	v_lshl_add_u64 v[30:31], s[16:17], 0, v[18:19]
	global_load_dwordx4 v[18:21], v[30:31], off
	global_load_dwordx4 v[22:25], v[30:31], off offset:32
	global_load_dwordx4 v[26:29], v[30:31], off offset:16
	s_nop 0
	global_load_dwordx4 v[30:33], v[30:31], off offset:48
	v_lshl_add_u64 v[34:35], v[38:39], 4, s[14:15]
	global_load_dwordx4 v[34:37], v[34:35], off
	v_or_b32_e32 v54, 64, v38
	v_ashrrev_i32_e32 v55, 31, v54
	v_lshlrev_b64 v[38:39], 6, v[54:55]
	v_lshl_add_u64 v[50:51], s[16:17], 0, v[38:39]
	global_load_dwordx4 v[38:41], v[50:51], off
	global_load_dwordx4 v[42:45], v[50:51], off offset:32
	global_load_dwordx4 v[46:49], v[50:51], off offset:16
	s_nop 0
	global_load_dwordx4 v[50:53], v[50:51], off offset:48
	v_or_b32_e32 v58, s8, v167
	v_and_or_b32 v56, v58, 3, s6
	v_lshl_add_u64 v[54:55], v[54:55], 4, s[14:15]
	v_lshlrev_b32_e32 v60, 5, v56
	global_load_dwordx4 v[54:57], v[54:55], off
	v_lshlrev_b32_e32 v62, 9, v58
	v_bitop3_b32 v156, s7, v176, v172 bitop3:0xde
	v_bitop3_b32 v160, v60, v62, v168 bitop3:0xde
	v_or_b32_e32 v61, s39, v1
	v_bitop3_b32 v157, s40, v176, v172 bitop3:0xde
	v_bitop3_b32 v155, s51, v176, v172 bitop3:0xde
	v_bitop3_b32 v153, s52, v176, v172 bitop3:0xde
	v_mov_b32_e32 v60, v147
	v_mov_b32_e32 v62, 0
	v_mov_b32_e32 v63, v147
	v_mov_b32_e32 v64, v147
	v_mov_b32_e32 v65, v147
	v_mov_b32_e32 v66, 0
	v_mov_b32_e32 v67, v147
	v_mov_b32_e32 v68, v147
	v_mov_b32_e32 v69, v147
	v_mov_b32_e32 v70, 0
	v_mov_b32_e32 v71, v147
	v_mov_b32_e32 v72, v147
	v_mov_b32_e32 v73, v147
	v_mov_b32_e32 v74, 0
	v_mov_b32_e32 v75, v147
	s_waitcnt vmcnt(10)
	v_mov_b32_e32 v76, v147
	v_mov_b32_e32 v77, v147
	v_mov_b32_e32 v78, 0
	v_mov_b32_e32 v79, v147
	v_mov_b32_e32 v80, v147
	v_mov_b32_e32 v81, v147
	v_mov_b32_e32 v82, 0
	v_mov_b32_e32 v83, v147
	v_mov_b32_e32 v84, v147
	v_mov_b32_e32 v85, v147
	v_mov_b32_e32 v86, 0
	v_mov_b32_e32 v87, v147
	v_mov_b32_e32 v88, v147
	v_mov_b32_e32 v89, v147
	v_mov_b32_e32 v90, 0
	v_mov_b32_e32 v91, v147
	v_mov_b32_e32 v92, v147
	v_mov_b32_e32 v93, v147
	v_mov_b32_e32 v94, 0
	v_mov_b32_e32 v95, v147
	v_mov_b32_e32 v96, v147
	v_mov_b32_e32 v97, v147
	v_mov_b32_e32 v98, 0
	v_mov_b32_e32 v99, v147
	v_mov_b32_e32 v100, v147
	v_mov_b32_e32 v101, v147
	v_mov_b32_e32 v102, 0
	v_mov_b32_e32 v103, v147
	v_mov_b32_e32 v104, v147
	v_mov_b32_e32 v105, v147
	v_mov_b32_e32 v106, 0
	v_mov_b32_e32 v107, v147
	v_mov_b32_e32 v108, v147
	v_mov_b32_e32 v109, v147
	v_mov_b32_e32 v110, 0
	v_mov_b32_e32 v111, v147
	v_mov_b32_e32 v112, v147
	v_mov_b32_e32 v113, v147
	v_mov_b32_e32 v114, 0
	v_mov_b32_e32 v115, v147
	v_mov_b32_e32 v116, v147
	v_mov_b32_e32 v117, v147
	s_waitcnt vmcnt(9)
	v_mov_b32_e32 v58, v18
	s_waitcnt vmcnt(8)
	v_mov_b32_e32 v59, v22
	v_mov_b32_e32 v22, v19
	v_pk_add_f32 v[18:19], v[58:59], v[22:23]
	v_mov_b32_e32 v22, v20
	v_mov_b32_e32 v23, v24
	v_mov_b32_e32 v24, v21
	v_pk_add_f32 v[20:21], v[22:23], v[24:25]
	s_waitcnt vmcnt(7)
	v_mov_b32_e32 v22, v28
	v_pk_add_f32 v[18:19], v[18:19], v[20:21]
	v_mov_b32_e32 v20, v26
	s_waitcnt vmcnt(6)
	v_mov_b32_e32 v21, v30
	v_mov_b32_e32 v30, v27
	v_mov_b32_e32 v23, v32
	v_mov_b32_e32 v32, v29
	v_pk_add_f32 v[20:21], v[20:21], v[30:31]
	v_pk_add_f32 v[22:23], v[22:23], v[32:33]
	v_mov_b32_e32 v58, 0
	v_pk_add_f32 v[20:21], v[20:21], v[22:23]
	v_mov_b32_e32 v59, v147
	v_pk_add_f32 v[18:19], v[18:19], v[20:21]
	s_waitcnt vmcnt(5)
	v_mov_b32_e32 v20, v35
	v_mov_b32_e32 v21, v36
	v_mov_b32_e32 v35, v37
	v_pk_add_f32 v[20:21], v[20:21], v[34:35]
	v_mov_b32_e32 v23, v18
	v_mov_b32_e32 v22, v20
	v_mov_b32_e32 v18, v21
	v_pk_add_f32 v[18:19], v[22:23], v[18:19]
	s_waitcnt vmcnt(1)
	v_mov_b32_e32 v23, v52
	v_pk_fma_f32 v[18:19], v[18:19], s[20:21], v[150:151] op_sel_hi:[1,0,0]
	v_mov_b32_e32 v52, v49
	v_mul_f32_e32 v20, 0x4b800000, v19
	v_cmp_gt_f32_e32 vcc, s31, v19
	v_mul_f32_e32 v22, 0x4b800000, v18
	v_cmp_gt_f32_e64 s[4:5], s31, v18
	v_cndmask_b32_e32 v20, v19, v20, vcc
	v_rsq_f32_e32 v20, v20
	v_cndmask_b32_e64 v18, v18, v22, s[4:5]
	v_mul_f32_e32 v22, 0x4f800000, v19
	v_cmp_gt_f32_e64 s[6:7], s33, v19
	v_rsq_f32_e32 v18, v18
	v_mul_f32_e32 v21, 0x45800000, v20
	v_cndmask_b32_e64 v24, v19, v22, s[6:7]
	v_sqrt_f32_e32 v19, v24
	v_cndmask_b32_e32 v183, v20, v21, vcc
	v_mul_f32_e32 v20, 0x45800000, v18
	v_cndmask_b32_e64 v25, v18, v20, s[4:5]
	v_add_u32_e32 v18, -1, v19
	v_fma_f32 v20, -v18, v19, v24
	v_cmp_ge_f32_e32 vcc, 0, v20
	v_add_u32_e32 v20, 1, v19
	v_mov_b32_e32 v21, v44
	v_cndmask_b32_e32 v18, v19, v18, vcc
	v_fma_f32 v19, -v20, v19, v24
	v_cmp_lt_f32_e32 vcc, 0, v19
	v_mov_b32_e32 v44, v41
	v_mov_b32_e32 v22, v48
	v_cndmask_b32_e32 v18, v18, v20, vcc
	v_mul_f32_e32 v19, 0x37800000, v18
	v_cndmask_b32_e64 v26, v18, v19, s[6:7]
	v_mov_b32_e32 v18, v38
	v_mov_b32_e32 v19, v42
	v_mov_b32_e32 v42, v39
	v_mov_b32_e32 v20, v40
	v_pk_add_f32 v[18:19], v[18:19], v[42:43]
	v_pk_add_f32 v[20:21], v[20:21], v[44:45]
	v_pk_add_f32 v[22:23], v[22:23], v[52:53]
	v_pk_add_f32 v[18:19], v[18:19], v[20:21]
	v_mov_b32_e32 v20, v46
	v_mov_b32_e32 v21, v50
	v_mov_b32_e32 v50, v47
	v_pk_add_f32 v[20:21], v[20:21], v[50:51]
	v_cmp_class_f32_e64 s[4:5], v24, v179
	v_pk_add_f32 v[20:21], v[20:21], v[22:23]
	v_lshlrev_b32_e32 v34, 7, v61
	v_pk_add_f32 v[18:19], v[18:19], v[20:21]
	s_waitcnt vmcnt(0)
	v_mov_b32_e32 v20, v55
	v_mov_b32_e32 v21, v56
	v_mov_b32_e32 v55, v57
	v_pk_add_f32 v[20:21], v[20:21], v[54:55]
	v_mov_b32_e32 v23, v18
	v_mov_b32_e32 v22, v20
	v_mov_b32_e32 v18, v21
	v_pk_add_f32 v[18:19], v[22:23], v[18:19]
	v_cndmask_b32_e64 v21, v26, v24, s[4:5]
	v_pk_fma_f32 v[18:19], v[18:19], s[20:21], v[150:151] op_sel_hi:[1,0,0]
	v_mul_f32_e32 v165, v21, v25
	v_mul_f32_e32 v20, 0x4b800000, v19
	v_cmp_gt_f32_e32 vcc, s31, v19
	v_mul_f32_e32 v22, 0x4b800000, v18
	v_cmp_gt_f32_e64 s[4:5], s31, v18
	v_cndmask_b32_e32 v20, v19, v20, vcc
	v_rsq_f32_e32 v20, v20
	v_cndmask_b32_e64 v18, v18, v22, s[4:5]
	v_mul_f32_e32 v22, 0x4f800000, v19
	v_cmp_gt_f32_e64 s[6:7], s33, v19
	v_rsq_f32_e32 v18, v18
	v_mul_f32_e32 v21, 0x45800000, v20
	v_cndmask_b32_e64 v19, v19, v22, s[6:7]
	v_sqrt_f32_e32 v22, v19
	v_cndmask_b32_e32 v182, v20, v21, vcc
	v_mul_f32_e32 v20, 0x45800000, v18
	v_cndmask_b32_e64 v18, v18, v20, s[4:5]
	v_add_u32_e32 v20, -1, v22
	v_fma_f32 v21, -v20, v22, v19
	v_cmp_ge_f32_e32 vcc, 0, v21
	v_add_u32_e32 v21, 1, v22
	s_add_i32 s4, s8, 64
	v_cndmask_b32_e32 v20, v22, v20, vcc
	v_fma_f32 v22, -v21, v22, v19
	v_cmp_lt_f32_e32 vcc, 0, v22
	s_mov_b32 s5, s9
	s_lshl_b64 s[4:5], s[4:5], 12
	v_cndmask_b32_e32 v20, v20, v21, vcc
	v_mul_f32_e32 v21, 0x37800000, v20
	v_cndmask_b32_e64 v20, v20, v21, s[6:7]
	v_cmp_class_f32_e32 vcc, v19, v179
	s_add_u32 s4, s49, s4
	s_addc_u32 s5, s50, s5
	v_cndmask_b32_e32 v19, v20, v19, vcc
	v_mul_f32_e32 v184, v19, v18
	s_waitcnt vmcnt(4)
	v_or_b32_e32 v161, v34, v169
	v_add_u32_e32 v18, 0, v160
	v_add_u32_e32 v163, 0x18000, v18
	ds_write_b128 v163, v[2:5]
	ds_write_b128 v163, v[6:9] offset:8192
	ds_write_b128 v163, v[10:13] offset:16384
	ds_write_b128 v163, v[14:17] offset:24576
	global_load_dwordx4 v[14:17], v173, s[4:5]
	s_add_i32 s4, s8, 0x50
	s_mov_b32 s5, s9
	s_lshl_b64 s[4:5], s[4:5], 12
	s_add_u32 s4, s49, s4
	s_addc_u32 s5, s50, s5
	global_load_dwordx4 v[10:13], v173, s[4:5]
	s_add_i32 s4, s8, 0x60
	s_mov_b32 s5, s9
	s_lshl_b64 s[4:5], s[4:5], 12
	s_add_u32 s4, s49, s4
	s_addc_u32 s5, s50, s5
	s_addk_i32 s8, 0x70
	global_load_dwordx4 v[6:9], v173, s[4:5]
	s_lshl_b64 s[4:5], s[8:9], 12
	s_add_u32 s4, s49, s4
	s_addc_u32 s5, s50, s5
	global_load_dwordx4 v[2:5], v173, s[4:5]
	s_lshl_b64 s[4:5], s[26:27], 7
	s_waitcnt lgkmcnt(0)
	s_barrier
	s_and_b32 s5, s5, 0x7f
	s_and_b32 s4, s4, 0xffffe000
	v_lshl_or_b32 v18, s41, 23, v180
	s_add_u32 s6, s49, s4
	v_lshl_or_b32 v164, s48, 20, v18
	v_or_b32_e32 v162, v34, v171
	s_addc_u32 s7, s50, s5
	v_add_u32_e32 v152, v177, v164
	s_mov_b32 s8, 0
	s_mov_b64 s[4:5], 0
	s_mov_b32 s26, 0x8000
	s_mov_b32 s48, 0x10000
	v_mov_b32_e32 v18, 0
	v_mov_b32_e32 v19, v147
	v_mov_b32_e32 v20, v147
	v_mov_b32_e32 v21, v147
	v_mov_b32_e32 v22, 0
	v_mov_b32_e32 v23, v147
	v_mov_b32_e32 v24, v147
	v_mov_b32_e32 v25, v147
	v_mov_b32_e32 v26, 0
	v_mov_b32_e32 v27, v147
	v_mov_b32_e32 v28, v147
	v_mov_b32_e32 v29, v147
	v_mov_b32_e32 v30, 0
	v_mov_b32_e32 v31, v147
	v_mov_b32_e32 v32, v147
	v_mov_b32_e32 v33, v147
	v_mov_b32_e32 v34, 0
	v_mov_b32_e32 v35, v147
	v_mov_b32_e32 v36, v147
	v_mov_b32_e32 v37, v147
	v_mov_b32_e32 v38, 0
	v_mov_b32_e32 v39, v147
	v_mov_b32_e32 v40, v147
	v_mov_b32_e32 v41, v147
	v_mov_b32_e32 v42, 0
	v_mov_b32_e32 v43, v147
	v_mov_b32_e32 v44, v147
	v_mov_b32_e32 v45, v147
	v_mov_b32_e32 v46, 0
	v_mov_b32_e32 v47, v147
	v_mov_b32_e32 v48, v147
	v_mov_b32_e32 v49, v147
	v_mov_b32_e32 v50, 0
	v_mov_b32_e32 v51, v147
	v_mov_b32_e32 v52, v147
	v_mov_b32_e32 v53, v147
	v_mov_b32_e32 v54, 0
	v_mov_b32_e32 v55, v147
	v_mov_b32_e32 v56, v147
	v_mov_b32_e32 v57, v147
	v_mov_b32_e32 v61, v147
	v_mov_b32_e32 v118, 0
	v_mov_b32_e32 v119, v147
	v_mov_b32_e32 v120, v147
	v_mov_b32_e32 v121, v147
	v_mov_b32_e32 v122, 0
	v_mov_b32_e32 v123, v147
	v_mov_b32_e32 v124, v147
	v_mov_b32_e32 v125, v147
	v_mov_b32_e32 v126, 0
	v_mov_b32_e32 v127, v147
	v_mov_b32_e32 v128, v147
	v_mov_b32_e32 v129, v147
	v_mov_b32_e32 v130, 0
	v_mov_b32_e32 v131, v147
	v_mov_b32_e32 v132, v147
	v_mov_b32_e32 v133, v147
	v_mov_b32_e32 v134, 0
	v_mov_b32_e32 v135, v147
	v_mov_b32_e32 v136, v147
	v_mov_b32_e32 v137, v147
	v_mov_b32_e32 v138, 0
	v_mov_b32_e32 v139, v147
	v_mov_b32_e32 v140, v147
	v_mov_b32_e32 v141, v147
	v_mov_b32_e32 v142, 0
	v_mov_b32_e32 v143, v147
	v_mov_b32_e32 v144, v147
	v_mov_b32_e32 v145, v147
	s_cmp_lt_u32 s80, 4
	s_cbranch_scc1 .Lprio_o1
	s_setprio 1
.Lprio_o1:
.LBB0_1129:
	s_add_i32 s50, s26, 0xffff8000
	s_and_b32 s50, s50, 0x8000
	s_add_i32 s50, s50, 0
	s_add_i32 s49, s8, 0
	s_add_i32 s50, s50, 0x18000
	v_add_u32_e32 v154, s50, v157
	v_add_u32_e32 v218, s49, v161
	v_add_u32_e32 v224, s50, v155
	v_add_u32_e32 v185, s50, v156
.Lrot_o1:
	ds_read_b64_tr_b16 v[186:187], v154
	ds_read_b64_tr_b16 v[188:189], v154 offset:2048
	ds_read_b64_tr_b16 v[190:191], v185
	ds_read_b64_tr_b16 v[192:193], v185 offset:2048
	ds_read_b128 v[194:197], v218
	ds_read_b128 v[198:201], v218 offset:2048
	ds_read_b64_tr_b16 v[202:203], v224
	ds_read_b64_tr_b16 v[204:205], v224 offset:2048
	v_add_u32_e32 v226, s50, v153
	ds_read_b64_tr_b16 v[206:207], v226
	ds_read_b64_tr_b16 v[208:209], v226 offset:2048
	ds_read_b128 v[210:213], v218 offset:4096
	s_waitcnt lgkmcnt(6)
	v_mfma_f32_16x16x32_bf16 v[18:21], v[186:189], v[194:197], v[18:21]
	s_add_i32 s50, s48, 0
	v_add_u32_e32 v214, 0xfff40000, v152
	s_add_i32 s51, s50, s44
	v_mfma_f32_16x16x32_bf16 v[22:25], v[190:193], v[194:197], v[22:25]
	s_mov_b32 s52, m0
	s_mov_b32 m0, s51
	s_nop 0
	global_load_lds_dwordx4 v214, s[10:11]
	s_mov_b32 m0, s52
	s_waitcnt lgkmcnt(3)
	v_mfma_f32_16x16x32_bf16 v[26:29], v[202:205], v[194:197], v[26:29]
	s_waitcnt lgkmcnt(1)
	v_mfma_f32_16x16x32_bf16 v[30:33], v[206:209], v[194:197], v[30:33]
	v_mfma_f32_16x16x32_bf16 v[34:37], v[186:189], v[198:201], v[34:37]
	ds_read_b128 v[194:197], v218 offset:6144
	v_add_u32_e32 v214, 0xfff80000, v152
	s_add_i32 s51, s50, s45
	v_mfma_f32_16x16x32_bf16 v[38:41], v[190:193], v[198:201], v[38:41]
	s_mov_b32 s52, m0
	s_mov_b32 m0, s51
	s_nop 0
	global_load_lds_dwordx4 v214, s[10:11]
	s_mov_b32 m0, s52
	v_mfma_f32_16x16x32_bf16 v[42:45], v[202:205], v[198:201], v[42:45]
	v_mfma_f32_16x16x32_bf16 v[46:49], v[206:209], v[198:201], v[46:49]
	s_waitcnt lgkmcnt(1)
	v_mfma_f32_16x16x32_bf16 v[50:53], v[186:189], v[210:213], v[50:53]
	ds_read_b128 v[198:201], v218 offset:8192
	v_add_u32_e32 v214, 0xfffc0000, v152
	s_add_i32 s51, s50, s46
	v_mfma_f32_16x16x32_bf16 v[54:57], v[190:193], v[210:213], v[54:57]
	s_mov_b32 s52, m0
	s_mov_b32 m0, s51
	s_nop 0
	global_load_lds_dwordx4 v214, s[10:11]
	s_mov_b32 m0, s52
	v_mfma_f32_16x16x32_bf16 v[58:61], v[202:205], v[210:213], v[58:61]
	v_mfma_f32_16x16x32_bf16 v[62:65], v[206:209], v[210:213], v[62:65]
	s_waitcnt lgkmcnt(1)
	v_mfma_f32_16x16x32_bf16 v[66:69], v[186:189], v[194:197], v[66:69]
	ds_read_b128 v[210:213], v218 offset:10240
	s_add_i32 s50, s50, s47
	s_mov_b32 s51, m0
	s_mov_b32 m0, s50
	s_nop 0
	global_load_lds_dwordx4 v152, s[10:11]
	s_mov_b32 m0, s51
	v_mfma_f32_16x16x32_bf16 v[70:73], v[190:193], v[194:197], v[70:73]
	v_mfma_f32_16x16x32_bf16 v[74:77], v[202:205], v[194:197], v[74:77]
	v_mfma_f32_16x16x32_bf16 v[78:81], v[206:209], v[194:197], v[78:81]
	ds_read_b128 v[194:197], v218 offset:12288
	ds_read_b64_tr_b16 v[214:215], v154 offset:16384
	ds_read_b64_tr_b16 v[216:217], v154 offset:18432
	s_waitcnt lgkmcnt(4)
	v_mfma_f32_16x16x32_bf16 v[82:85], v[186:189], v[198:201], v[82:85]
	v_mfma_f32_16x16x32_bf16 v[86:89], v[190:193], v[198:201], v[86:89]
	v_mfma_f32_16x16x32_bf16 v[90:93], v[202:205], v[198:201], v[90:93]
	v_mfma_f32_16x16x32_bf16 v[94:97], v[206:209], v[198:201], v[94:97]
	ds_read_b128 v[198:201], v218 offset:14336
	ds_read_b64_tr_b16 v[218:219], v185 offset:16384
	ds_read_b64_tr_b16 v[220:221], v185 offset:18432
	s_waitcnt lgkmcnt(6)
	v_mfma_f32_16x16x32_bf16 v[98:101], v[186:189], v[210:213], v[98:101]
	v_mfma_f32_16x16x32_bf16 v[102:105], v[190:193], v[210:213], v[102:105]
	v_mfma_f32_16x16x32_bf16 v[106:109], v[202:205], v[210:213], v[106:109]
	v_mfma_f32_16x16x32_bf16 v[110:113], v[206:209], v[210:213], v[110:113]
	v_add_u32_e32 v154, s49, v162
	ds_read_b128 v[210:213], v154
	ds_read_b64_tr_b16 v[222:223], v224 offset:16384
	ds_read_b64_tr_b16 v[224:225], v224 offset:18432
	s_waitcnt lgkmcnt(8)
	v_mfma_f32_16x16x32_bf16 v[114:117], v[186:189], v[194:197], v[114:117]
	v_mfma_f32_16x16x32_bf16 v[118:121], v[190:193], v[194:197], v[118:121]
	v_mfma_f32_16x16x32_bf16 v[122:125], v[202:205], v[194:197], v[122:125]
	v_mfma_f32_16x16x32_bf16 v[126:129], v[206:209], v[194:197], v[126:129]
	s_waitcnt lgkmcnt(5)
	v_mfma_f32_16x16x32_bf16 v[130:133], v[186:189], v[198:201], v[130:133]
	ds_read_b128 v[186:189], v154 offset:2048
	s_and_b32 s49, s26, 0x8000
	v_mfma_f32_16x16x32_bf16 v[134:137], v[190:193], v[198:201], v[134:137]
	ds_read_b64_tr_b16 v[190:191], v226 offset:16384
	ds_read_b64_tr_b16 v[192:193], v226 offset:18432
	v_mfma_f32_16x16x32_bf16 v[138:141], v[202:205], v[198:201], v[138:141]
	v_mfma_f32_16x16x32_bf16 v[142:145], v[206:209], v[198:201], v[142:145]
	s_waitcnt lgkmcnt(5)
	v_mfma_f32_16x16x32_bf16 v[18:21], v[214:217], v[210:213], v[18:21]
	ds_read_b128 v[194:197], v154 offset:4096
	v_add_u32_e32 v185, s49, v163
	s_add_u32 s49, s6, s4
	v_mfma_f32_16x16x32_bf16 v[22:25], v[218:221], v[210:213], v[22:25]
	s_addc_u32 s52, s7, s5
	s_waitcnt vmcnt(7)
	s_add_u32 s50, s49, 0x80000
	s_waitcnt lgkmcnt(4)
	v_mfma_f32_16x16x32_bf16 v[26:29], v[222:225], v[210:213], v[26:29]
	ds_write_b128 v185, v[14:17]
	s_addc_u32 s51, s52, 0
	global_load_dwordx4 v[14:17], v173, s[50:51]
	s_waitcnt lgkmcnt(2)
	v_mfma_f32_16x16x32_bf16 v[30:33], v[190:193], v[210:213], v[30:33]
	v_mfma_f32_16x16x32_bf16 v[34:37], v[214:217], v[186:189], v[34:37]
	ds_read_b128 v[198:201], v154 offset:6144
	s_waitcnt vmcnt(7)
	s_add_u32 s50, s49, 0x90000
	v_mfma_f32_16x16x32_bf16 v[38:41], v[218:221], v[186:189], v[38:41]
	ds_write_b128 v185, v[10:13] offset:8192
	s_addc_u32 s51, s52, 0
	global_load_dwordx4 v[10:13], v173, s[50:51]
	v_mfma_f32_16x16x32_bf16 v[42:45], v[222:225], v[186:189], v[42:45]
	v_mfma_f32_16x16x32_bf16 v[46:49], v[190:193], v[186:189], v[46:49]
	s_waitcnt lgkmcnt(3)
	v_mfma_f32_16x16x32_bf16 v[50:53], v[214:217], v[194:197], v[50:53]
	ds_read_b128 v[186:189], v154 offset:8192
	s_waitcnt vmcnt(7)
	s_add_u32 s50, s49, 0xa0000
	v_mfma_f32_16x16x32_bf16 v[54:57], v[218:221], v[194:197], v[54:57]
	ds_write_b128 v185, v[6:9] offset:16384
	s_addc_u32 s51, s52, 0
	global_load_dwordx4 v[6:9], v173, s[50:51]
	v_mfma_f32_16x16x32_bf16 v[58:61], v[222:225], v[194:197], v[58:61]
	v_mfma_f32_16x16x32_bf16 v[62:65], v[190:193], v[194:197], v[62:65]
	s_waitcnt lgkmcnt(3)
	v_mfma_f32_16x16x32_bf16 v[66:69], v[214:217], v[198:201], v[66:69]
	ds_read_b128 v[194:197], v154 offset:10240
	s_waitcnt vmcnt(7)
	s_add_u32 s50, s49, 0xb0000
	v_mfma_f32_16x16x32_bf16 v[70:73], v[218:221], v[198:201], v[70:73]
	ds_write_b128 v185, v[2:5] offset:24576
	s_addc_u32 s51, s52, 0
	global_load_dwordx4 v[2:5], v173, s[50:51]
	v_mfma_f32_16x16x32_bf16 v[74:77], v[222:225], v[198:201], v[74:77]
	v_mfma_f32_16x16x32_bf16 v[78:81], v[190:193], v[198:201], v[78:81]
	s_waitcnt lgkmcnt(3)
	v_mfma_f32_16x16x32_bf16 v[82:85], v[214:217], v[186:189], v[82:85]
	ds_read_b128 v[198:201], v154 offset:12288
	v_mfma_f32_16x16x32_bf16 v[86:89], v[218:221], v[186:189], v[86:89]
	v_mfma_f32_16x16x32_bf16 v[90:93], v[222:225], v[186:189], v[90:93]
	v_mfma_f32_16x16x32_bf16 v[94:97], v[190:193], v[186:189], v[94:97]
	s_waitcnt lgkmcnt(2)
	v_mfma_f32_16x16x32_bf16 v[98:101], v[214:217], v[194:197], v[98:101]
	ds_read_b128 v[186:189], v154 offset:14336
	v_mfma_f32_16x16x32_bf16 v[102:105], v[218:221], v[194:197], v[102:105]
	v_mfma_f32_16x16x32_bf16 v[106:109], v[222:225], v[194:197], v[106:109]
	v_mfma_f32_16x16x32_bf16 v[110:113], v[190:193], v[194:197], v[110:113]
	s_waitcnt lgkmcnt(1)
	v_mfma_f32_16x16x32_bf16 v[114:117], v[214:217], v[198:201], v[114:117]
	v_mfma_f32_16x16x32_bf16 v[118:121], v[218:221], v[198:201], v[118:121]
	v_mfma_f32_16x16x32_bf16 v[122:125], v[222:225], v[198:201], v[122:125]
	v_mfma_f32_16x16x32_bf16 v[126:129], v[190:193], v[198:201], v[126:129]
	s_waitcnt lgkmcnt(0)
	v_mfma_f32_16x16x32_bf16 v[130:133], v[214:217], v[186:189], v[130:133]
	v_mfma_f32_16x16x32_bf16 v[134:137], v[218:221], v[186:189], v[134:137]
	v_mfma_f32_16x16x32_bf16 v[138:141], v[222:225], v[186:189], v[138:141]
	v_mfma_f32_16x16x32_bf16 v[142:145], v[190:193], v[186:189], v[142:145]
	s_add_i32 s49, s8, 0x8000
	s_cmp_lg_u32 s8, 0x10000
	s_cselect_b32 s8, s49, 0
	s_add_i32 s49, s48, 0x8000
	s_cmp_lg_u32 s48, 0x10000
	s_cselect_b32 s48, s49, 0
	s_add_u32 s4, s4, 0x40000
	s_addc_u32 s5, s5, 0
	s_add_i32 s26, s26, 0x8000
	v_add_u32_e32 v152, 0x80, v152
	s_add_i32 s50, s26, 0xffff8000
	s_and_b32 s50, s50, 0x8000
	s_add_i32 s50, s50, 0
	s_add_i32 s49, s8, 0
	s_add_i32 s50, s50, 0x18000
	v_add_u32_e32 v154, s50, v157
	v_add_u32_e32 v218, s49, v161
	v_add_u32_e32 v224, s50, v155
	v_add_u32_e32 v185, s50, v156
	s_waitcnt lgkmcnt(0)
	s_barrier
	s_cmp_eq_u32 s4, 0x400000
	s_cbranch_scc0 .Lrot_o1
	s_setprio 0
	v_or_b32_e32 v152, v181, v1
	v_lshlrev_b32_e32 v185, 2, v152
	ds_bpermute_b32 v152, v185, v165
	ds_bpermute_b32 v154, v185, v165 offset:64
	ds_bpermute_b32 v186, v185, v165 offset:128
	ds_bpermute_b32 v188, v185, v184 offset:192
	ds_bpermute_b32 v190, v185, v165 offset:192
	ds_bpermute_b32 v192, v185, v184
	ds_bpermute_b32 v194, v185, v184 offset:64
	ds_bpermute_b32 v184, v185, v184 offset:128
	s_mov_b32 s8, 0
	s_waitcnt lgkmcnt(4)
	v_pk_mul_f32 v[144:145], v[144:145], v[188:189] op_sel_hi:[1,0]
	v_pk_mul_f32 v[142:143], v[142:143], v[188:189] op_sel_hi:[1,0]
	v_pk_mul_f32 v[140:141], v[140:141], v[188:189] op_sel_hi:[1,0]
	v_pk_mul_f32 v[138:139], v[138:139], v[188:189] op_sel_hi:[1,0]
	v_pk_mul_f32 v[136:137], v[136:137], v[188:189] op_sel_hi:[1,0]
	v_pk_mul_f32 v[134:135], v[134:135], v[188:189] op_sel_hi:[1,0]
	v_pk_mul_f32 v[132:133], v[132:133], v[188:189] op_sel_hi:[1,0]
	v_pk_mul_f32 v[130:131], v[130:131], v[188:189] op_sel_hi:[1,0]
	s_waitcnt lgkmcnt(0)
	v_pk_mul_f32 v[128:129], v[128:129], v[184:185] op_sel_hi:[1,0]
	v_pk_mul_f32 v[126:127], v[126:127], v[184:185] op_sel_hi:[1,0]
	v_pk_mul_f32 v[124:125], v[124:125], v[184:185] op_sel_hi:[1,0]
	v_pk_mul_f32 v[122:123], v[122:123], v[184:185] op_sel_hi:[1,0]
	v_pk_mul_f32 v[120:121], v[120:121], v[184:185] op_sel_hi:[1,0]
	v_pk_mul_f32 v[118:119], v[118:119], v[184:185] op_sel_hi:[1,0]
	v_pk_mul_f32 v[116:117], v[116:117], v[184:185] op_sel_hi:[1,0]
	v_pk_mul_f32 v[114:115], v[114:115], v[184:185] op_sel_hi:[1,0]
	v_pk_mul_f32 v[112:113], v[112:113], v[194:195] op_sel_hi:[1,0]
	v_pk_mul_f32 v[110:111], v[110:111], v[194:195] op_sel_hi:[1,0]
	v_pk_mul_f32 v[108:109], v[108:109], v[194:195] op_sel_hi:[1,0]
	v_pk_mul_f32 v[106:107], v[106:107], v[194:195] op_sel_hi:[1,0]
	v_pk_mul_f32 v[104:105], v[104:105], v[194:195] op_sel_hi:[1,0]
	v_pk_mul_f32 v[102:103], v[102:103], v[194:195] op_sel_hi:[1,0]
	v_pk_mul_f32 v[100:101], v[100:101], v[194:195] op_sel_hi:[1,0]
	v_pk_mul_f32 v[98:99], v[98:99], v[194:195] op_sel_hi:[1,0]
	v_pk_mul_f32 v[96:97], v[96:97], v[192:193] op_sel_hi:[1,0]
	v_pk_mul_f32 v[94:95], v[94:95], v[192:193] op_sel_hi:[1,0]
	v_pk_mul_f32 v[92:93], v[92:93], v[192:193] op_sel_hi:[1,0]
	v_pk_mul_f32 v[90:91], v[90:91], v[192:193] op_sel_hi:[1,0]
	v_pk_mul_f32 v[88:89], v[88:89], v[192:193] op_sel_hi:[1,0]
	v_pk_mul_f32 v[86:87], v[86:87], v[192:193] op_sel_hi:[1,0]
	v_pk_mul_f32 v[84:85], v[84:85], v[192:193] op_sel_hi:[1,0]
	v_pk_mul_f32 v[82:83], v[82:83], v[192:193] op_sel_hi:[1,0]
	v_pk_mul_f32 v[80:81], v[80:81], v[190:191] op_sel_hi:[1,0]
	v_pk_mul_f32 v[78:79], v[78:79], v[190:191] op_sel_hi:[1,0]
	v_pk_mul_f32 v[76:77], v[76:77], v[190:191] op_sel_hi:[1,0]
	v_pk_mul_f32 v[74:75], v[74:75], v[190:191] op_sel_hi:[1,0]
	v_pk_mul_f32 v[72:73], v[72:73], v[190:191] op_sel_hi:[1,0]
	v_pk_mul_f32 v[70:71], v[70:71], v[190:191] op_sel_hi:[1,0]
	v_pk_mul_f32 v[68:69], v[68:69], v[190:191] op_sel_hi:[1,0]
	v_pk_mul_f32 v[66:67], v[66:67], v[190:191] op_sel_hi:[1,0]
	v_pk_mul_f32 v[64:65], v[64:65], v[186:187] op_sel_hi:[1,0]
	v_pk_mul_f32 v[62:63], v[62:63], v[186:187] op_sel_hi:[1,0]
	v_pk_mul_f32 v[60:61], v[60:61], v[186:187] op_sel_hi:[1,0]
	v_pk_mul_f32 v[58:59], v[58:59], v[186:187] op_sel_hi:[1,0]
	v_pk_mul_f32 v[56:57], v[56:57], v[186:187] op_sel_hi:[1,0]
	v_pk_mul_f32 v[54:55], v[54:55], v[186:187] op_sel_hi:[1,0]
	v_pk_mul_f32 v[52:53], v[52:53], v[186:187] op_sel_hi:[1,0]
	v_pk_mul_f32 v[50:51], v[50:51], v[186:187] op_sel_hi:[1,0]
	v_pk_mul_f32 v[48:49], v[48:49], v[154:155] op_sel_hi:[1,0]
	v_pk_mul_f32 v[46:47], v[46:47], v[154:155] op_sel_hi:[1,0]
	v_pk_mul_f32 v[44:45], v[44:45], v[154:155] op_sel_hi:[1,0]
	v_pk_mul_f32 v[42:43], v[42:43], v[154:155] op_sel_hi:[1,0]
	v_pk_mul_f32 v[40:41], v[40:41], v[154:155] op_sel_hi:[1,0]
	v_pk_mul_f32 v[38:39], v[38:39], v[154:155] op_sel_hi:[1,0]
	v_pk_mul_f32 v[36:37], v[36:37], v[154:155] op_sel_hi:[1,0]
	v_pk_mul_f32 v[34:35], v[34:35], v[154:155] op_sel_hi:[1,0]
	v_pk_mul_f32 v[32:33], v[32:33], v[152:153] op_sel_hi:[1,0]
	v_pk_mul_f32 v[30:31], v[30:31], v[152:153] op_sel_hi:[1,0]
	v_pk_mul_f32 v[28:29], v[28:29], v[152:153] op_sel_hi:[1,0]
	v_pk_mul_f32 v[26:27], v[26:27], v[152:153] op_sel_hi:[1,0]
	v_pk_mul_f32 v[24:25], v[24:25], v[152:153] op_sel_hi:[1,0]
	v_pk_mul_f32 v[22:23], v[22:23], v[152:153] op_sel_hi:[1,0]
	v_pk_mul_f32 v[20:21], v[20:21], v[152:153] op_sel_hi:[1,0]
	v_pk_mul_f32 v[18:19], v[18:19], v[152:153] op_sel_hi:[1,0]
	v_add_u32_e32 v152, v178, v164
	s_mov_b32 s26, 0x8000
	s_mov_b64 s[4:5], 0
	s_mov_b32 s48, 0x88000
	s_cmp_lt_u32 s80, 4
	s_cbranch_scc1 .Lprio_o2
	s_setprio 1
.Lprio_o2:
.LBB0_1131:
	s_add_i32 s50, s48, 0xffff8000
	s_and_b32 s50, s50, 0x8000
	s_add_i32 s50, s50, 0
	s_add_i32 s49, s26, 0
	s_add_i32 s50, s50, 0x18000
	v_add_u32_e32 v154, s50, v157
	v_add_u32_e32 v165, s49, v161
	v_add_u32_e32 v222, s50, v155
	v_add_u32_e32 v164, s50, v156
.Lrot_o2:
	ds_read_b64_tr_b16 v[184:185], v154
	ds_read_b64_tr_b16 v[186:187], v154 offset:2048
	ds_read_b64_tr_b16 v[188:189], v164
	ds_read_b64_tr_b16 v[190:191], v164 offset:2048
	ds_read_b128 v[192:195], v165
	ds_read_b128 v[196:199], v165 offset:2048
	ds_read_b64_tr_b16 v[200:201], v222
	ds_read_b64_tr_b16 v[202:203], v222 offset:2048
	v_add_u32_e32 v224, s50, v153
	ds_read_b64_tr_b16 v[204:205], v224
	ds_read_b64_tr_b16 v[206:207], v224 offset:2048
	ds_read_b128 v[208:211], v165 offset:4096
	s_waitcnt lgkmcnt(6)
	v_mfma_f32_16x16x32_bf16 v[18:21], v[184:187], v[192:195], v[18:21]
	s_add_i32 s50, s8, 0
	v_add_u32_e32 v212, 0xfff40000, v152
	s_add_i32 s51, s50, s44
	v_mfma_f32_16x16x32_bf16 v[22:25], v[188:191], v[192:195], v[22:25]
	s_mov_b32 s52, m0
	s_mov_b32 m0, s51
	s_nop 0
	global_load_lds_dwordx4 v212, s[10:11]
	s_mov_b32 m0, s52
	s_waitcnt lgkmcnt(3)
	v_mfma_f32_16x16x32_bf16 v[26:29], v[200:203], v[192:195], v[26:29]
	s_waitcnt lgkmcnt(1)
	v_mfma_f32_16x16x32_bf16 v[30:33], v[204:207], v[192:195], v[30:33]
	v_mfma_f32_16x16x32_bf16 v[34:37], v[184:187], v[196:199], v[34:37]
	ds_read_b128 v[192:195], v165 offset:6144
	v_add_u32_e32 v212, 0xfff80000, v152
	s_add_i32 s51, s50, s45
	v_mfma_f32_16x16x32_bf16 v[38:41], v[188:191], v[196:199], v[38:41]
	s_mov_b32 s52, m0
	s_mov_b32 m0, s51
	s_nop 0
	global_load_lds_dwordx4 v212, s[10:11]
	s_mov_b32 m0, s52
	v_mfma_f32_16x16x32_bf16 v[42:45], v[200:203], v[196:199], v[42:45]
	v_mfma_f32_16x16x32_bf16 v[46:49], v[204:207], v[196:199], v[46:49]
	s_waitcnt lgkmcnt(1)
	v_mfma_f32_16x16x32_bf16 v[50:53], v[184:187], v[208:211], v[50:53]
	ds_read_b128 v[196:199], v165 offset:8192
	v_add_u32_e32 v212, 0xfffc0000, v152
	s_add_i32 s51, s50, s46
	v_mfma_f32_16x16x32_bf16 v[54:57], v[188:191], v[208:211], v[54:57]
	s_mov_b32 s52, m0
	s_mov_b32 m0, s51
	s_nop 0
	global_load_lds_dwordx4 v212, s[10:11]
	s_mov_b32 m0, s52
	v_mfma_f32_16x16x32_bf16 v[58:61], v[200:203], v[208:211], v[58:61]
	v_mfma_f32_16x16x32_bf16 v[62:65], v[204:207], v[208:211], v[62:65]
	s_waitcnt lgkmcnt(1)
	v_mfma_f32_16x16x32_bf16 v[66:69], v[184:187], v[192:195], v[66:69]
	ds_read_b128 v[208:211], v165 offset:10240
	s_add_i32 s50, s50, s47
	s_mov_b32 s51, m0
	s_mov_b32 m0, s50
	s_nop 0
	global_load_lds_dwordx4 v152, s[10:11]
	s_mov_b32 m0, s51
	v_mfma_f32_16x16x32_bf16 v[70:73], v[188:191], v[192:195], v[70:73]
	v_mfma_f32_16x16x32_bf16 v[74:77], v[200:203], v[192:195], v[74:77]
	v_mfma_f32_16x16x32_bf16 v[78:81], v[204:207], v[192:195], v[78:81]
	ds_read_b128 v[192:195], v165 offset:12288
	ds_read_b64_tr_b16 v[212:213], v154 offset:16384
	ds_read_b64_tr_b16 v[214:215], v154 offset:18432
	s_waitcnt lgkmcnt(4)
	v_mfma_f32_16x16x32_bf16 v[82:85], v[184:187], v[196:199], v[82:85]
	v_mfma_f32_16x16x32_bf16 v[86:89], v[188:191], v[196:199], v[86:89]
	v_mfma_f32_16x16x32_bf16 v[90:93], v[200:203], v[196:199], v[90:93]
	v_mfma_f32_16x16x32_bf16 v[94:97], v[204:207], v[196:199], v[94:97]
	ds_read_b128 v[196:199], v165 offset:14336
	ds_read_b64_tr_b16 v[216:217], v164 offset:16384
	ds_read_b64_tr_b16 v[218:219], v164 offset:18432
	s_waitcnt lgkmcnt(6)
	v_mfma_f32_16x16x32_bf16 v[98:101], v[184:187], v[208:211], v[98:101]
	v_mfma_f32_16x16x32_bf16 v[102:105], v[188:191], v[208:211], v[102:105]
	v_mfma_f32_16x16x32_bf16 v[106:109], v[200:203], v[208:211], v[106:109]
	v_mfma_f32_16x16x32_bf16 v[110:113], v[204:207], v[208:211], v[110:113]
	v_add_u32_e32 v154, s49, v162
	ds_read_b128 v[208:211], v154
	ds_read_b64_tr_b16 v[220:221], v222 offset:16384
	ds_read_b64_tr_b16 v[222:223], v222 offset:18432
	s_waitcnt lgkmcnt(8)
	v_mfma_f32_16x16x32_bf16 v[114:117], v[184:187], v[192:195], v[114:117]
	v_mfma_f32_16x16x32_bf16 v[118:121], v[188:191], v[192:195], v[118:121]
	v_mfma_f32_16x16x32_bf16 v[122:125], v[200:203], v[192:195], v[122:125]
	v_mfma_f32_16x16x32_bf16 v[126:129], v[204:207], v[192:195], v[126:129]
	s_waitcnt lgkmcnt(5)
	v_mfma_f32_16x16x32_bf16 v[130:133], v[184:187], v[196:199], v[130:133]
	ds_read_b128 v[184:187], v154 offset:2048
	s_and_b32 s49, s48, 0x8000
	v_mfma_f32_16x16x32_bf16 v[134:137], v[188:191], v[196:199], v[134:137]
	ds_read_b64_tr_b16 v[188:189], v224 offset:16384
	ds_read_b64_tr_b16 v[190:191], v224 offset:18432
	v_mfma_f32_16x16x32_bf16 v[138:141], v[200:203], v[196:199], v[138:141]
	v_mfma_f32_16x16x32_bf16 v[142:145], v[204:207], v[196:199], v[142:145]
	s_waitcnt lgkmcnt(5)
	v_mfma_f32_16x16x32_bf16 v[18:21], v[212:215], v[208:211], v[18:21]
	ds_read_b128 v[192:195], v154 offset:4096
	v_add_u32_e32 v164, s49, v163
	s_add_u32 s49, s6, s4
	v_mfma_f32_16x16x32_bf16 v[22:25], v[216:219], v[208:211], v[22:25]
	s_addc_u32 s52, s7, s5
	s_waitcnt vmcnt(7)
	s_add_u32 s50, s49, 0x480000
	s_waitcnt lgkmcnt(4)
	v_mfma_f32_16x16x32_bf16 v[26:29], v[220:223], v[208:211], v[26:29]
	ds_write_b128 v164, v[14:17]
	s_addc_u32 s51, s52, 0
	global_load_dwordx4 v[14:17], v173, s[50:51]
	s_waitcnt lgkmcnt(2)
	v_mfma_f32_16x16x32_bf16 v[30:33], v[188:191], v[208:211], v[30:33]
	v_mfma_f32_16x16x32_bf16 v[34:37], v[212:215], v[184:187], v[34:37]
	ds_read_b128 v[196:199], v154 offset:6144
	s_waitcnt vmcnt(7)
	s_add_u32 s50, s49, 0x490000
	v_mfma_f32_16x16x32_bf16 v[38:41], v[216:219], v[184:187], v[38:41]
	ds_write_b128 v164, v[10:13] offset:8192
	s_addc_u32 s51, s52, 0
	global_load_dwordx4 v[10:13], v173, s[50:51]
	v_mfma_f32_16x16x32_bf16 v[42:45], v[220:223], v[184:187], v[42:45]
	v_mfma_f32_16x16x32_bf16 v[46:49], v[188:191], v[184:187], v[46:49]
	s_waitcnt lgkmcnt(3)
	v_mfma_f32_16x16x32_bf16 v[50:53], v[212:215], v[192:195], v[50:53]
	ds_read_b128 v[184:187], v154 offset:8192
	s_waitcnt vmcnt(7)
	s_add_u32 s50, s49, 0x4a0000
	v_mfma_f32_16x16x32_bf16 v[54:57], v[216:219], v[192:195], v[54:57]
	ds_write_b128 v164, v[6:9] offset:16384
	s_addc_u32 s51, s52, 0
	global_load_dwordx4 v[6:9], v173, s[50:51]
	v_mfma_f32_16x16x32_bf16 v[58:61], v[220:223], v[192:195], v[58:61]
	v_mfma_f32_16x16x32_bf16 v[62:65], v[188:191], v[192:195], v[62:65]
	s_waitcnt lgkmcnt(3)
	v_mfma_f32_16x16x32_bf16 v[66:69], v[212:215], v[196:199], v[66:69]
	ds_read_b128 v[192:195], v154 offset:10240
	s_waitcnt vmcnt(7)
	s_add_u32 s50, s49, 0x4b0000
	v_mfma_f32_16x16x32_bf16 v[70:73], v[216:219], v[196:199], v[70:73]
	ds_write_b128 v164, v[2:5] offset:24576
	s_addc_u32 s51, s52, 0
	global_load_dwordx4 v[2:5], v173, s[50:51]
	v_mfma_f32_16x16x32_bf16 v[74:77], v[220:223], v[196:199], v[74:77]
	v_mfma_f32_16x16x32_bf16 v[78:81], v[188:191], v[196:199], v[78:81]
	s_waitcnt lgkmcnt(3)
	v_mfma_f32_16x16x32_bf16 v[82:85], v[212:215], v[184:187], v[82:85]
	ds_read_b128 v[196:199], v154 offset:12288
	v_mfma_f32_16x16x32_bf16 v[86:89], v[216:219], v[184:187], v[86:89]
	v_mfma_f32_16x16x32_bf16 v[90:93], v[220:223], v[184:187], v[90:93]
	v_mfma_f32_16x16x32_bf16 v[94:97], v[188:191], v[184:187], v[94:97]
	s_waitcnt lgkmcnt(2)
	v_mfma_f32_16x16x32_bf16 v[98:101], v[212:215], v[192:195], v[98:101]
	ds_read_b128 v[184:187], v154 offset:14336
	v_mfma_f32_16x16x32_bf16 v[102:105], v[216:219], v[192:195], v[102:105]
	v_mfma_f32_16x16x32_bf16 v[106:109], v[220:223], v[192:195], v[106:109]
	v_mfma_f32_16x16x32_bf16 v[110:113], v[188:191], v[192:195], v[110:113]
	s_waitcnt lgkmcnt(1)
	v_mfma_f32_16x16x32_bf16 v[114:117], v[212:215], v[196:199], v[114:117]
	v_mfma_f32_16x16x32_bf16 v[118:121], v[216:219], v[196:199], v[118:121]
	v_mfma_f32_16x16x32_bf16 v[122:125], v[220:223], v[196:199], v[122:125]
	v_mfma_f32_16x16x32_bf16 v[126:129], v[188:191], v[196:199], v[126:129]
	s_waitcnt lgkmcnt(0)
	v_mfma_f32_16x16x32_bf16 v[130:133], v[212:215], v[184:187], v[130:133]
	v_mfma_f32_16x16x32_bf16 v[134:137], v[216:219], v[184:187], v[134:137]
	v_mfma_f32_16x16x32_bf16 v[138:141], v[220:223], v[184:187], v[138:141]
	v_mfma_f32_16x16x32_bf16 v[142:145], v[188:191], v[184:187], v[142:145]
	s_add_i32 s49, s26, 0x8000
	s_cmp_lg_u32 s26, 0x10000
	s_cselect_b32 s26, s49, 0
	s_add_i32 s49, s8, 0x8000
	s_cmp_lg_u32 s8, 0x10000
	s_cselect_b32 s8, s49, 0
	s_add_u32 s4, s4, 0x40000
	s_addc_u32 s5, s5, 0
	s_add_i32 s48, s48, 0x8000
	v_add_u32_e32 v152, 0x80, v152
	s_add_i32 s50, s48, 0xffff8000
	s_and_b32 s50, s50, 0x8000
	s_add_i32 s50, s50, 0
	s_add_i32 s49, s26, 0
	s_add_i32 s50, s50, 0x18000
	v_add_u32_e32 v154, s50, v157
	v_add_u32_e32 v165, s49, v161
	v_add_u32_e32 v222, s50, v155
	v_add_u32_e32 v164, s50, v156
	s_waitcnt lgkmcnt(0)
	s_barrier
	s_cmp_lg_u32 s4, 0x380000
	s_cbranch_scc1 .Lrot_o2
	s_setprio 0
	s_add_i32 s4, 0, 0x18000
	v_add_u32_e32 v152, s4, v157
	v_add_u32_e32 v220, 0, v161
	v_add_u32_e32 v161, s4, v155
	v_add_u32_e32 v221, s4, v153
	ds_read_b64_tr_b16 v[184:185], v152
	ds_read_b64_tr_b16 v[186:187], v152 offset:2048
	v_add_u32_e32 v154, s4, v156
	ds_read_b128 v[188:191], v220
	ds_read_b64_tr_b16 v[192:193], v154
	ds_read_b64_tr_b16 v[194:195], v154 offset:2048
	ds_read_b128 v[196:199], v220 offset:2048
	ds_read_b64_tr_b16 v[200:201], v161
	ds_read_b64_tr_b16 v[202:203], v161 offset:2048
	ds_read_b64_tr_b16 v[204:205], v221
	ds_read_b64_tr_b16 v[206:207], v221 offset:2048
	ds_read_b128 v[208:211], v220 offset:4096
	s_waitcnt lgkmcnt(8)
	v_mfma_f32_16x16x32_bf16 v[18:21], v[184:187], v[188:191], v[18:21]
	s_waitcnt lgkmcnt(6)
	v_mfma_f32_16x16x32_bf16 v[22:25], v[192:195], v[188:191], v[22:25]
	s_waitcnt lgkmcnt(3)
	v_mfma_f32_16x16x32_bf16 v[26:29], v[200:203], v[188:191], v[26:29]
	s_waitcnt lgkmcnt(1)
	v_mfma_f32_16x16x32_bf16 v[30:33], v[204:207], v[188:191], v[30:33]
	ds_read_b128 v[188:191], v220 offset:6144
	v_mfma_f32_16x16x32_bf16 v[34:37], v[184:187], v[196:199], v[34:37]
	v_mfma_f32_16x16x32_bf16 v[38:41], v[192:195], v[196:199], v[38:41]
	v_mfma_f32_16x16x32_bf16 v[42:45], v[200:203], v[196:199], v[42:45]
	v_mfma_f32_16x16x32_bf16 v[46:49], v[204:207], v[196:199], v[46:49]
	ds_read_b128 v[196:199], v220 offset:8192
	s_waitcnt lgkmcnt(2)
	v_mfma_f32_16x16x32_bf16 v[50:53], v[184:187], v[208:211], v[50:53]
	v_mfma_f32_16x16x32_bf16 v[54:57], v[192:195], v[208:211], v[54:57]
	v_mfma_f32_16x16x32_bf16 v[58:61], v[200:203], v[208:211], v[58:61]
	v_mfma_f32_16x16x32_bf16 v[62:65], v[204:207], v[208:211], v[62:65]
	ds_read_b128 v[208:211], v220 offset:10240
	s_waitcnt lgkmcnt(2)
	v_mfma_f32_16x16x32_bf16 v[66:69], v[184:187], v[188:191], v[66:69]
	v_mfma_f32_16x16x32_bf16 v[70:73], v[192:195], v[188:191], v[70:73]
	v_mfma_f32_16x16x32_bf16 v[74:77], v[200:203], v[188:191], v[74:77]
	v_mfma_f32_16x16x32_bf16 v[78:81], v[204:207], v[188:191], v[78:81]
	ds_read_b128 v[188:191], v220 offset:12288
	ds_read_b64_tr_b16 v[212:213], v152 offset:16384
	ds_read_b64_tr_b16 v[214:215], v152 offset:18432
	s_waitcnt lgkmcnt(4)
	v_mfma_f32_16x16x32_bf16 v[82:85], v[184:187], v[196:199], v[82:85]
	v_mfma_f32_16x16x32_bf16 v[86:89], v[192:195], v[196:199], v[86:89]
	v_mfma_f32_16x16x32_bf16 v[90:93], v[200:203], v[196:199], v[90:93]
	v_mfma_f32_16x16x32_bf16 v[94:97], v[204:207], v[196:199], v[94:97]
	ds_read_b128 v[196:199], v220 offset:14336
	ds_read_b64_tr_b16 v[216:217], v154 offset:16384
	ds_read_b64_tr_b16 v[218:219], v154 offset:18432
	s_waitcnt lgkmcnt(6)
	v_mfma_f32_16x16x32_bf16 v[98:101], v[184:187], v[208:211], v[98:101]
	v_mfma_f32_16x16x32_bf16 v[102:105], v[192:195], v[208:211], v[102:105]
	v_mfma_f32_16x16x32_bf16 v[106:109], v[200:203], v[208:211], v[106:109]
	v_mfma_f32_16x16x32_bf16 v[110:113], v[204:207], v[208:211], v[110:113]
	v_add_u32_e32 v236, 0, v162
	ds_read_b128 v[162:165], v236
	ds_read_b64_tr_b16 v[208:209], v161 offset:16384
	ds_read_b64_tr_b16 v[210:211], v161 offset:18432
	s_waitcnt lgkmcnt(8)
	v_mfma_f32_16x16x32_bf16 v[114:117], v[184:187], v[188:191], v[114:117]
	v_mfma_f32_16x16x32_bf16 v[118:121], v[192:195], v[188:191], v[118:121]
	v_mfma_f32_16x16x32_bf16 v[122:125], v[200:203], v[188:191], v[122:125]
	v_mfma_f32_16x16x32_bf16 v[126:129], v[204:207], v[188:191], v[126:129]
	s_waitcnt lgkmcnt(5)
	v_mfma_f32_16x16x32_bf16 v[130:133], v[184:187], v[196:199], v[130:133]
	ds_read_b128 v[184:187], v236 offset:2048
	ds_read_b64_tr_b16 v[188:189], v221 offset:16384
	ds_read_b64_tr_b16 v[190:191], v221 offset:18432
	v_mfma_f32_16x16x32_bf16 v[134:137], v[192:195], v[196:199], v[134:137]
	v_mfma_f32_16x16x32_bf16 v[138:141], v[200:203], v[196:199], v[138:141]
	v_mfma_f32_16x16x32_bf16 v[142:145], v[204:207], v[196:199], v[142:145]
	ds_read_b128 v[192:195], v236 offset:4096
	s_waitcnt vmcnt(3)
	v_add_u32_e32 v152, s34, v160
	s_waitcnt lgkmcnt(6)
	v_mfma_f32_16x16x32_bf16 v[18:21], v[212:215], v[162:165], v[18:21]
	ds_write_b128 v152, v[14:17]
	v_mfma_f32_16x16x32_bf16 v[22:25], v[216:219], v[162:165], v[22:25]
	s_waitcnt lgkmcnt(5)
	v_mfma_f32_16x16x32_bf16 v[26:29], v[208:211], v[162:165], v[26:29]
	s_waitcnt lgkmcnt(2)
	v_mfma_f32_16x16x32_bf16 v[14:17], v[188:191], v[162:165], v[30:33]
	v_mfma_f32_16x16x32_bf16 v[30:33], v[212:215], v[184:187], v[34:37]
	v_mfma_f32_16x16x32_bf16 v[34:37], v[216:219], v[184:187], v[38:41]
	v_mfma_f32_16x16x32_bf16 v[38:41], v[208:211], v[184:187], v[42:45]
	s_nop 2
	ds_read_b128 v[42:45], v236 offset:6144
	s_waitcnt vmcnt(2)
	ds_write_b128 v152, v[10:13] offset:8192
	v_mfma_f32_16x16x32_bf16 v[10:13], v[188:191], v[184:187], v[46:49]
	s_waitcnt lgkmcnt(3)
	v_mfma_f32_16x16x32_bf16 v[46:49], v[212:215], v[192:195], v[50:53]
	v_mfma_f32_16x16x32_bf16 v[50:53], v[216:219], v[192:195], v[54:57]
	v_mfma_f32_16x16x32_bf16 v[54:57], v[208:211], v[192:195], v[58:61]
	s_nop 2
	ds_read_b128 v[58:61], v236 offset:8192
	s_waitcnt vmcnt(1)
	ds_write_b128 v152, v[6:9] offset:16384
	v_mfma_f32_16x16x32_bf16 v[6:9], v[188:191], v[192:195], v[62:65]
	s_waitcnt lgkmcnt(3)
	v_mfma_f32_16x16x32_bf16 v[62:65], v[212:215], v[42:45], v[66:69]
	v_mfma_f32_16x16x32_bf16 v[66:69], v[216:219], v[42:45], v[70:73]
	v_mfma_f32_16x16x32_bf16 v[70:73], v[208:211], v[42:45], v[74:77]
	s_nop 2
	ds_read_b128 v[74:77], v236 offset:10240
	s_waitcnt vmcnt(0)
	ds_write_b128 v152, v[2:5] offset:24576
	v_mfma_f32_16x16x32_bf16 v[2:5], v[188:191], v[42:45], v[78:81]
	s_waitcnt lgkmcnt(3)
	v_mfma_f32_16x16x32_bf16 v[78:81], v[216:219], v[58:61], v[86:89]
	s_nop 2
	ds_read_b128 v[86:89], v236 offset:12288
	v_mfma_f32_16x16x32_bf16 v[42:45], v[212:215], v[58:61], v[82:85]
	v_mfma_f32_16x16x32_bf16 v[82:85], v[208:211], v[58:61], v[90:93]
	v_mfma_f32_16x16x32_bf16 v[58:61], v[188:191], v[58:61], v[94:97]
	s_waitcnt lgkmcnt(2)
	v_mfma_f32_16x16x32_bf16 v[94:97], v[216:219], v[74:77], v[102:105]
	s_nop 2
	ds_read_b128 v[102:105], v236 offset:14336
	v_mfma_f32_16x16x32_bf16 v[90:93], v[212:215], v[74:77], v[98:101]
	v_mfma_f32_16x16x32_bf16 v[98:101], v[208:211], v[74:77], v[106:109]
	v_mfma_f32_16x16x32_bf16 v[74:77], v[188:191], v[74:77], v[110:113]
	s_waitcnt lgkmcnt(1)
	v_mfma_f32_16x16x32_bf16 v[106:109], v[212:215], v[86:89], v[114:117]
	v_mfma_f32_16x16x32_bf16 v[110:113], v[216:219], v[86:89], v[118:121]
	v_mfma_f32_16x16x32_bf16 v[114:117], v[208:211], v[86:89], v[122:125]
	v_mfma_f32_16x16x32_bf16 v[86:89], v[188:191], v[86:89], v[126:129]
	s_waitcnt lgkmcnt(0)
	v_mfma_f32_16x16x32_bf16 v[118:121], v[212:215], v[102:105], v[130:133]
	v_mfma_f32_16x16x32_bf16 v[122:125], v[216:219], v[102:105], v[134:137]
	v_mfma_f32_16x16x32_bf16 v[126:129], v[208:211], v[102:105], v[138:141]
	v_mfma_f32_16x16x32_bf16 v[102:105], v[188:191], v[102:105], v[142:145]
	s_waitcnt lgkmcnt(0)
	s_barrier
	v_add_u32_e32 v164, s34, v157
	v_add_u32_e32 v165, s34, v156
	v_add_u32_e32 v198, s34, v155
	ds_read_b64_tr_b16 v[130:131], v164
	ds_read_b64_tr_b16 v[132:133], v164 offset:2048
	ds_read_b64_tr_b16 v[134:135], v165
	ds_read_b64_tr_b16 v[136:137], v165 offset:2048
	ds_read_b128 v[138:141], v220 offset:32768
	ds_read_b64_tr_b16 v[142:143], v198
	ds_read_b128 v[154:157], v220 offset:34816
	ds_read_b128 v[160:163], v220 offset:36864
	ds_read_b64_tr_b16 v[144:145], v198 offset:2048
	v_add_u32_e32 v200, s34, v153
	ds_read_b64_tr_b16 v[184:185], v200
	ds_read_b64_tr_b16 v[186:187], v200 offset:2048
	s_waitcnt lgkmcnt(6)
	v_mfma_f32_16x16x32_bf16 v[18:21], v[130:133], v[138:141], v[18:21]
	v_mfma_f32_16x16x32_bf16 v[22:25], v[134:137], v[138:141], v[22:25]
	s_waitcnt lgkmcnt(2)
	v_mfma_f32_16x16x32_bf16 v[26:29], v[142:145], v[138:141], v[26:29]
	s_waitcnt lgkmcnt(0)
	v_mfma_f32_16x16x32_bf16 v[14:17], v[184:187], v[138:141], v[14:17]
	ds_read_b128 v[138:141], v220 offset:38912
	v_mfma_f32_16x16x32_bf16 v[30:33], v[130:133], v[154:157], v[30:33]
	v_mfma_f32_16x16x32_bf16 v[34:37], v[134:137], v[154:157], v[34:37]
	v_mfma_f32_16x16x32_bf16 v[38:41], v[142:145], v[154:157], v[38:41]
	v_mfma_f32_16x16x32_bf16 v[10:13], v[184:187], v[154:157], v[10:13]
	ds_read_b128 v[152:155], v220 offset:40960
	v_mfma_f32_16x16x32_bf16 v[46:49], v[130:133], v[160:163], v[46:49]
	v_mfma_f32_16x16x32_bf16 v[50:53], v[134:137], v[160:163], v[50:53]
	v_mfma_f32_16x16x32_bf16 v[54:57], v[142:145], v[160:163], v[54:57]
	v_mfma_f32_16x16x32_bf16 v[6:9], v[184:187], v[160:163], v[6:9]
	ds_read_b128 v[160:163], v220 offset:43008
	s_waitcnt lgkmcnt(2)
	v_mfma_f32_16x16x32_bf16 v[62:65], v[130:133], v[138:141], v[62:65]
	v_mfma_f32_16x16x32_bf16 v[66:69], v[134:137], v[138:141], v[66:69]
	v_mfma_f32_16x16x32_bf16 v[70:73], v[142:145], v[138:141], v[70:73]
	v_mfma_f32_16x16x32_bf16 v[2:5], v[184:187], v[138:141], v[2:5]
	s_waitcnt lgkmcnt(1)
	v_mfma_f32_16x16x32_bf16 v[138:141], v[134:137], v[152:155], v[78:81]
	s_nop 2
	ds_read_b128 v[78:81], v220 offset:45056
	ds_read_b64_tr_b16 v[188:189], v164 offset:16384
	ds_read_b64_tr_b16 v[190:191], v164 offset:18432
	v_mfma_f32_16x16x32_bf16 v[42:45], v[130:133], v[152:155], v[42:45]
	v_mfma_f32_16x16x32_bf16 v[82:85], v[142:145], v[152:155], v[82:85]
	v_mfma_f32_16x16x32_bf16 v[152:155], v[184:187], v[152:155], v[58:61]
	s_nop 2
	ds_read_b128 v[58:61], v220 offset:47104
	ds_read_b64_tr_b16 v[192:193], v165 offset:16384
	ds_read_b64_tr_b16 v[194:195], v165 offset:18432
	s_waitcnt lgkmcnt(6)
	v_mfma_f32_16x16x32_bf16 v[90:93], v[130:133], v[160:163], v[90:93]
	v_mfma_f32_16x16x32_bf16 v[94:97], v[134:137], v[160:163], v[94:97]
	v_mfma_f32_16x16x32_bf16 v[98:101], v[142:145], v[160:163], v[98:101]
	v_mfma_f32_16x16x32_bf16 v[160:163], v[184:187], v[160:163], v[74:77]
	s_nop 2
	ds_read_b128 v[74:77], v236 offset:32768
	ds_read_b64_tr_b16 v[196:197], v198 offset:16384
	ds_read_b64_tr_b16 v[198:199], v198 offset:18432
	s_waitcnt lgkmcnt(8)
	v_mfma_f32_16x16x32_bf16 v[106:109], v[130:133], v[78:81], v[106:109]
	v_mfma_f32_16x16x32_bf16 v[110:113], v[134:137], v[78:81], v[110:113]
	v_mfma_f32_16x16x32_bf16 v[114:117], v[142:145], v[78:81], v[114:117]
	v_mfma_f32_16x16x32_bf16 v[86:89], v[184:187], v[78:81], v[86:89]
	s_waitcnt lgkmcnt(5)
	v_mfma_f32_16x16x32_bf16 v[118:121], v[130:133], v[58:61], v[118:121]
	ds_read_b128 v[78:81], v236 offset:34816
	ds_read_b64_tr_b16 v[130:131], v200 offset:16384
	ds_read_b64_tr_b16 v[132:133], v200 offset:18432
	v_mfma_f32_16x16x32_bf16 v[122:125], v[134:137], v[58:61], v[122:125]
	v_mfma_f32_16x16x32_bf16 v[126:129], v[142:145], v[58:61], v[126:129]
	v_mfma_f32_16x16x32_bf16 v[102:105], v[184:187], v[58:61], v[102:105]
	s_waitcnt lgkmcnt(5)
	v_mfma_f32_16x16x32_bf16 v[134:137], v[188:191], v[74:77], v[18:21]
	s_nop 2
	ds_read_b128 v[18:21], v236 offset:36864
	v_mfma_f32_16x16x32_bf16 v[142:145], v[192:195], v[74:77], v[22:25]
	s_waitcnt lgkmcnt(4)
	v_mfma_f32_16x16x32_bf16 v[184:187], v[196:199], v[74:77], v[26:29]
	s_waitcnt lgkmcnt(1)
	v_mfma_f32_16x16x32_bf16 v[14:17], v[130:133], v[74:77], v[14:17]
	ds_read_b128 v[22:25], v236 offset:38912
	v_mfma_f32_16x16x32_bf16 v[200:203], v[188:191], v[78:81], v[30:33]
	v_mfma_f32_16x16x32_bf16 v[204:207], v[192:195], v[78:81], v[34:37]
	v_mfma_f32_16x16x32_bf16 v[208:211], v[196:199], v[78:81], v[38:41]
	v_mfma_f32_16x16x32_bf16 v[10:13], v[130:133], v[78:81], v[10:13]
	ds_read_b128 v[26:29], v236 offset:40960
	s_waitcnt lgkmcnt(2)
	v_mfma_f32_16x16x32_bf16 v[212:215], v[188:191], v[18:21], v[46:49]
	v_mfma_f32_16x16x32_bf16 v[216:219], v[192:195], v[18:21], v[50:53]
	v_mfma_f32_16x16x32_bf16 v[220:223], v[196:199], v[18:21], v[54:57]
	v_mfma_f32_16x16x32_bf16 v[6:9], v[130:133], v[18:21], v[6:9]
	ds_read_b128 v[18:21], v236 offset:43008
	s_waitcnt lgkmcnt(2)
	v_mfma_f32_16x16x32_bf16 v[224:227], v[188:191], v[22:25], v[62:65]
	v_mfma_f32_16x16x32_bf16 v[228:231], v[192:195], v[22:25], v[66:69]
	v_mfma_f32_16x16x32_bf16 v[232:235], v[196:199], v[22:25], v[70:73]
	v_mfma_f32_16x16x32_bf16 v[2:5], v[130:133], v[22:25], v[2:5]
	ds_read_b128 v[22:25], v236 offset:45056
	s_waitcnt lgkmcnt(2)
	v_mfma_f32_16x16x32_bf16 v[78:81], v[188:191], v[26:29], v[42:45]
	v_mfma_f32_16x16x32_bf16 v[74:77], v[192:195], v[26:29], v[138:141]
	v_mfma_f32_16x16x32_bf16 v[58:61], v[196:199], v[26:29], v[82:85]
	v_mfma_f32_16x16x32_bf16 v[62:65], v[130:133], v[26:29], v[152:155]
	s_nop 1
	ds_read_b128 v[82:85], v236 offset:47104
	s_waitcnt lgkmcnt(2)
	v_mfma_f32_16x16x32_bf16 v[70:73], v[188:191], v[18:21], v[90:93]
	v_mfma_f32_16x16x32_bf16 v[66:69], v[192:195], v[18:21], v[94:97]
	v_mfma_f32_16x16x32_bf16 v[50:53], v[196:199], v[18:21], v[98:101]
	v_mfma_f32_16x16x32_bf16 v[54:57], v[130:133], v[18:21], v[160:163]
	s_waitcnt lgkmcnt(1)
	v_mfma_f32_16x16x32_bf16 v[46:49], v[188:191], v[22:25], v[106:109]
	v_mfma_f32_16x16x32_bf16 v[42:45], v[192:195], v[22:25], v[110:113]
	v_mfma_f32_16x16x32_bf16 v[38:41], v[196:199], v[22:25], v[114:117]
	v_mfma_f32_16x16x32_bf16 v[30:33], v[130:133], v[22:25], v[86:89]
	s_waitcnt lgkmcnt(0)
	v_mfma_f32_16x16x32_bf16 v[34:37], v[188:191], v[82:85], v[118:121]
	v_mfma_f32_16x16x32_bf16 v[26:29], v[192:195], v[82:85], v[122:125]
	v_mfma_f32_16x16x32_bf16 v[22:25], v[196:199], v[82:85], v[126:129]
	v_mfma_f32_16x16x32_bf16 v[18:21], v[130:133], v[82:85], v[102:105]
	v_mov_b32_e32 v236, v1
	v_mov_b32_e32 v237, v166
	s_waitcnt lgkmcnt(0)
	s_barrier
	s_lshl_b32 s4, s42, 6
	v_and_or_b32 v82, v236, 63, v181
	v_lshlrev_b32_e32 v122, 2, v82
	ds_bpermute_b32 v82, v122, v183
	v_xor_b32_e32 v239, 0x80, v122
	s_or_b32 s4, s4, s24
	v_lshlrev_b32_e32 v240, 3, v237
	s_waitcnt lgkmcnt(0)
	v_pk_mul_f32 v[162:163], v[136:137], v[82:83] op_sel_hi:[1,0]
	v_pk_mul_f32 v[164:165], v[134:135], v[82:83] op_sel_hi:[1,0]
	v_pk_mul_f32 v[152:153], v[144:145], v[82:83] op_sel_hi:[1,0]
	v_pk_mul_f32 v[154:155], v[142:143], v[82:83] op_sel_hi:[1,0]
	v_add_u32_e32 v83, 16, v236
	v_and_or_b32 v83, v83, 63, v181
	v_lshlrev_b32_e32 v238, 2, v83
	ds_bpermute_b32 v84, v238, v183
	v_pk_mul_f32 v[138:139], v[14:15], v[82:83] op_sel_hi:[1,0]
	ds_bpermute_b32 v14, v239, v183
	v_add_u32_e32 v144, s43, v236
	v_ashrrev_i32_e32 v145, 31, v144
	s_waitcnt lgkmcnt(1)
	v_pk_mul_f32 v[116:117], v[10:11], v[84:85] op_sel_hi:[1,0]
	v_add_u32_e32 v10, 48, v236
	v_and_or_b32 v10, v10, 63, v181
	s_waitcnt lgkmcnt(0)
	v_pk_mul_f32 v[112:113], v[212:213], v[14:15] op_sel_hi:[1,0]
	v_lshlrev_b32_e32 v213, 2, v10
	ds_bpermute_b32 v10, v213, v183
	v_pk_mul_f32 v[98:99], v[8:9], v[14:15] op_sel_hi:[1,0]
	v_lshlrev_b64 v[8:9], 13, v[144:145]
	v_pk_mul_f32 v[118:119], v[208:209], v[84:85] op_sel_hi:[1,0]
	v_pk_mul_f32 v[100:101], v[6:7], v[14:15] op_sel_hi:[1,0]
	s_waitcnt lgkmcnt(0)
	v_pk_mul_f32 v[86:87], v[2:3], v[10:11] op_sel_hi:[1,0]
	v_lshl_add_u32 v2, v237, 2, s4
	s_mul_i32 s4, s41, 0x3000
	s_ashr_i32 s5, s4, 31
	s_lshl_b64 s[4:5], s[4:5], 2
	s_add_u32 s4, s70, s4
	s_addc_u32 s5, s71, s5
	s_add_u32 s4, s4, 0xc000
	v_ashrrev_i32_e32 v3, 31, v2
	ds_bpermute_b32 v208, v122, v182
	s_addc_u32 s5, s5, 0
	v_lshlrev_b64 v[122:123], 2, v[2:3]
	v_add_u32_e32 v6, 16, v2
	v_lshl_add_u64 v[8:9], s[12:13], 0, v[8:9]
	v_pk_mul_f32 v[128:129], v[202:203], v[84:85] op_sel_hi:[1,0]
	v_pk_mul_f32 v[130:131], v[200:201], v[84:85] op_sel_hi:[1,0]
	v_pk_mul_f32 v[124:125], v[206:207], v[84:85] op_sel_hi:[1,0]
	v_pk_mul_f32 v[126:127], v[204:205], v[84:85] op_sel_hi:[1,0]
	v_pk_mul_f32 v[120:121], v[210:211], v[84:85] op_sel_hi:[1,0]
	v_pk_mul_f32 v[114:115], v[12:13], v[84:85] op_sel_hi:[1,0]
	v_pk_mul_f32 v[84:85], v[4:5], v[10:11] op_sel_hi:[1,0]
	v_lshl_add_u64 v[4:5], s[4:5], 0, v[122:123]
	v_ashrrev_i32_e32 v7, 31, v6
	v_lshl_add_u64 v[132:133], v[8:9], 0, v[122:123]
	v_pk_mul_f32 v[156:157], v[186:187], v[82:83] op_sel_hi:[1,0]
	v_pk_mul_f32 v[160:161], v[184:185], v[82:83] op_sel_hi:[1,0]
	v_pk_mul_f32 v[136:137], v[16:17], v[82:83] op_sel_hi:[1,0]
	v_pk_mul_f32 v[110:111], v[214:215], v[14:15] op_sel_hi:[1,0]
	v_pk_mul_f32 v[106:107], v[218:219], v[14:15] op_sel_hi:[1,0]
	v_pk_mul_f32 v[108:109], v[216:217], v[14:15] op_sel_hi:[1,0]
	v_pk_mul_f32 v[102:103], v[222:223], v[14:15] op_sel_hi:[1,0]
	v_pk_mul_f32 v[104:105], v[220:221], v[14:15] op_sel_hi:[1,0]
	v_pk_mul_f32 v[94:95], v[226:227], v[10:11] op_sel_hi:[1,0]
	v_pk_mul_f32 v[96:97], v[224:225], v[10:11] op_sel_hi:[1,0]
	v_pk_mul_f32 v[90:91], v[230:231], v[10:11] op_sel_hi:[1,0]
	v_pk_mul_f32 v[92:93], v[228:229], v[10:11] op_sel_hi:[1,0]
	v_pk_mul_f32 v[88:89], v[234:235], v[10:11] op_sel_hi:[1,0]
	v_pk_mul_f32 v[82:83], v[232:233], v[10:11] op_sel_hi:[1,0]
	v_lshl_add_u64 v[6:7], v[6:7], 2, s[4:5]
	global_load_dwordx4 v[184:187], v[132:133], off nt
	global_load_dwordx4 v[14:17], v[4:5], off
	global_load_dwordx4 v[10:13], v[6:7], off
	v_add_u32_e32 v4, 32, v2
	v_add_u32_e32 v2, 48, v2
	v_ashrrev_i32_e32 v5, 31, v4
	v_ashrrev_i32_e32 v3, 31, v2
	v_lshl_add_u64 v[4:5], v[4:5], 2, s[4:5]
	v_lshl_add_u64 v[2:3], v[2:3], 2, s[4:5]
	global_load_dwordx4 v[188:191], v[132:133], off offset:64 nt
	global_load_dwordx4 v[192:195], v[132:133], off offset:128 nt
	global_load_dwordx4 v[6:9], v[4:5], off
	s_nop 0
	global_load_dwordx4 v[2:5], v[2:3], off
	s_nop 0
	global_load_dwordx4 v[196:199], v[132:133], off offset:192 nt
	v_add_u32_e32 v132, 16, v144
	ds_bpermute_b32 v212, v238, v182
	ds_bpermute_b32 v216, v239, v182
	v_ashrrev_i32_e32 v133, 31, v132
	v_lshlrev_b64 v[132:133], 13, v[132:133]
	v_lshl_add_u64 v[132:133], s[12:13], 0, v[132:133]
	v_lshl_add_u64 v[210:211], v[132:133], 0, v[122:123]
	global_load_dwordx4 v[200:203], v[210:211], off nt
	global_load_dwordx4 v[204:207], v[210:211], off offset:64 nt
	s_waitcnt lgkmcnt(2)
	v_pk_mul_f32 v[142:143], v[78:79], v[208:209] op_sel_hi:[1,0]
	v_pk_mul_f32 v[78:79], v[60:61], v[208:209] op_sel_hi:[1,0]
	s_waitcnt lgkmcnt(1)
	v_pk_mul_f32 v[60:61], v[50:51], v[212:213] op_sel_hi:[1,0]
	s_waitcnt lgkmcnt(0)
	v_pk_mul_f32 v[50:51], v[48:49], v[216:217] op_sel_hi:[1,0]
	v_pk_mul_f32 v[48:49], v[42:43], v[216:217] op_sel_hi:[1,0]
	v_add_u32_e32 v42, 32, v144
	ds_bpermute_b32 v182, v213, v182
	v_ashrrev_i32_e32 v43, 31, v42
	v_pk_mul_f32 v[132:133], v[76:77], v[208:209] op_sel_hi:[1,0]
	v_pk_mul_f32 v[134:135], v[74:75], v[208:209] op_sel_hi:[1,0]
	v_pk_mul_f32 v[74:75], v[64:65], v[208:209] op_sel_hi:[1,0]
	v_pk_mul_f32 v[76:77], v[62:63], v[208:209] op_sel_hi:[1,0]
	v_pk_mul_f32 v[62:63], v[68:69], v[212:213] op_sel_hi:[1,0]
	v_pk_mul_f32 v[64:65], v[66:67], v[212:213] op_sel_hi:[1,0]
	global_load_dwordx4 v[66:69], v[210:211], off offset:128 nt
	v_lshlrev_b64 v[42:43], 13, v[42:43]
	v_lshl_add_u64 v[42:43], s[12:13], 0, v[42:43]
	v_lshl_add_u64 v[220:221], v[42:43], 0, v[122:123]
	v_pk_mul_f32 v[140:141], v[80:81], v[208:209] op_sel_hi:[1,0]
	v_pk_mul_f32 v[80:81], v[58:59], v[208:209] op_sel_hi:[1,0]
	v_pk_mul_f32 v[72:73], v[72:73], v[212:213] op_sel_hi:[1,0]
	v_pk_mul_f32 v[70:71], v[70:71], v[212:213] op_sel_hi:[1,0]
	v_pk_mul_f32 v[58:59], v[52:53], v[212:213] op_sel_hi:[1,0]
	v_pk_mul_f32 v[56:57], v[56:57], v[212:213] op_sel_hi:[1,0]
	v_pk_mul_f32 v[54:55], v[54:55], v[212:213] op_sel_hi:[1,0]
	global_load_dwordx4 v[212:215], v[220:221], off nt
	v_pk_mul_f32 v[52:53], v[46:47], v[216:217] op_sel_hi:[1,0]
	global_load_dwordx4 v[208:211], v[210:211], off offset:192 nt
	v_pk_mul_f32 v[46:47], v[44:45], v[216:217] op_sel_hi:[1,0]
	v_pk_mul_f32 v[42:43], v[32:33], v[216:217] op_sel_hi:[1,0]
	v_pk_mul_f32 v[44:45], v[30:31], v[216:217] op_sel_hi:[1,0]
	s_waitcnt lgkmcnt(0)
	v_pk_mul_f32 v[30:31], v[36:37], v[182:183] op_sel_hi:[1,0]
	v_pk_mul_f32 v[32:33], v[34:35], v[182:183] op_sel_hi:[1,0]
	global_load_dwordx4 v[34:37], v[220:221], off offset:64 nt
	v_pk_mul_f32 v[40:41], v[40:41], v[216:217] op_sel_hi:[1,0]
	v_pk_mul_f32 v[38:39], v[38:39], v[216:217] op_sel_hi:[1,0]
	global_load_dwordx4 v[216:219], v[220:221], off offset:128 nt
	s_nop 0
	global_load_dwordx4 v[220:223], v[220:221], off offset:192 nt
	v_pk_mul_f32 v[28:29], v[28:29], v[182:183] op_sel_hi:[1,0]
	v_pk_mul_f32 v[26:27], v[26:27], v[182:183] op_sel_hi:[1,0]
	v_pk_mul_f32 v[24:25], v[24:25], v[182:183] op_sel_hi:[1,0]
	v_pk_mul_f32 v[22:23], v[22:23], v[182:183] op_sel_hi:[1,0]
	v_pk_mul_f32 v[20:21], v[20:21], v[182:183] op_sel_hi:[1,0]
	v_pk_mul_f32 v[18:19], v[18:19], v[182:183] op_sel_hi:[1,0]
	v_add_u32_e32 v182, 48, v144
	v_ashrrev_i32_e32 v183, 31, v182
	v_lshlrev_b64 v[182:183], 13, v[182:183]
	v_lshl_add_u64 v[182:183], s[12:13], 0, v[182:183]
	v_lshl_add_u64 v[182:183], v[182:183], 0, v[122:123]
	v_add_u32_e32 v145, s39, v236
	global_load_dwordx4 v[224:227], v[182:183], off nt
	global_load_dwordx4 v[228:231], v[182:183], off offset:64 nt
	global_load_dwordx4 v[232:235], v[182:183], off offset:128 nt
	global_load_dwordx4 v[236:239], v[182:183], off offset:192 nt
	s_add_i32 s40, s40, 0
	v_mul_lo_u32 v145, v145, s35
	v_add3_u32 v240, s40, v240, v145
	v_add_u32_e32 v145, 0x2000, v240
	s_andn2_b64 vcc, exec, s[76:77]
	s_waitcnt vmcnt(18)
	v_pk_fma_f32 v[162:163], v[162:163], v[16:17], v[186:187]
	v_pk_fma_f32 v[164:165], v[164:165], v[14:15], v[184:185]
	s_waitcnt vmcnt(16)
	v_pk_fma_f32 v[152:153], v[152:153], v[12:13], v[190:191]
	v_pk_fma_f32 v[154:155], v[154:155], v[10:11], v[188:189]
	v_cvt_pk_bf16_f32 v164, v164, v165
	v_cvt_pk_bf16_f32 v165, v162, v163
	v_cvt_pk_bf16_f32 v154, v154, v155
	v_cvt_pk_bf16_f32 v155, v152, v153
	ds_write2_b64 v240, v[164:165], v[154:155] offset1:4
	s_waitcnt vmcnt(14)
	v_pk_fma_f32 v[152:153], v[156:157], v[8:9], v[194:195]
	v_pk_fma_f32 v[154:155], v[160:161], v[6:7], v[192:193]
	s_waitcnt vmcnt(12)
	v_pk_fma_f32 v[136:137], v[136:137], v[4:5], v[198:199]
	v_pk_fma_f32 v[138:139], v[138:139], v[2:3], v[196:197]
	s_waitcnt vmcnt(11)
	v_pk_fma_f32 v[128:129], v[128:129], v[16:17], v[202:203]
	v_pk_fma_f32 v[130:131], v[130:131], v[14:15], v[200:201]
	s_waitcnt vmcnt(10)
	v_pk_fma_f32 v[124:125], v[124:125], v[12:13], v[206:207]
	v_cvt_pk_bf16_f32 v130, v130, v131
	v_cvt_pk_bf16_f32 v131, v128, v129
	v_cvt_pk_bf16_f32 v129, v124, v125
	v_add_u32_e32 v124, 64, v144
	v_ashrrev_i32_e32 v125, 31, v124
	v_lshlrev_b64 v[124:125], 13, v[124:125]
	v_pk_fma_f32 v[126:127], v[126:127], v[10:11], v[204:205]
	v_lshl_add_u64 v[124:125], s[12:13], 0, v[124:125]
	v_cvt_pk_bf16_f32 v154, v154, v155
	v_cvt_pk_bf16_f32 v155, v152, v153
	v_cvt_pk_bf16_f32 v138, v138, v139
	v_cvt_pk_bf16_f32 v139, v136, v137
	v_cvt_pk_bf16_f32 v128, v126, v127
	s_waitcnt vmcnt(9)
	v_pk_fma_f32 v[66:67], v[118:119], v[6:7], v[66:67]
	v_add_u32_e32 v118, 0x50, v144
	v_ashrrev_i32_e32 v119, 31, v118
	v_lshlrev_b64 v[118:119], 13, v[118:119]
	v_lshl_add_u64 v[136:137], v[124:125], 0, v[122:123]
	v_pk_fma_f32 v[68:69], v[120:121], v[8:9], v[68:69]
	v_lshl_add_u64 v[118:119], s[12:13], 0, v[118:119]
	ds_write2_b64 v240, v[154:155], v[138:139] offset0:8 offset1:12
	global_load_dwordx4 v[124:127], v[136:137], off nt
	ds_write2_b64 v145, v[130:131], v[128:129] offset0:32 offset1:36
	global_load_dwordx4 v[128:131], v[136:137], off offset:64 nt
	v_cvt_pk_bf16_f32 v138, v66, v67
	v_cvt_pk_bf16_f32 v139, v68, v69
	s_waitcnt vmcnt(9)
	v_pk_fma_f32 v[114:115], v[114:115], v[4:5], v[210:211]
	v_pk_fma_f32 v[116:117], v[116:117], v[2:3], v[208:209]
	global_load_dwordx4 v[66:69], v[136:137], off offset:128 nt
	v_cvt_pk_bf16_f32 v152, v116, v117
	v_cvt_pk_bf16_f32 v153, v114, v115
	global_load_dwordx4 v[114:117], v[136:137], off offset:192 nt
	v_lshl_add_u64 v[136:137], v[118:119], 0, v[122:123]
	s_waitcnt vmcnt(10)
	v_pk_fma_f32 v[106:107], v[106:107], v[12:13], v[36:37]
	v_pk_fma_f32 v[34:35], v[108:109], v[10:11], v[34:35]
	global_load_dwordx4 v[118:121], v[136:137], off nt
	ds_write2_b64 v145, v[138:139], v[152:153] offset0:40 offset1:44
	v_pk_fma_f32 v[138:139], v[110:111], v[16:17], v[214:215]
	v_pk_fma_f32 v[152:153], v[112:113], v[14:15], v[212:213]
	global_load_dwordx4 v[110:113], v[136:137], off offset:64 nt
	v_cvt_pk_bf16_f32 v154, v34, v35
	global_load_dwordx4 v[34:37], v[136:137], off offset:128 nt
	v_cvt_pk_bf16_f32 v155, v106, v107
	global_load_dwordx4 v[106:109], v[136:137], off offset:192 nt
	v_add_u32_e32 v136, 0x60, v144
	v_cvt_pk_bf16_f32 v152, v152, v153
	v_cvt_pk_bf16_f32 v153, v138, v139
	v_add_u32_e32 v145, 0x4000, v240
	v_ashrrev_i32_e32 v137, 31, v136
	v_lshlrev_b64 v[136:137], 13, v[136:137]
	ds_write2_b64 v145, v[152:153], v[154:155] offset0:64 offset1:68
	s_waitcnt vmcnt(13)
	v_pk_fma_f32 v[152:153], v[102:103], v[8:9], v[218:219]
	v_pk_fma_f32 v[154:155], v[104:105], v[6:7], v[216:217]
	v_lshl_add_u64 v[136:137], s[12:13], 0, v[136:137]
	v_cvt_pk_bf16_f32 v154, v154, v155
	v_cvt_pk_bf16_f32 v155, v152, v153
	s_waitcnt vmcnt(12)
	v_pk_fma_f32 v[152:153], v[98:99], v[4:5], v[222:223]
	v_pk_fma_f32 v[98:99], v[100:101], v[2:3], v[220:221]
	v_lshl_add_u64 v[156:157], v[136:137], 0, v[122:123]
	v_cvt_pk_bf16_f32 v160, v98, v99
	v_cvt_pk_bf16_f32 v161, v152, v153
	v_add_u32_e32 v144, 0x70, v144
	global_load_dwordx4 v[136:139], v[156:157], off nt
	global_load_dwordx4 v[102:105], v[156:157], off offset:64 nt
	ds_write2_b64 v145, v[154:155], v[160:161] offset0:72 offset1:76
	v_ashrrev_i32_e32 v145, 31, v144
	v_lshlrev_b64 v[144:145], 13, v[144:145]
	v_lshl_add_u64 v[144:145], s[12:13], 0, v[144:145]
	global_load_dwordx4 v[98:101], v[156:157], off offset:128 nt
	global_load_dwordx4 v[152:155], v[156:157], off offset:192 nt
	v_lshl_add_u64 v[122:123], v[144:145], 0, v[122:123]
	s_waitcnt vmcnt(15)
	v_pk_fma_f32 v[144:145], v[94:95], v[16:17], v[226:227]
	v_pk_fma_f32 v[94:95], v[96:97], v[14:15], v[224:225]
	s_waitcnt vmcnt(14)
	v_pk_fma_f32 v[90:91], v[90:91], v[12:13], v[230:231]
	v_pk_fma_f32 v[92:93], v[92:93], v[10:11], v[228:229]
	global_load_dwordx4 v[160:163], v[122:123], off nt
	v_cvt_pk_bf16_f32 v156, v94, v95
	global_load_dwordx4 v[94:97], v[122:123], off offset:64 nt
	v_cvt_pk_bf16_f32 v157, v144, v145
	v_cvt_pk_bf16_f32 v144, v92, v93
	v_cvt_pk_bf16_f32 v145, v90, v91
	global_load_dwordx4 v[90:93], v[122:123], off offset:128 nt
	global_load_dwordx4 v[182:185], v[122:123], off offset:192 nt
	s_waitcnt vmcnt(17)
	v_pk_fma_f32 v[88:89], v[88:89], v[8:9], v[234:235]
	v_pk_fma_f32 v[82:83], v[82:83], v[6:7], v[232:233]
	s_waitcnt vmcnt(16)
	v_pk_fma_f32 v[84:85], v[84:85], v[4:5], v[238:239]
	v_pk_fma_f32 v[86:87], v[86:87], v[2:3], v[236:237]
	v_add_u32_e32 v164, 0x6000, v240
	v_cvt_pk_bf16_f32 v82, v82, v83
	v_cvt_pk_bf16_f32 v83, v88, v89
	v_cvt_pk_bf16_f32 v86, v86, v87
	v_cvt_pk_bf16_f32 v87, v84, v85
	ds_write2_b64 v164, v[82:83], v[86:87] offset0:104 offset1:108
	ds_write2_b64 v164, v[156:157], v[144:145] offset0:96 offset1:100
	s_waitcnt vmcnt(15)
	v_pk_fma_f32 v[82:83], v[140:141], v[16:17], v[126:127]
	v_pk_fma_f32 v[84:85], v[142:143], v[14:15], v[124:125]
	s_waitcnt vmcnt(14)
	v_pk_fma_f32 v[86:87], v[134:135], v[10:11], v[128:129]
	v_cvt_pk_bf16_f32 v84, v84, v85
	v_cvt_pk_bf16_f32 v85, v82, v83
	v_pk_fma_f32 v[82:83], v[132:133], v[12:13], v[130:131]
	v_cvt_pk_bf16_f32 v86, v86, v87
	s_waitcnt vmcnt(13)
	v_pk_fma_f32 v[68:69], v[78:79], v[8:9], v[68:69]
	v_pk_fma_f32 v[66:67], v[80:81], v[6:7], v[66:67]
	v_cvt_pk_bf16_f32 v87, v82, v83
	v_cvt_pk_bf16_f32 v66, v66, v67
	v_cvt_pk_bf16_f32 v67, v68, v69
	s_waitcnt vmcnt(12)
	v_pk_fma_f32 v[68:69], v[74:75], v[4:5], v[116:117]
	v_pk_fma_f32 v[74:75], v[76:77], v[2:3], v[114:115]
	v_add_u32_e32 v82, 0x8000, v240
	v_cvt_pk_bf16_f32 v74, v74, v75
	v_cvt_pk_bf16_f32 v75, v68, v69
	ds_write2_b64 v82, v[66:67], v[74:75] offset0:136 offset1:140
	s_waitcnt vmcnt(10)
	v_pk_fma_f32 v[62:63], v[62:63], v[12:13], v[112:113]
	v_pk_fma_f32 v[64:65], v[64:65], v[10:11], v[110:111]
	s_waitcnt vmcnt(9)
	v_pk_fma_f32 v[36:37], v[58:59], v[8:9], v[36:37]
	v_pk_fma_f32 v[34:35], v[60:61], v[6:7], v[34:35]
	s_waitcnt vmcnt(8)
	v_pk_fma_f32 v[54:55], v[54:55], v[2:3], v[106:107]
	v_cvt_pk_bf16_f32 v34, v34, v35
	v_cvt_pk_bf16_f32 v35, v36, v37
	v_pk_fma_f32 v[36:37], v[56:57], v[4:5], v[108:109]
	v_cvt_pk_bf16_f32 v64, v64, v65
	v_cvt_pk_bf16_f32 v65, v62, v63
	v_add_u32_e32 v62, 0xa000, v240
	v_cvt_pk_bf16_f32 v54, v54, v55
	v_cvt_pk_bf16_f32 v55, v36, v37
	ds_write2_b64 v62, v[34:35], v[54:55] offset0:168 offset1:172
	v_pk_fma_f32 v[66:67], v[16:17], v[72:73], v[120:121]
	v_pk_fma_f32 v[68:69], v[14:15], v[70:71], v[118:119]
	ds_write2_b64 v82, v[84:85], v[86:87] offset0:128 offset1:132
	v_cvt_pk_bf16_f32 v68, v68, v69
	v_cvt_pk_bf16_f32 v69, v66, v67
	ds_write2_b64 v62, v[68:69], v[64:65] offset0:160 offset1:164
	s_waitcnt vmcnt(7)
	v_pk_fma_f32 v[34:35], v[16:17], v[50:51], v[138:139]
	v_pk_fma_f32 v[36:37], v[14:15], v[52:53], v[136:137]
	s_waitcnt vmcnt(3)
	v_pk_fma_f32 v[16:17], v[16:17], v[30:31], v[162:163]
	v_cvt_pk_bf16_f32 v36, v36, v37
	v_cvt_pk_bf16_f32 v37, v34, v35
	v_pk_fma_f32 v[34:35], v[12:13], v[46:47], v[104:105]
	v_pk_fma_f32 v[46:47], v[10:11], v[48:49], v[102:103]
	v_add_u32_e32 v48, 0xc000, v240
	v_cvt_pk_bf16_f32 v46, v46, v47
	v_cvt_pk_bf16_f32 v47, v34, v35
	ds_write2_b64 v48, v[36:37], v[46:47] offset0:192 offset1:196
	v_pk_fma_f32 v[34:35], v[40:41], v[8:9], v[100:101]
	v_pk_fma_f32 v[36:37], v[38:39], v[6:7], v[98:99]
	v_pk_fma_f32 v[38:39], v[44:45], v[2:3], v[152:153]
	v_cvt_pk_bf16_f32 v36, v36, v37
	v_cvt_pk_bf16_f32 v37, v34, v35
	v_pk_fma_f32 v[34:35], v[42:43], v[4:5], v[154:155]
	s_waitcnt vmcnt(2)
	v_pk_fma_f32 v[12:13], v[12:13], v[28:29], v[96:97]
	v_pk_fma_f32 v[10:11], v[10:11], v[26:27], v[94:95]
	s_waitcnt vmcnt(1)
	v_pk_fma_f32 v[8:9], v[8:9], v[24:25], v[92:93]
	v_pk_fma_f32 v[6:7], v[6:7], v[22:23], v[90:91]
	s_waitcnt vmcnt(0)
	v_pk_fma_f32 v[4:5], v[20:21], v[4:5], v[184:185]
	v_pk_fma_f32 v[2:3], v[18:19], v[2:3], v[182:183]
	v_cvt_pk_bf16_f32 v10, v10, v11
	v_cvt_pk_bf16_f32 v11, v12, v13
	v_add_u32_e32 v12, 0xe000, v240
	v_cvt_pk_bf16_f32 v6, v6, v7
	v_cvt_pk_bf16_f32 v7, v8, v9
	v_cvt_pk_bf16_f32 v2, v2, v3
	v_cvt_pk_bf16_f32 v3, v4, v5
	v_lshl_or_b32 v8, s38, 5, v167
	v_pk_fma_f32 v[14:15], v[14:15], v[32:33], v[160:161]
	ds_write2_b64 v12, v[6:7], v[2:3] offset0:232 offset1:236
	v_mad_u64_u32 v[6:7], s[4:5], v8, s35, v[148:149]
	v_add_u32_e32 v8, s25, v8
	v_cvt_pk_bf16_f32 v14, v14, v15
	v_cvt_pk_bf16_f32 v15, v16, v17
	v_ashrrev_i32_e32 v9, 31, v8
	ds_write2_b64 v12, v[14:15], v[10:11] offset0:224 offset1:228
	v_lshlrev_b64 v[10:11], 12, v[8:9]
	v_cvt_pk_bf16_f32 v38, v38, v39
	v_cvt_pk_bf16_f32 v39, v34, v35
	v_lshl_add_u64 v[10:11], s[18:19], 0, v[10:11]
	ds_write2_b64 v48, v[36:37], v[38:39] offset0:200 offset1:204
	v_lshl_add_u64 v[10:11], v[10:11], 0, s[22:23]
	s_waitcnt lgkmcnt(0)
	s_barrier
	v_lshl_add_u64 v[10:11], v[10:11], 0, v[146:147]
	ds_read_b128 v[2:5], v6
	s_waitcnt lgkmcnt(0)
	global_store_dwordx4 v[10:11], v[2:5], off sc1
	s_nop 1
	v_add_u32_e32 v10, 2, v8
	v_ashrrev_i32_e32 v11, 31, v10
	v_lshlrev_b64 v[10:11], 12, v[10:11]
	v_lshl_add_u64 v[10:11], s[18:19], 0, v[10:11]
	v_lshl_add_u64 v[10:11], v[10:11], 0, s[22:23]
	v_lshl_add_u64 v[10:11], v[10:11], 0, v[146:147]
	ds_read_b128 v[2:5], v6 offset:1056
	s_waitcnt lgkmcnt(0)
	global_store_dwordx4 v[10:11], v[2:5], off sc1
	s_nop 1
	v_add_u32_e32 v10, 4, v8
	v_ashrrev_i32_e32 v11, 31, v10
	v_lshlrev_b64 v[10:11], 12, v[10:11]
	v_lshl_add_u64 v[10:11], s[18:19], 0, v[10:11]
	v_lshl_add_u64 v[10:11], v[10:11], 0, s[22:23]
	v_lshl_add_u64 v[10:11], v[10:11], 0, v[146:147]
	ds_read_b128 v[2:5], v6 offset:2112
	s_waitcnt lgkmcnt(0)
	global_store_dwordx4 v[10:11], v[2:5], off sc1
	s_nop 1
	v_add_u32_e32 v10, 6, v8
	v_ashrrev_i32_e32 v11, 31, v10
	v_lshlrev_b64 v[10:11], 12, v[10:11]
	v_lshl_add_u64 v[10:11], s[18:19], 0, v[10:11]
	v_lshl_add_u64 v[10:11], v[10:11], 0, s[22:23]
	v_lshl_add_u64 v[10:11], v[10:11], 0, v[146:147]
	ds_read_b128 v[2:5], v6 offset:3168
	s_waitcnt lgkmcnt(0)
	global_store_dwordx4 v[10:11], v[2:5], off sc1
	s_nop 1
	v_add_u32_e32 v10, 8, v8
	v_ashrrev_i32_e32 v11, 31, v10
	v_lshlrev_b64 v[10:11], 12, v[10:11]
	v_lshl_add_u64 v[10:11], s[18:19], 0, v[10:11]
	v_lshl_add_u64 v[10:11], v[10:11], 0, s[22:23]
	v_lshl_add_u64 v[10:11], v[10:11], 0, v[146:147]
	ds_read_b128 v[2:5], v6 offset:4224
	s_waitcnt lgkmcnt(0)
	global_store_dwordx4 v[10:11], v[2:5], off sc1
	s_nop 1
	v_add_u32_e32 v10, 10, v8
	v_ashrrev_i32_e32 v11, 31, v10
	v_lshlrev_b64 v[10:11], 12, v[10:11]
	v_lshl_add_u64 v[10:11], s[18:19], 0, v[10:11]
	v_lshl_add_u64 v[10:11], v[10:11], 0, s[22:23]
	v_lshl_add_u64 v[10:11], v[10:11], 0, v[146:147]
	ds_read_b128 v[2:5], v6 offset:5280
	s_waitcnt lgkmcnt(0)
	global_store_dwordx4 v[10:11], v[2:5], off sc1
	s_nop 1
	v_add_u32_e32 v10, 12, v8
	v_ashrrev_i32_e32 v11, 31, v10
	v_lshlrev_b64 v[10:11], 12, v[10:11]
	v_lshl_add_u64 v[10:11], s[18:19], 0, v[10:11]
	v_lshl_add_u64 v[10:11], v[10:11], 0, s[22:23]
	v_lshl_add_u64 v[10:11], v[10:11], 0, v[146:147]
	ds_read_b128 v[2:5], v6 offset:6336
	s_waitcnt lgkmcnt(0)
	global_store_dwordx4 v[10:11], v[2:5], off sc1
	s_nop 1
	v_add_u32_e32 v10, 14, v8
	v_ashrrev_i32_e32 v11, 31, v10
	v_lshlrev_b64 v[10:11], 12, v[10:11]
	v_lshl_add_u64 v[10:11], s[18:19], 0, v[10:11]
	v_lshl_add_u64 v[10:11], v[10:11], 0, s[22:23]
	v_lshl_add_u64 v[10:11], v[10:11], 0, v[146:147]
	ds_read_b128 v[2:5], v6 offset:7392
	s_waitcnt lgkmcnt(0)
	global_store_dwordx4 v[10:11], v[2:5], off sc1
	s_nop 1
	v_add_u32_e32 v10, 16, v8
	v_ashrrev_i32_e32 v11, 31, v10
	v_lshlrev_b64 v[10:11], 12, v[10:11]
	v_lshl_add_u64 v[10:11], s[18:19], 0, v[10:11]
	v_lshl_add_u64 v[10:11], v[10:11], 0, s[22:23]
	v_lshl_add_u64 v[10:11], v[10:11], 0, v[146:147]
	ds_read_b128 v[2:5], v6 offset:8448
	s_waitcnt lgkmcnt(0)
	global_store_dwordx4 v[10:11], v[2:5], off sc1
	s_nop 1
	v_add_u32_e32 v10, 18, v8
	v_ashrrev_i32_e32 v11, 31, v10
	v_lshlrev_b64 v[10:11], 12, v[10:11]
	v_lshl_add_u64 v[10:11], s[18:19], 0, v[10:11]
	v_lshl_add_u64 v[10:11], v[10:11], 0, s[22:23]
	v_lshl_add_u64 v[10:11], v[10:11], 0, v[146:147]
	ds_read_b128 v[2:5], v6 offset:9504
	s_waitcnt lgkmcnt(0)
	global_store_dwordx4 v[10:11], v[2:5], off sc1
	s_nop 1
	v_add_u32_e32 v10, 20, v8
	v_ashrrev_i32_e32 v11, 31, v10
	v_lshlrev_b64 v[10:11], 12, v[10:11]
	v_lshl_add_u64 v[10:11], s[18:19], 0, v[10:11]
	v_lshl_add_u64 v[10:11], v[10:11], 0, s[22:23]
	v_lshl_add_u64 v[10:11], v[10:11], 0, v[146:147]
	ds_read_b128 v[2:5], v6 offset:10560
	s_waitcnt lgkmcnt(0)
	global_store_dwordx4 v[10:11], v[2:5], off sc1
	s_nop 1
	v_add_u32_e32 v10, 22, v8
	v_ashrrev_i32_e32 v11, 31, v10
	v_lshlrev_b64 v[10:11], 12, v[10:11]
	v_lshl_add_u64 v[10:11], s[18:19], 0, v[10:11]
	v_lshl_add_u64 v[10:11], v[10:11], 0, s[22:23]
	v_lshl_add_u64 v[10:11], v[10:11], 0, v[146:147]
	ds_read_b128 v[2:5], v6 offset:11616
	s_waitcnt lgkmcnt(0)
	global_store_dwordx4 v[10:11], v[2:5], off sc1
	s_nop 1
	v_add_u32_e32 v10, 24, v8
	v_ashrrev_i32_e32 v11, 31, v10
	v_lshlrev_b64 v[10:11], 12, v[10:11]
	v_lshl_add_u64 v[10:11], s[18:19], 0, v[10:11]
	v_lshl_add_u64 v[10:11], v[10:11], 0, s[22:23]
	v_lshl_add_u64 v[10:11], v[10:11], 0, v[146:147]
	ds_read_b128 v[2:5], v6 offset:12672
	s_waitcnt lgkmcnt(0)
	global_store_dwordx4 v[10:11], v[2:5], off sc1
	s_nop 1
	v_add_u32_e32 v10, 26, v8
	v_ashrrev_i32_e32 v11, 31, v10
	v_lshlrev_b64 v[10:11], 12, v[10:11]
	v_lshl_add_u64 v[10:11], s[18:19], 0, v[10:11]
	v_lshl_add_u64 v[10:11], v[10:11], 0, s[22:23]
	v_lshl_add_u64 v[10:11], v[10:11], 0, v[146:147]
	ds_read_b128 v[2:5], v6 offset:13728
	s_waitcnt lgkmcnt(0)
	global_store_dwordx4 v[10:11], v[2:5], off sc1
	s_nop 1
	v_add_u32_e32 v10, 28, v8
	v_ashrrev_i32_e32 v11, 31, v10
	v_lshlrev_b64 v[10:11], 12, v[10:11]
	v_lshl_add_u64 v[10:11], s[18:19], 0, v[10:11]
	v_lshl_add_u64 v[10:11], v[10:11], 0, s[22:23]
	ds_read_b128 v[2:5], v6 offset:14784
	v_lshl_add_u64 v[10:11], v[10:11], 0, v[146:147]
	s_waitcnt lgkmcnt(0)
	global_store_dwordx4 v[10:11], v[2:5], off sc1
	s_nop 1
	ds_read_b128 v[2:5], v6 offset:15840
	v_add_u32_e32 v6, 30, v8
	v_ashrrev_i32_e32 v7, 31, v6
	v_lshlrev_b64 v[6:7], 12, v[6:7]
	v_lshl_add_u64 v[6:7], s[18:19], 0, v[6:7]
	v_lshl_add_u64 v[6:7], v[6:7], 0, s[22:23]
	v_lshl_add_u64 v[6:7], v[6:7], 0, v[146:147]
	s_waitcnt lgkmcnt(0)
	global_store_dwordx4 v[6:7], v[2:5], off sc1
	s_nop 1
	s_waitcnt lgkmcnt(0)
	s_barrier
	s_cbranch_vccnz .LBB0_1127
	s_waitcnt vmcnt(0)
	s_barrier
	s_and_saveexec_b64 s[4:5], s[0:1]
	s_cbranch_execz .LBB0_1126
	s_mov_b64 s[6:7], exec
	v_mbcnt_lo_u32_b32 v2, s6, 0
	v_mbcnt_hi_u32_b32 v2, s7, v2
	v_cmp_eq_u32_e32 vcc, 0, v2
	s_and_b64 s[22:23], exec, vcc
	s_mov_b64 exec, s[22:23]
	s_cbranch_execz .LBB0_1126
	s_lshl_b32 s22, s37, 4
	s_ashr_i32 s23, s22, 31
	s_lshl_b64 s[22:23], s[22:23], 2
	s_add_u32 s22, s29, s22
	s_addc_u32 s23, s30, s23
	s_bcnt1_i32_b64 s6, s[6:7]
	v_mov_b32_e32 v2, s6
	global_atomic_add v147, v2, s[22:23]
	s_branch .LBB0_1126
